# prologue int8 weight strips: both passes hand software-pipelined (ring of 24 row-slices in flight, scalar-base addressing, fully unrolled)
# speedup vs baseline: 1.0166x; 1.0061x over previous
;     ...
;     for (int kb = 0; kb < D / 64; ++kb) {
; #pragma unroll
;         for (int i = 0; i < 8; ++i) { const int k = 64 * kb + 8 * i + kr; const f32x4 v = __builtin_nontemporal_load((const f32x4*)(W + (size_t)k * pitch)) * g[k];
;             mx[0] = __builtin_fmaxf(mx[0], __builtin_fabsf(v[0])); mx[1] = __builtin_fmaxf(mx[1], __builtin_fabsf(v[1])); mx[2] = __builtin_fmaxf(mx[2], __builtin_fabsf(v[2])); mx[3] = __builtin_fmaxf(mx[3], __builtin_fabsf(v[3])); } }
.LBB0_127:
	v_readfirstlane_b32 s4, v2
	v_readfirstlane_b32 s5, v3
	v_readfirstlane_b32 s6, v4
	v_readfirstlane_b32 s7, v5
	s_nop 1
	v_subrev_u32_e32 v250, s4, v2
	v_subrev_u32_e32 v251, s6, v4
	s_nop 4
	global_load_dwordx4 v[106:109], v250, s[4:5] nt
	global_load_dword v202, v251, s[6:7] offset:-480
	s_add_u32 s4, s4, 0x18000
	s_addc_u32 s5, s5, 0
	global_load_dwordx4 v[110:113], v250, s[4:5] nt
	global_load_dword v204, v251, s[6:7] offset:-448
	s_add_u32 s4, s4, 0x18000
	s_addc_u32 s5, s5, 0
	global_load_dwordx4 v[114:117], v250, s[4:5] nt
	global_load_dword v206, v251, s[6:7] offset:-416
	s_add_u32 s4, s4, 0x18000
	s_addc_u32 s5, s5, 0
	global_load_dwordx4 v[118:121], v250, s[4:5] nt
	global_load_dword v208, v251, s[6:7] offset:-384
	s_add_u32 s4, s4, 0x18000
	s_addc_u32 s5, s5, 0
	global_load_dwordx4 v[122:125], v250, s[4:5] nt
	global_load_dword v210, v251, s[6:7] offset:-352
	s_add_u32 s4, s4, 0x18000
	s_addc_u32 s5, s5, 0
	global_load_dwordx4 v[126:129], v250, s[4:5] nt
	global_load_dword v212, v251, s[6:7] offset:-320
	s_add_u32 s4, s4, 0x18000
	s_addc_u32 s5, s5, 0
	global_load_dwordx4 v[130:133], v250, s[4:5] nt
	global_load_dword v214, v251, s[6:7] offset:-288
	s_add_u32 s4, s4, 0x18000
	s_addc_u32 s5, s5, 0
	global_load_dwordx4 v[134:137], v250, s[4:5] nt
	global_load_dword v216, v251, s[6:7] offset:-256
	s_add_u32 s4, s4, 0x18000
	s_addc_u32 s5, s5, 0
	global_load_dwordx4 v[138:141], v250, s[4:5] nt
	global_load_dword v218, v251, s[6:7] offset:-224
	s_add_u32 s4, s4, 0x18000
	s_addc_u32 s5, s5, 0
	global_load_dwordx4 v[142:145], v250, s[4:5] nt
	global_load_dword v220, v251, s[6:7] offset:-192
	s_add_u32 s4, s4, 0x18000
	s_addc_u32 s5, s5, 0
	global_load_dwordx4 v[146:149], v250, s[4:5] nt
	global_load_dword v222, v251, s[6:7] offset:-160
	s_add_u32 s4, s4, 0x18000
	s_addc_u32 s5, s5, 0
	global_load_dwordx4 v[150:153], v250, s[4:5] nt
	global_load_dword v224, v251, s[6:7] offset:-128
	s_add_u32 s4, s4, 0x18000
	s_addc_u32 s5, s5, 0
	global_load_dwordx4 v[154:157], v250, s[4:5] nt
	global_load_dword v226, v251, s[6:7] offset:-96
	s_add_u32 s4, s4, 0x18000
	s_addc_u32 s5, s5, 0
	global_load_dwordx4 v[158:161], v250, s[4:5] nt
	global_load_dword v228, v251, s[6:7] offset:-64
	s_add_u32 s4, s4, 0x18000
	s_addc_u32 s5, s5, 0
	global_load_dwordx4 v[162:165], v250, s[4:5] nt
	global_load_dword v230, v251, s[6:7] offset:-32
	s_add_u32 s4, s4, 0x18000
	s_addc_u32 s5, s5, 0
	global_load_dwordx4 v[166:169], v250, s[4:5] nt
	global_load_dword v232, v251, s[6:7]
	s_add_u32 s4, s4, 0x18000
	s_addc_u32 s5, s5, 0
	global_load_dwordx4 v[170:173], v250, s[4:5] nt
	global_load_dword v234, v251, s[6:7] offset:32
	s_add_u32 s4, s4, 0x18000
	s_addc_u32 s5, s5, 0
	global_load_dwordx4 v[174:177], v250, s[4:5] nt
	global_load_dword v236, v251, s[6:7] offset:64
	s_add_u32 s4, s4, 0x18000
	s_addc_u32 s5, s5, 0
	global_load_dwordx4 v[178:181], v250, s[4:5] nt
	global_load_dword v238, v251, s[6:7] offset:96
	s_add_u32 s4, s4, 0x18000
	s_addc_u32 s5, s5, 0
	global_load_dwordx4 v[182:185], v250, s[4:5] nt
	global_load_dword v240, v251, s[6:7] offset:128
	s_add_u32 s4, s4, 0x18000
	s_addc_u32 s5, s5, 0
	global_load_dwordx4 v[186:189], v250, s[4:5] nt
	global_load_dword v242, v251, s[6:7] offset:160
	s_add_u32 s4, s4, 0x18000
	s_addc_u32 s5, s5, 0
	global_load_dwordx4 v[190:193], v250, s[4:5] nt
	global_load_dword v244, v251, s[6:7] offset:192
	s_add_u32 s4, s4, 0x18000
	s_addc_u32 s5, s5, 0
	global_load_dwordx4 v[194:197], v250, s[4:5] nt
	global_load_dword v246, v251, s[6:7] offset:224
	s_add_u32 s4, s4, 0x18000
	s_addc_u32 s5, s5, 0
	global_load_dwordx4 v[198:201], v250, s[4:5] nt
	global_load_dword v248, v251, s[6:7] offset:256
	s_waitcnt vmcnt(44)
	v_pk_mul_f32 v[16:17], v[106:107], v[202:203] op_sel_hi:[1,0]
	v_pk_mul_f32 v[18:19], v[108:109], v[202:203] op_sel_hi:[1,0]
	v_pk_mul_f32 v[20:21], v[110:111], v[204:205] op_sel_hi:[1,0]
	v_pk_mul_f32 v[22:23], v[112:113], v[204:205] op_sel_hi:[1,0]
	v_max3_f32 v15, v15, |v16|, |v20|
	v_max3_f32 v13, v13, |v17|, |v21|
	v_max3_f32 v9, v9, |v18|, |v22|
	v_max3_f32 v7, v7, |v19|, |v23|
	s_add_u32 s4, s4, 0x18000
	s_addc_u32 s5, s5, 0
	global_load_dwordx4 v[106:109], v250, s[4:5] nt
	global_load_dword v202, v251, s[6:7] offset:288
	s_add_u32 s4, s4, 0x18000
	s_addc_u32 s5, s5, 0
	global_load_dwordx4 v[110:113], v250, s[4:5] nt
	global_load_dword v204, v251, s[6:7] offset:320
	s_waitcnt vmcnt(44)
	v_pk_mul_f32 v[16:17], v[114:115], v[206:207] op_sel_hi:[1,0]
	v_pk_mul_f32 v[18:19], v[116:117], v[206:207] op_sel_hi:[1,0]
	v_pk_mul_f32 v[20:21], v[118:119], v[208:209] op_sel_hi:[1,0]
	v_pk_mul_f32 v[22:23], v[120:121], v[208:209] op_sel_hi:[1,0]
	v_max3_f32 v15, v15, |v16|, |v20|
	v_max3_f32 v13, v13, |v17|, |v21|
	v_max3_f32 v9, v9, |v18|, |v22|
	v_max3_f32 v7, v7, |v19|, |v23|
	s_add_u32 s4, s4, 0x18000
	s_addc_u32 s5, s5, 0
	global_load_dwordx4 v[114:117], v250, s[4:5] nt
	global_load_dword v206, v251, s[6:7] offset:352
	s_add_u32 s4, s4, 0x18000
	s_addc_u32 s5, s5, 0
	global_load_dwordx4 v[118:121], v250, s[4:5] nt
	global_load_dword v208, v251, s[6:7] offset:384
	s_waitcnt vmcnt(44)
	v_pk_mul_f32 v[16:17], v[122:123], v[210:211] op_sel_hi:[1,0]
	v_pk_mul_f32 v[18:19], v[124:125], v[210:211] op_sel_hi:[1,0]
	v_pk_mul_f32 v[20:21], v[126:127], v[212:213] op_sel_hi:[1,0]
	v_pk_mul_f32 v[22:23], v[128:129], v[212:213] op_sel_hi:[1,0]
	v_max3_f32 v15, v15, |v16|, |v20|
	v_max3_f32 v13, v13, |v17|, |v21|
	v_max3_f32 v9, v9, |v18|, |v22|
	v_max3_f32 v7, v7, |v19|, |v23|
	s_add_u32 s4, s4, 0x18000
	s_addc_u32 s5, s5, 0
	global_load_dwordx4 v[122:125], v250, s[4:5] nt
	global_load_dword v210, v251, s[6:7] offset:416
	s_add_u32 s4, s4, 0x18000
	s_addc_u32 s5, s5, 0
	global_load_dwordx4 v[126:129], v250, s[4:5] nt
	global_load_dword v212, v251, s[6:7] offset:448
	s_waitcnt vmcnt(44)
;     ...
;     for (int kb = 0; kb < D / 64; ++kb) {
; #pragma unroll
;         for (int i = 0; i < 8; ++i) { const int k = 64 * kb + 8 * i + kr; const f32x4 v = __builtin_nontemporal_load((const f32x4*)(W + (size_t)k * pitch)) * g[k];
;             mx[0] = __builtin_fmaxf(mx[0], __builtin_fabsf(v[0])); mx[1] = __builtin_fmaxf(mx[1], __builtin_fabsf(v[1])); mx[2] = __builtin_fmaxf(mx[2], __builtin_fabsf(v[2])); mx[3] = __builtin_fmaxf(mx[3], __builtin_fabsf(v[3])); } }
	v_pk_mul_f32 v[16:17], v[130:131], v[214:215] op_sel_hi:[1,0]
	v_pk_mul_f32 v[18:19], v[132:133], v[214:215] op_sel_hi:[1,0]
	v_pk_mul_f32 v[20:21], v[134:135], v[216:217] op_sel_hi:[1,0]
	v_pk_mul_f32 v[22:23], v[136:137], v[216:217] op_sel_hi:[1,0]
	v_max3_f32 v15, v15, |v16|, |v20|
	v_max3_f32 v13, v13, |v17|, |v21|
	v_max3_f32 v9, v9, |v18|, |v22|
	v_max3_f32 v7, v7, |v19|, |v23|
	s_add_u32 s4, s4, 0x18000
	s_addc_u32 s5, s5, 0
	global_load_dwordx4 v[130:133], v250, s[4:5] nt
	global_load_dword v214, v251, s[6:7] offset:480
	s_add_u32 s4, s4, 0x18000
	s_addc_u32 s5, s5, 0
	global_load_dwordx4 v[134:137], v250, s[4:5] nt
	global_load_dword v216, v251, s[6:7] offset:512
	s_waitcnt vmcnt(44)
	v_pk_mul_f32 v[16:17], v[138:139], v[218:219] op_sel_hi:[1,0]
	v_pk_mul_f32 v[18:19], v[140:141], v[218:219] op_sel_hi:[1,0]
	v_pk_mul_f32 v[20:21], v[142:143], v[220:221] op_sel_hi:[1,0]
	v_pk_mul_f32 v[22:23], v[144:145], v[220:221] op_sel_hi:[1,0]
	v_max3_f32 v15, v15, |v16|, |v20|
	v_max3_f32 v13, v13, |v17|, |v21|
	v_max3_f32 v9, v9, |v18|, |v22|
	v_max3_f32 v7, v7, |v19|, |v23|
	s_add_u32 s4, s4, 0x18000
	s_addc_u32 s5, s5, 0
	global_load_dwordx4 v[138:141], v250, s[4:5] nt
	global_load_dword v218, v251, s[6:7] offset:544
	s_add_u32 s4, s4, 0x18000
	s_addc_u32 s5, s5, 0
	global_load_dwordx4 v[142:145], v250, s[4:5] nt
	global_load_dword v220, v251, s[6:7] offset:576
	s_waitcnt vmcnt(44)
	v_pk_mul_f32 v[16:17], v[146:147], v[222:223] op_sel_hi:[1,0]
	v_pk_mul_f32 v[18:19], v[148:149], v[222:223] op_sel_hi:[1,0]
	v_pk_mul_f32 v[20:21], v[150:151], v[224:225] op_sel_hi:[1,0]
	v_pk_mul_f32 v[22:23], v[152:153], v[224:225] op_sel_hi:[1,0]
	v_max3_f32 v15, v15, |v16|, |v20|
	v_max3_f32 v13, v13, |v17|, |v21|
	v_max3_f32 v9, v9, |v18|, |v22|
	v_max3_f32 v7, v7, |v19|, |v23|
	s_add_u32 s4, s4, 0x18000
	s_addc_u32 s5, s5, 0
	global_load_dwordx4 v[146:149], v250, s[4:5] nt
	global_load_dword v222, v251, s[6:7] offset:608
	s_add_u32 s4, s4, 0x18000
	s_addc_u32 s5, s5, 0
	global_load_dwordx4 v[150:153], v250, s[4:5] nt
	global_load_dword v224, v251, s[6:7] offset:640
	s_waitcnt vmcnt(44)
	v_pk_mul_f32 v[16:17], v[154:155], v[226:227] op_sel_hi:[1,0]
	v_pk_mul_f32 v[18:19], v[156:157], v[226:227] op_sel_hi:[1,0]
	v_pk_mul_f32 v[20:21], v[158:159], v[228:229] op_sel_hi:[1,0]
	v_pk_mul_f32 v[22:23], v[160:161], v[228:229] op_sel_hi:[1,0]
	v_max3_f32 v15, v15, |v16|, |v20|
	v_max3_f32 v13, v13, |v17|, |v21|
	v_max3_f32 v9, v9, |v18|, |v22|
	v_max3_f32 v7, v7, |v19|, |v23|
	s_add_u32 s4, s4, 0x18000
	s_addc_u32 s5, s5, 0
	global_load_dwordx4 v[154:157], v250, s[4:5] nt
	global_load_dword v226, v251, s[6:7] offset:672
	s_add_u32 s4, s4, 0x18000
	s_addc_u32 s5, s5, 0
	global_load_dwordx4 v[158:161], v250, s[4:5] nt
	global_load_dword v228, v251, s[6:7] offset:704
	s_waitcnt vmcnt(44)
	v_pk_mul_f32 v[16:17], v[162:163], v[230:231] op_sel_hi:[1,0]
	v_pk_mul_f32 v[18:19], v[164:165], v[230:231] op_sel_hi:[1,0]
	v_pk_mul_f32 v[20:21], v[166:167], v[232:233] op_sel_hi:[1,0]
	v_pk_mul_f32 v[22:23], v[168:169], v[232:233] op_sel_hi:[1,0]
	v_max3_f32 v15, v15, |v16|, |v20|
	v_max3_f32 v13, v13, |v17|, |v21|
	v_max3_f32 v9, v9, |v18|, |v22|
	v_max3_f32 v7, v7, |v19|, |v23|
	s_add_u32 s4, s4, 0x18000
	s_addc_u32 s5, s5, 0
	global_load_dwordx4 v[162:165], v250, s[4:5] nt
	global_load_dword v230, v251, s[6:7] offset:736
	s_add_u32 s4, s4, 0x18000
	s_addc_u32 s5, s5, 0
	global_load_dwordx4 v[166:169], v250, s[4:5] nt
	global_load_dword v232, v251, s[6:7] offset:768
	s_waitcnt vmcnt(44)
	v_pk_mul_f32 v[16:17], v[170:171], v[234:235] op_sel_hi:[1,0]
	v_pk_mul_f32 v[18:19], v[172:173], v[234:235] op_sel_hi:[1,0]
	v_pk_mul_f32 v[20:21], v[174:175], v[236:237] op_sel_hi:[1,0]
	v_pk_mul_f32 v[22:23], v[176:177], v[236:237] op_sel_hi:[1,0]
	v_max3_f32 v15, v15, |v16|, |v20|
	v_max3_f32 v13, v13, |v17|, |v21|
	v_max3_f32 v9, v9, |v18|, |v22|
	v_max3_f32 v7, v7, |v19|, |v23|
	s_add_u32 s4, s4, 0x18000
	s_addc_u32 s5, s5, 0
	global_load_dwordx4 v[170:173], v250, s[4:5] nt
	global_load_dword v234, v251, s[6:7] offset:800
	s_add_u32 s4, s4, 0x18000
	s_addc_u32 s5, s5, 0
	global_load_dwordx4 v[174:177], v250, s[4:5] nt
	global_load_dword v236, v251, s[6:7] offset:832
	s_waitcnt vmcnt(44)
	v_pk_mul_f32 v[16:17], v[178:179], v[238:239] op_sel_hi:[1,0]
	v_pk_mul_f32 v[18:19], v[180:181], v[238:239] op_sel_hi:[1,0]
	v_pk_mul_f32 v[20:21], v[182:183], v[240:241] op_sel_hi:[1,0]
	v_pk_mul_f32 v[22:23], v[184:185], v[240:241] op_sel_hi:[1,0]
	v_max3_f32 v15, v15, |v16|, |v20|
	v_max3_f32 v13, v13, |v17|, |v21|
	v_max3_f32 v9, v9, |v18|, |v22|
	v_max3_f32 v7, v7, |v19|, |v23|
	s_add_u32 s4, s4, 0x18000
	s_addc_u32 s5, s5, 0
	global_load_dwordx4 v[178:181], v250, s[4:5] nt
	global_load_dword v238, v251, s[6:7] offset:864
	s_add_u32 s4, s4, 0x18000
	s_addc_u32 s5, s5, 0
	global_load_dwordx4 v[182:185], v250, s[4:5] nt
	global_load_dword v240, v251, s[6:7] offset:896
	s_waitcnt vmcnt(44)
	v_pk_mul_f32 v[16:17], v[186:187], v[242:243] op_sel_hi:[1,0]
	v_pk_mul_f32 v[18:19], v[188:189], v[242:243] op_sel_hi:[1,0]
	v_pk_mul_f32 v[20:21], v[190:191], v[244:245] op_sel_hi:[1,0]
	v_pk_mul_f32 v[22:23], v[192:193], v[244:245] op_sel_hi:[1,0]
	v_max3_f32 v15, v15, |v16|, |v20|
	v_max3_f32 v13, v13, |v17|, |v21|
	v_max3_f32 v9, v9, |v18|, |v22|
	v_max3_f32 v7, v7, |v19|, |v23|
	s_add_u32 s4, s4, 0x18000
	s_addc_u32 s5, s5, 0
	global_load_dwordx4 v[186:189], v250, s[4:5] nt
	global_load_dword v242, v251, s[6:7] offset:928
	s_add_u32 s4, s4, 0x18000
	s_addc_u32 s5, s5, 0
	global_load_dwordx4 v[190:193], v250, s[4:5] nt
	global_load_dword v244, v251, s[6:7] offset:960
	s_waitcnt vmcnt(44)
;     ...
;     for (int kb = 0; kb < D / 64; ++kb) {
; #pragma unroll
;         for (int i = 0; i < 8; ++i) { const int k = 64 * kb + 8 * i + kr; const f32x4 v = __builtin_nontemporal_load((const f32x4*)(W + (size_t)k * pitch)) * g[k];
;             mx[0] = __builtin_fmaxf(mx[0], __builtin_fabsf(v[0])); mx[1] = __builtin_fmaxf(mx[1], __builtin_fabsf(v[1])); mx[2] = __builtin_fmaxf(mx[2], __builtin_fabsf(v[2])); mx[3] = __builtin_fmaxf(mx[3], __builtin_fabsf(v[3])); } }
	v_pk_mul_f32 v[16:17], v[194:195], v[246:247] op_sel_hi:[1,0]
	v_pk_mul_f32 v[18:19], v[196:197], v[246:247] op_sel_hi:[1,0]
	v_pk_mul_f32 v[20:21], v[198:199], v[248:249] op_sel_hi:[1,0]
	v_pk_mul_f32 v[22:23], v[200:201], v[248:249] op_sel_hi:[1,0]
	v_max3_f32 v15, v15, |v16|, |v20|
	v_max3_f32 v13, v13, |v17|, |v21|
	v_max3_f32 v9, v9, |v18|, |v22|
	v_max3_f32 v7, v7, |v19|, |v23|
	s_add_u32 s4, s4, 0x18000
	s_addc_u32 s5, s5, 0
	global_load_dwordx4 v[194:197], v250, s[4:5] nt
	global_load_dword v246, v251, s[6:7] offset:992
	s_add_u32 s4, s4, 0x18000
	s_addc_u32 s5, s5, 0
	global_load_dwordx4 v[198:201], v250, s[4:5] nt
	global_load_dword v248, v251, s[6:7] offset:1024
	s_waitcnt vmcnt(44)
	v_pk_mul_f32 v[16:17], v[106:107], v[202:203] op_sel_hi:[1,0]
	v_pk_mul_f32 v[18:19], v[108:109], v[202:203] op_sel_hi:[1,0]
	v_pk_mul_f32 v[20:21], v[110:111], v[204:205] op_sel_hi:[1,0]
	v_pk_mul_f32 v[22:23], v[112:113], v[204:205] op_sel_hi:[1,0]
	v_max3_f32 v15, v15, |v16|, |v20|
	v_max3_f32 v13, v13, |v17|, |v21|
	v_max3_f32 v9, v9, |v18|, |v22|
	v_max3_f32 v7, v7, |v19|, |v23|
	s_add_u32 s4, s4, 0x18000
	s_addc_u32 s5, s5, 0
	global_load_dwordx4 v[106:109], v250, s[4:5] nt
	global_load_dword v202, v251, s[6:7] offset:1056
	s_add_u32 s4, s4, 0x18000
	s_addc_u32 s5, s5, 0
	global_load_dwordx4 v[110:113], v250, s[4:5] nt
	global_load_dword v204, v251, s[6:7] offset:1088
	s_waitcnt vmcnt(44)
	v_pk_mul_f32 v[16:17], v[114:115], v[206:207] op_sel_hi:[1,0]
	v_pk_mul_f32 v[18:19], v[116:117], v[206:207] op_sel_hi:[1,0]
	v_pk_mul_f32 v[20:21], v[118:119], v[208:209] op_sel_hi:[1,0]
	v_pk_mul_f32 v[22:23], v[120:121], v[208:209] op_sel_hi:[1,0]
	v_max3_f32 v15, v15, |v16|, |v20|
	v_max3_f32 v13, v13, |v17|, |v21|
	v_max3_f32 v9, v9, |v18|, |v22|
	v_max3_f32 v7, v7, |v19|, |v23|
	s_add_u32 s4, s4, 0x18000
	s_addc_u32 s5, s5, 0
	global_load_dwordx4 v[114:117], v250, s[4:5] nt
	global_load_dword v206, v251, s[6:7] offset:1120
	s_add_u32 s4, s4, 0x18000
	s_addc_u32 s5, s5, 0
	global_load_dwordx4 v[118:121], v250, s[4:5] nt
	global_load_dword v208, v251, s[6:7] offset:1152
	s_waitcnt vmcnt(44)
	v_pk_mul_f32 v[16:17], v[122:123], v[210:211] op_sel_hi:[1,0]
	v_pk_mul_f32 v[18:19], v[124:125], v[210:211] op_sel_hi:[1,0]
	v_pk_mul_f32 v[20:21], v[126:127], v[212:213] op_sel_hi:[1,0]
	v_pk_mul_f32 v[22:23], v[128:129], v[212:213] op_sel_hi:[1,0]
	v_max3_f32 v15, v15, |v16|, |v20|
	v_max3_f32 v13, v13, |v17|, |v21|
	v_max3_f32 v9, v9, |v18|, |v22|
	v_max3_f32 v7, v7, |v19|, |v23|
	s_add_u32 s4, s4, 0x18000
	s_addc_u32 s5, s5, 0
	global_load_dwordx4 v[122:125], v250, s[4:5] nt
	global_load_dword v210, v251, s[6:7] offset:1184
	s_add_u32 s4, s4, 0x18000
	s_addc_u32 s5, s5, 0
	global_load_dwordx4 v[126:129], v250, s[4:5] nt
	global_load_dword v212, v251, s[6:7] offset:1216
	s_waitcnt vmcnt(44)
	v_pk_mul_f32 v[16:17], v[130:131], v[214:215] op_sel_hi:[1,0]
	v_pk_mul_f32 v[18:19], v[132:133], v[214:215] op_sel_hi:[1,0]
	v_pk_mul_f32 v[20:21], v[134:135], v[216:217] op_sel_hi:[1,0]
	v_pk_mul_f32 v[22:23], v[136:137], v[216:217] op_sel_hi:[1,0]
	v_max3_f32 v15, v15, |v16|, |v20|
	v_max3_f32 v13, v13, |v17|, |v21|
	v_max3_f32 v9, v9, |v18|, |v22|
	v_max3_f32 v7, v7, |v19|, |v23|
	s_add_u32 s4, s4, 0x18000
	s_addc_u32 s5, s5, 0
	global_load_dwordx4 v[130:133], v250, s[4:5] nt
	global_load_dword v214, v251, s[6:7] offset:1248
	s_add_u32 s4, s4, 0x18000
	s_addc_u32 s5, s5, 0
	global_load_dwordx4 v[134:137], v250, s[4:5] nt
	global_load_dword v216, v251, s[6:7] offset:1280
	s_waitcnt vmcnt(44)
	v_pk_mul_f32 v[16:17], v[138:139], v[218:219] op_sel_hi:[1,0]
	v_pk_mul_f32 v[18:19], v[140:141], v[218:219] op_sel_hi:[1,0]
	v_pk_mul_f32 v[20:21], v[142:143], v[220:221] op_sel_hi:[1,0]
	v_pk_mul_f32 v[22:23], v[144:145], v[220:221] op_sel_hi:[1,0]
	v_max3_f32 v15, v15, |v16|, |v20|
	v_max3_f32 v13, v13, |v17|, |v21|
	v_max3_f32 v9, v9, |v18|, |v22|
	v_max3_f32 v7, v7, |v19|, |v23|
	s_add_u32 s4, s4, 0x18000
	s_addc_u32 s5, s5, 0
	global_load_dwordx4 v[138:141], v250, s[4:5] nt
	global_load_dword v218, v251, s[6:7] offset:1312
	s_add_u32 s4, s4, 0x18000
	s_addc_u32 s5, s5, 0
	global_load_dwordx4 v[142:145], v250, s[4:5] nt
	global_load_dword v220, v251, s[6:7] offset:1344
	s_waitcnt vmcnt(44)
	v_pk_mul_f32 v[16:17], v[146:147], v[222:223] op_sel_hi:[1,0]
	v_pk_mul_f32 v[18:19], v[148:149], v[222:223] op_sel_hi:[1,0]
	v_pk_mul_f32 v[20:21], v[150:151], v[224:225] op_sel_hi:[1,0]
	v_pk_mul_f32 v[22:23], v[152:153], v[224:225] op_sel_hi:[1,0]
	v_max3_f32 v15, v15, |v16|, |v20|
	v_max3_f32 v13, v13, |v17|, |v21|
	v_max3_f32 v9, v9, |v18|, |v22|
	v_max3_f32 v7, v7, |v19|, |v23|
	s_add_u32 s4, s4, 0x18000
	s_addc_u32 s5, s5, 0
	global_load_dwordx4 v[146:149], v250, s[4:5] nt
	global_load_dword v222, v251, s[6:7] offset:1376
	s_add_u32 s4, s4, 0x18000
	s_addc_u32 s5, s5, 0
	global_load_dwordx4 v[150:153], v250, s[4:5] nt
	global_load_dword v224, v251, s[6:7] offset:1408
	s_waitcnt vmcnt(44)
	v_pk_mul_f32 v[16:17], v[154:155], v[226:227] op_sel_hi:[1,0]
	v_pk_mul_f32 v[18:19], v[156:157], v[226:227] op_sel_hi:[1,0]
	v_pk_mul_f32 v[20:21], v[158:159], v[228:229] op_sel_hi:[1,0]
	v_pk_mul_f32 v[22:23], v[160:161], v[228:229] op_sel_hi:[1,0]
	v_max3_f32 v15, v15, |v16|, |v20|
	v_max3_f32 v13, v13, |v17|, |v21|
	v_max3_f32 v9, v9, |v18|, |v22|
	v_max3_f32 v7, v7, |v19|, |v23|
	s_add_u32 s4, s4, 0x18000
	s_addc_u32 s5, s5, 0
	global_load_dwordx4 v[154:157], v250, s[4:5] nt
	global_load_dword v226, v251, s[6:7] offset:1440
	s_add_u32 s4, s4, 0x18000
	s_addc_u32 s5, s5, 0
	global_load_dwordx4 v[158:161], v250, s[4:5] nt
	global_load_dword v228, v251, s[6:7] offset:1472
	s_waitcnt vmcnt(44)
;     ...
;     for (int kb = 0; kb < D / 64; ++kb) {
; #pragma unroll
;         for (int i = 0; i < 8; ++i) { const int k = 64 * kb + 8 * i + kr; const f32x4 v = __builtin_nontemporal_load((const f32x4*)(W + (size_t)k * pitch)) * g[k];
;             mx[0] = __builtin_fmaxf(mx[0], __builtin_fabsf(v[0])); mx[1] = __builtin_fmaxf(mx[1], __builtin_fabsf(v[1])); mx[2] = __builtin_fmaxf(mx[2], __builtin_fabsf(v[2])); mx[3] = __builtin_fmaxf(mx[3], __builtin_fabsf(v[3])); } }
	v_pk_mul_f32 v[16:17], v[162:163], v[230:231] op_sel_hi:[1,0]
	v_pk_mul_f32 v[18:19], v[164:165], v[230:231] op_sel_hi:[1,0]
	v_pk_mul_f32 v[20:21], v[166:167], v[232:233] op_sel_hi:[1,0]
	v_pk_mul_f32 v[22:23], v[168:169], v[232:233] op_sel_hi:[1,0]
	v_max3_f32 v15, v15, |v16|, |v20|
	v_max3_f32 v13, v13, |v17|, |v21|
	v_max3_f32 v9, v9, |v18|, |v22|
	v_max3_f32 v7, v7, |v19|, |v23|
	s_add_u32 s4, s4, 0x18000
	s_addc_u32 s5, s5, 0
	global_load_dwordx4 v[162:165], v250, s[4:5] nt
	global_load_dword v230, v251, s[6:7] offset:1504
	s_add_u32 s4, s4, 0x18000
	s_addc_u32 s5, s5, 0
	global_load_dwordx4 v[166:169], v250, s[4:5] nt
	global_load_dword v232, v251, s[6:7] offset:1536
	s_waitcnt vmcnt(44)
	v_pk_mul_f32 v[16:17], v[170:171], v[234:235] op_sel_hi:[1,0]
	v_pk_mul_f32 v[18:19], v[172:173], v[234:235] op_sel_hi:[1,0]
	v_pk_mul_f32 v[20:21], v[174:175], v[236:237] op_sel_hi:[1,0]
	v_pk_mul_f32 v[22:23], v[176:177], v[236:237] op_sel_hi:[1,0]
	v_max3_f32 v15, v15, |v16|, |v20|
	v_max3_f32 v13, v13, |v17|, |v21|
	v_max3_f32 v9, v9, |v18|, |v22|
	v_max3_f32 v7, v7, |v19|, |v23|
	s_add_u32 s4, s4, 0x18000
	s_addc_u32 s5, s5, 0
	global_load_dwordx4 v[170:173], v250, s[4:5] nt
	global_load_dword v234, v251, s[6:7] offset:1568
	s_add_u32 s4, s4, 0x18000
	s_addc_u32 s5, s5, 0
	global_load_dwordx4 v[174:177], v250, s[4:5] nt
	global_load_dword v236, v251, s[6:7] offset:1600
	s_waitcnt vmcnt(44)
	v_pk_mul_f32 v[16:17], v[178:179], v[238:239] op_sel_hi:[1,0]
	v_pk_mul_f32 v[18:19], v[180:181], v[238:239] op_sel_hi:[1,0]
	v_pk_mul_f32 v[20:21], v[182:183], v[240:241] op_sel_hi:[1,0]
	v_pk_mul_f32 v[22:23], v[184:185], v[240:241] op_sel_hi:[1,0]
	v_max3_f32 v15, v15, |v16|, |v20|
	v_max3_f32 v13, v13, |v17|, |v21|
	v_max3_f32 v9, v9, |v18|, |v22|
	v_max3_f32 v7, v7, |v19|, |v23|
	s_add_u32 s4, s4, 0x18000
	s_addc_u32 s5, s5, 0
	global_load_dwordx4 v[178:181], v250, s[4:5] nt
	global_load_dword v238, v251, s[6:7] offset:1632
	s_add_u32 s4, s4, 0x18000
	s_addc_u32 s5, s5, 0
	global_load_dwordx4 v[182:185], v250, s[4:5] nt
	global_load_dword v240, v251, s[6:7] offset:1664
	s_waitcnt vmcnt(44)
	v_pk_mul_f32 v[16:17], v[186:187], v[242:243] op_sel_hi:[1,0]
	v_pk_mul_f32 v[18:19], v[188:189], v[242:243] op_sel_hi:[1,0]
	v_pk_mul_f32 v[20:21], v[190:191], v[244:245] op_sel_hi:[1,0]
	v_pk_mul_f32 v[22:23], v[192:193], v[244:245] op_sel_hi:[1,0]
	v_max3_f32 v15, v15, |v16|, |v20|
	v_max3_f32 v13, v13, |v17|, |v21|
	v_max3_f32 v9, v9, |v18|, |v22|
	v_max3_f32 v7, v7, |v19|, |v23|
	s_add_u32 s4, s4, 0x18000
	s_addc_u32 s5, s5, 0
	global_load_dwordx4 v[186:189], v250, s[4:5] nt
	global_load_dword v242, v251, s[6:7] offset:1696
	s_add_u32 s4, s4, 0x18000
	s_addc_u32 s5, s5, 0
	global_load_dwordx4 v[190:193], v250, s[4:5] nt
	global_load_dword v244, v251, s[6:7] offset:1728
	s_waitcnt vmcnt(44)
	v_pk_mul_f32 v[16:17], v[194:195], v[246:247] op_sel_hi:[1,0]
	v_pk_mul_f32 v[18:19], v[196:197], v[246:247] op_sel_hi:[1,0]
	v_pk_mul_f32 v[20:21], v[198:199], v[248:249] op_sel_hi:[1,0]
	v_pk_mul_f32 v[22:23], v[200:201], v[248:249] op_sel_hi:[1,0]
	v_max3_f32 v15, v15, |v16|, |v20|
	v_max3_f32 v13, v13, |v17|, |v21|
	v_max3_f32 v9, v9, |v18|, |v22|
	v_max3_f32 v7, v7, |v19|, |v23|
	s_add_u32 s4, s4, 0x18000
	s_addc_u32 s5, s5, 0
	global_load_dwordx4 v[194:197], v250, s[4:5] nt
	global_load_dword v246, v251, s[6:7] offset:1760
	s_add_u32 s4, s4, 0x18000
	s_addc_u32 s5, s5, 0
	global_load_dwordx4 v[198:201], v250, s[4:5] nt
	global_load_dword v248, v251, s[6:7] offset:1792
	s_waitcnt vmcnt(44)
	v_pk_mul_f32 v[16:17], v[106:107], v[202:203] op_sel_hi:[1,0]
	v_pk_mul_f32 v[18:19], v[108:109], v[202:203] op_sel_hi:[1,0]
	v_pk_mul_f32 v[20:21], v[110:111], v[204:205] op_sel_hi:[1,0]
	v_pk_mul_f32 v[22:23], v[112:113], v[204:205] op_sel_hi:[1,0]
	v_max3_f32 v15, v15, |v16|, |v20|
	v_max3_f32 v13, v13, |v17|, |v21|
	v_max3_f32 v9, v9, |v18|, |v22|
	v_max3_f32 v7, v7, |v19|, |v23|
	s_add_u32 s4, s4, 0x18000
	s_addc_u32 s5, s5, 0
	global_load_dwordx4 v[106:109], v250, s[4:5] nt
	global_load_dword v202, v251, s[6:7] offset:1824
	s_add_u32 s4, s4, 0x18000
	s_addc_u32 s5, s5, 0
	global_load_dwordx4 v[110:113], v250, s[4:5] nt
	global_load_dword v204, v251, s[6:7] offset:1856
	s_waitcnt vmcnt(44)
	v_pk_mul_f32 v[16:17], v[114:115], v[206:207] op_sel_hi:[1,0]
	v_pk_mul_f32 v[18:19], v[116:117], v[206:207] op_sel_hi:[1,0]
	v_pk_mul_f32 v[20:21], v[118:119], v[208:209] op_sel_hi:[1,0]
	v_pk_mul_f32 v[22:23], v[120:121], v[208:209] op_sel_hi:[1,0]
	v_max3_f32 v15, v15, |v16|, |v20|
	v_max3_f32 v13, v13, |v17|, |v21|
	v_max3_f32 v9, v9, |v18|, |v22|
	v_max3_f32 v7, v7, |v19|, |v23|
	s_add_u32 s4, s4, 0x18000
	s_addc_u32 s5, s5, 0
	global_load_dwordx4 v[114:117], v250, s[4:5] nt
	global_load_dword v206, v251, s[6:7] offset:1888
	s_add_u32 s4, s4, 0x18000
	s_addc_u32 s5, s5, 0
	global_load_dwordx4 v[118:121], v250, s[4:5] nt
	global_load_dword v208, v251, s[6:7] offset:1920
	s_waitcnt vmcnt(44)
	v_pk_mul_f32 v[16:17], v[122:123], v[210:211] op_sel_hi:[1,0]
	v_pk_mul_f32 v[18:19], v[124:125], v[210:211] op_sel_hi:[1,0]
	v_pk_mul_f32 v[20:21], v[126:127], v[212:213] op_sel_hi:[1,0]
	v_pk_mul_f32 v[22:23], v[128:129], v[212:213] op_sel_hi:[1,0]
	v_max3_f32 v15, v15, |v16|, |v20|
	v_max3_f32 v13, v13, |v17|, |v21|
	v_max3_f32 v9, v9, |v18|, |v22|
	v_max3_f32 v7, v7, |v19|, |v23|
	s_add_u32 s4, s4, 0x18000
	s_addc_u32 s5, s5, 0
	global_load_dwordx4 v[122:125], v250, s[4:5] nt
	global_load_dword v210, v251, s[6:7] offset:1952
	s_add_u32 s4, s4, 0x18000
	s_addc_u32 s5, s5, 0
	global_load_dwordx4 v[126:129], v250, s[4:5] nt
	global_load_dword v212, v251, s[6:7] offset:1984
	s_waitcnt vmcnt(44)
;     ...
;     for (int kb = 0; kb < D / 64; ++kb) {
; #pragma unroll
;         for (int i = 0; i < 8; ++i) { const int k = 64 * kb + 8 * i + kr; const f32x4 v = __builtin_nontemporal_load((const f32x4*)(W + (size_t)k * pitch)) * g[k];
;             mx[0] = __builtin_fmaxf(mx[0], __builtin_fabsf(v[0])); mx[1] = __builtin_fmaxf(mx[1], __builtin_fabsf(v[1])); mx[2] = __builtin_fmaxf(mx[2], __builtin_fabsf(v[2])); mx[3] = __builtin_fmaxf(mx[3], __builtin_fabsf(v[3])); } }
	v_pk_mul_f32 v[16:17], v[130:131], v[214:215] op_sel_hi:[1,0]
	v_pk_mul_f32 v[18:19], v[132:133], v[214:215] op_sel_hi:[1,0]
	v_pk_mul_f32 v[20:21], v[134:135], v[216:217] op_sel_hi:[1,0]
	v_pk_mul_f32 v[22:23], v[136:137], v[216:217] op_sel_hi:[1,0]
	v_max3_f32 v15, v15, |v16|, |v20|
	v_max3_f32 v13, v13, |v17|, |v21|
	v_max3_f32 v9, v9, |v18|, |v22|
	v_max3_f32 v7, v7, |v19|, |v23|
	s_add_u32 s4, s4, 0x18000
	s_addc_u32 s5, s5, 0
	global_load_dwordx4 v[130:133], v250, s[4:5] nt
	global_load_dword v214, v251, s[6:7] offset:2016
	s_add_u32 s4, s4, 0x18000
	s_addc_u32 s5, s5, 0
	global_load_dwordx4 v[134:137], v250, s[4:5] nt
	global_load_dword v216, v251, s[6:7] offset:2048
	s_waitcnt vmcnt(44)
	v_pk_mul_f32 v[16:17], v[138:139], v[218:219] op_sel_hi:[1,0]
	v_pk_mul_f32 v[18:19], v[140:141], v[218:219] op_sel_hi:[1,0]
	v_pk_mul_f32 v[20:21], v[142:143], v[220:221] op_sel_hi:[1,0]
	v_pk_mul_f32 v[22:23], v[144:145], v[220:221] op_sel_hi:[1,0]
	v_max3_f32 v15, v15, |v16|, |v20|
	v_max3_f32 v13, v13, |v17|, |v21|
	v_max3_f32 v9, v9, |v18|, |v22|
	v_max3_f32 v7, v7, |v19|, |v23|
	s_add_u32 s4, s4, 0x18000
	s_addc_u32 s5, s5, 0
	global_load_dwordx4 v[138:141], v250, s[4:5] nt
	global_load_dword v218, v251, s[6:7] offset:2080
	s_add_u32 s4, s4, 0x18000
	s_addc_u32 s5, s5, 0
	global_load_dwordx4 v[142:145], v250, s[4:5] nt
	global_load_dword v220, v251, s[6:7] offset:2112
	s_waitcnt vmcnt(44)
	v_pk_mul_f32 v[16:17], v[146:147], v[222:223] op_sel_hi:[1,0]
	v_pk_mul_f32 v[18:19], v[148:149], v[222:223] op_sel_hi:[1,0]
	v_pk_mul_f32 v[20:21], v[150:151], v[224:225] op_sel_hi:[1,0]
	v_pk_mul_f32 v[22:23], v[152:153], v[224:225] op_sel_hi:[1,0]
	v_max3_f32 v15, v15, |v16|, |v20|
	v_max3_f32 v13, v13, |v17|, |v21|
	v_max3_f32 v9, v9, |v18|, |v22|
	v_max3_f32 v7, v7, |v19|, |v23|
	s_add_u32 s4, s4, 0x18000
	s_addc_u32 s5, s5, 0
	global_load_dwordx4 v[146:149], v250, s[4:5] nt
	global_load_dword v222, v251, s[6:7] offset:2144
	s_add_u32 s4, s4, 0x18000
	s_addc_u32 s5, s5, 0
	global_load_dwordx4 v[150:153], v250, s[4:5] nt
	global_load_dword v224, v251, s[6:7] offset:2176
	s_waitcnt vmcnt(44)
	v_pk_mul_f32 v[16:17], v[154:155], v[226:227] op_sel_hi:[1,0]
	v_pk_mul_f32 v[18:19], v[156:157], v[226:227] op_sel_hi:[1,0]
	v_pk_mul_f32 v[20:21], v[158:159], v[228:229] op_sel_hi:[1,0]
	v_pk_mul_f32 v[22:23], v[160:161], v[228:229] op_sel_hi:[1,0]
	v_max3_f32 v15, v15, |v16|, |v20|
	v_max3_f32 v13, v13, |v17|, |v21|
	v_max3_f32 v9, v9, |v18|, |v22|
	v_max3_f32 v7, v7, |v19|, |v23|
	s_add_u32 s4, s4, 0x18000
	s_addc_u32 s5, s5, 0
	global_load_dwordx4 v[154:157], v250, s[4:5] nt
	global_load_dword v226, v251, s[6:7] offset:2208
	s_add_u32 s4, s4, 0x18000
	s_addc_u32 s5, s5, 0
	global_load_dwordx4 v[158:161], v250, s[4:5] nt
	global_load_dword v228, v251, s[6:7] offset:2240
	s_waitcnt vmcnt(44)
	v_pk_mul_f32 v[16:17], v[162:163], v[230:231] op_sel_hi:[1,0]
	v_pk_mul_f32 v[18:19], v[164:165], v[230:231] op_sel_hi:[1,0]
	v_pk_mul_f32 v[20:21], v[166:167], v[232:233] op_sel_hi:[1,0]
	v_pk_mul_f32 v[22:23], v[168:169], v[232:233] op_sel_hi:[1,0]
	v_max3_f32 v15, v15, |v16|, |v20|
	v_max3_f32 v13, v13, |v17|, |v21|
	v_max3_f32 v9, v9, |v18|, |v22|
	v_max3_f32 v7, v7, |v19|, |v23|
	s_add_u32 s4, s4, 0x18000
	s_addc_u32 s5, s5, 0
	global_load_dwordx4 v[162:165], v250, s[4:5] nt
	global_load_dword v230, v251, s[6:7] offset:2272
	s_add_u32 s4, s4, 0x18000
	s_addc_u32 s5, s5, 0
	global_load_dwordx4 v[166:169], v250, s[4:5] nt
	global_load_dword v232, v251, s[6:7] offset:2304
	s_waitcnt vmcnt(44)
	v_pk_mul_f32 v[16:17], v[170:171], v[234:235] op_sel_hi:[1,0]
	v_pk_mul_f32 v[18:19], v[172:173], v[234:235] op_sel_hi:[1,0]
	v_pk_mul_f32 v[20:21], v[174:175], v[236:237] op_sel_hi:[1,0]
	v_pk_mul_f32 v[22:23], v[176:177], v[236:237] op_sel_hi:[1,0]
	v_max3_f32 v15, v15, |v16|, |v20|
	v_max3_f32 v13, v13, |v17|, |v21|
	v_max3_f32 v9, v9, |v18|, |v22|
	v_max3_f32 v7, v7, |v19|, |v23|
	s_add_u32 s4, s4, 0x18000
	s_addc_u32 s5, s5, 0
	global_load_dwordx4 v[170:173], v250, s[4:5] nt
	global_load_dword v234, v251, s[6:7] offset:2336
	s_add_u32 s4, s4, 0x18000
	s_addc_u32 s5, s5, 0
	global_load_dwordx4 v[174:177], v250, s[4:5] nt
	global_load_dword v236, v251, s[6:7] offset:2368
	s_waitcnt vmcnt(44)
	v_pk_mul_f32 v[16:17], v[178:179], v[238:239] op_sel_hi:[1,0]
	v_pk_mul_f32 v[18:19], v[180:181], v[238:239] op_sel_hi:[1,0]
	v_pk_mul_f32 v[20:21], v[182:183], v[240:241] op_sel_hi:[1,0]
	v_pk_mul_f32 v[22:23], v[184:185], v[240:241] op_sel_hi:[1,0]
	v_max3_f32 v15, v15, |v16|, |v20|
	v_max3_f32 v13, v13, |v17|, |v21|
	v_max3_f32 v9, v9, |v18|, |v22|
	v_max3_f32 v7, v7, |v19|, |v23|
	s_add_u32 s4, s4, 0x18000
	s_addc_u32 s5, s5, 0
	global_load_dwordx4 v[178:181], v250, s[4:5] nt
	global_load_dword v238, v251, s[6:7] offset:2400
	s_add_u32 s4, s4, 0x18000
	s_addc_u32 s5, s5, 0
	global_load_dwordx4 v[182:185], v250, s[4:5] nt
	global_load_dword v240, v251, s[6:7] offset:2432
	s_waitcnt vmcnt(44)
	v_pk_mul_f32 v[16:17], v[186:187], v[242:243] op_sel_hi:[1,0]
	v_pk_mul_f32 v[18:19], v[188:189], v[242:243] op_sel_hi:[1,0]
	v_pk_mul_f32 v[20:21], v[190:191], v[244:245] op_sel_hi:[1,0]
	v_pk_mul_f32 v[22:23], v[192:193], v[244:245] op_sel_hi:[1,0]
	v_max3_f32 v15, v15, |v16|, |v20|
	v_max3_f32 v13, v13, |v17|, |v21|
	v_max3_f32 v9, v9, |v18|, |v22|
	v_max3_f32 v7, v7, |v19|, |v23|
	s_add_u32 s4, s4, 0x18000
	s_addc_u32 s5, s5, 0
	global_load_dwordx4 v[186:189], v250, s[4:5] nt
	global_load_dword v242, v251, s[6:7] offset:2464
	s_add_u32 s4, s4, 0x18000
	s_addc_u32 s5, s5, 0
	global_load_dwordx4 v[190:193], v250, s[4:5] nt
	global_load_dword v244, v251, s[6:7] offset:2496
	s_waitcnt vmcnt(44)
;     ...
;     for (int kb = 0; kb < D / 64; ++kb) {
; #pragma unroll
;         for (int i = 0; i < 8; ++i) { const int k = 64 * kb + 8 * i + kr; const f32x4 v = __builtin_nontemporal_load((const f32x4*)(W + (size_t)k * pitch)) * g[k];
;             mx[0] = __builtin_fmaxf(mx[0], __builtin_fabsf(v[0])); mx[1] = __builtin_fmaxf(mx[1], __builtin_fabsf(v[1])); mx[2] = __builtin_fmaxf(mx[2], __builtin_fabsf(v[2])); mx[3] = __builtin_fmaxf(mx[3], __builtin_fabsf(v[3])); } }
	v_pk_mul_f32 v[16:17], v[194:195], v[246:247] op_sel_hi:[1,0]
	v_pk_mul_f32 v[18:19], v[196:197], v[246:247] op_sel_hi:[1,0]
	v_pk_mul_f32 v[20:21], v[198:199], v[248:249] op_sel_hi:[1,0]
	v_pk_mul_f32 v[22:23], v[200:201], v[248:249] op_sel_hi:[1,0]
	v_max3_f32 v15, v15, |v16|, |v20|
	v_max3_f32 v13, v13, |v17|, |v21|
	v_max3_f32 v9, v9, |v18|, |v22|
	v_max3_f32 v7, v7, |v19|, |v23|
	s_add_u32 s4, s4, 0x18000
	s_addc_u32 s5, s5, 0
	global_load_dwordx4 v[194:197], v250, s[4:5] nt
	global_load_dword v246, v251, s[6:7] offset:2528
	s_add_u32 s4, s4, 0x18000
	s_addc_u32 s5, s5, 0
	global_load_dwordx4 v[198:201], v250, s[4:5] nt
	global_load_dword v248, v251, s[6:7] offset:2560
	s_waitcnt vmcnt(44)
	v_pk_mul_f32 v[16:17], v[106:107], v[202:203] op_sel_hi:[1,0]
	v_pk_mul_f32 v[18:19], v[108:109], v[202:203] op_sel_hi:[1,0]
	v_pk_mul_f32 v[20:21], v[110:111], v[204:205] op_sel_hi:[1,0]
	v_pk_mul_f32 v[22:23], v[112:113], v[204:205] op_sel_hi:[1,0]
	v_max3_f32 v15, v15, |v16|, |v20|
	v_max3_f32 v13, v13, |v17|, |v21|
	v_max3_f32 v9, v9, |v18|, |v22|
	v_max3_f32 v7, v7, |v19|, |v23|
	s_add_u32 s4, s4, 0x18000
	s_addc_u32 s5, s5, 0
	global_load_dwordx4 v[106:109], v250, s[4:5] nt
	global_load_dword v202, v251, s[6:7] offset:2592
	s_add_u32 s4, s4, 0x18000
	s_addc_u32 s5, s5, 0
	global_load_dwordx4 v[110:113], v250, s[4:5] nt
	global_load_dword v204, v251, s[6:7] offset:2624
	s_waitcnt vmcnt(44)
	v_pk_mul_f32 v[16:17], v[114:115], v[206:207] op_sel_hi:[1,0]
	v_pk_mul_f32 v[18:19], v[116:117], v[206:207] op_sel_hi:[1,0]
	v_pk_mul_f32 v[20:21], v[118:119], v[208:209] op_sel_hi:[1,0]
	v_pk_mul_f32 v[22:23], v[120:121], v[208:209] op_sel_hi:[1,0]
	v_max3_f32 v15, v15, |v16|, |v20|
	v_max3_f32 v13, v13, |v17|, |v21|
	v_max3_f32 v9, v9, |v18|, |v22|
	v_max3_f32 v7, v7, |v19|, |v23|
	s_add_u32 s4, s4, 0x18000
	s_addc_u32 s5, s5, 0
	global_load_dwordx4 v[114:117], v250, s[4:5] nt
	global_load_dword v206, v251, s[6:7] offset:2656
	s_add_u32 s4, s4, 0x18000
	s_addc_u32 s5, s5, 0
	global_load_dwordx4 v[118:121], v250, s[4:5] nt
	global_load_dword v208, v251, s[6:7] offset:2688
	s_waitcnt vmcnt(44)
	v_pk_mul_f32 v[16:17], v[122:123], v[210:211] op_sel_hi:[1,0]
	v_pk_mul_f32 v[18:19], v[124:125], v[210:211] op_sel_hi:[1,0]
	v_pk_mul_f32 v[20:21], v[126:127], v[212:213] op_sel_hi:[1,0]
	v_pk_mul_f32 v[22:23], v[128:129], v[212:213] op_sel_hi:[1,0]
	v_max3_f32 v15, v15, |v16|, |v20|
	v_max3_f32 v13, v13, |v17|, |v21|
	v_max3_f32 v9, v9, |v18|, |v22|
	v_max3_f32 v7, v7, |v19|, |v23|
	s_add_u32 s4, s4, 0x18000
	s_addc_u32 s5, s5, 0
	global_load_dwordx4 v[122:125], v250, s[4:5] nt
	global_load_dword v210, v251, s[6:7] offset:2720
	s_add_u32 s4, s4, 0x18000
	s_addc_u32 s5, s5, 0
	global_load_dwordx4 v[126:129], v250, s[4:5] nt
	global_load_dword v212, v251, s[6:7] offset:2752
	s_waitcnt vmcnt(44)
	v_pk_mul_f32 v[16:17], v[130:131], v[214:215] op_sel_hi:[1,0]
	v_pk_mul_f32 v[18:19], v[132:133], v[214:215] op_sel_hi:[1,0]
	v_pk_mul_f32 v[20:21], v[134:135], v[216:217] op_sel_hi:[1,0]
	v_pk_mul_f32 v[22:23], v[136:137], v[216:217] op_sel_hi:[1,0]
	v_max3_f32 v15, v15, |v16|, |v20|
	v_max3_f32 v13, v13, |v17|, |v21|
	v_max3_f32 v9, v9, |v18|, |v22|
	v_max3_f32 v7, v7, |v19|, |v23|
	s_add_u32 s4, s4, 0x18000
	s_addc_u32 s5, s5, 0
	global_load_dwordx4 v[130:133], v250, s[4:5] nt
	global_load_dword v214, v251, s[6:7] offset:2784
	s_add_u32 s4, s4, 0x18000
	s_addc_u32 s5, s5, 0
	global_load_dwordx4 v[134:137], v250, s[4:5] nt
	global_load_dword v216, v251, s[6:7] offset:2816
	s_waitcnt vmcnt(44)
	v_pk_mul_f32 v[16:17], v[138:139], v[218:219] op_sel_hi:[1,0]
	v_pk_mul_f32 v[18:19], v[140:141], v[218:219] op_sel_hi:[1,0]
	v_pk_mul_f32 v[20:21], v[142:143], v[220:221] op_sel_hi:[1,0]
	v_pk_mul_f32 v[22:23], v[144:145], v[220:221] op_sel_hi:[1,0]
	v_max3_f32 v15, v15, |v16|, |v20|
	v_max3_f32 v13, v13, |v17|, |v21|
	v_max3_f32 v9, v9, |v18|, |v22|
	v_max3_f32 v7, v7, |v19|, |v23|
	s_add_u32 s4, s4, 0x18000
	s_addc_u32 s5, s5, 0
	global_load_dwordx4 v[138:141], v250, s[4:5] nt
	global_load_dword v218, v251, s[6:7] offset:2848
	s_add_u32 s4, s4, 0x18000
	s_addc_u32 s5, s5, 0
	global_load_dwordx4 v[142:145], v250, s[4:5] nt
	global_load_dword v220, v251, s[6:7] offset:2880
	s_waitcnt vmcnt(44)
	v_pk_mul_f32 v[16:17], v[146:147], v[222:223] op_sel_hi:[1,0]
	v_pk_mul_f32 v[18:19], v[148:149], v[222:223] op_sel_hi:[1,0]
	v_pk_mul_f32 v[20:21], v[150:151], v[224:225] op_sel_hi:[1,0]
	v_pk_mul_f32 v[22:23], v[152:153], v[224:225] op_sel_hi:[1,0]
	v_max3_f32 v15, v15, |v16|, |v20|
	v_max3_f32 v13, v13, |v17|, |v21|
	v_max3_f32 v9, v9, |v18|, |v22|
	v_max3_f32 v7, v7, |v19|, |v23|
	s_add_u32 s4, s4, 0x18000
	s_addc_u32 s5, s5, 0
	global_load_dwordx4 v[146:149], v250, s[4:5] nt
	global_load_dword v222, v251, s[6:7] offset:2912
	s_add_u32 s4, s4, 0x18000
	s_addc_u32 s5, s5, 0
	global_load_dwordx4 v[150:153], v250, s[4:5] nt
	global_load_dword v224, v251, s[6:7] offset:2944
	s_waitcnt vmcnt(44)
	v_pk_mul_f32 v[16:17], v[154:155], v[226:227] op_sel_hi:[1,0]
	v_pk_mul_f32 v[18:19], v[156:157], v[226:227] op_sel_hi:[1,0]
	v_pk_mul_f32 v[20:21], v[158:159], v[228:229] op_sel_hi:[1,0]
	v_pk_mul_f32 v[22:23], v[160:161], v[228:229] op_sel_hi:[1,0]
	v_max3_f32 v15, v15, |v16|, |v20|
	v_max3_f32 v13, v13, |v17|, |v21|
	v_max3_f32 v9, v9, |v18|, |v22|
	v_max3_f32 v7, v7, |v19|, |v23|
	s_add_u32 s4, s4, 0x18000
	s_addc_u32 s5, s5, 0
	global_load_dwordx4 v[154:157], v250, s[4:5] nt
	global_load_dword v226, v251, s[6:7] offset:2976
	s_add_u32 s4, s4, 0x18000
	s_addc_u32 s5, s5, 0
	global_load_dwordx4 v[158:161], v250, s[4:5] nt
	global_load_dword v228, v251, s[6:7] offset:3008
	s_waitcnt vmcnt(44)
;     ...
;     for (int kb = 0; kb < D / 64; ++kb) {
; #pragma unroll
;         for (int i = 0; i < 8; ++i) { const int k = 64 * kb + 8 * i + kr; const f32x4 v = __builtin_nontemporal_load((const f32x4*)(W + (size_t)k * pitch)) * g[k];
;             mx[0] = __builtin_fmaxf(mx[0], __builtin_fabsf(v[0])); mx[1] = __builtin_fmaxf(mx[1], __builtin_fabsf(v[1])); mx[2] = __builtin_fmaxf(mx[2], __builtin_fabsf(v[2])); mx[3] = __builtin_fmaxf(mx[3], __builtin_fabsf(v[3])); } }
	v_pk_mul_f32 v[16:17], v[162:163], v[230:231] op_sel_hi:[1,0]
	v_pk_mul_f32 v[18:19], v[164:165], v[230:231] op_sel_hi:[1,0]
	v_pk_mul_f32 v[20:21], v[166:167], v[232:233] op_sel_hi:[1,0]
	v_pk_mul_f32 v[22:23], v[168:169], v[232:233] op_sel_hi:[1,0]
	v_max3_f32 v15, v15, |v16|, |v20|
	v_max3_f32 v13, v13, |v17|, |v21|
	v_max3_f32 v9, v9, |v18|, |v22|
	v_max3_f32 v7, v7, |v19|, |v23|
	s_add_u32 s4, s4, 0x18000
	s_addc_u32 s5, s5, 0
	global_load_dwordx4 v[162:165], v250, s[4:5] nt
	global_load_dword v230, v251, s[6:7] offset:3040
	s_add_u32 s4, s4, 0x18000
	s_addc_u32 s5, s5, 0
	global_load_dwordx4 v[166:169], v250, s[4:5] nt
	global_load_dword v232, v251, s[6:7] offset:3072
	s_waitcnt vmcnt(44)
	v_pk_mul_f32 v[16:17], v[170:171], v[234:235] op_sel_hi:[1,0]
	v_pk_mul_f32 v[18:19], v[172:173], v[234:235] op_sel_hi:[1,0]
	v_pk_mul_f32 v[20:21], v[174:175], v[236:237] op_sel_hi:[1,0]
	v_pk_mul_f32 v[22:23], v[176:177], v[236:237] op_sel_hi:[1,0]
	v_max3_f32 v15, v15, |v16|, |v20|
	v_max3_f32 v13, v13, |v17|, |v21|
	v_max3_f32 v9, v9, |v18|, |v22|
	v_max3_f32 v7, v7, |v19|, |v23|
	s_add_u32 s4, s4, 0x18000
	s_addc_u32 s5, s5, 0
	global_load_dwordx4 v[170:173], v250, s[4:5] nt
	global_load_dword v234, v251, s[6:7] offset:3104
	s_add_u32 s4, s4, 0x18000
	s_addc_u32 s5, s5, 0
	global_load_dwordx4 v[174:177], v250, s[4:5] nt
	global_load_dword v236, v251, s[6:7] offset:3136
	s_waitcnt vmcnt(44)
	v_pk_mul_f32 v[16:17], v[178:179], v[238:239] op_sel_hi:[1,0]
	v_pk_mul_f32 v[18:19], v[180:181], v[238:239] op_sel_hi:[1,0]
	v_pk_mul_f32 v[20:21], v[182:183], v[240:241] op_sel_hi:[1,0]
	v_pk_mul_f32 v[22:23], v[184:185], v[240:241] op_sel_hi:[1,0]
	v_max3_f32 v15, v15, |v16|, |v20|
	v_max3_f32 v13, v13, |v17|, |v21|
	v_max3_f32 v9, v9, |v18|, |v22|
	v_max3_f32 v7, v7, |v19|, |v23|
	s_add_u32 s4, s4, 0x18000
	s_addc_u32 s5, s5, 0
	global_load_dwordx4 v[178:181], v250, s[4:5] nt
	global_load_dword v238, v251, s[6:7] offset:3168
	s_add_u32 s4, s4, 0x18000
	s_addc_u32 s5, s5, 0
	global_load_dwordx4 v[182:185], v250, s[4:5] nt
	global_load_dword v240, v251, s[6:7] offset:3200
	s_waitcnt vmcnt(44)
	v_pk_mul_f32 v[16:17], v[186:187], v[242:243] op_sel_hi:[1,0]
	v_pk_mul_f32 v[18:19], v[188:189], v[242:243] op_sel_hi:[1,0]
	v_pk_mul_f32 v[20:21], v[190:191], v[244:245] op_sel_hi:[1,0]
	v_pk_mul_f32 v[22:23], v[192:193], v[244:245] op_sel_hi:[1,0]
	v_max3_f32 v15, v15, |v16|, |v20|
	v_max3_f32 v13, v13, |v17|, |v21|
	v_max3_f32 v9, v9, |v18|, |v22|
	v_max3_f32 v7, v7, |v19|, |v23|
	s_add_u32 s4, s4, 0x18000
	s_addc_u32 s5, s5, 0
	global_load_dwordx4 v[186:189], v250, s[4:5] nt
	global_load_dword v242, v251, s[6:7] offset:3232
	s_add_u32 s4, s4, 0x18000
	s_addc_u32 s5, s5, 0
	global_load_dwordx4 v[190:193], v250, s[4:5] nt
	global_load_dword v244, v251, s[6:7] offset:3264
	s_waitcnt vmcnt(44)
	v_pk_mul_f32 v[16:17], v[194:195], v[246:247] op_sel_hi:[1,0]
	v_pk_mul_f32 v[18:19], v[196:197], v[246:247] op_sel_hi:[1,0]
	v_pk_mul_f32 v[20:21], v[198:199], v[248:249] op_sel_hi:[1,0]
	v_pk_mul_f32 v[22:23], v[200:201], v[248:249] op_sel_hi:[1,0]
	v_max3_f32 v15, v15, |v16|, |v20|
	v_max3_f32 v13, v13, |v17|, |v21|
	v_max3_f32 v9, v9, |v18|, |v22|
	v_max3_f32 v7, v7, |v19|, |v23|
	s_add_u32 s4, s4, 0x18000
	s_addc_u32 s5, s5, 0
	global_load_dwordx4 v[194:197], v250, s[4:5] nt
	global_load_dword v246, v251, s[6:7] offset:3296
	s_add_u32 s4, s4, 0x18000
	s_addc_u32 s5, s5, 0
	global_load_dwordx4 v[198:201], v250, s[4:5] nt
	global_load_dword v248, v251, s[6:7] offset:3328
	s_waitcnt vmcnt(44)
	v_pk_mul_f32 v[16:17], v[106:107], v[202:203] op_sel_hi:[1,0]
	v_pk_mul_f32 v[18:19], v[108:109], v[202:203] op_sel_hi:[1,0]
	v_pk_mul_f32 v[20:21], v[110:111], v[204:205] op_sel_hi:[1,0]
	v_pk_mul_f32 v[22:23], v[112:113], v[204:205] op_sel_hi:[1,0]
	v_max3_f32 v15, v15, |v16|, |v20|
	v_max3_f32 v13, v13, |v17|, |v21|
	v_max3_f32 v9, v9, |v18|, |v22|
	v_max3_f32 v7, v7, |v19|, |v23|
	s_add_u32 s4, s4, 0x18000
	s_addc_u32 s5, s5, 0
	global_load_dwordx4 v[106:109], v250, s[4:5] nt
	global_load_dword v202, v251, s[6:7] offset:3360
	s_add_u32 s4, s4, 0x18000
	s_addc_u32 s5, s5, 0
	global_load_dwordx4 v[110:113], v250, s[4:5] nt
	global_load_dword v204, v251, s[6:7] offset:3392
	s_waitcnt vmcnt(44)
	v_pk_mul_f32 v[16:17], v[114:115], v[206:207] op_sel_hi:[1,0]
	v_pk_mul_f32 v[18:19], v[116:117], v[206:207] op_sel_hi:[1,0]
	v_pk_mul_f32 v[20:21], v[118:119], v[208:209] op_sel_hi:[1,0]
	v_pk_mul_f32 v[22:23], v[120:121], v[208:209] op_sel_hi:[1,0]
	v_max3_f32 v15, v15, |v16|, |v20|
	v_max3_f32 v13, v13, |v17|, |v21|
	v_max3_f32 v9, v9, |v18|, |v22|
	v_max3_f32 v7, v7, |v19|, |v23|
	s_add_u32 s4, s4, 0x18000
	s_addc_u32 s5, s5, 0
	global_load_dwordx4 v[114:117], v250, s[4:5] nt
	global_load_dword v206, v251, s[6:7] offset:3424
	s_add_u32 s4, s4, 0x18000
	s_addc_u32 s5, s5, 0
	global_load_dwordx4 v[118:121], v250, s[4:5] nt
	global_load_dword v208, v251, s[6:7] offset:3456
	s_waitcnt vmcnt(44)
	v_pk_mul_f32 v[16:17], v[122:123], v[210:211] op_sel_hi:[1,0]
	v_pk_mul_f32 v[18:19], v[124:125], v[210:211] op_sel_hi:[1,0]
	v_pk_mul_f32 v[20:21], v[126:127], v[212:213] op_sel_hi:[1,0]
	v_pk_mul_f32 v[22:23], v[128:129], v[212:213] op_sel_hi:[1,0]
	v_max3_f32 v15, v15, |v16|, |v20|
	v_max3_f32 v13, v13, |v17|, |v21|
	v_max3_f32 v9, v9, |v18|, |v22|
	v_max3_f32 v7, v7, |v19|, |v23|
	s_add_u32 s4, s4, 0x18000
	s_addc_u32 s5, s5, 0
	global_load_dwordx4 v[122:125], v250, s[4:5] nt
	global_load_dword v210, v251, s[6:7] offset:3488
	s_add_u32 s4, s4, 0x18000
	s_addc_u32 s5, s5, 0
	global_load_dwordx4 v[126:129], v250, s[4:5] nt
	global_load_dword v212, v251, s[6:7] offset:3520
	s_waitcnt vmcnt(44)
;     ...
;     for (int kb = 0; kb < D / 64; ++kb) {
; #pragma unroll
;         for (int i = 0; i < 8; ++i) { const int k = 64 * kb + 8 * i + kr; const f32x4 v = __builtin_nontemporal_load((const f32x4*)(W + (size_t)k * pitch)) * g[k];
;             mx[0] = __builtin_fmaxf(mx[0], __builtin_fabsf(v[0])); mx[1] = __builtin_fmaxf(mx[1], __builtin_fabsf(v[1])); mx[2] = __builtin_fmaxf(mx[2], __builtin_fabsf(v[2])); mx[3] = __builtin_fmaxf(mx[3], __builtin_fabsf(v[3])); } }
	v_pk_mul_f32 v[16:17], v[130:131], v[214:215] op_sel_hi:[1,0]
	v_pk_mul_f32 v[18:19], v[132:133], v[214:215] op_sel_hi:[1,0]
	v_pk_mul_f32 v[20:21], v[134:135], v[216:217] op_sel_hi:[1,0]
	v_pk_mul_f32 v[22:23], v[136:137], v[216:217] op_sel_hi:[1,0]
	v_max3_f32 v15, v15, |v16|, |v20|
	v_max3_f32 v13, v13, |v17|, |v21|
	v_max3_f32 v9, v9, |v18|, |v22|
	v_max3_f32 v7, v7, |v19|, |v23|
	s_add_u32 s4, s4, 0x18000
	s_addc_u32 s5, s5, 0
	global_load_dwordx4 v[130:133], v250, s[4:5] nt
	global_load_dword v214, v251, s[6:7] offset:3552
	s_add_u32 s4, s4, 0x18000
	s_addc_u32 s5, s5, 0
	global_load_dwordx4 v[134:137], v250, s[4:5] nt
	global_load_dword v216, v251, s[6:7] offset:3584
	s_waitcnt vmcnt(44)
	v_pk_mul_f32 v[16:17], v[138:139], v[218:219] op_sel_hi:[1,0]
	v_pk_mul_f32 v[18:19], v[140:141], v[218:219] op_sel_hi:[1,0]
	v_pk_mul_f32 v[20:21], v[142:143], v[220:221] op_sel_hi:[1,0]
	v_pk_mul_f32 v[22:23], v[144:145], v[220:221] op_sel_hi:[1,0]
	v_max3_f32 v15, v15, |v16|, |v20|
	v_max3_f32 v13, v13, |v17|, |v21|
	v_max3_f32 v9, v9, |v18|, |v22|
	v_max3_f32 v7, v7, |v19|, |v23|
	s_waitcnt vmcnt(40)
	v_pk_mul_f32 v[16:17], v[146:147], v[222:223] op_sel_hi:[1,0]
	v_pk_mul_f32 v[18:19], v[148:149], v[222:223] op_sel_hi:[1,0]
	v_pk_mul_f32 v[20:21], v[150:151], v[224:225] op_sel_hi:[1,0]
	v_pk_mul_f32 v[22:23], v[152:153], v[224:225] op_sel_hi:[1,0]
	v_max3_f32 v15, v15, |v16|, |v20|
	v_max3_f32 v13, v13, |v17|, |v21|
	v_max3_f32 v9, v9, |v18|, |v22|
	v_max3_f32 v7, v7, |v19|, |v23|
	s_waitcnt vmcnt(36)
	v_pk_mul_f32 v[16:17], v[154:155], v[226:227] op_sel_hi:[1,0]
	v_pk_mul_f32 v[18:19], v[156:157], v[226:227] op_sel_hi:[1,0]
	v_pk_mul_f32 v[20:21], v[158:159], v[228:229] op_sel_hi:[1,0]
	v_pk_mul_f32 v[22:23], v[160:161], v[228:229] op_sel_hi:[1,0]
	v_max3_f32 v15, v15, |v16|, |v20|
	v_max3_f32 v13, v13, |v17|, |v21|
	v_max3_f32 v9, v9, |v18|, |v22|
	v_max3_f32 v7, v7, |v19|, |v23|
	s_waitcnt vmcnt(32)
	v_pk_mul_f32 v[16:17], v[162:163], v[230:231] op_sel_hi:[1,0]
	v_pk_mul_f32 v[18:19], v[164:165], v[230:231] op_sel_hi:[1,0]
	v_pk_mul_f32 v[20:21], v[166:167], v[232:233] op_sel_hi:[1,0]
	v_pk_mul_f32 v[22:23], v[168:169], v[232:233] op_sel_hi:[1,0]
	v_max3_f32 v15, v15, |v16|, |v20|
	v_max3_f32 v13, v13, |v17|, |v21|
	v_max3_f32 v9, v9, |v18|, |v22|
	v_max3_f32 v7, v7, |v19|, |v23|
	s_waitcnt vmcnt(28)
	v_pk_mul_f32 v[16:17], v[170:171], v[234:235] op_sel_hi:[1,0]
	v_pk_mul_f32 v[18:19], v[172:173], v[234:235] op_sel_hi:[1,0]
	v_pk_mul_f32 v[20:21], v[174:175], v[236:237] op_sel_hi:[1,0]
	v_pk_mul_f32 v[22:23], v[176:177], v[236:237] op_sel_hi:[1,0]
	v_max3_f32 v15, v15, |v16|, |v20|
	v_max3_f32 v13, v13, |v17|, |v21|
	v_max3_f32 v9, v9, |v18|, |v22|
	v_max3_f32 v7, v7, |v19|, |v23|
	s_waitcnt vmcnt(24)
	v_pk_mul_f32 v[16:17], v[178:179], v[238:239] op_sel_hi:[1,0]
	v_pk_mul_f32 v[18:19], v[180:181], v[238:239] op_sel_hi:[1,0]
	v_pk_mul_f32 v[20:21], v[182:183], v[240:241] op_sel_hi:[1,0]
	v_pk_mul_f32 v[22:23], v[184:185], v[240:241] op_sel_hi:[1,0]
	v_max3_f32 v15, v15, |v16|, |v20|
	v_max3_f32 v13, v13, |v17|, |v21|
	v_max3_f32 v9, v9, |v18|, |v22|
	v_max3_f32 v7, v7, |v19|, |v23|
	s_waitcnt vmcnt(20)
	v_pk_mul_f32 v[16:17], v[186:187], v[242:243] op_sel_hi:[1,0]
	v_pk_mul_f32 v[18:19], v[188:189], v[242:243] op_sel_hi:[1,0]
	v_pk_mul_f32 v[20:21], v[190:191], v[244:245] op_sel_hi:[1,0]
	v_pk_mul_f32 v[22:23], v[192:193], v[244:245] op_sel_hi:[1,0]
	v_max3_f32 v15, v15, |v16|, |v20|
	v_max3_f32 v13, v13, |v17|, |v21|
	v_max3_f32 v9, v9, |v18|, |v22|
	v_max3_f32 v7, v7, |v19|, |v23|
	s_waitcnt vmcnt(16)
	v_pk_mul_f32 v[16:17], v[194:195], v[246:247] op_sel_hi:[1,0]
	v_pk_mul_f32 v[18:19], v[196:197], v[246:247] op_sel_hi:[1,0]
	v_pk_mul_f32 v[20:21], v[198:199], v[248:249] op_sel_hi:[1,0]
	v_pk_mul_f32 v[22:23], v[200:201], v[248:249] op_sel_hi:[1,0]
	v_max3_f32 v15, v15, |v16|, |v20|
	v_max3_f32 v13, v13, |v17|, |v21|
	v_max3_f32 v9, v9, |v18|, |v22|
	v_max3_f32 v7, v7, |v19|, |v23|
	s_waitcnt vmcnt(12)
; __device__ __forceinline__ float shfl_xor_f(float v, int mask, int lane) { return __int_as_float(__builtin_amdgcn_ds_bpermute((lane ^ mask) << 2, __float_as_int(v))); }
;     ...
;     for (int kb = 0; kb < D / 64; ++kb) {
; #pragma unroll
;         for (int i = 0; i < 8; ++i) { const int k = 64 * kb + 8 * i + kr; const f32x4 v = __builtin_nontemporal_load((const f32x4*)(W + (size_t)k * pitch)) * g[k];
;             mx[0] = __builtin_fmaxf(mx[0], __builtin_fabsf(v[0])); mx[1] = __builtin_fmaxf(mx[1], __builtin_fabsf(v[1])); mx[2] = __builtin_fmaxf(mx[2], __builtin_fabsf(v[2])); mx[3] = __builtin_fmaxf(mx[3], __builtin_fabsf(v[3])); } }
; #pragma unroll
;     for (int c = 0; c < 4; ++c) { float m = mx[c]; m = __builtin_fmaxf(m, shfl_xor_f(m, 8, lane)); m = __builtin_fmaxf(m, shfl_xor_f(m, 16, lane)); m = __builtin_fmaxf(m, shfl_xor_f(m, 32, lane)); mx[c] = m; }
;     f32x4 inv, step;
; #pragma unroll
;     for (int c = 0; c < 4; ++c) { step[c] = mx[c] > 0.f ? mx[c] * (1.0f / 127.0f) : 1.0f; inv[c] = mx[c] > 0.f ? 127.0f / mx[c] : 0.f; }
;     if (lane < 8) *(f32x4*)(sw + n0 + 4 * lane) = step * swm;
	v_pk_mul_f32 v[16:17], v[106:107], v[202:203] op_sel_hi:[1,0]
	v_pk_mul_f32 v[18:19], v[108:109], v[202:203] op_sel_hi:[1,0]
	v_pk_mul_f32 v[20:21], v[110:111], v[204:205] op_sel_hi:[1,0]
	v_pk_mul_f32 v[22:23], v[112:113], v[204:205] op_sel_hi:[1,0]
	v_max3_f32 v15, v15, |v16|, |v20|
	v_max3_f32 v13, v13, |v17|, |v21|
	v_max3_f32 v9, v9, |v18|, |v22|
	v_max3_f32 v7, v7, |v19|, |v23|
	s_waitcnt vmcnt(8)
	v_pk_mul_f32 v[16:17], v[114:115], v[206:207] op_sel_hi:[1,0]
	v_pk_mul_f32 v[18:19], v[116:117], v[206:207] op_sel_hi:[1,0]
	v_pk_mul_f32 v[20:21], v[118:119], v[208:209] op_sel_hi:[1,0]
	v_pk_mul_f32 v[22:23], v[120:121], v[208:209] op_sel_hi:[1,0]
	v_max3_f32 v15, v15, |v16|, |v20|
	v_max3_f32 v13, v13, |v17|, |v21|
	v_max3_f32 v9, v9, |v18|, |v22|
	v_max3_f32 v7, v7, |v19|, |v23|
	s_waitcnt vmcnt(4)
	v_pk_mul_f32 v[16:17], v[122:123], v[210:211] op_sel_hi:[1,0]
	v_pk_mul_f32 v[18:19], v[124:125], v[210:211] op_sel_hi:[1,0]
	v_pk_mul_f32 v[20:21], v[126:127], v[212:213] op_sel_hi:[1,0]
	v_pk_mul_f32 v[22:23], v[128:129], v[212:213] op_sel_hi:[1,0]
	v_max3_f32 v15, v15, |v16|, |v20|
	v_max3_f32 v13, v13, |v17|, |v21|
	v_max3_f32 v9, v9, |v18|, |v22|
	v_max3_f32 v7, v7, |v19|, |v23|
	s_waitcnt vmcnt(0)
	v_pk_mul_f32 v[16:17], v[130:131], v[214:215] op_sel_hi:[1,0]
	v_pk_mul_f32 v[18:19], v[132:133], v[214:215] op_sel_hi:[1,0]
	v_pk_mul_f32 v[20:21], v[134:135], v[216:217] op_sel_hi:[1,0]
	v_pk_mul_f32 v[22:23], v[136:137], v[216:217] op_sel_hi:[1,0]
	v_max3_f32 v15, v15, |v16|, |v20|
	v_max3_f32 v13, v13, |v17|, |v21|
	v_max3_f32 v9, v9, |v18|, |v22|
	v_max3_f32 v7, v7, |v19|, |v23|
	v_lshlrev_b32_e32 v2, 2, v68
	v_xor_b32_e32 v3, 32, v2
	ds_bpermute_b32 v4, v3, v15
	v_max_f32_e32 v5, v15, v15
	v_xor_b32_e32 v8, 64, v2
	ds_bpermute_b32 v10, v3, v13
	v_max_f32_e32 v6, v13, v13
	s_waitcnt lgkmcnt(1)
	v_max_f32_e32 v4, v4, v4
	v_max_f32_e32 v4, v5, v4
	ds_bpermute_b32 v5, v8, v4
	s_waitcnt lgkmcnt(1)
	v_max_f32_e32 v10, v10, v10
	v_xor_b32_e32 v11, 0x80, v2
	v_max_f32_e32 v6, v6, v10
	ds_bpermute_b32 v10, v8, v6
	s_waitcnt lgkmcnt(1)
	v_max_f32_e32 v5, v5, v5
	v_max_f32_e32 v4, v4, v5
	ds_bpermute_b32 v5, v11, v4
	ds_bpermute_b32 v12, v3, v9
	ds_bpermute_b32 v3, v3, v7
	s_waitcnt lgkmcnt(3)
	v_max_f32_e32 v10, v10, v10
	v_max_f32_e32 v10, v6, v10
	s_waitcnt lgkmcnt(2)
	v_max_f32_e32 v5, v5, v5
	v_max_f32_e32 v6, v4, v5
	s_waitcnt lgkmcnt(1)
	v_max_f32_e32 v4, v12, v12
	v_max_f32_e32 v5, v9, v9
	v_max_f32_e32 v4, v5, v4
	s_waitcnt lgkmcnt(0)
	v_max_f32_e32 v3, v3, v3
	v_max_f32_e32 v7, v7, v7
	ds_bpermute_b32 v5, v8, v4
	v_max_f32_e32 v3, v7, v3
	ds_bpermute_b32 v7, v8, v3
	ds_bpermute_b32 v8, v11, v10
	v_cmp_lt_f32_e64 s[10:11], 0, v6
	s_waitcnt lgkmcnt(2)
	v_max_f32_e32 v5, v5, v5
	v_max_f32_e32 v4, v4, v5
	s_waitcnt lgkmcnt(1)
	v_max_f32_e32 v5, v7, v7
	v_max_f32_e32 v3, v3, v5
	ds_bpermute_b32 v9, v11, v4
	ds_bpermute_b32 v7, v11, v3
	s_waitcnt lgkmcnt(2)
	v_max_f32_e32 v5, v8, v8
	v_max_f32_e32 v5, v10, v5
	v_cmp_lt_f32_e64 s[8:9], 0, v5
	s_waitcnt lgkmcnt(1)
	v_max_f32_e32 v8, v9, v9
	s_waitcnt lgkmcnt(0)
	v_max_f32_e32 v7, v7, v7
	v_max_f32_e32 v4, v4, v8
	v_max_f32_e32 v3, v3, v7
	v_cmp_lt_f32_e64 s[6:7], 0, v4
	v_cmp_lt_f32_e64 s[4:5], 0, v3
	v_cmp_gt_u32_e32 vcc, 8, v68
	s_and_saveexec_b64 s[38:39], vcc
	s_cbranch_execz .LBB0_130
	s_mul_i32 s40, s28, 0x3000
	s_mul_hi_u32 s29, s28, 0x3000
	s_add_u32 s40, s14, s40
	s_addc_u32 s29, s15, s29
	v_mul_f32_e32 v7, 0x3c010204, v6
	s_add_u32 s40, s40, s30
	v_cndmask_b32_e64 v8, 1.0, v7, s[10:11]
	v_mul_f32_e32 v7, 0x3c010204, v5
	s_addc_u32 s41, s29, s31
	v_lshlrev_b32_e32 v12, 2, v2
	v_mov_b32_e32 v13, 0
	v_cndmask_b32_e64 v9, 1.0, v7, s[8:9]
	v_mul_f32_e32 v7, 0x3c010204, v4
	v_lshl_add_u64 v[12:13], s[40:41], 0, v[12:13]
	v_cndmask_b32_e64 v10, 1.0, v7, s[6:7]
	v_mul_f32_e32 v7, 0x3c010204, v3
	v_add_co_u32_e32 v12, vcc, 0x80000, v12
	v_cndmask_b32_e64 v11, 1.0, v7, s[4:5]
	s_nop 0
	v_addc_co_u32_e32 v13, vcc, 0, v13, vcc
	global_store_dwordx4 v[12:13], v[8:11], off

; #define LAS __attribute__((address_space(3)))
;     ...
;     for (int kb = 0; kb < D / 64; ++kb) {
; #pragma unroll
;         for (int i = 0; i < 8; ++i) { const int kk = 8 * i + kr; const int k = 64 * kb + kk; const f32x4 v = __builtin_nontemporal_load((const f32x4*)(W + (size_t)k * pitch)) * g[k];
;             LAS float* p = scr + kk * 33 + 4 * (lane & 7); p[0] = __builtin_rintf(v[0] * inv[0]); p[1] = __builtin_rintf(v[1] * inv[1]); p[2] = __builtin_rintf(v[2] * inv[2]); p[3] = __builtin_rintf(v[3] * inv[3]); }
.LBB0_131:
	v_readfirstlane_b32 s4, v0
	v_readfirstlane_b32 s5, v1
	v_readfirstlane_b32 s6, v2
	v_readfirstlane_b32 s7, v3
	s_nop 1
	v_subrev_u32_e32 v250, s4, v0
	v_subrev_u32_e32 v251, s6, v2
	s_add_u32 s4, s4, 0xfff58000
	s_addc_u32 s5, s5, -1
	s_add_u32 s6, s6, 0x1000
	s_addc_u32 s7, s7, 0
	s_nop 4
	global_load_dwordx4 v[106:109], v250, s[4:5] nt
	global_load_dword v202, v251, s[6:7]
	s_add_u32 s4, s4, 0x18000
	s_addc_u32 s5, s5, 0
	global_load_dwordx4 v[110:113], v250, s[4:5] nt
	global_load_dword v204, v251, s[6:7] offset:32
	s_add_u32 s4, s4, 0x18000
	s_addc_u32 s5, s5, 0
	global_load_dwordx4 v[114:117], v250, s[4:5] nt
	global_load_dword v206, v251, s[6:7] offset:64
	s_add_u32 s4, s4, 0x18000
	s_addc_u32 s5, s5, 0
	global_load_dwordx4 v[118:121], v250, s[4:5] nt
	global_load_dword v208, v251, s[6:7] offset:96
	s_add_u32 s4, s4, 0x18000
	s_addc_u32 s5, s5, 0
	global_load_dwordx4 v[122:125], v250, s[4:5] nt
	global_load_dword v210, v251, s[6:7] offset:128
	s_add_u32 s4, s4, 0x18000
	s_addc_u32 s5, s5, 0
	global_load_dwordx4 v[126:129], v250, s[4:5] nt
	global_load_dword v212, v251, s[6:7] offset:160
	s_add_u32 s4, s4, 0x18000
	s_addc_u32 s5, s5, 0
	global_load_dwordx4 v[130:133], v250, s[4:5] nt
	global_load_dword v214, v251, s[6:7] offset:192
	s_add_u32 s4, s4, 0x18000
	s_addc_u32 s5, s5, 0
	global_load_dwordx4 v[134:137], v250, s[4:5] nt
	global_load_dword v216, v251, s[6:7] offset:224
	s_add_u32 s4, s4, 0x18000
	s_addc_u32 s5, s5, 0
	global_load_dwordx4 v[138:141], v250, s[4:5] nt
	global_load_dword v218, v251, s[6:7] offset:256
	s_add_u32 s4, s4, 0x18000
	s_addc_u32 s5, s5, 0
	global_load_dwordx4 v[142:145], v250, s[4:5] nt
	global_load_dword v220, v251, s[6:7] offset:288
	s_add_u32 s4, s4, 0x18000
	s_addc_u32 s5, s5, 0
	global_load_dwordx4 v[146:149], v250, s[4:5] nt
	global_load_dword v222, v251, s[6:7] offset:320
	s_add_u32 s4, s4, 0x18000
	s_addc_u32 s5, s5, 0
	global_load_dwordx4 v[150:153], v250, s[4:5] nt
	global_load_dword v224, v251, s[6:7] offset:352
	s_add_u32 s4, s4, 0x18000
	s_addc_u32 s5, s5, 0
	global_load_dwordx4 v[154:157], v250, s[4:5] nt
	global_load_dword v226, v251, s[6:7] offset:384
	s_add_u32 s4, s4, 0x18000
	s_addc_u32 s5, s5, 0
	global_load_dwordx4 v[158:161], v250, s[4:5] nt
	global_load_dword v228, v251, s[6:7] offset:416
	s_add_u32 s4, s4, 0x18000
	s_addc_u32 s5, s5, 0
	global_load_dwordx4 v[162:165], v250, s[4:5] nt
	global_load_dword v230, v251, s[6:7] offset:448
	s_add_u32 s4, s4, 0x18000
	s_addc_u32 s5, s5, 0
	global_load_dwordx4 v[166:169], v250, s[4:5] nt
	global_load_dword v232, v251, s[6:7] offset:480
	s_add_u32 s4, s4, 0x18000
	s_addc_u32 s5, s5, 0
	global_load_dwordx4 v[170:173], v250, s[4:5] nt
	global_load_dword v234, v251, s[6:7] offset:512
	s_add_u32 s4, s4, 0x18000
	s_addc_u32 s5, s5, 0
	global_load_dwordx4 v[174:177], v250, s[4:5] nt
	global_load_dword v236, v251, s[6:7] offset:544
	s_add_u32 s4, s4, 0x18000
	s_addc_u32 s5, s5, 0
	global_load_dwordx4 v[178:181], v250, s[4:5] nt
	global_load_dword v238, v251, s[6:7] offset:576
	s_add_u32 s4, s4, 0x18000
	s_addc_u32 s5, s5, 0
	global_load_dwordx4 v[182:185], v250, s[4:5] nt
	global_load_dword v240, v251, s[6:7] offset:608
	s_add_u32 s4, s4, 0x18000
	s_addc_u32 s5, s5, 0
	global_load_dwordx4 v[186:189], v250, s[4:5] nt
	global_load_dword v242, v251, s[6:7] offset:640
	s_add_u32 s4, s4, 0x18000
	s_addc_u32 s5, s5, 0
	global_load_dwordx4 v[190:193], v250, s[4:5] nt
	global_load_dword v244, v251, s[6:7] offset:672
	s_add_u32 s4, s4, 0x18000
	s_addc_u32 s5, s5, 0
	global_load_dwordx4 v[194:197], v250, s[4:5] nt
	global_load_dword v246, v251, s[6:7] offset:704
	s_add_u32 s4, s4, 0x18000
	s_addc_u32 s5, s5, 0
	global_load_dwordx4 v[198:201], v250, s[4:5] nt
	global_load_dword v248, v251, s[6:7] offset:736
	v_add_u32_e32 v87, 0x14a0, v31
	v_add_u32_e32 v88, 0x14a8, v31
	v_add_u32_e32 v89, 0x18c0, v31
	v_add_u32_e32 v90, 0x18c8, v31
	v_add_u32_e32 v91, 0x1ce0, v31
	v_add_u32_e32 v92, 0x1ce8, v31
	v_lshl_add_u64 v[18:19], v[6:7], 0, v[12:13]
	v_lshl_add_u64 v[22:23], v[6:7], 0, v[10:11]
	v_lshl_add_u64 v[82:83], v[6:7], 0, v[8:9]
	v_lshl_add_u64 v[84:85], v[6:7], 0, v[4:5]
	v_lshl_add_u64 v[6:7], v[6:7], 0, 64
	s_waitcnt vmcnt(32)
	v_pk_mul_f32 v[46:47], v[112:113], v[204:205] op_sel_hi:[1,0]
	v_pk_mul_f32 v[20:21], v[110:111], v[204:205] op_sel_hi:[1,0]
	v_pk_mul_f32 v[44:45], v[116:117], v[206:207] op_sel_hi:[1,0]
	v_pk_mul_f32 v[24:25], v[114:115], v[206:207] op_sel_hi:[1,0]
	v_pk_mul_f32 v[48:49], v[120:121], v[208:209] op_sel_hi:[1,0]
	v_pk_mul_f32 v[16:17], v[108:109], v[202:203] op_sel_hi:[1,0]
	v_pk_mul_f32 v[14:15], v[106:107], v[202:203] op_sel_hi:[1,0]
	v_pk_mul_f32 v[50:51], v[118:119], v[208:209] op_sel_hi:[1,0]
	v_pk_mul_f32 v[52:53], v[124:125], v[210:211] op_sel_hi:[1,0]
	v_pk_mul_f32 v[54:55], v[122:123], v[210:211] op_sel_hi:[1,0]
	v_pk_mul_f32 v[56:57], v[128:129], v[212:213] op_sel_hi:[1,0]
	v_pk_mul_f32 v[58:59], v[126:127], v[212:213] op_sel_hi:[1,0]
	v_pk_mul_f32 v[60:61], v[132:133], v[214:215] op_sel_hi:[1,0]
	v_pk_mul_f32 v[62:63], v[130:131], v[214:215] op_sel_hi:[1,0]
	v_pk_mul_f32 v[42:43], v[136:137], v[216:217] op_sel_hi:[1,0]
	v_pk_mul_f32 v[40:41], v[134:135], v[216:217] op_sel_hi:[1,0]
	s_add_u32 s4, s4, 0x18000
	s_addc_u32 s5, s5, 0
	global_load_dwordx4 v[106:109], v250, s[4:5] nt
	global_load_dword v202, v251, s[6:7] offset:768
	s_add_u32 s4, s4, 0x18000
	s_addc_u32 s5, s5, 0
	global_load_dwordx4 v[110:113], v250, s[4:5] nt
	global_load_dword v204, v251, s[6:7] offset:800
	s_add_u32 s4, s4, 0x18000
	s_addc_u32 s5, s5, 0
	global_load_dwordx4 v[114:117], v250, s[4:5] nt
	global_load_dword v206, v251, s[6:7] offset:832
; #define LAS __attribute__((address_space(3)))
; #define GAS __attribute__((address_space(1)))
; #define LDS_WAIT() asm volatile("s_waitcnt lgkmcnt(0)" ::: "memory")
;     ...
;     for (int kb = 0; kb < D / 64; ++kb) {
; #pragma unroll
;         for (int i = 0; i < 8; ++i) { const int kk = 8 * i + kr; const int k = 64 * kb + kk; const f32x4 v = __builtin_nontemporal_load((const f32x4*)(W + (size_t)k * pitch)) * g[k];
;             LAS float* p = scr + kk * 33 + 4 * (lane & 7); p[0] = __builtin_rintf(v[0] * inv[0]); p[1] = __builtin_rintf(v[1] * inv[1]); p[2] = __builtin_rintf(v[2] * inv[2]); p[3] = __builtin_rintf(v[3] * inv[3]); }
;         LDS_WAIT(); asm volatile("" ::: "memory");
;         const int c = lane & 7;
; #pragma unroll
;         for (int j = 0; j < 4; ++j) { const int n = (lane >> 3) + 8 * j; const LAS float* sp = scr + (8 * c) * 33 + n;
;             u32x2 o;
;             o.x = ((unsigned)(int)sp[0 * 33] & 0xFFu) | (((unsigned)(int)sp[1 * 33] & 0xFFu) << 8) | (((unsigned)(int)sp[2 * 33] & 0xFFu) << 16) | (((unsigned)(int)sp[3 * 33] & 0xFFu) << 24);
;             o.y = ((unsigned)(int)sp[4 * 33] & 0xFFu) | (((unsigned)(int)sp[5 * 33] & 0xFFu) << 8) | (((unsigned)(int)sp[6 * 33] & 0xFFu) << 16) | (((unsigned)(int)sp[7 * 33] & 0xFFu) << 24);
;             *(GAS u32x2*)(dst + (size_t)(n0 + n) * D + 64 * kb + 8 * c) = o; }
	s_add_u32 s4, s4, 0x18000
	s_addc_u32 s5, s5, 0
	global_load_dwordx4 v[118:121], v250, s[4:5] nt
	global_load_dword v208, v251, s[6:7] offset:864
	s_add_u32 s4, s4, 0x18000
	s_addc_u32 s5, s5, 0
	global_load_dwordx4 v[122:125], v250, s[4:5] nt
	global_load_dword v210, v251, s[6:7] offset:896
	s_add_u32 s4, s4, 0x18000
	s_addc_u32 s5, s5, 0
	global_load_dwordx4 v[126:129], v250, s[4:5] nt
	global_load_dword v212, v251, s[6:7] offset:928
	s_add_u32 s4, s4, 0x18000
	s_addc_u32 s5, s5, 0
	global_load_dwordx4 v[130:133], v250, s[4:5] nt
	global_load_dword v214, v251, s[6:7] offset:960
	s_add_u32 s4, s4, 0x18000
	s_addc_u32 s5, s5, 0
	global_load_dwordx4 v[134:137], v250, s[4:5] nt
	global_load_dword v216, v251, s[6:7] offset:992
	v_mul_f32_e32 v14, v26, v14
	v_mul_f32_e32 v15, v27, v15
	v_mul_f32_e32 v16, v28, v16
	v_mul_f32_e32 v17, v29, v17
	v_mul_f32_e32 v20, v26, v20
	v_mul_f32_e32 v21, v27, v21
	v_mul_f32_e32 v46, v28, v46
	v_mul_f32_e32 v47, v29, v47
	v_mul_f32_e32 v24, v26, v24
	v_mul_f32_e32 v25, v27, v25
	v_mul_f32_e32 v44, v28, v44
	v_mul_f32_e32 v45, v29, v45
	v_mul_f32_e32 v50, v26, v50
	v_mul_f32_e32 v51, v27, v51
	v_mul_f32_e32 v48, v28, v48
	v_mul_f32_e32 v49, v29, v49
	v_mul_f32_e32 v54, v26, v54
	v_mul_f32_e32 v55, v27, v55
	v_mul_f32_e32 v52, v28, v52
	v_mul_f32_e32 v53, v29, v53
	v_mul_f32_e32 v58, v26, v58
	v_mul_f32_e32 v59, v27, v59
	v_mul_f32_e32 v56, v28, v56
	v_mul_f32_e32 v57, v29, v57
	v_mul_f32_e32 v62, v26, v62
	v_mul_f32_e32 v63, v27, v63
	v_mul_f32_e32 v60, v28, v60
	v_mul_f32_e32 v61, v29, v61
	v_mul_f32_e32 v40, v26, v40
	v_mul_f32_e32 v41, v27, v41
	v_mul_f32_e32 v42, v28, v42
	v_mul_f32_e32 v43, v29, v43
	v_rndne_f32_e32 v14, v14
	v_rndne_f32_e32 v15, v15
	v_rndne_f32_e32 v16, v16
	v_rndne_f32_e32 v17, v17
	v_rndne_f32_e32 v20, v20
	v_rndne_f32_e32 v21, v21
	v_rndne_f32_e32 v46, v46
	v_rndne_f32_e32 v47, v47
	v_rndne_f32_e32 v24, v24
	v_rndne_f32_e32 v25, v25
	v_rndne_f32_e32 v44, v44
	v_rndne_f32_e32 v45, v45
	v_rndne_f32_e32 v50, v50
	v_rndne_f32_e32 v51, v51
	v_rndne_f32_e32 v48, v48
	v_rndne_f32_e32 v49, v49
	v_rndne_f32_e32 v54, v54
	v_rndne_f32_e32 v55, v55
	v_rndne_f32_e32 v52, v52
	v_rndne_f32_e32 v53, v53
	v_rndne_f32_e32 v58, v58
	v_rndne_f32_e32 v59, v59
	v_rndne_f32_e32 v56, v56
	v_rndne_f32_e32 v57, v57
	v_rndne_f32_e32 v62, v62
	v_rndne_f32_e32 v63, v63
	v_rndne_f32_e32 v60, v60
	v_rndne_f32_e32 v61, v61
	v_rndne_f32_e32 v40, v40
	v_rndne_f32_e32 v41, v41
	v_rndne_f32_e32 v42, v42
	v_rndne_f32_e32 v43, v43
	ds_write2_b32 v31, v14, v15 offset1:1
	ds_write2_b32 v31, v16, v17 offset0:2 offset1:3
	ds_write2_b32 v32, v20, v21 offset1:1
	ds_write2_b32 v33, v46, v47 offset1:1
	ds_write2_b32 v34, v24, v25 offset1:1
	ds_write2_b32 v35, v44, v45 offset1:1
	ds_write2_b32 v36, v50, v51 offset1:1
	ds_write2_b32 v37, v48, v49 offset1:1
	ds_write2_b32 v38, v54, v55 offset1:1
	ds_write2_b32 v39, v52, v53 offset1:1
	ds_write2_b32 v87, v58, v59 offset1:1
	ds_write2_b32 v88, v56, v57 offset1:1
	ds_write2_b32 v89, v62, v63 offset1:1
	ds_write2_b32 v90, v60, v61 offset1:1
	ds_write2_b32 v91, v40, v41 offset1:1
	ds_write2_b32 v92, v42, v43 offset1:1
	s_waitcnt lgkmcnt(0)
	ds_read2_b32 v[14:15], v30 offset1:8
	ds_read2_b32 v[16:17], v30 offset0:33 offset1:41
	ds_read2_b32 v[20:21], v30 offset0:66 offset1:74
	ds_read2_b32 v[24:25], v30 offset0:99 offset1:107
	ds_read2_b32 v[40:41], v30 offset0:132 offset1:140
	ds_read2_b32 v[42:43], v30 offset0:165 offset1:173
	ds_read2_b32 v[44:45], v30 offset0:198 offset1:206
	ds_read2_b32 v[46:47], v30 offset0:231 offset1:239
	ds_read2_b32 v[48:49], v30 offset0:16 offset1:24
	ds_read2_b32 v[50:51], v30 offset0:49 offset1:57
	ds_read2_b32 v[52:53], v30 offset0:82 offset1:90
	ds_read2_b32 v[54:55], v30 offset0:115 offset1:123
	ds_read2_b32 v[56:57], v30 offset0:148 offset1:156
	ds_read2_b32 v[58:59], v30 offset0:181 offset1:189
	ds_read2_b32 v[60:61], v30 offset0:214 offset1:222
	ds_read2_b32 v[62:63], v30 offset0:247 offset1:255
	s_waitcnt lgkmcnt(14)
	v_cvt_i32_f32_e32 v16, v16
	s_waitcnt lgkmcnt(10)
	v_cvt_i32_f32_e32 v42, v42
	v_cvt_i32_f32_e32 v14, v14
	v_cvt_i32_f32_sdwa v20, v20 dst_sel:WORD_1 dst_unused:UNUSED_PAD src0_sel:DWORD
	v_cvt_i32_f32_e32 v40, v40
	s_waitcnt lgkmcnt(9)
	v_cvt_i32_f32_sdwa v44, v44 dst_sel:WORD_1 dst_unused:UNUSED_PAD src0_sel:DWORD
	v_cvt_i32_f32_e32 v17, v17
	v_cvt_i32_f32_e32 v43, v43
	s_waitcnt lgkmcnt(6)
	v_cvt_i32_f32_e32 v50, v50
	s_waitcnt lgkmcnt(2)
	v_cvt_i32_f32_e32 v58, v58
	v_cvt_i32_f32_e32 v51, v51
	v_cvt_i32_f32_e32 v59, v59
	v_cvt_i32_f32_sdwa v24, v24 dst_sel:BYTE_3 dst_unused:UNUSED_PAD src0_sel:DWORD
	v_cvt_i32_f32_sdwa v46, v46 dst_sel:BYTE_3 dst_unused:UNUSED_PAD src0_sel:DWORD
	v_cvt_i32_f32_e32 v15, v15
	v_cvt_i32_f32_sdwa v21, v21 dst_sel:WORD_1 dst_unused:UNUSED_PAD src0_sel:DWORD
	v_cvt_i32_f32_e32 v41, v41
	v_cvt_i32_f32_sdwa v45, v45 dst_sel:WORD_1 dst_unused:UNUSED_PAD src0_sel:DWORD
	v_cvt_i32_f32_e32 v48, v48
	v_cvt_i32_f32_sdwa v52, v52 dst_sel:WORD_1 dst_unused:UNUSED_PAD src0_sel:DWORD
	v_cvt_i32_f32_e32 v56, v56
	s_waitcnt lgkmcnt(1)
	v_cvt_i32_f32_sdwa v60, v60 dst_sel:WORD_1 dst_unused:UNUSED_PAD src0_sel:DWORD
	v_cvt_i32_f32_e32 v49, v49
	v_cvt_i32_f32_sdwa v53, v53 dst_sel:WORD_1 dst_unused:UNUSED_PAD src0_sel:DWORD
	v_cvt_i32_f32_e32 v57, v57
	v_cvt_i32_f32_sdwa v61, v61 dst_sel:WORD_1 dst_unused:UNUSED_PAD src0_sel:DWORD
	v_cvt_i32_f32_sdwa v25, v25 dst_sel:BYTE_3 dst_unused:UNUSED_PAD src0_sel:DWORD
	v_cvt_i32_f32_sdwa v47, v47 dst_sel:BYTE_3 dst_unused:UNUSED_PAD src0_sel:DWORD
	v_cvt_i32_f32_sdwa v54, v54 dst_sel:BYTE_3 dst_unused:UNUSED_PAD src0_sel:DWORD
	s_waitcnt lgkmcnt(0)
; #define LAS __attribute__((address_space(3)))
; #define GAS __attribute__((address_space(1)))
; #define LDS_WAIT() asm volatile("s_waitcnt lgkmcnt(0)" ::: "memory")
;     ...
;     for (int kb = 0; kb < D / 64; ++kb) {
; #pragma unroll
;         for (int i = 0; i < 8; ++i) { const int kk = 8 * i + kr; const int k = 64 * kb + kk; const f32x4 v = __builtin_nontemporal_load((const f32x4*)(W + (size_t)k * pitch)) * g[k];
;             LAS float* p = scr + kk * 33 + 4 * (lane & 7); p[0] = __builtin_rintf(v[0] * inv[0]); p[1] = __builtin_rintf(v[1] * inv[1]); p[2] = __builtin_rintf(v[2] * inv[2]); p[3] = __builtin_rintf(v[3] * inv[3]); }
;         LDS_WAIT(); asm volatile("" ::: "memory");
;         const int c = lane & 7;
; #pragma unroll
;         for (int j = 0; j < 4; ++j) { const int n = (lane >> 3) + 8 * j; const LAS float* sp = scr + (8 * c) * 33 + n;
;             u32x2 o;
;             o.x = ((unsigned)(int)sp[0 * 33] & 0xFFu) | (((unsigned)(int)sp[1 * 33] & 0xFFu) << 8) | (((unsigned)(int)sp[2 * 33] & 0xFFu) << 16) | (((unsigned)(int)sp[3 * 33] & 0xFFu) << 24);
;             o.y = ((unsigned)(int)sp[4 * 33] & 0xFFu) | (((unsigned)(int)sp[5 * 33] & 0xFFu) << 8) | (((unsigned)(int)sp[6 * 33] & 0xFFu) << 16) | (((unsigned)(int)sp[7 * 33] & 0xFFu) << 24);
;             *(GAS u32x2*)(dst + (size_t)(n0 + n) * D + 64 * kb + 8 * c) = o; }
;         LDS_WAIT(); asm volatile("" ::: "memory");
	v_cvt_i32_f32_sdwa v62, v62 dst_sel:BYTE_3 dst_unused:UNUSED_PAD src0_sel:DWORD
	v_cvt_i32_f32_sdwa v55, v55 dst_sel:BYTE_3 dst_unused:UNUSED_PAD src0_sel:DWORD
	v_cvt_i32_f32_sdwa v63, v63 dst_sel:BYTE_3 dst_unused:UNUSED_PAD src0_sel:DWORD
	v_lshlrev_b32_e32 v16, 8, v16
	v_lshlrev_b32_e32 v42, 8, v42
	v_and_b32_e32 v20, 0xff0000, v20
	v_and_b32_e32 v44, 0xff0000, v44
	v_lshlrev_b32_e32 v17, 8, v17
	v_lshlrev_b32_e32 v43, 8, v43
	v_lshlrev_b32_e32 v50, 8, v50
	v_lshlrev_b32_e32 v58, 8, v58
	v_lshlrev_b32_e32 v51, 8, v51
	v_lshlrev_b32_e32 v59, 8, v59
	v_perm_b32 v14, v16, v14, s28
	v_perm_b32 v16, v42, v40, s28
	v_and_b32_e32 v21, 0xff0000, v21
	v_and_b32_e32 v45, 0xff0000, v45
	v_and_b32_e32 v52, 0xff0000, v52
	v_and_b32_e32 v60, 0xff0000, v60
	v_and_b32_e32 v53, 0xff0000, v53
	v_and_b32_e32 v61, 0xff0000, v61
	v_perm_b32 v17, v17, v15, s28
	v_perm_b32 v40, v43, v41, s28
	v_perm_b32 v41, v50, v48, s28
	v_perm_b32 v42, v58, v56, s28
	v_perm_b32 v43, v51, v49, s28
	v_perm_b32 v48, v59, v57, s28
	v_or3_b32 v14, v14, v20, v24
	v_or3_b32 v15, v16, v44, v46
	v_or3_b32 v16, v17, v21, v25
	v_or3_b32 v17, v40, v45, v47
	v_or3_b32 v20, v41, v52, v54
	v_or3_b32 v21, v42, v60, v62
	v_or3_b32 v24, v43, v53, v55
	v_or3_b32 v25, v48, v61, v63
	global_store_dwordx2 v[18:19], v[14:15], off
	global_store_dwordx2 v[22:23], v[16:17], off
	global_store_dwordx2 v[82:83], v[20:21], off
	global_store_dwordx2 v[84:85], v[24:25], off
	s_waitcnt lgkmcnt(0)
	v_add_u32_e32 v87, 0x14a0, v31
	v_add_u32_e32 v88, 0x14a8, v31
	v_add_u32_e32 v89, 0x18c0, v31
	v_add_u32_e32 v90, 0x18c8, v31
	v_add_u32_e32 v91, 0x1ce0, v31
	v_add_u32_e32 v92, 0x1ce8, v31
	v_lshl_add_u64 v[18:19], v[6:7], 0, v[12:13]
	v_lshl_add_u64 v[22:23], v[6:7], 0, v[10:11]
	v_lshl_add_u64 v[82:83], v[6:7], 0, v[8:9]
	v_lshl_add_u64 v[84:85], v[6:7], 0, v[4:5]
	v_lshl_add_u64 v[6:7], v[6:7], 0, 64
	s_waitcnt vmcnt(36)
	v_pk_mul_f32 v[46:47], v[144:145], v[220:221] op_sel_hi:[1,0]
	v_pk_mul_f32 v[20:21], v[142:143], v[220:221] op_sel_hi:[1,0]
	v_pk_mul_f32 v[44:45], v[148:149], v[222:223] op_sel_hi:[1,0]
	v_pk_mul_f32 v[24:25], v[146:147], v[222:223] op_sel_hi:[1,0]
	v_pk_mul_f32 v[48:49], v[152:153], v[224:225] op_sel_hi:[1,0]
	v_pk_mul_f32 v[16:17], v[140:141], v[218:219] op_sel_hi:[1,0]
	v_pk_mul_f32 v[14:15], v[138:139], v[218:219] op_sel_hi:[1,0]
	v_pk_mul_f32 v[50:51], v[150:151], v[224:225] op_sel_hi:[1,0]
	v_pk_mul_f32 v[52:53], v[156:157], v[226:227] op_sel_hi:[1,0]
	v_pk_mul_f32 v[54:55], v[154:155], v[226:227] op_sel_hi:[1,0]
	v_pk_mul_f32 v[56:57], v[160:161], v[228:229] op_sel_hi:[1,0]
	v_pk_mul_f32 v[58:59], v[158:159], v[228:229] op_sel_hi:[1,0]
	v_pk_mul_f32 v[60:61], v[164:165], v[230:231] op_sel_hi:[1,0]
	v_pk_mul_f32 v[62:63], v[162:163], v[230:231] op_sel_hi:[1,0]
	v_pk_mul_f32 v[42:43], v[168:169], v[232:233] op_sel_hi:[1,0]
	v_pk_mul_f32 v[40:41], v[166:167], v[232:233] op_sel_hi:[1,0]
	s_add_u32 s4, s4, 0x18000
	s_addc_u32 s5, s5, 0
	global_load_dwordx4 v[138:141], v250, s[4:5] nt
	global_load_dword v218, v251, s[6:7] offset:1024
	s_add_u32 s4, s4, 0x18000
	s_addc_u32 s5, s5, 0
	global_load_dwordx4 v[142:145], v250, s[4:5] nt
	global_load_dword v220, v251, s[6:7] offset:1056
	s_add_u32 s4, s4, 0x18000
	s_addc_u32 s5, s5, 0
	global_load_dwordx4 v[146:149], v250, s[4:5] nt
	global_load_dword v222, v251, s[6:7] offset:1088
	s_add_u32 s4, s4, 0x18000
	s_addc_u32 s5, s5, 0
	global_load_dwordx4 v[150:153], v250, s[4:5] nt
	global_load_dword v224, v251, s[6:7] offset:1120
	s_add_u32 s4, s4, 0x18000
	s_addc_u32 s5, s5, 0
	global_load_dwordx4 v[154:157], v250, s[4:5] nt
	global_load_dword v226, v251, s[6:7] offset:1152
	s_add_u32 s4, s4, 0x18000
	s_addc_u32 s5, s5, 0
	global_load_dwordx4 v[158:161], v250, s[4:5] nt
	global_load_dword v228, v251, s[6:7] offset:1184
	s_add_u32 s4, s4, 0x18000
	s_addc_u32 s5, s5, 0
	global_load_dwordx4 v[162:165], v250, s[4:5] nt
	global_load_dword v230, v251, s[6:7] offset:1216
	s_add_u32 s4, s4, 0x18000
	s_addc_u32 s5, s5, 0
	global_load_dwordx4 v[166:169], v250, s[4:5] nt
	global_load_dword v232, v251, s[6:7] offset:1248
	v_mul_f32_e32 v14, v26, v14
	v_mul_f32_e32 v15, v27, v15
	v_mul_f32_e32 v16, v28, v16
	v_mul_f32_e32 v17, v29, v17
	v_mul_f32_e32 v20, v26, v20
	v_mul_f32_e32 v21, v27, v21
	v_mul_f32_e32 v46, v28, v46
	v_mul_f32_e32 v47, v29, v47
	v_mul_f32_e32 v24, v26, v24
	v_mul_f32_e32 v25, v27, v25
	v_mul_f32_e32 v44, v28, v44
	v_mul_f32_e32 v45, v29, v45
	v_mul_f32_e32 v50, v26, v50
	v_mul_f32_e32 v51, v27, v51
	v_mul_f32_e32 v48, v28, v48
	v_mul_f32_e32 v49, v29, v49
	v_mul_f32_e32 v54, v26, v54
	v_mul_f32_e32 v55, v27, v55
	v_mul_f32_e32 v52, v28, v52
	v_mul_f32_e32 v53, v29, v53
	v_mul_f32_e32 v58, v26, v58
	v_mul_f32_e32 v59, v27, v59
	v_mul_f32_e32 v56, v28, v56
	v_mul_f32_e32 v57, v29, v57
	v_mul_f32_e32 v62, v26, v62
	v_mul_f32_e32 v63, v27, v63
	v_mul_f32_e32 v60, v28, v60
	v_mul_f32_e32 v61, v29, v61
	v_mul_f32_e32 v40, v26, v40
	v_mul_f32_e32 v41, v27, v41
	v_mul_f32_e32 v42, v28, v42
	v_mul_f32_e32 v43, v29, v43
	v_rndne_f32_e32 v14, v14
	v_rndne_f32_e32 v15, v15
	v_rndne_f32_e32 v16, v16
	v_rndne_f32_e32 v17, v17
	v_rndne_f32_e32 v20, v20
	v_rndne_f32_e32 v21, v21
	v_rndne_f32_e32 v46, v46
	v_rndne_f32_e32 v47, v47
	v_rndne_f32_e32 v24, v24
	v_rndne_f32_e32 v25, v25
	v_rndne_f32_e32 v44, v44
	v_rndne_f32_e32 v45, v45
	v_rndne_f32_e32 v50, v50
	v_rndne_f32_e32 v51, v51
	v_rndne_f32_e32 v48, v48
	v_rndne_f32_e32 v49, v49
	v_rndne_f32_e32 v54, v54
	v_rndne_f32_e32 v55, v55
	v_rndne_f32_e32 v52, v52
	v_rndne_f32_e32 v53, v53
	v_rndne_f32_e32 v58, v58
	v_rndne_f32_e32 v59, v59
	v_rndne_f32_e32 v56, v56
	v_rndne_f32_e32 v57, v57
	v_rndne_f32_e32 v62, v62
	v_rndne_f32_e32 v63, v63
	v_rndne_f32_e32 v60, v60
	v_rndne_f32_e32 v61, v61
	v_rndne_f32_e32 v40, v40
	v_rndne_f32_e32 v41, v41
	v_rndne_f32_e32 v42, v42
	v_rndne_f32_e32 v43, v43
	ds_write2_b32 v31, v14, v15 offset1:1
	ds_write2_b32 v31, v16, v17 offset0:2 offset1:3
	ds_write2_b32 v32, v20, v21 offset1:1
	ds_write2_b32 v33, v46, v47 offset1:1
	ds_write2_b32 v34, v24, v25 offset1:1
	ds_write2_b32 v35, v44, v45 offset1:1
	ds_write2_b32 v36, v50, v51 offset1:1
	ds_write2_b32 v37, v48, v49 offset1:1
	ds_write2_b32 v38, v54, v55 offset1:1
	ds_write2_b32 v39, v52, v53 offset1:1
	ds_write2_b32 v87, v58, v59 offset1:1
	ds_write2_b32 v88, v56, v57 offset1:1
	ds_write2_b32 v89, v62, v63 offset1:1
	ds_write2_b32 v90, v60, v61 offset1:1
	ds_write2_b32 v91, v40, v41 offset1:1
	ds_write2_b32 v92, v42, v43 offset1:1
	s_waitcnt lgkmcnt(0)
; #define LAS __attribute__((address_space(3)))
; #define GAS __attribute__((address_space(1)))
; #define LDS_WAIT() asm volatile("s_waitcnt lgkmcnt(0)" ::: "memory")
;     ...
;         for (int i = 0; i < 8; ++i) { const int kk = 8 * i + kr; const int k = 64 * kb + kk; const f32x4 v = __builtin_nontemporal_load((const f32x4*)(W + (size_t)k * pitch)) * g[k];
;             LAS float* p = scr + kk * 33 + 4 * (lane & 7); p[0] = __builtin_rintf(v[0] * inv[0]); p[1] = __builtin_rintf(v[1] * inv[1]); p[2] = __builtin_rintf(v[2] * inv[2]); p[3] = __builtin_rintf(v[3] * inv[3]); }
;         LDS_WAIT(); asm volatile("" ::: "memory");
;         const int c = lane & 7;
; #pragma unroll
;         for (int j = 0; j < 4; ++j) { const int n = (lane >> 3) + 8 * j; const LAS float* sp = scr + (8 * c) * 33 + n;
;             u32x2 o;
;             o.x = ((unsigned)(int)sp[0 * 33] & 0xFFu) | (((unsigned)(int)sp[1 * 33] & 0xFFu) << 8) | (((unsigned)(int)sp[2 * 33] & 0xFFu) << 16) | (((unsigned)(int)sp[3 * 33] & 0xFFu) << 24);
;             o.y = ((unsigned)(int)sp[4 * 33] & 0xFFu) | (((unsigned)(int)sp[5 * 33] & 0xFFu) << 8) | (((unsigned)(int)sp[6 * 33] & 0xFFu) << 16) | (((unsigned)(int)sp[7 * 33] & 0xFFu) << 24);
;             *(GAS u32x2*)(dst + (size_t)(n0 + n) * D + 64 * kb + 8 * c) = o; }
;         LDS_WAIT(); asm volatile("" ::: "memory");
	ds_read2_b32 v[14:15], v30 offset1:8
	ds_read2_b32 v[16:17], v30 offset0:33 offset1:41
	ds_read2_b32 v[20:21], v30 offset0:66 offset1:74
	ds_read2_b32 v[24:25], v30 offset0:99 offset1:107
	ds_read2_b32 v[40:41], v30 offset0:132 offset1:140
	ds_read2_b32 v[42:43], v30 offset0:165 offset1:173
	ds_read2_b32 v[44:45], v30 offset0:198 offset1:206
	ds_read2_b32 v[46:47], v30 offset0:231 offset1:239
	ds_read2_b32 v[48:49], v30 offset0:16 offset1:24
	ds_read2_b32 v[50:51], v30 offset0:49 offset1:57
	ds_read2_b32 v[52:53], v30 offset0:82 offset1:90
	ds_read2_b32 v[54:55], v30 offset0:115 offset1:123
	ds_read2_b32 v[56:57], v30 offset0:148 offset1:156
	ds_read2_b32 v[58:59], v30 offset0:181 offset1:189
	ds_read2_b32 v[60:61], v30 offset0:214 offset1:222
	ds_read2_b32 v[62:63], v30 offset0:247 offset1:255
	s_waitcnt lgkmcnt(14)
	v_cvt_i32_f32_e32 v16, v16
	s_waitcnt lgkmcnt(10)
	v_cvt_i32_f32_e32 v42, v42
	v_cvt_i32_f32_e32 v14, v14
	v_cvt_i32_f32_sdwa v20, v20 dst_sel:WORD_1 dst_unused:UNUSED_PAD src0_sel:DWORD
	v_cvt_i32_f32_e32 v40, v40
	s_waitcnt lgkmcnt(9)
	v_cvt_i32_f32_sdwa v44, v44 dst_sel:WORD_1 dst_unused:UNUSED_PAD src0_sel:DWORD
	v_cvt_i32_f32_e32 v17, v17
	v_cvt_i32_f32_e32 v43, v43
	s_waitcnt lgkmcnt(6)
	v_cvt_i32_f32_e32 v50, v50
	s_waitcnt lgkmcnt(2)
	v_cvt_i32_f32_e32 v58, v58
	v_cvt_i32_f32_e32 v51, v51
	v_cvt_i32_f32_e32 v59, v59
	v_cvt_i32_f32_sdwa v24, v24 dst_sel:BYTE_3 dst_unused:UNUSED_PAD src0_sel:DWORD
	v_cvt_i32_f32_sdwa v46, v46 dst_sel:BYTE_3 dst_unused:UNUSED_PAD src0_sel:DWORD
	v_cvt_i32_f32_e32 v15, v15
	v_cvt_i32_f32_sdwa v21, v21 dst_sel:WORD_1 dst_unused:UNUSED_PAD src0_sel:DWORD
	v_cvt_i32_f32_e32 v41, v41
	v_cvt_i32_f32_sdwa v45, v45 dst_sel:WORD_1 dst_unused:UNUSED_PAD src0_sel:DWORD
	v_cvt_i32_f32_e32 v48, v48
	v_cvt_i32_f32_sdwa v52, v52 dst_sel:WORD_1 dst_unused:UNUSED_PAD src0_sel:DWORD
	v_cvt_i32_f32_e32 v56, v56
	s_waitcnt lgkmcnt(1)
	v_cvt_i32_f32_sdwa v60, v60 dst_sel:WORD_1 dst_unused:UNUSED_PAD src0_sel:DWORD
	v_cvt_i32_f32_e32 v49, v49
	v_cvt_i32_f32_sdwa v53, v53 dst_sel:WORD_1 dst_unused:UNUSED_PAD src0_sel:DWORD
	v_cvt_i32_f32_e32 v57, v57
	v_cvt_i32_f32_sdwa v61, v61 dst_sel:WORD_1 dst_unused:UNUSED_PAD src0_sel:DWORD
	v_cvt_i32_f32_sdwa v25, v25 dst_sel:BYTE_3 dst_unused:UNUSED_PAD src0_sel:DWORD
	v_cvt_i32_f32_sdwa v47, v47 dst_sel:BYTE_3 dst_unused:UNUSED_PAD src0_sel:DWORD
	v_cvt_i32_f32_sdwa v54, v54 dst_sel:BYTE_3 dst_unused:UNUSED_PAD src0_sel:DWORD
	s_waitcnt lgkmcnt(0)
	v_cvt_i32_f32_sdwa v62, v62 dst_sel:BYTE_3 dst_unused:UNUSED_PAD src0_sel:DWORD
	v_cvt_i32_f32_sdwa v55, v55 dst_sel:BYTE_3 dst_unused:UNUSED_PAD src0_sel:DWORD
	v_cvt_i32_f32_sdwa v63, v63 dst_sel:BYTE_3 dst_unused:UNUSED_PAD src0_sel:DWORD
	v_lshlrev_b32_e32 v16, 8, v16
	v_lshlrev_b32_e32 v42, 8, v42
	v_and_b32_e32 v20, 0xff0000, v20
	v_and_b32_e32 v44, 0xff0000, v44
	v_lshlrev_b32_e32 v17, 8, v17
	v_lshlrev_b32_e32 v43, 8, v43
	v_lshlrev_b32_e32 v50, 8, v50
	v_lshlrev_b32_e32 v58, 8, v58
	v_lshlrev_b32_e32 v51, 8, v51
	v_lshlrev_b32_e32 v59, 8, v59
	v_perm_b32 v14, v16, v14, s28
	v_perm_b32 v16, v42, v40, s28
	v_and_b32_e32 v21, 0xff0000, v21
	v_and_b32_e32 v45, 0xff0000, v45
	v_and_b32_e32 v52, 0xff0000, v52
	v_and_b32_e32 v60, 0xff0000, v60
	v_and_b32_e32 v53, 0xff0000, v53
	v_and_b32_e32 v61, 0xff0000, v61
	v_perm_b32 v17, v17, v15, s28
	v_perm_b32 v40, v43, v41, s28
	v_perm_b32 v41, v50, v48, s28
	v_perm_b32 v42, v58, v56, s28
	v_perm_b32 v43, v51, v49, s28
	v_perm_b32 v48, v59, v57, s28
	v_or3_b32 v14, v14, v20, v24
	v_or3_b32 v15, v16, v44, v46
	v_or3_b32 v16, v17, v21, v25
	v_or3_b32 v17, v40, v45, v47
	v_or3_b32 v20, v41, v52, v54
	v_or3_b32 v21, v42, v60, v62
	v_or3_b32 v24, v43, v53, v55
	v_or3_b32 v25, v48, v61, v63
	global_store_dwordx2 v[18:19], v[14:15], off
	global_store_dwordx2 v[22:23], v[16:17], off
	global_store_dwordx2 v[82:83], v[20:21], off
	global_store_dwordx2 v[84:85], v[24:25], off
	s_waitcnt lgkmcnt(0)
	v_add_u32_e32 v87, 0x14a0, v31
	v_add_u32_e32 v88, 0x14a8, v31
	v_add_u32_e32 v89, 0x18c0, v31
	v_add_u32_e32 v90, 0x18c8, v31
	v_add_u32_e32 v91, 0x1ce0, v31
	v_add_u32_e32 v92, 0x1ce8, v31
	v_lshl_add_u64 v[18:19], v[6:7], 0, v[12:13]
	v_lshl_add_u64 v[22:23], v[6:7], 0, v[10:11]
	v_lshl_add_u64 v[82:83], v[6:7], 0, v[8:9]
	v_lshl_add_u64 v[84:85], v[6:7], 0, v[4:5]
	v_lshl_add_u64 v[6:7], v[6:7], 0, 64
	s_waitcnt vmcnt(40)
; #define LAS __attribute__((address_space(3)))
; #define GAS __attribute__((address_space(1)))
; #define LDS_WAIT() asm volatile("s_waitcnt lgkmcnt(0)" ::: "memory")
;     ...
;     for (int kb = 0; kb < D / 64; ++kb) {
; #pragma unroll
;         for (int i = 0; i < 8; ++i) { const int kk = 8 * i + kr; const int k = 64 * kb + kk; const f32x4 v = __builtin_nontemporal_load((const f32x4*)(W + (size_t)k * pitch)) * g[k];
;             LAS float* p = scr + kk * 33 + 4 * (lane & 7); p[0] = __builtin_rintf(v[0] * inv[0]); p[1] = __builtin_rintf(v[1] * inv[1]); p[2] = __builtin_rintf(v[2] * inv[2]); p[3] = __builtin_rintf(v[3] * inv[3]); }
;         LDS_WAIT(); asm volatile("" ::: "memory");
;         const int c = lane & 7;
; #pragma unroll
;         for (int j = 0; j < 4; ++j) { const int n = (lane >> 3) + 8 * j; const LAS float* sp = scr + (8 * c) * 33 + n;
;             u32x2 o;
;             o.x = ((unsigned)(int)sp[0 * 33] & 0xFFu) | (((unsigned)(int)sp[1 * 33] & 0xFFu) << 8) | (((unsigned)(int)sp[2 * 33] & 0xFFu) << 16) | (((unsigned)(int)sp[3 * 33] & 0xFFu) << 24);
;             o.y = ((unsigned)(int)sp[4 * 33] & 0xFFu) | (((unsigned)(int)sp[5 * 33] & 0xFFu) << 8) | (((unsigned)(int)sp[6 * 33] & 0xFFu) << 16) | (((unsigned)(int)sp[7 * 33] & 0xFFu) << 24);
;             *(GAS u32x2*)(dst + (size_t)(n0 + n) * D + 64 * kb + 8 * c) = o; }
;         LDS_WAIT(); asm volatile("" ::: "memory");
	v_pk_mul_f32 v[46:47], v[176:177], v[236:237] op_sel_hi:[1,0]
	v_pk_mul_f32 v[20:21], v[174:175], v[236:237] op_sel_hi:[1,0]
	v_pk_mul_f32 v[44:45], v[180:181], v[238:239] op_sel_hi:[1,0]
	v_pk_mul_f32 v[24:25], v[178:179], v[238:239] op_sel_hi:[1,0]
	v_pk_mul_f32 v[48:49], v[184:185], v[240:241] op_sel_hi:[1,0]
	v_pk_mul_f32 v[16:17], v[172:173], v[234:235] op_sel_hi:[1,0]
	v_pk_mul_f32 v[14:15], v[170:171], v[234:235] op_sel_hi:[1,0]
	v_pk_mul_f32 v[50:51], v[182:183], v[240:241] op_sel_hi:[1,0]
	v_pk_mul_f32 v[52:53], v[188:189], v[242:243] op_sel_hi:[1,0]
	v_pk_mul_f32 v[54:55], v[186:187], v[242:243] op_sel_hi:[1,0]
	v_pk_mul_f32 v[56:57], v[192:193], v[244:245] op_sel_hi:[1,0]
	v_pk_mul_f32 v[58:59], v[190:191], v[244:245] op_sel_hi:[1,0]
	v_pk_mul_f32 v[60:61], v[196:197], v[246:247] op_sel_hi:[1,0]
	v_pk_mul_f32 v[62:63], v[194:195], v[246:247] op_sel_hi:[1,0]
	v_pk_mul_f32 v[42:43], v[200:201], v[248:249] op_sel_hi:[1,0]
	v_pk_mul_f32 v[40:41], v[198:199], v[248:249] op_sel_hi:[1,0]
	s_add_u32 s4, s4, 0x18000
	s_addc_u32 s5, s5, 0
	global_load_dwordx4 v[170:173], v250, s[4:5] nt
	global_load_dword v234, v251, s[6:7] offset:1280
	s_add_u32 s4, s4, 0x18000
	s_addc_u32 s5, s5, 0
	global_load_dwordx4 v[174:177], v250, s[4:5] nt
	global_load_dword v236, v251, s[6:7] offset:1312
	s_add_u32 s4, s4, 0x18000
	s_addc_u32 s5, s5, 0
	global_load_dwordx4 v[178:181], v250, s[4:5] nt
	global_load_dword v238, v251, s[6:7] offset:1344
	s_add_u32 s4, s4, 0x18000
	s_addc_u32 s5, s5, 0
	global_load_dwordx4 v[182:185], v250, s[4:5] nt
	global_load_dword v240, v251, s[6:7] offset:1376
	s_add_u32 s4, s4, 0x18000
	s_addc_u32 s5, s5, 0
	global_load_dwordx4 v[186:189], v250, s[4:5] nt
	global_load_dword v242, v251, s[6:7] offset:1408
	s_add_u32 s4, s4, 0x18000
	s_addc_u32 s5, s5, 0
	global_load_dwordx4 v[190:193], v250, s[4:5] nt
	global_load_dword v244, v251, s[6:7] offset:1440
	s_add_u32 s4, s4, 0x18000
	s_addc_u32 s5, s5, 0
	global_load_dwordx4 v[194:197], v250, s[4:5] nt
	global_load_dword v246, v251, s[6:7] offset:1472
	s_add_u32 s4, s4, 0x18000
	s_addc_u32 s5, s5, 0
	global_load_dwordx4 v[198:201], v250, s[4:5] nt
	global_load_dword v248, v251, s[6:7] offset:1504
	v_mul_f32_e32 v14, v26, v14
	v_mul_f32_e32 v15, v27, v15
	v_mul_f32_e32 v16, v28, v16
	v_mul_f32_e32 v17, v29, v17
	v_mul_f32_e32 v20, v26, v20
	v_mul_f32_e32 v21, v27, v21
	v_mul_f32_e32 v46, v28, v46
	v_mul_f32_e32 v47, v29, v47
	v_mul_f32_e32 v24, v26, v24
	v_mul_f32_e32 v25, v27, v25
	v_mul_f32_e32 v44, v28, v44
	v_mul_f32_e32 v45, v29, v45
	v_mul_f32_e32 v50, v26, v50
	v_mul_f32_e32 v51, v27, v51
	v_mul_f32_e32 v48, v28, v48
	v_mul_f32_e32 v49, v29, v49
	v_mul_f32_e32 v54, v26, v54
	v_mul_f32_e32 v55, v27, v55
	v_mul_f32_e32 v52, v28, v52
	v_mul_f32_e32 v53, v29, v53
	v_mul_f32_e32 v58, v26, v58
	v_mul_f32_e32 v59, v27, v59
	v_mul_f32_e32 v56, v28, v56
	v_mul_f32_e32 v57, v29, v57
	v_mul_f32_e32 v62, v26, v62
	v_mul_f32_e32 v63, v27, v63
	v_mul_f32_e32 v60, v28, v60
	v_mul_f32_e32 v61, v29, v61
	v_mul_f32_e32 v40, v26, v40
	v_mul_f32_e32 v41, v27, v41
	v_mul_f32_e32 v42, v28, v42
	v_mul_f32_e32 v43, v29, v43
	v_rndne_f32_e32 v14, v14
	v_rndne_f32_e32 v15, v15
	v_rndne_f32_e32 v16, v16
	v_rndne_f32_e32 v17, v17
	v_rndne_f32_e32 v20, v20
	v_rndne_f32_e32 v21, v21
	v_rndne_f32_e32 v46, v46
	v_rndne_f32_e32 v47, v47
	v_rndne_f32_e32 v24, v24
	v_rndne_f32_e32 v25, v25
	v_rndne_f32_e32 v44, v44
	v_rndne_f32_e32 v45, v45
	v_rndne_f32_e32 v50, v50
	v_rndne_f32_e32 v51, v51
	v_rndne_f32_e32 v48, v48
	v_rndne_f32_e32 v49, v49
	v_rndne_f32_e32 v54, v54
	v_rndne_f32_e32 v55, v55
	v_rndne_f32_e32 v52, v52
	v_rndne_f32_e32 v53, v53
	v_rndne_f32_e32 v58, v58
	v_rndne_f32_e32 v59, v59
	v_rndne_f32_e32 v56, v56
	v_rndne_f32_e32 v57, v57
	v_rndne_f32_e32 v62, v62
	v_rndne_f32_e32 v63, v63
	v_rndne_f32_e32 v60, v60
	v_rndne_f32_e32 v61, v61
	v_rndne_f32_e32 v40, v40
	v_rndne_f32_e32 v41, v41
	v_rndne_f32_e32 v42, v42
	v_rndne_f32_e32 v43, v43
	ds_write2_b32 v31, v14, v15 offset1:1
	ds_write2_b32 v31, v16, v17 offset0:2 offset1:3
	ds_write2_b32 v32, v20, v21 offset1:1
	ds_write2_b32 v33, v46, v47 offset1:1
	ds_write2_b32 v34, v24, v25 offset1:1
	ds_write2_b32 v35, v44, v45 offset1:1
	ds_write2_b32 v36, v50, v51 offset1:1
	ds_write2_b32 v37, v48, v49 offset1:1
	ds_write2_b32 v38, v54, v55 offset1:1
	ds_write2_b32 v39, v52, v53 offset1:1
	ds_write2_b32 v87, v58, v59 offset1:1
	ds_write2_b32 v88, v56, v57 offset1:1
	ds_write2_b32 v89, v62, v63 offset1:1
	ds_write2_b32 v90, v60, v61 offset1:1
	ds_write2_b32 v91, v40, v41 offset1:1
	ds_write2_b32 v92, v42, v43 offset1:1
	s_waitcnt lgkmcnt(0)
	ds_read2_b32 v[14:15], v30 offset1:8
	ds_read2_b32 v[16:17], v30 offset0:33 offset1:41
	ds_read2_b32 v[20:21], v30 offset0:66 offset1:74
	ds_read2_b32 v[24:25], v30 offset0:99 offset1:107
	ds_read2_b32 v[40:41], v30 offset0:132 offset1:140
	ds_read2_b32 v[42:43], v30 offset0:165 offset1:173
	ds_read2_b32 v[44:45], v30 offset0:198 offset1:206
	ds_read2_b32 v[46:47], v30 offset0:231 offset1:239
	ds_read2_b32 v[48:49], v30 offset0:16 offset1:24
	ds_read2_b32 v[50:51], v30 offset0:49 offset1:57
	ds_read2_b32 v[52:53], v30 offset0:82 offset1:90
	ds_read2_b32 v[54:55], v30 offset0:115 offset1:123
	ds_read2_b32 v[56:57], v30 offset0:148 offset1:156
	ds_read2_b32 v[58:59], v30 offset0:181 offset1:189
	ds_read2_b32 v[60:61], v30 offset0:214 offset1:222
	ds_read2_b32 v[62:63], v30 offset0:247 offset1:255
	s_waitcnt lgkmcnt(14)
	v_cvt_i32_f32_e32 v16, v16
	s_waitcnt lgkmcnt(10)
	v_cvt_i32_f32_e32 v42, v42
	v_cvt_i32_f32_e32 v14, v14
	v_cvt_i32_f32_sdwa v20, v20 dst_sel:WORD_1 dst_unused:UNUSED_PAD src0_sel:DWORD
	v_cvt_i32_f32_e32 v40, v40
	s_waitcnt lgkmcnt(9)
; #define LAS __attribute__((address_space(3)))
; #define GAS __attribute__((address_space(1)))
; #define LDS_WAIT() asm volatile("s_waitcnt lgkmcnt(0)" ::: "memory")
;     ...
;     for (int kb = 0; kb < D / 64; ++kb) {
; #pragma unroll
;         for (int i = 0; i < 8; ++i) { const int kk = 8 * i + kr; const int k = 64 * kb + kk; const f32x4 v = __builtin_nontemporal_load((const f32x4*)(W + (size_t)k * pitch)) * g[k];
;             LAS float* p = scr + kk * 33 + 4 * (lane & 7); p[0] = __builtin_rintf(v[0] * inv[0]); p[1] = __builtin_rintf(v[1] * inv[1]); p[2] = __builtin_rintf(v[2] * inv[2]); p[3] = __builtin_rintf(v[3] * inv[3]); }
;         LDS_WAIT(); asm volatile("" ::: "memory");
;         const int c = lane & 7;
; #pragma unroll
;         for (int j = 0; j < 4; ++j) { const int n = (lane >> 3) + 8 * j; const LAS float* sp = scr + (8 * c) * 33 + n;
;             u32x2 o;
;             o.x = ((unsigned)(int)sp[0 * 33] & 0xFFu) | (((unsigned)(int)sp[1 * 33] & 0xFFu) << 8) | (((unsigned)(int)sp[2 * 33] & 0xFFu) << 16) | (((unsigned)(int)sp[3 * 33] & 0xFFu) << 24);
;             o.y = ((unsigned)(int)sp[4 * 33] & 0xFFu) | (((unsigned)(int)sp[5 * 33] & 0xFFu) << 8) | (((unsigned)(int)sp[6 * 33] & 0xFFu) << 16) | (((unsigned)(int)sp[7 * 33] & 0xFFu) << 24);
;             *(GAS u32x2*)(dst + (size_t)(n0 + n) * D + 64 * kb + 8 * c) = o; }
;         LDS_WAIT(); asm volatile("" ::: "memory");
	v_cvt_i32_f32_sdwa v44, v44 dst_sel:WORD_1 dst_unused:UNUSED_PAD src0_sel:DWORD
	v_cvt_i32_f32_e32 v17, v17
	v_cvt_i32_f32_e32 v43, v43
	s_waitcnt lgkmcnt(6)
	v_cvt_i32_f32_e32 v50, v50
	s_waitcnt lgkmcnt(2)
	v_cvt_i32_f32_e32 v58, v58
	v_cvt_i32_f32_e32 v51, v51
	v_cvt_i32_f32_e32 v59, v59
	v_cvt_i32_f32_sdwa v24, v24 dst_sel:BYTE_3 dst_unused:UNUSED_PAD src0_sel:DWORD
	v_cvt_i32_f32_sdwa v46, v46 dst_sel:BYTE_3 dst_unused:UNUSED_PAD src0_sel:DWORD
	v_cvt_i32_f32_e32 v15, v15
	v_cvt_i32_f32_sdwa v21, v21 dst_sel:WORD_1 dst_unused:UNUSED_PAD src0_sel:DWORD
	v_cvt_i32_f32_e32 v41, v41
	v_cvt_i32_f32_sdwa v45, v45 dst_sel:WORD_1 dst_unused:UNUSED_PAD src0_sel:DWORD
	v_cvt_i32_f32_e32 v48, v48
	v_cvt_i32_f32_sdwa v52, v52 dst_sel:WORD_1 dst_unused:UNUSED_PAD src0_sel:DWORD
	v_cvt_i32_f32_e32 v56, v56
	s_waitcnt lgkmcnt(1)
	v_cvt_i32_f32_sdwa v60, v60 dst_sel:WORD_1 dst_unused:UNUSED_PAD src0_sel:DWORD
	v_cvt_i32_f32_e32 v49, v49
	v_cvt_i32_f32_sdwa v53, v53 dst_sel:WORD_1 dst_unused:UNUSED_PAD src0_sel:DWORD
	v_cvt_i32_f32_e32 v57, v57
	v_cvt_i32_f32_sdwa v61, v61 dst_sel:WORD_1 dst_unused:UNUSED_PAD src0_sel:DWORD
	v_cvt_i32_f32_sdwa v25, v25 dst_sel:BYTE_3 dst_unused:UNUSED_PAD src0_sel:DWORD
	v_cvt_i32_f32_sdwa v47, v47 dst_sel:BYTE_3 dst_unused:UNUSED_PAD src0_sel:DWORD
	v_cvt_i32_f32_sdwa v54, v54 dst_sel:BYTE_3 dst_unused:UNUSED_PAD src0_sel:DWORD
	s_waitcnt lgkmcnt(0)
	v_cvt_i32_f32_sdwa v62, v62 dst_sel:BYTE_3 dst_unused:UNUSED_PAD src0_sel:DWORD
	v_cvt_i32_f32_sdwa v55, v55 dst_sel:BYTE_3 dst_unused:UNUSED_PAD src0_sel:DWORD
	v_cvt_i32_f32_sdwa v63, v63 dst_sel:BYTE_3 dst_unused:UNUSED_PAD src0_sel:DWORD
	v_lshlrev_b32_e32 v16, 8, v16
	v_lshlrev_b32_e32 v42, 8, v42
	v_and_b32_e32 v20, 0xff0000, v20
	v_and_b32_e32 v44, 0xff0000, v44
	v_lshlrev_b32_e32 v17, 8, v17
	v_lshlrev_b32_e32 v43, 8, v43
	v_lshlrev_b32_e32 v50, 8, v50
	v_lshlrev_b32_e32 v58, 8, v58
	v_lshlrev_b32_e32 v51, 8, v51
	v_lshlrev_b32_e32 v59, 8, v59
	v_perm_b32 v14, v16, v14, s28
	v_perm_b32 v16, v42, v40, s28
	v_and_b32_e32 v21, 0xff0000, v21
	v_and_b32_e32 v45, 0xff0000, v45
	v_and_b32_e32 v52, 0xff0000, v52
	v_and_b32_e32 v60, 0xff0000, v60
	v_and_b32_e32 v53, 0xff0000, v53
	v_and_b32_e32 v61, 0xff0000, v61
	v_perm_b32 v17, v17, v15, s28
	v_perm_b32 v40, v43, v41, s28
	v_perm_b32 v41, v50, v48, s28
	v_perm_b32 v42, v58, v56, s28
	v_perm_b32 v43, v51, v49, s28
	v_perm_b32 v48, v59, v57, s28
	v_or3_b32 v14, v14, v20, v24
	v_or3_b32 v15, v16, v44, v46
	v_or3_b32 v16, v17, v21, v25
	v_or3_b32 v17, v40, v45, v47
	v_or3_b32 v20, v41, v52, v54
	v_or3_b32 v21, v42, v60, v62
	v_or3_b32 v24, v43, v53, v55
	v_or3_b32 v25, v48, v61, v63
	global_store_dwordx2 v[18:19], v[14:15], off
	global_store_dwordx2 v[22:23], v[16:17], off
	global_store_dwordx2 v[82:83], v[20:21], off
	global_store_dwordx2 v[84:85], v[24:25], off
	s_waitcnt lgkmcnt(0)
	v_add_u32_e32 v87, 0x14a0, v31
	v_add_u32_e32 v88, 0x14a8, v31
	v_add_u32_e32 v89, 0x18c0, v31
	v_add_u32_e32 v90, 0x18c8, v31
	v_add_u32_e32 v91, 0x1ce0, v31
	v_add_u32_e32 v92, 0x1ce8, v31
	v_lshl_add_u64 v[18:19], v[6:7], 0, v[12:13]
	v_lshl_add_u64 v[22:23], v[6:7], 0, v[10:11]
	v_lshl_add_u64 v[82:83], v[6:7], 0, v[8:9]
	v_lshl_add_u64 v[84:85], v[6:7], 0, v[4:5]
	v_lshl_add_u64 v[6:7], v[6:7], 0, 64
	s_waitcnt vmcnt(44)
	v_pk_mul_f32 v[46:47], v[112:113], v[204:205] op_sel_hi:[1,0]
	v_pk_mul_f32 v[20:21], v[110:111], v[204:205] op_sel_hi:[1,0]
	v_pk_mul_f32 v[44:45], v[116:117], v[206:207] op_sel_hi:[1,0]
	v_pk_mul_f32 v[24:25], v[114:115], v[206:207] op_sel_hi:[1,0]
	v_pk_mul_f32 v[48:49], v[120:121], v[208:209] op_sel_hi:[1,0]
	v_pk_mul_f32 v[16:17], v[108:109], v[202:203] op_sel_hi:[1,0]
	v_pk_mul_f32 v[14:15], v[106:107], v[202:203] op_sel_hi:[1,0]
	v_pk_mul_f32 v[50:51], v[118:119], v[208:209] op_sel_hi:[1,0]
	v_pk_mul_f32 v[52:53], v[124:125], v[210:211] op_sel_hi:[1,0]
	v_pk_mul_f32 v[54:55], v[122:123], v[210:211] op_sel_hi:[1,0]
	v_pk_mul_f32 v[56:57], v[128:129], v[212:213] op_sel_hi:[1,0]
	v_pk_mul_f32 v[58:59], v[126:127], v[212:213] op_sel_hi:[1,0]
	v_pk_mul_f32 v[60:61], v[132:133], v[214:215] op_sel_hi:[1,0]
	v_pk_mul_f32 v[62:63], v[130:131], v[214:215] op_sel_hi:[1,0]
	v_pk_mul_f32 v[42:43], v[136:137], v[216:217] op_sel_hi:[1,0]
	v_pk_mul_f32 v[40:41], v[134:135], v[216:217] op_sel_hi:[1,0]
	s_add_u32 s4, s4, 0x18000
	s_addc_u32 s5, s5, 0
	global_load_dwordx4 v[106:109], v250, s[4:5] nt
	global_load_dword v202, v251, s[6:7] offset:1536
	s_add_u32 s4, s4, 0x18000
	s_addc_u32 s5, s5, 0
	global_load_dwordx4 v[110:113], v250, s[4:5] nt
	global_load_dword v204, v251, s[6:7] offset:1568
	s_add_u32 s4, s4, 0x18000
	s_addc_u32 s5, s5, 0
	global_load_dwordx4 v[114:117], v250, s[4:5] nt
	global_load_dword v206, v251, s[6:7] offset:1600
	s_add_u32 s4, s4, 0x18000
	s_addc_u32 s5, s5, 0
	global_load_dwordx4 v[118:121], v250, s[4:5] nt
	global_load_dword v208, v251, s[6:7] offset:1632
	s_add_u32 s4, s4, 0x18000
	s_addc_u32 s5, s5, 0
	global_load_dwordx4 v[122:125], v250, s[4:5] nt
	global_load_dword v210, v251, s[6:7] offset:1664
	s_add_u32 s4, s4, 0x18000
	s_addc_u32 s5, s5, 0
	global_load_dwordx4 v[126:129], v250, s[4:5] nt
	global_load_dword v212, v251, s[6:7] offset:1696
	s_add_u32 s4, s4, 0x18000
	s_addc_u32 s5, s5, 0
	global_load_dwordx4 v[130:133], v250, s[4:5] nt
	global_load_dword v214, v251, s[6:7] offset:1728
	s_add_u32 s4, s4, 0x18000
	s_addc_u32 s5, s5, 0
	global_load_dwordx4 v[134:137], v250, s[4:5] nt
	global_load_dword v216, v251, s[6:7] offset:1760
	v_mul_f32_e32 v14, v26, v14
	v_mul_f32_e32 v15, v27, v15
	v_mul_f32_e32 v16, v28, v16
	v_mul_f32_e32 v17, v29, v17
	v_mul_f32_e32 v20, v26, v20
	v_mul_f32_e32 v21, v27, v21
; #define LAS __attribute__((address_space(3)))
; #define GAS __attribute__((address_space(1)))
; #define LDS_WAIT() asm volatile("s_waitcnt lgkmcnt(0)" ::: "memory")
;     ...
;         for (int i = 0; i < 8; ++i) { const int kk = 8 * i + kr; const int k = 64 * kb + kk; const f32x4 v = __builtin_nontemporal_load((const f32x4*)(W + (size_t)k * pitch)) * g[k];
;             LAS float* p = scr + kk * 33 + 4 * (lane & 7); p[0] = __builtin_rintf(v[0] * inv[0]); p[1] = __builtin_rintf(v[1] * inv[1]); p[2] = __builtin_rintf(v[2] * inv[2]); p[3] = __builtin_rintf(v[3] * inv[3]); }
;         LDS_WAIT(); asm volatile("" ::: "memory");
;         const int c = lane & 7;
; #pragma unroll
;         for (int j = 0; j < 4; ++j) { const int n = (lane >> 3) + 8 * j; const LAS float* sp = scr + (8 * c) * 33 + n;
;             u32x2 o;
;             o.x = ((unsigned)(int)sp[0 * 33] & 0xFFu) | (((unsigned)(int)sp[1 * 33] & 0xFFu) << 8) | (((unsigned)(int)sp[2 * 33] & 0xFFu) << 16) | (((unsigned)(int)sp[3 * 33] & 0xFFu) << 24);
;             o.y = ((unsigned)(int)sp[4 * 33] & 0xFFu) | (((unsigned)(int)sp[5 * 33] & 0xFFu) << 8) | (((unsigned)(int)sp[6 * 33] & 0xFFu) << 16) | (((unsigned)(int)sp[7 * 33] & 0xFFu) << 24);
;             *(GAS u32x2*)(dst + (size_t)(n0 + n) * D + 64 * kb + 8 * c) = o; }
;         LDS_WAIT(); asm volatile("" ::: "memory");
	v_mul_f32_e32 v46, v28, v46
	v_mul_f32_e32 v47, v29, v47
	v_mul_f32_e32 v24, v26, v24
	v_mul_f32_e32 v25, v27, v25
	v_mul_f32_e32 v44, v28, v44
	v_mul_f32_e32 v45, v29, v45
	v_mul_f32_e32 v50, v26, v50
	v_mul_f32_e32 v51, v27, v51
	v_mul_f32_e32 v48, v28, v48
	v_mul_f32_e32 v49, v29, v49
	v_mul_f32_e32 v54, v26, v54
	v_mul_f32_e32 v55, v27, v55
	v_mul_f32_e32 v52, v28, v52
	v_mul_f32_e32 v53, v29, v53
	v_mul_f32_e32 v58, v26, v58
	v_mul_f32_e32 v59, v27, v59
	v_mul_f32_e32 v56, v28, v56
	v_mul_f32_e32 v57, v29, v57
	v_mul_f32_e32 v62, v26, v62
	v_mul_f32_e32 v63, v27, v63
	v_mul_f32_e32 v60, v28, v60
	v_mul_f32_e32 v61, v29, v61
	v_mul_f32_e32 v40, v26, v40
	v_mul_f32_e32 v41, v27, v41
	v_mul_f32_e32 v42, v28, v42
	v_mul_f32_e32 v43, v29, v43
	v_rndne_f32_e32 v14, v14
	v_rndne_f32_e32 v15, v15
	v_rndne_f32_e32 v16, v16
	v_rndne_f32_e32 v17, v17
	v_rndne_f32_e32 v20, v20
	v_rndne_f32_e32 v21, v21
	v_rndne_f32_e32 v46, v46
	v_rndne_f32_e32 v47, v47
	v_rndne_f32_e32 v24, v24
	v_rndne_f32_e32 v25, v25
	v_rndne_f32_e32 v44, v44
	v_rndne_f32_e32 v45, v45
	v_rndne_f32_e32 v50, v50
	v_rndne_f32_e32 v51, v51
	v_rndne_f32_e32 v48, v48
	v_rndne_f32_e32 v49, v49
	v_rndne_f32_e32 v54, v54
	v_rndne_f32_e32 v55, v55
	v_rndne_f32_e32 v52, v52
	v_rndne_f32_e32 v53, v53
	v_rndne_f32_e32 v58, v58
	v_rndne_f32_e32 v59, v59
	v_rndne_f32_e32 v56, v56
	v_rndne_f32_e32 v57, v57
	v_rndne_f32_e32 v62, v62
	v_rndne_f32_e32 v63, v63
	v_rndne_f32_e32 v60, v60
	v_rndne_f32_e32 v61, v61
	v_rndne_f32_e32 v40, v40
	v_rndne_f32_e32 v41, v41
	v_rndne_f32_e32 v42, v42
	v_rndne_f32_e32 v43, v43
	ds_write2_b32 v31, v14, v15 offset1:1
	ds_write2_b32 v31, v16, v17 offset0:2 offset1:3
	ds_write2_b32 v32, v20, v21 offset1:1
	ds_write2_b32 v33, v46, v47 offset1:1
	ds_write2_b32 v34, v24, v25 offset1:1
	ds_write2_b32 v35, v44, v45 offset1:1
	ds_write2_b32 v36, v50, v51 offset1:1
	ds_write2_b32 v37, v48, v49 offset1:1
	ds_write2_b32 v38, v54, v55 offset1:1
	ds_write2_b32 v39, v52, v53 offset1:1
	ds_write2_b32 v87, v58, v59 offset1:1
	ds_write2_b32 v88, v56, v57 offset1:1
	ds_write2_b32 v89, v62, v63 offset1:1
	ds_write2_b32 v90, v60, v61 offset1:1
	ds_write2_b32 v91, v40, v41 offset1:1
	ds_write2_b32 v92, v42, v43 offset1:1
	s_waitcnt lgkmcnt(0)
	ds_read2_b32 v[14:15], v30 offset1:8
	ds_read2_b32 v[16:17], v30 offset0:33 offset1:41
	ds_read2_b32 v[20:21], v30 offset0:66 offset1:74
	ds_read2_b32 v[24:25], v30 offset0:99 offset1:107
	ds_read2_b32 v[40:41], v30 offset0:132 offset1:140
	ds_read2_b32 v[42:43], v30 offset0:165 offset1:173
	ds_read2_b32 v[44:45], v30 offset0:198 offset1:206
	ds_read2_b32 v[46:47], v30 offset0:231 offset1:239
	ds_read2_b32 v[48:49], v30 offset0:16 offset1:24
	ds_read2_b32 v[50:51], v30 offset0:49 offset1:57
	ds_read2_b32 v[52:53], v30 offset0:82 offset1:90
	ds_read2_b32 v[54:55], v30 offset0:115 offset1:123
	ds_read2_b32 v[56:57], v30 offset0:148 offset1:156
	ds_read2_b32 v[58:59], v30 offset0:181 offset1:189
	ds_read2_b32 v[60:61], v30 offset0:214 offset1:222
	ds_read2_b32 v[62:63], v30 offset0:247 offset1:255
	s_waitcnt lgkmcnt(14)
	v_cvt_i32_f32_e32 v16, v16
	s_waitcnt lgkmcnt(10)
	v_cvt_i32_f32_e32 v42, v42
	v_cvt_i32_f32_e32 v14, v14
	v_cvt_i32_f32_sdwa v20, v20 dst_sel:WORD_1 dst_unused:UNUSED_PAD src0_sel:DWORD
	v_cvt_i32_f32_e32 v40, v40
	s_waitcnt lgkmcnt(9)
	v_cvt_i32_f32_sdwa v44, v44 dst_sel:WORD_1 dst_unused:UNUSED_PAD src0_sel:DWORD
	v_cvt_i32_f32_e32 v17, v17
	v_cvt_i32_f32_e32 v43, v43
	s_waitcnt lgkmcnt(6)
	v_cvt_i32_f32_e32 v50, v50
	s_waitcnt lgkmcnt(2)
	v_cvt_i32_f32_e32 v58, v58
	v_cvt_i32_f32_e32 v51, v51
	v_cvt_i32_f32_e32 v59, v59
	v_cvt_i32_f32_sdwa v24, v24 dst_sel:BYTE_3 dst_unused:UNUSED_PAD src0_sel:DWORD
	v_cvt_i32_f32_sdwa v46, v46 dst_sel:BYTE_3 dst_unused:UNUSED_PAD src0_sel:DWORD
	v_cvt_i32_f32_e32 v15, v15
	v_cvt_i32_f32_sdwa v21, v21 dst_sel:WORD_1 dst_unused:UNUSED_PAD src0_sel:DWORD
	v_cvt_i32_f32_e32 v41, v41
	v_cvt_i32_f32_sdwa v45, v45 dst_sel:WORD_1 dst_unused:UNUSED_PAD src0_sel:DWORD
	v_cvt_i32_f32_e32 v48, v48
	v_cvt_i32_f32_sdwa v52, v52 dst_sel:WORD_1 dst_unused:UNUSED_PAD src0_sel:DWORD
	v_cvt_i32_f32_e32 v56, v56
	s_waitcnt lgkmcnt(1)
	v_cvt_i32_f32_sdwa v60, v60 dst_sel:WORD_1 dst_unused:UNUSED_PAD src0_sel:DWORD
	v_cvt_i32_f32_e32 v49, v49
	v_cvt_i32_f32_sdwa v53, v53 dst_sel:WORD_1 dst_unused:UNUSED_PAD src0_sel:DWORD
	v_cvt_i32_f32_e32 v57, v57
	v_cvt_i32_f32_sdwa v61, v61 dst_sel:WORD_1 dst_unused:UNUSED_PAD src0_sel:DWORD
	v_cvt_i32_f32_sdwa v25, v25 dst_sel:BYTE_3 dst_unused:UNUSED_PAD src0_sel:DWORD
	v_cvt_i32_f32_sdwa v47, v47 dst_sel:BYTE_3 dst_unused:UNUSED_PAD src0_sel:DWORD
	v_cvt_i32_f32_sdwa v54, v54 dst_sel:BYTE_3 dst_unused:UNUSED_PAD src0_sel:DWORD
	s_waitcnt lgkmcnt(0)
	v_cvt_i32_f32_sdwa v62, v62 dst_sel:BYTE_3 dst_unused:UNUSED_PAD src0_sel:DWORD
	v_cvt_i32_f32_sdwa v55, v55 dst_sel:BYTE_3 dst_unused:UNUSED_PAD src0_sel:DWORD
	v_cvt_i32_f32_sdwa v63, v63 dst_sel:BYTE_3 dst_unused:UNUSED_PAD src0_sel:DWORD
	v_lshlrev_b32_e32 v16, 8, v16
	v_lshlrev_b32_e32 v42, 8, v42
	v_and_b32_e32 v20, 0xff0000, v20
	v_and_b32_e32 v44, 0xff0000, v44
	v_lshlrev_b32_e32 v17, 8, v17
	v_lshlrev_b32_e32 v43, 8, v43
	v_lshlrev_b32_e32 v50, 8, v50
	v_lshlrev_b32_e32 v58, 8, v58
	v_lshlrev_b32_e32 v51, 8, v51
	v_lshlrev_b32_e32 v59, 8, v59
	v_perm_b32 v14, v16, v14, s28
	v_perm_b32 v16, v42, v40, s28
	v_and_b32_e32 v21, 0xff0000, v21
	v_and_b32_e32 v45, 0xff0000, v45
	v_and_b32_e32 v52, 0xff0000, v52
	v_and_b32_e32 v60, 0xff0000, v60
	v_and_b32_e32 v53, 0xff0000, v53
	v_and_b32_e32 v61, 0xff0000, v61
	v_perm_b32 v17, v17, v15, s28
	v_perm_b32 v40, v43, v41, s28
	v_perm_b32 v41, v50, v48, s28
	v_perm_b32 v42, v58, v56, s28
	v_perm_b32 v43, v51, v49, s28
	v_perm_b32 v48, v59, v57, s28
	v_or3_b32 v14, v14, v20, v24
	v_or3_b32 v15, v16, v44, v46
	v_or3_b32 v16, v17, v21, v25
	v_or3_b32 v17, v40, v45, v47
	v_or3_b32 v20, v41, v52, v54
	v_or3_b32 v21, v42, v60, v62
	v_or3_b32 v24, v43, v53, v55
	v_or3_b32 v25, v48, v61, v63
	global_store_dwordx2 v[18:19], v[14:15], off
	global_store_dwordx2 v[22:23], v[16:17], off
	global_store_dwordx2 v[82:83], v[20:21], off
	global_store_dwordx2 v[84:85], v[24:25], off
	s_waitcnt lgkmcnt(0)
; #define LAS __attribute__((address_space(3)))
; #define GAS __attribute__((address_space(1)))
; #define LDS_WAIT() asm volatile("s_waitcnt lgkmcnt(0)" ::: "memory")
;     ...
;     for (int kb = 0; kb < D / 64; ++kb) {
; #pragma unroll
;         for (int i = 0; i < 8; ++i) { const int kk = 8 * i + kr; const int k = 64 * kb + kk; const f32x4 v = __builtin_nontemporal_load((const f32x4*)(W + (size_t)k * pitch)) * g[k];
;             LAS float* p = scr + kk * 33 + 4 * (lane & 7); p[0] = __builtin_rintf(v[0] * inv[0]); p[1] = __builtin_rintf(v[1] * inv[1]); p[2] = __builtin_rintf(v[2] * inv[2]); p[3] = __builtin_rintf(v[3] * inv[3]); }
;         LDS_WAIT(); asm volatile("" ::: "memory");
;         const int c = lane & 7;
; #pragma unroll
;         for (int j = 0; j < 4; ++j) { const int n = (lane >> 3) + 8 * j; const LAS float* sp = scr + (8 * c) * 33 + n;
;             u32x2 o;
;             o.x = ((unsigned)(int)sp[0 * 33] & 0xFFu) | (((unsigned)(int)sp[1 * 33] & 0xFFu) << 8) | (((unsigned)(int)sp[2 * 33] & 0xFFu) << 16) | (((unsigned)(int)sp[3 * 33] & 0xFFu) << 24);
;             o.y = ((unsigned)(int)sp[4 * 33] & 0xFFu) | (((unsigned)(int)sp[5 * 33] & 0xFFu) << 8) | (((unsigned)(int)sp[6 * 33] & 0xFFu) << 16) | (((unsigned)(int)sp[7 * 33] & 0xFFu) << 24);
;             *(GAS u32x2*)(dst + (size_t)(n0 + n) * D + 64 * kb + 8 * c) = o; }
;         LDS_WAIT(); asm volatile("" ::: "memory");
;     }
	v_add_u32_e32 v87, 0x14a0, v31
	v_add_u32_e32 v88, 0x14a8, v31
	v_add_u32_e32 v89, 0x18c0, v31
	v_add_u32_e32 v90, 0x18c8, v31
	v_add_u32_e32 v91, 0x1ce0, v31
	v_add_u32_e32 v92, 0x1ce8, v31
	v_lshl_add_u64 v[18:19], v[6:7], 0, v[12:13]
	v_lshl_add_u64 v[22:23], v[6:7], 0, v[10:11]
	v_lshl_add_u64 v[82:83], v[6:7], 0, v[8:9]
	v_lshl_add_u64 v[84:85], v[6:7], 0, v[4:5]
	v_lshl_add_u64 v[6:7], v[6:7], 0, 64
	s_waitcnt vmcnt(44)
	v_pk_mul_f32 v[46:47], v[144:145], v[220:221] op_sel_hi:[1,0]
	v_pk_mul_f32 v[20:21], v[142:143], v[220:221] op_sel_hi:[1,0]
	v_pk_mul_f32 v[44:45], v[148:149], v[222:223] op_sel_hi:[1,0]
	v_pk_mul_f32 v[24:25], v[146:147], v[222:223] op_sel_hi:[1,0]
	v_pk_mul_f32 v[48:49], v[152:153], v[224:225] op_sel_hi:[1,0]
	v_pk_mul_f32 v[16:17], v[140:141], v[218:219] op_sel_hi:[1,0]
	v_pk_mul_f32 v[14:15], v[138:139], v[218:219] op_sel_hi:[1,0]
	v_pk_mul_f32 v[50:51], v[150:151], v[224:225] op_sel_hi:[1,0]
	v_pk_mul_f32 v[52:53], v[156:157], v[226:227] op_sel_hi:[1,0]
	v_pk_mul_f32 v[54:55], v[154:155], v[226:227] op_sel_hi:[1,0]
	v_pk_mul_f32 v[56:57], v[160:161], v[228:229] op_sel_hi:[1,0]
	v_pk_mul_f32 v[58:59], v[158:159], v[228:229] op_sel_hi:[1,0]
	v_pk_mul_f32 v[60:61], v[164:165], v[230:231] op_sel_hi:[1,0]
	v_pk_mul_f32 v[62:63], v[162:163], v[230:231] op_sel_hi:[1,0]
	v_pk_mul_f32 v[42:43], v[168:169], v[232:233] op_sel_hi:[1,0]
	v_pk_mul_f32 v[40:41], v[166:167], v[232:233] op_sel_hi:[1,0]
	s_add_u32 s4, s4, 0x18000
	s_addc_u32 s5, s5, 0
	global_load_dwordx4 v[138:141], v250, s[4:5] nt
	global_load_dword v218, v251, s[6:7] offset:1792
	s_add_u32 s4, s4, 0x18000
	s_addc_u32 s5, s5, 0
	global_load_dwordx4 v[142:145], v250, s[4:5] nt
	global_load_dword v220, v251, s[6:7] offset:1824
	s_add_u32 s4, s4, 0x18000
	s_addc_u32 s5, s5, 0
	global_load_dwordx4 v[146:149], v250, s[4:5] nt
	global_load_dword v222, v251, s[6:7] offset:1856
	s_add_u32 s4, s4, 0x18000
	s_addc_u32 s5, s5, 0
	global_load_dwordx4 v[150:153], v250, s[4:5] nt
	global_load_dword v224, v251, s[6:7] offset:1888
	s_add_u32 s4, s4, 0x18000
	s_addc_u32 s5, s5, 0
	global_load_dwordx4 v[154:157], v250, s[4:5] nt
	global_load_dword v226, v251, s[6:7] offset:1920
	s_add_u32 s4, s4, 0x18000
	s_addc_u32 s5, s5, 0
	global_load_dwordx4 v[158:161], v250, s[4:5] nt
	global_load_dword v228, v251, s[6:7] offset:1952
	s_add_u32 s4, s4, 0x18000
	s_addc_u32 s5, s5, 0
	global_load_dwordx4 v[162:165], v250, s[4:5] nt
	global_load_dword v230, v251, s[6:7] offset:1984
	s_add_u32 s4, s4, 0x18000
	s_addc_u32 s5, s5, 0
	global_load_dwordx4 v[166:169], v250, s[4:5] nt
	global_load_dword v232, v251, s[6:7] offset:2016
	v_mul_f32_e32 v14, v26, v14
	v_mul_f32_e32 v15, v27, v15
	v_mul_f32_e32 v16, v28, v16
	v_mul_f32_e32 v17, v29, v17
	v_mul_f32_e32 v20, v26, v20
	v_mul_f32_e32 v21, v27, v21
	v_mul_f32_e32 v46, v28, v46
	v_mul_f32_e32 v47, v29, v47
	v_mul_f32_e32 v24, v26, v24
	v_mul_f32_e32 v25, v27, v25
	v_mul_f32_e32 v44, v28, v44
	v_mul_f32_e32 v45, v29, v45
	v_mul_f32_e32 v50, v26, v50
	v_mul_f32_e32 v51, v27, v51
	v_mul_f32_e32 v48, v28, v48
	v_mul_f32_e32 v49, v29, v49
	v_mul_f32_e32 v54, v26, v54
	v_mul_f32_e32 v55, v27, v55
	v_mul_f32_e32 v52, v28, v52
	v_mul_f32_e32 v53, v29, v53
	v_mul_f32_e32 v58, v26, v58
	v_mul_f32_e32 v59, v27, v59
	v_mul_f32_e32 v56, v28, v56
	v_mul_f32_e32 v57, v29, v57
	v_mul_f32_e32 v62, v26, v62
	v_mul_f32_e32 v63, v27, v63
	v_mul_f32_e32 v60, v28, v60
	v_mul_f32_e32 v61, v29, v61
	v_mul_f32_e32 v40, v26, v40
	v_mul_f32_e32 v41, v27, v41
	v_mul_f32_e32 v42, v28, v42
	v_mul_f32_e32 v43, v29, v43
	v_rndne_f32_e32 v14, v14
	v_rndne_f32_e32 v15, v15
	v_rndne_f32_e32 v16, v16
	v_rndne_f32_e32 v17, v17
	v_rndne_f32_e32 v20, v20
	v_rndne_f32_e32 v21, v21
	v_rndne_f32_e32 v46, v46
	v_rndne_f32_e32 v47, v47
	v_rndne_f32_e32 v24, v24
	v_rndne_f32_e32 v25, v25
	v_rndne_f32_e32 v44, v44
	v_rndne_f32_e32 v45, v45
	v_rndne_f32_e32 v50, v50
	v_rndne_f32_e32 v51, v51
	v_rndne_f32_e32 v48, v48
	v_rndne_f32_e32 v49, v49
	v_rndne_f32_e32 v54, v54
	v_rndne_f32_e32 v55, v55
	v_rndne_f32_e32 v52, v52
	v_rndne_f32_e32 v53, v53
	v_rndne_f32_e32 v58, v58
	v_rndne_f32_e32 v59, v59
	v_rndne_f32_e32 v56, v56
	v_rndne_f32_e32 v57, v57
	v_rndne_f32_e32 v62, v62
	v_rndne_f32_e32 v63, v63
	v_rndne_f32_e32 v60, v60
	v_rndne_f32_e32 v61, v61
	v_rndne_f32_e32 v40, v40
	v_rndne_f32_e32 v41, v41
	v_rndne_f32_e32 v42, v42
	v_rndne_f32_e32 v43, v43
	ds_write2_b32 v31, v14, v15 offset1:1
	ds_write2_b32 v31, v16, v17 offset0:2 offset1:3
	ds_write2_b32 v32, v20, v21 offset1:1
	ds_write2_b32 v33, v46, v47 offset1:1
	ds_write2_b32 v34, v24, v25 offset1:1
	ds_write2_b32 v35, v44, v45 offset1:1
	ds_write2_b32 v36, v50, v51 offset1:1
	ds_write2_b32 v37, v48, v49 offset1:1
	ds_write2_b32 v38, v54, v55 offset1:1
	ds_write2_b32 v39, v52, v53 offset1:1
	ds_write2_b32 v87, v58, v59 offset1:1
	ds_write2_b32 v88, v56, v57 offset1:1
	ds_write2_b32 v89, v62, v63 offset1:1
	ds_write2_b32 v90, v60, v61 offset1:1
	ds_write2_b32 v91, v40, v41 offset1:1
	ds_write2_b32 v92, v42, v43 offset1:1
	s_waitcnt lgkmcnt(0)
	ds_read2_b32 v[14:15], v30 offset1:8
	ds_read2_b32 v[16:17], v30 offset0:33 offset1:41
	ds_read2_b32 v[20:21], v30 offset0:66 offset1:74
	ds_read2_b32 v[24:25], v30 offset0:99 offset1:107
	ds_read2_b32 v[40:41], v30 offset0:132 offset1:140
	ds_read2_b32 v[42:43], v30 offset0:165 offset1:173
	ds_read2_b32 v[44:45], v30 offset0:198 offset1:206
	ds_read2_b32 v[46:47], v30 offset0:231 offset1:239
	ds_read2_b32 v[48:49], v30 offset0:16 offset1:24
	ds_read2_b32 v[50:51], v30 offset0:49 offset1:57
	ds_read2_b32 v[52:53], v30 offset0:82 offset1:90
	ds_read2_b32 v[54:55], v30 offset0:115 offset1:123
	ds_read2_b32 v[56:57], v30 offset0:148 offset1:156
	ds_read2_b32 v[58:59], v30 offset0:181 offset1:189
	ds_read2_b32 v[60:61], v30 offset0:214 offset1:222
	ds_read2_b32 v[62:63], v30 offset0:247 offset1:255
	s_waitcnt lgkmcnt(14)
; #define LAS __attribute__((address_space(3)))
; #define GAS __attribute__((address_space(1)))
; #define LDS_WAIT() asm volatile("s_waitcnt lgkmcnt(0)" ::: "memory")
;     ...
;     for (int kb = 0; kb < D / 64; ++kb) {
; #pragma unroll
;         for (int i = 0; i < 8; ++i) { const int kk = 8 * i + kr; const int k = 64 * kb + kk; const f32x4 v = __builtin_nontemporal_load((const f32x4*)(W + (size_t)k * pitch)) * g[k];
;             LAS float* p = scr + kk * 33 + 4 * (lane & 7); p[0] = __builtin_rintf(v[0] * inv[0]); p[1] = __builtin_rintf(v[1] * inv[1]); p[2] = __builtin_rintf(v[2] * inv[2]); p[3] = __builtin_rintf(v[3] * inv[3]); }
;         LDS_WAIT(); asm volatile("" ::: "memory");
;         const int c = lane & 7;
; #pragma unroll
;         for (int j = 0; j < 4; ++j) { const int n = (lane >> 3) + 8 * j; const LAS float* sp = scr + (8 * c) * 33 + n;
;             u32x2 o;
;             o.x = ((unsigned)(int)sp[0 * 33] & 0xFFu) | (((unsigned)(int)sp[1 * 33] & 0xFFu) << 8) | (((unsigned)(int)sp[2 * 33] & 0xFFu) << 16) | (((unsigned)(int)sp[3 * 33] & 0xFFu) << 24);
;             o.y = ((unsigned)(int)sp[4 * 33] & 0xFFu) | (((unsigned)(int)sp[5 * 33] & 0xFFu) << 8) | (((unsigned)(int)sp[6 * 33] & 0xFFu) << 16) | (((unsigned)(int)sp[7 * 33] & 0xFFu) << 24);
;             *(GAS u32x2*)(dst + (size_t)(n0 + n) * D + 64 * kb + 8 * c) = o; }
;         LDS_WAIT(); asm volatile("" ::: "memory");
;     }
	v_cvt_i32_f32_e32 v16, v16
	s_waitcnt lgkmcnt(10)
	v_cvt_i32_f32_e32 v42, v42
	v_cvt_i32_f32_e32 v14, v14
	v_cvt_i32_f32_sdwa v20, v20 dst_sel:WORD_1 dst_unused:UNUSED_PAD src0_sel:DWORD
	v_cvt_i32_f32_e32 v40, v40
	s_waitcnt lgkmcnt(9)
	v_cvt_i32_f32_sdwa v44, v44 dst_sel:WORD_1 dst_unused:UNUSED_PAD src0_sel:DWORD
	v_cvt_i32_f32_e32 v17, v17
	v_cvt_i32_f32_e32 v43, v43
	s_waitcnt lgkmcnt(6)
	v_cvt_i32_f32_e32 v50, v50
	s_waitcnt lgkmcnt(2)
	v_cvt_i32_f32_e32 v58, v58
	v_cvt_i32_f32_e32 v51, v51
	v_cvt_i32_f32_e32 v59, v59
	v_cvt_i32_f32_sdwa v24, v24 dst_sel:BYTE_3 dst_unused:UNUSED_PAD src0_sel:DWORD
	v_cvt_i32_f32_sdwa v46, v46 dst_sel:BYTE_3 dst_unused:UNUSED_PAD src0_sel:DWORD
	v_cvt_i32_f32_e32 v15, v15
	v_cvt_i32_f32_sdwa v21, v21 dst_sel:WORD_1 dst_unused:UNUSED_PAD src0_sel:DWORD
	v_cvt_i32_f32_e32 v41, v41
	v_cvt_i32_f32_sdwa v45, v45 dst_sel:WORD_1 dst_unused:UNUSED_PAD src0_sel:DWORD
	v_cvt_i32_f32_e32 v48, v48
	v_cvt_i32_f32_sdwa v52, v52 dst_sel:WORD_1 dst_unused:UNUSED_PAD src0_sel:DWORD
	v_cvt_i32_f32_e32 v56, v56
	s_waitcnt lgkmcnt(1)
	v_cvt_i32_f32_sdwa v60, v60 dst_sel:WORD_1 dst_unused:UNUSED_PAD src0_sel:DWORD
	v_cvt_i32_f32_e32 v49, v49
	v_cvt_i32_f32_sdwa v53, v53 dst_sel:WORD_1 dst_unused:UNUSED_PAD src0_sel:DWORD
	v_cvt_i32_f32_e32 v57, v57
	v_cvt_i32_f32_sdwa v61, v61 dst_sel:WORD_1 dst_unused:UNUSED_PAD src0_sel:DWORD
	v_cvt_i32_f32_sdwa v25, v25 dst_sel:BYTE_3 dst_unused:UNUSED_PAD src0_sel:DWORD
	v_cvt_i32_f32_sdwa v47, v47 dst_sel:BYTE_3 dst_unused:UNUSED_PAD src0_sel:DWORD
	v_cvt_i32_f32_sdwa v54, v54 dst_sel:BYTE_3 dst_unused:UNUSED_PAD src0_sel:DWORD
	s_waitcnt lgkmcnt(0)
	v_cvt_i32_f32_sdwa v62, v62 dst_sel:BYTE_3 dst_unused:UNUSED_PAD src0_sel:DWORD
	v_cvt_i32_f32_sdwa v55, v55 dst_sel:BYTE_3 dst_unused:UNUSED_PAD src0_sel:DWORD
	v_cvt_i32_f32_sdwa v63, v63 dst_sel:BYTE_3 dst_unused:UNUSED_PAD src0_sel:DWORD
	v_lshlrev_b32_e32 v16, 8, v16
	v_lshlrev_b32_e32 v42, 8, v42
	v_and_b32_e32 v20, 0xff0000, v20
	v_and_b32_e32 v44, 0xff0000, v44
	v_lshlrev_b32_e32 v17, 8, v17
	v_lshlrev_b32_e32 v43, 8, v43
	v_lshlrev_b32_e32 v50, 8, v50
	v_lshlrev_b32_e32 v58, 8, v58
	v_lshlrev_b32_e32 v51, 8, v51
	v_lshlrev_b32_e32 v59, 8, v59
	v_perm_b32 v14, v16, v14, s28
	v_perm_b32 v16, v42, v40, s28
	v_and_b32_e32 v21, 0xff0000, v21
	v_and_b32_e32 v45, 0xff0000, v45
	v_and_b32_e32 v52, 0xff0000, v52
	v_and_b32_e32 v60, 0xff0000, v60
	v_and_b32_e32 v53, 0xff0000, v53
	v_and_b32_e32 v61, 0xff0000, v61
	v_perm_b32 v17, v17, v15, s28
	v_perm_b32 v40, v43, v41, s28
	v_perm_b32 v41, v50, v48, s28
	v_perm_b32 v42, v58, v56, s28
	v_perm_b32 v43, v51, v49, s28
	v_perm_b32 v48, v59, v57, s28
	v_or3_b32 v14, v14, v20, v24
	v_or3_b32 v15, v16, v44, v46
	v_or3_b32 v16, v17, v21, v25
	v_or3_b32 v17, v40, v45, v47
	v_or3_b32 v20, v41, v52, v54
	v_or3_b32 v21, v42, v60, v62
	v_or3_b32 v24, v43, v53, v55
	v_or3_b32 v25, v48, v61, v63
	global_store_dwordx2 v[18:19], v[14:15], off
	global_store_dwordx2 v[22:23], v[16:17], off
	global_store_dwordx2 v[82:83], v[20:21], off
	global_store_dwordx2 v[84:85], v[24:25], off
	s_waitcnt lgkmcnt(0)
	v_add_u32_e32 v87, 0x14a0, v31
	v_add_u32_e32 v88, 0x14a8, v31
	v_add_u32_e32 v89, 0x18c0, v31
	v_add_u32_e32 v90, 0x18c8, v31
	v_add_u32_e32 v91, 0x1ce0, v31
	v_add_u32_e32 v92, 0x1ce8, v31
	v_lshl_add_u64 v[18:19], v[6:7], 0, v[12:13]
	v_lshl_add_u64 v[22:23], v[6:7], 0, v[10:11]
	v_lshl_add_u64 v[82:83], v[6:7], 0, v[8:9]
	v_lshl_add_u64 v[84:85], v[6:7], 0, v[4:5]
	v_lshl_add_u64 v[6:7], v[6:7], 0, 64
	s_waitcnt vmcnt(44)
	v_pk_mul_f32 v[46:47], v[176:177], v[236:237] op_sel_hi:[1,0]
	v_pk_mul_f32 v[20:21], v[174:175], v[236:237] op_sel_hi:[1,0]
	v_pk_mul_f32 v[44:45], v[180:181], v[238:239] op_sel_hi:[1,0]
	v_pk_mul_f32 v[24:25], v[178:179], v[238:239] op_sel_hi:[1,0]
	v_pk_mul_f32 v[48:49], v[184:185], v[240:241] op_sel_hi:[1,0]
	v_pk_mul_f32 v[16:17], v[172:173], v[234:235] op_sel_hi:[1,0]
	v_pk_mul_f32 v[14:15], v[170:171], v[234:235] op_sel_hi:[1,0]
	v_pk_mul_f32 v[50:51], v[182:183], v[240:241] op_sel_hi:[1,0]
	v_pk_mul_f32 v[52:53], v[188:189], v[242:243] op_sel_hi:[1,0]
	v_pk_mul_f32 v[54:55], v[186:187], v[242:243] op_sel_hi:[1,0]
	v_pk_mul_f32 v[56:57], v[192:193], v[244:245] op_sel_hi:[1,0]
	v_pk_mul_f32 v[58:59], v[190:191], v[244:245] op_sel_hi:[1,0]
	v_pk_mul_f32 v[60:61], v[196:197], v[246:247] op_sel_hi:[1,0]
	v_pk_mul_f32 v[62:63], v[194:195], v[246:247] op_sel_hi:[1,0]
	v_pk_mul_f32 v[42:43], v[200:201], v[248:249] op_sel_hi:[1,0]
	v_pk_mul_f32 v[40:41], v[198:199], v[248:249] op_sel_hi:[1,0]
	s_add_u32 s4, s4, 0x18000
	s_addc_u32 s5, s5, 0
	global_load_dwordx4 v[170:173], v250, s[4:5] nt
	global_load_dword v234, v251, s[6:7] offset:2048
	s_add_u32 s4, s4, 0x18000
	s_addc_u32 s5, s5, 0
	global_load_dwordx4 v[174:177], v250, s[4:5] nt
	global_load_dword v236, v251, s[6:7] offset:2080
	s_add_u32 s4, s4, 0x18000
	s_addc_u32 s5, s5, 0
	global_load_dwordx4 v[178:181], v250, s[4:5] nt
	global_load_dword v238, v251, s[6:7] offset:2112
	s_add_u32 s4, s4, 0x18000
	s_addc_u32 s5, s5, 0
	global_load_dwordx4 v[182:185], v250, s[4:5] nt
	global_load_dword v240, v251, s[6:7] offset:2144
	s_add_u32 s4, s4, 0x18000
	s_addc_u32 s5, s5, 0
	global_load_dwordx4 v[186:189], v250, s[4:5] nt
	global_load_dword v242, v251, s[6:7] offset:2176
	s_add_u32 s4, s4, 0x18000
	s_addc_u32 s5, s5, 0
	global_load_dwordx4 v[190:193], v250, s[4:5] nt
	global_load_dword v244, v251, s[6:7] offset:2208
	s_add_u32 s4, s4, 0x18000
	s_addc_u32 s5, s5, 0
	global_load_dwordx4 v[194:197], v250, s[4:5] nt
	global_load_dword v246, v251, s[6:7] offset:2240
	s_add_u32 s4, s4, 0x18000
	s_addc_u32 s5, s5, 0
	global_load_dwordx4 v[198:201], v250, s[4:5] nt
; #define LAS __attribute__((address_space(3)))
; #define GAS __attribute__((address_space(1)))
; #define LDS_WAIT() asm volatile("s_waitcnt lgkmcnt(0)" ::: "memory")
;     ...
;         for (int i = 0; i < 8; ++i) { const int kk = 8 * i + kr; const int k = 64 * kb + kk; const f32x4 v = __builtin_nontemporal_load((const f32x4*)(W + (size_t)k * pitch)) * g[k];
;             LAS float* p = scr + kk * 33 + 4 * (lane & 7); p[0] = __builtin_rintf(v[0] * inv[0]); p[1] = __builtin_rintf(v[1] * inv[1]); p[2] = __builtin_rintf(v[2] * inv[2]); p[3] = __builtin_rintf(v[3] * inv[3]); }
;         LDS_WAIT(); asm volatile("" ::: "memory");
;         const int c = lane & 7;
; #pragma unroll
;         for (int j = 0; j < 4; ++j) { const int n = (lane >> 3) + 8 * j; const LAS float* sp = scr + (8 * c) * 33 + n;
;             u32x2 o;
;             o.x = ((unsigned)(int)sp[0 * 33] & 0xFFu) | (((unsigned)(int)sp[1 * 33] & 0xFFu) << 8) | (((unsigned)(int)sp[2 * 33] & 0xFFu) << 16) | (((unsigned)(int)sp[3 * 33] & 0xFFu) << 24);
;             o.y = ((unsigned)(int)sp[4 * 33] & 0xFFu) | (((unsigned)(int)sp[5 * 33] & 0xFFu) << 8) | (((unsigned)(int)sp[6 * 33] & 0xFFu) << 16) | (((unsigned)(int)sp[7 * 33] & 0xFFu) << 24);
;             *(GAS u32x2*)(dst + (size_t)(n0 + n) * D + 64 * kb + 8 * c) = o; }
;         LDS_WAIT(); asm volatile("" ::: "memory");
	global_load_dword v248, v251, s[6:7] offset:2272
	v_mul_f32_e32 v14, v26, v14
	v_mul_f32_e32 v15, v27, v15
	v_mul_f32_e32 v16, v28, v16
	v_mul_f32_e32 v17, v29, v17
	v_mul_f32_e32 v20, v26, v20
	v_mul_f32_e32 v21, v27, v21
	v_mul_f32_e32 v46, v28, v46
	v_mul_f32_e32 v47, v29, v47
	v_mul_f32_e32 v24, v26, v24
	v_mul_f32_e32 v25, v27, v25
	v_mul_f32_e32 v44, v28, v44
	v_mul_f32_e32 v45, v29, v45
	v_mul_f32_e32 v50, v26, v50
	v_mul_f32_e32 v51, v27, v51
	v_mul_f32_e32 v48, v28, v48
	v_mul_f32_e32 v49, v29, v49
	v_mul_f32_e32 v54, v26, v54
	v_mul_f32_e32 v55, v27, v55
	v_mul_f32_e32 v52, v28, v52
	v_mul_f32_e32 v53, v29, v53
	v_mul_f32_e32 v58, v26, v58
	v_mul_f32_e32 v59, v27, v59
	v_mul_f32_e32 v56, v28, v56
	v_mul_f32_e32 v57, v29, v57
	v_mul_f32_e32 v62, v26, v62
	v_mul_f32_e32 v63, v27, v63
	v_mul_f32_e32 v60, v28, v60
	v_mul_f32_e32 v61, v29, v61
	v_mul_f32_e32 v40, v26, v40
	v_mul_f32_e32 v41, v27, v41
	v_mul_f32_e32 v42, v28, v42
	v_mul_f32_e32 v43, v29, v43
	v_rndne_f32_e32 v14, v14
	v_rndne_f32_e32 v15, v15
	v_rndne_f32_e32 v16, v16
	v_rndne_f32_e32 v17, v17
	v_rndne_f32_e32 v20, v20
	v_rndne_f32_e32 v21, v21
	v_rndne_f32_e32 v46, v46
	v_rndne_f32_e32 v47, v47
	v_rndne_f32_e32 v24, v24
	v_rndne_f32_e32 v25, v25
	v_rndne_f32_e32 v44, v44
	v_rndne_f32_e32 v45, v45
	v_rndne_f32_e32 v50, v50
	v_rndne_f32_e32 v51, v51
	v_rndne_f32_e32 v48, v48
	v_rndne_f32_e32 v49, v49
	v_rndne_f32_e32 v54, v54
	v_rndne_f32_e32 v55, v55
	v_rndne_f32_e32 v52, v52
	v_rndne_f32_e32 v53, v53
	v_rndne_f32_e32 v58, v58
	v_rndne_f32_e32 v59, v59
	v_rndne_f32_e32 v56, v56
	v_rndne_f32_e32 v57, v57
	v_rndne_f32_e32 v62, v62
	v_rndne_f32_e32 v63, v63
	v_rndne_f32_e32 v60, v60
	v_rndne_f32_e32 v61, v61
	v_rndne_f32_e32 v40, v40
	v_rndne_f32_e32 v41, v41
	v_rndne_f32_e32 v42, v42
	v_rndne_f32_e32 v43, v43
	ds_write2_b32 v31, v14, v15 offset1:1
	ds_write2_b32 v31, v16, v17 offset0:2 offset1:3
	ds_write2_b32 v32, v20, v21 offset1:1
	ds_write2_b32 v33, v46, v47 offset1:1
	ds_write2_b32 v34, v24, v25 offset1:1
	ds_write2_b32 v35, v44, v45 offset1:1
	ds_write2_b32 v36, v50, v51 offset1:1
	ds_write2_b32 v37, v48, v49 offset1:1
	ds_write2_b32 v38, v54, v55 offset1:1
	ds_write2_b32 v39, v52, v53 offset1:1
	ds_write2_b32 v87, v58, v59 offset1:1
	ds_write2_b32 v88, v56, v57 offset1:1
	ds_write2_b32 v89, v62, v63 offset1:1
	ds_write2_b32 v90, v60, v61 offset1:1
	ds_write2_b32 v91, v40, v41 offset1:1
	ds_write2_b32 v92, v42, v43 offset1:1
	s_waitcnt lgkmcnt(0)
	ds_read2_b32 v[14:15], v30 offset1:8
	ds_read2_b32 v[16:17], v30 offset0:33 offset1:41
	ds_read2_b32 v[20:21], v30 offset0:66 offset1:74
	ds_read2_b32 v[24:25], v30 offset0:99 offset1:107
	ds_read2_b32 v[40:41], v30 offset0:132 offset1:140
	ds_read2_b32 v[42:43], v30 offset0:165 offset1:173
	ds_read2_b32 v[44:45], v30 offset0:198 offset1:206
	ds_read2_b32 v[46:47], v30 offset0:231 offset1:239
	ds_read2_b32 v[48:49], v30 offset0:16 offset1:24
	ds_read2_b32 v[50:51], v30 offset0:49 offset1:57
	ds_read2_b32 v[52:53], v30 offset0:82 offset1:90
	ds_read2_b32 v[54:55], v30 offset0:115 offset1:123
	ds_read2_b32 v[56:57], v30 offset0:148 offset1:156
	ds_read2_b32 v[58:59], v30 offset0:181 offset1:189
	ds_read2_b32 v[60:61], v30 offset0:214 offset1:222
	ds_read2_b32 v[62:63], v30 offset0:247 offset1:255
	s_waitcnt lgkmcnt(14)
	v_cvt_i32_f32_e32 v16, v16
	s_waitcnt lgkmcnt(10)
	v_cvt_i32_f32_e32 v42, v42
	v_cvt_i32_f32_e32 v14, v14
	v_cvt_i32_f32_sdwa v20, v20 dst_sel:WORD_1 dst_unused:UNUSED_PAD src0_sel:DWORD
	v_cvt_i32_f32_e32 v40, v40
	s_waitcnt lgkmcnt(9)
	v_cvt_i32_f32_sdwa v44, v44 dst_sel:WORD_1 dst_unused:UNUSED_PAD src0_sel:DWORD
	v_cvt_i32_f32_e32 v17, v17
	v_cvt_i32_f32_e32 v43, v43
	s_waitcnt lgkmcnt(6)
	v_cvt_i32_f32_e32 v50, v50
	s_waitcnt lgkmcnt(2)
	v_cvt_i32_f32_e32 v58, v58
	v_cvt_i32_f32_e32 v51, v51
	v_cvt_i32_f32_e32 v59, v59
	v_cvt_i32_f32_sdwa v24, v24 dst_sel:BYTE_3 dst_unused:UNUSED_PAD src0_sel:DWORD
	v_cvt_i32_f32_sdwa v46, v46 dst_sel:BYTE_3 dst_unused:UNUSED_PAD src0_sel:DWORD
	v_cvt_i32_f32_e32 v15, v15
	v_cvt_i32_f32_sdwa v21, v21 dst_sel:WORD_1 dst_unused:UNUSED_PAD src0_sel:DWORD
	v_cvt_i32_f32_e32 v41, v41
	v_cvt_i32_f32_sdwa v45, v45 dst_sel:WORD_1 dst_unused:UNUSED_PAD src0_sel:DWORD
	v_cvt_i32_f32_e32 v48, v48
	v_cvt_i32_f32_sdwa v52, v52 dst_sel:WORD_1 dst_unused:UNUSED_PAD src0_sel:DWORD
	v_cvt_i32_f32_e32 v56, v56
	s_waitcnt lgkmcnt(1)
	v_cvt_i32_f32_sdwa v60, v60 dst_sel:WORD_1 dst_unused:UNUSED_PAD src0_sel:DWORD
	v_cvt_i32_f32_e32 v49, v49
	v_cvt_i32_f32_sdwa v53, v53 dst_sel:WORD_1 dst_unused:UNUSED_PAD src0_sel:DWORD
	v_cvt_i32_f32_e32 v57, v57
	v_cvt_i32_f32_sdwa v61, v61 dst_sel:WORD_1 dst_unused:UNUSED_PAD src0_sel:DWORD
	v_cvt_i32_f32_sdwa v25, v25 dst_sel:BYTE_3 dst_unused:UNUSED_PAD src0_sel:DWORD
	v_cvt_i32_f32_sdwa v47, v47 dst_sel:BYTE_3 dst_unused:UNUSED_PAD src0_sel:DWORD
	v_cvt_i32_f32_sdwa v54, v54 dst_sel:BYTE_3 dst_unused:UNUSED_PAD src0_sel:DWORD
	s_waitcnt lgkmcnt(0)
; #define LAS __attribute__((address_space(3)))
; #define GAS __attribute__((address_space(1)))
; #define LDS_WAIT() asm volatile("s_waitcnt lgkmcnt(0)" ::: "memory")
;     ...
;     for (int kb = 0; kb < D / 64; ++kb) {
; #pragma unroll
;         for (int i = 0; i < 8; ++i) { const int kk = 8 * i + kr; const int k = 64 * kb + kk; const f32x4 v = __builtin_nontemporal_load((const f32x4*)(W + (size_t)k * pitch)) * g[k];
;             LAS float* p = scr + kk * 33 + 4 * (lane & 7); p[0] = __builtin_rintf(v[0] * inv[0]); p[1] = __builtin_rintf(v[1] * inv[1]); p[2] = __builtin_rintf(v[2] * inv[2]); p[3] = __builtin_rintf(v[3] * inv[3]); }
;         LDS_WAIT(); asm volatile("" ::: "memory");
;         const int c = lane & 7;
; #pragma unroll
;         for (int j = 0; j < 4; ++j) { const int n = (lane >> 3) + 8 * j; const LAS float* sp = scr + (8 * c) * 33 + n;
;             u32x2 o;
;             o.x = ((unsigned)(int)sp[0 * 33] & 0xFFu) | (((unsigned)(int)sp[1 * 33] & 0xFFu) << 8) | (((unsigned)(int)sp[2 * 33] & 0xFFu) << 16) | (((unsigned)(int)sp[3 * 33] & 0xFFu) << 24);
;             o.y = ((unsigned)(int)sp[4 * 33] & 0xFFu) | (((unsigned)(int)sp[5 * 33] & 0xFFu) << 8) | (((unsigned)(int)sp[6 * 33] & 0xFFu) << 16) | (((unsigned)(int)sp[7 * 33] & 0xFFu) << 24);
;             *(GAS u32x2*)(dst + (size_t)(n0 + n) * D + 64 * kb + 8 * c) = o; }
;         LDS_WAIT(); asm volatile("" ::: "memory");
;     }
	v_cvt_i32_f32_sdwa v62, v62 dst_sel:BYTE_3 dst_unused:UNUSED_PAD src0_sel:DWORD
	v_cvt_i32_f32_sdwa v55, v55 dst_sel:BYTE_3 dst_unused:UNUSED_PAD src0_sel:DWORD
	v_cvt_i32_f32_sdwa v63, v63 dst_sel:BYTE_3 dst_unused:UNUSED_PAD src0_sel:DWORD
	v_lshlrev_b32_e32 v16, 8, v16
	v_lshlrev_b32_e32 v42, 8, v42
	v_and_b32_e32 v20, 0xff0000, v20
	v_and_b32_e32 v44, 0xff0000, v44
	v_lshlrev_b32_e32 v17, 8, v17
	v_lshlrev_b32_e32 v43, 8, v43
	v_lshlrev_b32_e32 v50, 8, v50
	v_lshlrev_b32_e32 v58, 8, v58
	v_lshlrev_b32_e32 v51, 8, v51
	v_lshlrev_b32_e32 v59, 8, v59
	v_perm_b32 v14, v16, v14, s28
	v_perm_b32 v16, v42, v40, s28
	v_and_b32_e32 v21, 0xff0000, v21
	v_and_b32_e32 v45, 0xff0000, v45
	v_and_b32_e32 v52, 0xff0000, v52
	v_and_b32_e32 v60, 0xff0000, v60
	v_and_b32_e32 v53, 0xff0000, v53
	v_and_b32_e32 v61, 0xff0000, v61
	v_perm_b32 v17, v17, v15, s28
	v_perm_b32 v40, v43, v41, s28
	v_perm_b32 v41, v50, v48, s28
	v_perm_b32 v42, v58, v56, s28
	v_perm_b32 v43, v51, v49, s28
	v_perm_b32 v48, v59, v57, s28
	v_or3_b32 v14, v14, v20, v24
	v_or3_b32 v15, v16, v44, v46
	v_or3_b32 v16, v17, v21, v25
	v_or3_b32 v17, v40, v45, v47
	v_or3_b32 v20, v41, v52, v54
	v_or3_b32 v21, v42, v60, v62
	v_or3_b32 v24, v43, v53, v55
	v_or3_b32 v25, v48, v61, v63
	global_store_dwordx2 v[18:19], v[14:15], off
	global_store_dwordx2 v[22:23], v[16:17], off
	global_store_dwordx2 v[82:83], v[20:21], off
	global_store_dwordx2 v[84:85], v[24:25], off
	s_waitcnt lgkmcnt(0)
	v_add_u32_e32 v87, 0x14a0, v31
	v_add_u32_e32 v88, 0x14a8, v31
	v_add_u32_e32 v89, 0x18c0, v31
	v_add_u32_e32 v90, 0x18c8, v31
	v_add_u32_e32 v91, 0x1ce0, v31
	v_add_u32_e32 v92, 0x1ce8, v31
	v_lshl_add_u64 v[18:19], v[6:7], 0, v[12:13]
	v_lshl_add_u64 v[22:23], v[6:7], 0, v[10:11]
	v_lshl_add_u64 v[82:83], v[6:7], 0, v[8:9]
	v_lshl_add_u64 v[84:85], v[6:7], 0, v[4:5]
	v_lshl_add_u64 v[6:7], v[6:7], 0, 64
	s_waitcnt vmcnt(44)
	v_pk_mul_f32 v[46:47], v[112:113], v[204:205] op_sel_hi:[1,0]
	v_pk_mul_f32 v[20:21], v[110:111], v[204:205] op_sel_hi:[1,0]
	v_pk_mul_f32 v[44:45], v[116:117], v[206:207] op_sel_hi:[1,0]
	v_pk_mul_f32 v[24:25], v[114:115], v[206:207] op_sel_hi:[1,0]
	v_pk_mul_f32 v[48:49], v[120:121], v[208:209] op_sel_hi:[1,0]
	v_pk_mul_f32 v[16:17], v[108:109], v[202:203] op_sel_hi:[1,0]
	v_pk_mul_f32 v[14:15], v[106:107], v[202:203] op_sel_hi:[1,0]
	v_pk_mul_f32 v[50:51], v[118:119], v[208:209] op_sel_hi:[1,0]
	v_pk_mul_f32 v[52:53], v[124:125], v[210:211] op_sel_hi:[1,0]
	v_pk_mul_f32 v[54:55], v[122:123], v[210:211] op_sel_hi:[1,0]
	v_pk_mul_f32 v[56:57], v[128:129], v[212:213] op_sel_hi:[1,0]
	v_pk_mul_f32 v[58:59], v[126:127], v[212:213] op_sel_hi:[1,0]
	v_pk_mul_f32 v[60:61], v[132:133], v[214:215] op_sel_hi:[1,0]
	v_pk_mul_f32 v[62:63], v[130:131], v[214:215] op_sel_hi:[1,0]
	v_pk_mul_f32 v[42:43], v[136:137], v[216:217] op_sel_hi:[1,0]
	v_pk_mul_f32 v[40:41], v[134:135], v[216:217] op_sel_hi:[1,0]
	s_add_u32 s4, s4, 0x18000
	s_addc_u32 s5, s5, 0
	global_load_dwordx4 v[106:109], v250, s[4:5] nt
	global_load_dword v202, v251, s[6:7] offset:2304
	s_add_u32 s4, s4, 0x18000
	s_addc_u32 s5, s5, 0
	global_load_dwordx4 v[110:113], v250, s[4:5] nt
	global_load_dword v204, v251, s[6:7] offset:2336
	s_add_u32 s4, s4, 0x18000
	s_addc_u32 s5, s5, 0
	global_load_dwordx4 v[114:117], v250, s[4:5] nt
	global_load_dword v206, v251, s[6:7] offset:2368
	s_add_u32 s4, s4, 0x18000
	s_addc_u32 s5, s5, 0
	global_load_dwordx4 v[118:121], v250, s[4:5] nt
	global_load_dword v208, v251, s[6:7] offset:2400
	s_add_u32 s4, s4, 0x18000
	s_addc_u32 s5, s5, 0
	global_load_dwordx4 v[122:125], v250, s[4:5] nt
	global_load_dword v210, v251, s[6:7] offset:2432
	s_add_u32 s4, s4, 0x18000
	s_addc_u32 s5, s5, 0
	global_load_dwordx4 v[126:129], v250, s[4:5] nt
	global_load_dword v212, v251, s[6:7] offset:2464
	s_add_u32 s4, s4, 0x18000
	s_addc_u32 s5, s5, 0
	global_load_dwordx4 v[130:133], v250, s[4:5] nt
	global_load_dword v214, v251, s[6:7] offset:2496
	s_add_u32 s4, s4, 0x18000
	s_addc_u32 s5, s5, 0
	global_load_dwordx4 v[134:137], v250, s[4:5] nt
	global_load_dword v216, v251, s[6:7] offset:2528
	v_mul_f32_e32 v14, v26, v14
	v_mul_f32_e32 v15, v27, v15
	v_mul_f32_e32 v16, v28, v16
	v_mul_f32_e32 v17, v29, v17
	v_mul_f32_e32 v20, v26, v20
	v_mul_f32_e32 v21, v27, v21
	v_mul_f32_e32 v46, v28, v46
	v_mul_f32_e32 v47, v29, v47
	v_mul_f32_e32 v24, v26, v24
	v_mul_f32_e32 v25, v27, v25
	v_mul_f32_e32 v44, v28, v44
	v_mul_f32_e32 v45, v29, v45
	v_mul_f32_e32 v50, v26, v50
	v_mul_f32_e32 v51, v27, v51
	v_mul_f32_e32 v48, v28, v48
	v_mul_f32_e32 v49, v29, v49
	v_mul_f32_e32 v54, v26, v54
	v_mul_f32_e32 v55, v27, v55
	v_mul_f32_e32 v52, v28, v52
	v_mul_f32_e32 v53, v29, v53
	v_mul_f32_e32 v58, v26, v58
	v_mul_f32_e32 v59, v27, v59
	v_mul_f32_e32 v56, v28, v56
	v_mul_f32_e32 v57, v29, v57
	v_mul_f32_e32 v62, v26, v62
	v_mul_f32_e32 v63, v27, v63
	v_mul_f32_e32 v60, v28, v60
	v_mul_f32_e32 v61, v29, v61
	v_mul_f32_e32 v40, v26, v40
	v_mul_f32_e32 v41, v27, v41
	v_mul_f32_e32 v42, v28, v42
	v_mul_f32_e32 v43, v29, v43
	v_rndne_f32_e32 v14, v14
	v_rndne_f32_e32 v15, v15
	v_rndne_f32_e32 v16, v16
	v_rndne_f32_e32 v17, v17
	v_rndne_f32_e32 v20, v20
	v_rndne_f32_e32 v21, v21
	v_rndne_f32_e32 v46, v46
	v_rndne_f32_e32 v47, v47
	v_rndne_f32_e32 v24, v24
	v_rndne_f32_e32 v25, v25
	v_rndne_f32_e32 v44, v44
	v_rndne_f32_e32 v45, v45
	v_rndne_f32_e32 v50, v50
	v_rndne_f32_e32 v51, v51
	v_rndne_f32_e32 v48, v48
	v_rndne_f32_e32 v49, v49
	v_rndne_f32_e32 v54, v54
	v_rndne_f32_e32 v55, v55
	v_rndne_f32_e32 v52, v52
	v_rndne_f32_e32 v53, v53
	v_rndne_f32_e32 v58, v58
	v_rndne_f32_e32 v59, v59
	v_rndne_f32_e32 v56, v56
	v_rndne_f32_e32 v57, v57
	v_rndne_f32_e32 v62, v62
	v_rndne_f32_e32 v63, v63
	v_rndne_f32_e32 v60, v60
	v_rndne_f32_e32 v61, v61
	v_rndne_f32_e32 v40, v40
	v_rndne_f32_e32 v41, v41
	v_rndne_f32_e32 v42, v42
	v_rndne_f32_e32 v43, v43
	ds_write2_b32 v31, v14, v15 offset1:1
	ds_write2_b32 v31, v16, v17 offset0:2 offset1:3
	ds_write2_b32 v32, v20, v21 offset1:1
	ds_write2_b32 v33, v46, v47 offset1:1
	ds_write2_b32 v34, v24, v25 offset1:1
	ds_write2_b32 v35, v44, v45 offset1:1
	ds_write2_b32 v36, v50, v51 offset1:1
	ds_write2_b32 v37, v48, v49 offset1:1
	ds_write2_b32 v38, v54, v55 offset1:1
	ds_write2_b32 v39, v52, v53 offset1:1
	ds_write2_b32 v87, v58, v59 offset1:1
	ds_write2_b32 v88, v56, v57 offset1:1
	ds_write2_b32 v89, v62, v63 offset1:1
	ds_write2_b32 v90, v60, v61 offset1:1
	ds_write2_b32 v91, v40, v41 offset1:1
	ds_write2_b32 v92, v42, v43 offset1:1
	s_waitcnt lgkmcnt(0)
; #define LAS __attribute__((address_space(3)))
; #define GAS __attribute__((address_space(1)))
; #define LDS_WAIT() asm volatile("s_waitcnt lgkmcnt(0)" ::: "memory")
;     ...
;         LDS_WAIT(); asm volatile("" ::: "memory");
;         const int c = lane & 7;
; #pragma unroll
;         for (int j = 0; j < 4; ++j) { const int n = (lane >> 3) + 8 * j; const LAS float* sp = scr + (8 * c) * 33 + n;
;             u32x2 o;
;             o.x = ((unsigned)(int)sp[0 * 33] & 0xFFu) | (((unsigned)(int)sp[1 * 33] & 0xFFu) << 8) | (((unsigned)(int)sp[2 * 33] & 0xFFu) << 16) | (((unsigned)(int)sp[3 * 33] & 0xFFu) << 24);
;             o.y = ((unsigned)(int)sp[4 * 33] & 0xFFu) | (((unsigned)(int)sp[5 * 33] & 0xFFu) << 8) | (((unsigned)(int)sp[6 * 33] & 0xFFu) << 16) | (((unsigned)(int)sp[7 * 33] & 0xFFu) << 24);
;             *(GAS u32x2*)(dst + (size_t)(n0 + n) * D + 64 * kb + 8 * c) = o; }
;         LDS_WAIT(); asm volatile("" ::: "memory");
;     }
	ds_read2_b32 v[14:15], v30 offset1:8
	ds_read2_b32 v[16:17], v30 offset0:33 offset1:41
	ds_read2_b32 v[20:21], v30 offset0:66 offset1:74
	ds_read2_b32 v[24:25], v30 offset0:99 offset1:107
	ds_read2_b32 v[40:41], v30 offset0:132 offset1:140
	ds_read2_b32 v[42:43], v30 offset0:165 offset1:173
	ds_read2_b32 v[44:45], v30 offset0:198 offset1:206
	ds_read2_b32 v[46:47], v30 offset0:231 offset1:239
	ds_read2_b32 v[48:49], v30 offset0:16 offset1:24
	ds_read2_b32 v[50:51], v30 offset0:49 offset1:57
	ds_read2_b32 v[52:53], v30 offset0:82 offset1:90
	ds_read2_b32 v[54:55], v30 offset0:115 offset1:123
	ds_read2_b32 v[56:57], v30 offset0:148 offset1:156
	ds_read2_b32 v[58:59], v30 offset0:181 offset1:189
	ds_read2_b32 v[60:61], v30 offset0:214 offset1:222
	ds_read2_b32 v[62:63], v30 offset0:247 offset1:255
	s_waitcnt lgkmcnt(14)
	v_cvt_i32_f32_e32 v16, v16
	s_waitcnt lgkmcnt(10)
	v_cvt_i32_f32_e32 v42, v42
	v_cvt_i32_f32_e32 v14, v14
	v_cvt_i32_f32_sdwa v20, v20 dst_sel:WORD_1 dst_unused:UNUSED_PAD src0_sel:DWORD
	v_cvt_i32_f32_e32 v40, v40
	s_waitcnt lgkmcnt(9)
	v_cvt_i32_f32_sdwa v44, v44 dst_sel:WORD_1 dst_unused:UNUSED_PAD src0_sel:DWORD
	v_cvt_i32_f32_e32 v17, v17
	v_cvt_i32_f32_e32 v43, v43
	s_waitcnt lgkmcnt(6)
	v_cvt_i32_f32_e32 v50, v50
	s_waitcnt lgkmcnt(2)
	v_cvt_i32_f32_e32 v58, v58
	v_cvt_i32_f32_e32 v51, v51
	v_cvt_i32_f32_e32 v59, v59
	v_cvt_i32_f32_sdwa v24, v24 dst_sel:BYTE_3 dst_unused:UNUSED_PAD src0_sel:DWORD
	v_cvt_i32_f32_sdwa v46, v46 dst_sel:BYTE_3 dst_unused:UNUSED_PAD src0_sel:DWORD
	v_cvt_i32_f32_e32 v15, v15
	v_cvt_i32_f32_sdwa v21, v21 dst_sel:WORD_1 dst_unused:UNUSED_PAD src0_sel:DWORD
	v_cvt_i32_f32_e32 v41, v41
	v_cvt_i32_f32_sdwa v45, v45 dst_sel:WORD_1 dst_unused:UNUSED_PAD src0_sel:DWORD
	v_cvt_i32_f32_e32 v48, v48
	v_cvt_i32_f32_sdwa v52, v52 dst_sel:WORD_1 dst_unused:UNUSED_PAD src0_sel:DWORD
	v_cvt_i32_f32_e32 v56, v56
	s_waitcnt lgkmcnt(1)
	v_cvt_i32_f32_sdwa v60, v60 dst_sel:WORD_1 dst_unused:UNUSED_PAD src0_sel:DWORD
	v_cvt_i32_f32_e32 v49, v49
	v_cvt_i32_f32_sdwa v53, v53 dst_sel:WORD_1 dst_unused:UNUSED_PAD src0_sel:DWORD
	v_cvt_i32_f32_e32 v57, v57
	v_cvt_i32_f32_sdwa v61, v61 dst_sel:WORD_1 dst_unused:UNUSED_PAD src0_sel:DWORD
	v_cvt_i32_f32_sdwa v25, v25 dst_sel:BYTE_3 dst_unused:UNUSED_PAD src0_sel:DWORD
	v_cvt_i32_f32_sdwa v47, v47 dst_sel:BYTE_3 dst_unused:UNUSED_PAD src0_sel:DWORD
	v_cvt_i32_f32_sdwa v54, v54 dst_sel:BYTE_3 dst_unused:UNUSED_PAD src0_sel:DWORD
	s_waitcnt lgkmcnt(0)
	v_cvt_i32_f32_sdwa v62, v62 dst_sel:BYTE_3 dst_unused:UNUSED_PAD src0_sel:DWORD
	v_cvt_i32_f32_sdwa v55, v55 dst_sel:BYTE_3 dst_unused:UNUSED_PAD src0_sel:DWORD
	v_cvt_i32_f32_sdwa v63, v63 dst_sel:BYTE_3 dst_unused:UNUSED_PAD src0_sel:DWORD
	v_lshlrev_b32_e32 v16, 8, v16
	v_lshlrev_b32_e32 v42, 8, v42
	v_and_b32_e32 v20, 0xff0000, v20
	v_and_b32_e32 v44, 0xff0000, v44
	v_lshlrev_b32_e32 v17, 8, v17
	v_lshlrev_b32_e32 v43, 8, v43
	v_lshlrev_b32_e32 v50, 8, v50
	v_lshlrev_b32_e32 v58, 8, v58
	v_lshlrev_b32_e32 v51, 8, v51
	v_lshlrev_b32_e32 v59, 8, v59
	v_perm_b32 v14, v16, v14, s28
	v_perm_b32 v16, v42, v40, s28
	v_and_b32_e32 v21, 0xff0000, v21
	v_and_b32_e32 v45, 0xff0000, v45
	v_and_b32_e32 v52, 0xff0000, v52
	v_and_b32_e32 v60, 0xff0000, v60
	v_and_b32_e32 v53, 0xff0000, v53
	v_and_b32_e32 v61, 0xff0000, v61
	v_perm_b32 v17, v17, v15, s28
	v_perm_b32 v40, v43, v41, s28
	v_perm_b32 v41, v50, v48, s28
	v_perm_b32 v42, v58, v56, s28
	v_perm_b32 v43, v51, v49, s28
	v_perm_b32 v48, v59, v57, s28
	v_or3_b32 v14, v14, v20, v24
	v_or3_b32 v15, v16, v44, v46
	v_or3_b32 v16, v17, v21, v25
	v_or3_b32 v17, v40, v45, v47
	v_or3_b32 v20, v41, v52, v54
	v_or3_b32 v21, v42, v60, v62
	v_or3_b32 v24, v43, v53, v55
	v_or3_b32 v25, v48, v61, v63
	global_store_dwordx2 v[18:19], v[14:15], off
	global_store_dwordx2 v[22:23], v[16:17], off
	global_store_dwordx2 v[82:83], v[20:21], off
	global_store_dwordx2 v[84:85], v[24:25], off
	s_waitcnt lgkmcnt(0)
	v_add_u32_e32 v87, 0x14a0, v31
	v_add_u32_e32 v88, 0x14a8, v31
	v_add_u32_e32 v89, 0x18c0, v31
	v_add_u32_e32 v90, 0x18c8, v31
	v_add_u32_e32 v91, 0x1ce0, v31
	v_add_u32_e32 v92, 0x1ce8, v31
	v_lshl_add_u64 v[18:19], v[6:7], 0, v[12:13]
	v_lshl_add_u64 v[22:23], v[6:7], 0, v[10:11]
	v_lshl_add_u64 v[82:83], v[6:7], 0, v[8:9]
	v_lshl_add_u64 v[84:85], v[6:7], 0, v[4:5]
	v_lshl_add_u64 v[6:7], v[6:7], 0, 64
	s_waitcnt vmcnt(44)
; #define LAS __attribute__((address_space(3)))
; #define GAS __attribute__((address_space(1)))
; #define LDS_WAIT() asm volatile("s_waitcnt lgkmcnt(0)" ::: "memory")
;     ...
;     for (int kb = 0; kb < D / 64; ++kb) {
; #pragma unroll
;         for (int i = 0; i < 8; ++i) { const int kk = 8 * i + kr; const int k = 64 * kb + kk; const f32x4 v = __builtin_nontemporal_load((const f32x4*)(W + (size_t)k * pitch)) * g[k];
;             LAS float* p = scr + kk * 33 + 4 * (lane & 7); p[0] = __builtin_rintf(v[0] * inv[0]); p[1] = __builtin_rintf(v[1] * inv[1]); p[2] = __builtin_rintf(v[2] * inv[2]); p[3] = __builtin_rintf(v[3] * inv[3]); }
;         LDS_WAIT(); asm volatile("" ::: "memory");
;         const int c = lane & 7;
; #pragma unroll
;         for (int j = 0; j < 4; ++j) { const int n = (lane >> 3) + 8 * j; const LAS float* sp = scr + (8 * c) * 33 + n;
;             u32x2 o;
;             o.x = ((unsigned)(int)sp[0 * 33] & 0xFFu) | (((unsigned)(int)sp[1 * 33] & 0xFFu) << 8) | (((unsigned)(int)sp[2 * 33] & 0xFFu) << 16) | (((unsigned)(int)sp[3 * 33] & 0xFFu) << 24);
;             o.y = ((unsigned)(int)sp[4 * 33] & 0xFFu) | (((unsigned)(int)sp[5 * 33] & 0xFFu) << 8) | (((unsigned)(int)sp[6 * 33] & 0xFFu) << 16) | (((unsigned)(int)sp[7 * 33] & 0xFFu) << 24);
;             *(GAS u32x2*)(dst + (size_t)(n0 + n) * D + 64 * kb + 8 * c) = o; }
;         LDS_WAIT(); asm volatile("" ::: "memory");
;     }
	v_pk_mul_f32 v[46:47], v[144:145], v[220:221] op_sel_hi:[1,0]
	v_pk_mul_f32 v[20:21], v[142:143], v[220:221] op_sel_hi:[1,0]
	v_pk_mul_f32 v[44:45], v[148:149], v[222:223] op_sel_hi:[1,0]
	v_pk_mul_f32 v[24:25], v[146:147], v[222:223] op_sel_hi:[1,0]
	v_pk_mul_f32 v[48:49], v[152:153], v[224:225] op_sel_hi:[1,0]
	v_pk_mul_f32 v[16:17], v[140:141], v[218:219] op_sel_hi:[1,0]
	v_pk_mul_f32 v[14:15], v[138:139], v[218:219] op_sel_hi:[1,0]
	v_pk_mul_f32 v[50:51], v[150:151], v[224:225] op_sel_hi:[1,0]
	v_pk_mul_f32 v[52:53], v[156:157], v[226:227] op_sel_hi:[1,0]
	v_pk_mul_f32 v[54:55], v[154:155], v[226:227] op_sel_hi:[1,0]
	v_pk_mul_f32 v[56:57], v[160:161], v[228:229] op_sel_hi:[1,0]
	v_pk_mul_f32 v[58:59], v[158:159], v[228:229] op_sel_hi:[1,0]
	v_pk_mul_f32 v[60:61], v[164:165], v[230:231] op_sel_hi:[1,0]
	v_pk_mul_f32 v[62:63], v[162:163], v[230:231] op_sel_hi:[1,0]
	v_pk_mul_f32 v[42:43], v[168:169], v[232:233] op_sel_hi:[1,0]
	v_pk_mul_f32 v[40:41], v[166:167], v[232:233] op_sel_hi:[1,0]
	s_add_u32 s4, s4, 0x18000
	s_addc_u32 s5, s5, 0
	global_load_dwordx4 v[138:141], v250, s[4:5] nt
	global_load_dword v218, v251, s[6:7] offset:2560
	s_add_u32 s4, s4, 0x18000
	s_addc_u32 s5, s5, 0
	global_load_dwordx4 v[142:145], v250, s[4:5] nt
	global_load_dword v220, v251, s[6:7] offset:2592
	s_add_u32 s4, s4, 0x18000
	s_addc_u32 s5, s5, 0
	global_load_dwordx4 v[146:149], v250, s[4:5] nt
	global_load_dword v222, v251, s[6:7] offset:2624
	s_add_u32 s4, s4, 0x18000
	s_addc_u32 s5, s5, 0
	global_load_dwordx4 v[150:153], v250, s[4:5] nt
	global_load_dword v224, v251, s[6:7] offset:2656
	s_add_u32 s4, s4, 0x18000
	s_addc_u32 s5, s5, 0
	global_load_dwordx4 v[154:157], v250, s[4:5] nt
	global_load_dword v226, v251, s[6:7] offset:2688
	s_add_u32 s4, s4, 0x18000
	s_addc_u32 s5, s5, 0
	global_load_dwordx4 v[158:161], v250, s[4:5] nt
	global_load_dword v228, v251, s[6:7] offset:2720
	s_add_u32 s4, s4, 0x18000
	s_addc_u32 s5, s5, 0
	global_load_dwordx4 v[162:165], v250, s[4:5] nt
	global_load_dword v230, v251, s[6:7] offset:2752
	s_add_u32 s4, s4, 0x18000
	s_addc_u32 s5, s5, 0
	global_load_dwordx4 v[166:169], v250, s[4:5] nt
	global_load_dword v232, v251, s[6:7] offset:2784
	v_mul_f32_e32 v14, v26, v14
	v_mul_f32_e32 v15, v27, v15
	v_mul_f32_e32 v16, v28, v16
	v_mul_f32_e32 v17, v29, v17
	v_mul_f32_e32 v20, v26, v20
	v_mul_f32_e32 v21, v27, v21
	v_mul_f32_e32 v46, v28, v46
	v_mul_f32_e32 v47, v29, v47
	v_mul_f32_e32 v24, v26, v24
	v_mul_f32_e32 v25, v27, v25
	v_mul_f32_e32 v44, v28, v44
	v_mul_f32_e32 v45, v29, v45
	v_mul_f32_e32 v50, v26, v50
	v_mul_f32_e32 v51, v27, v51
	v_mul_f32_e32 v48, v28, v48
	v_mul_f32_e32 v49, v29, v49
	v_mul_f32_e32 v54, v26, v54
	v_mul_f32_e32 v55, v27, v55
	v_mul_f32_e32 v52, v28, v52
	v_mul_f32_e32 v53, v29, v53
	v_mul_f32_e32 v58, v26, v58
	v_mul_f32_e32 v59, v27, v59
	v_mul_f32_e32 v56, v28, v56
	v_mul_f32_e32 v57, v29, v57
	v_mul_f32_e32 v62, v26, v62
	v_mul_f32_e32 v63, v27, v63
	v_mul_f32_e32 v60, v28, v60
	v_mul_f32_e32 v61, v29, v61
	v_mul_f32_e32 v40, v26, v40
	v_mul_f32_e32 v41, v27, v41
	v_mul_f32_e32 v42, v28, v42
	v_mul_f32_e32 v43, v29, v43
	v_rndne_f32_e32 v14, v14
	v_rndne_f32_e32 v15, v15
	v_rndne_f32_e32 v16, v16
	v_rndne_f32_e32 v17, v17
	v_rndne_f32_e32 v20, v20
	v_rndne_f32_e32 v21, v21
	v_rndne_f32_e32 v46, v46
	v_rndne_f32_e32 v47, v47
	v_rndne_f32_e32 v24, v24
	v_rndne_f32_e32 v25, v25
	v_rndne_f32_e32 v44, v44
	v_rndne_f32_e32 v45, v45
	v_rndne_f32_e32 v50, v50
	v_rndne_f32_e32 v51, v51
	v_rndne_f32_e32 v48, v48
	v_rndne_f32_e32 v49, v49
	v_rndne_f32_e32 v54, v54
	v_rndne_f32_e32 v55, v55
	v_rndne_f32_e32 v52, v52
	v_rndne_f32_e32 v53, v53
	v_rndne_f32_e32 v58, v58
	v_rndne_f32_e32 v59, v59
	v_rndne_f32_e32 v56, v56
	v_rndne_f32_e32 v57, v57
	v_rndne_f32_e32 v62, v62
	v_rndne_f32_e32 v63, v63
	v_rndne_f32_e32 v60, v60
	v_rndne_f32_e32 v61, v61
	v_rndne_f32_e32 v40, v40
	v_rndne_f32_e32 v41, v41
	v_rndne_f32_e32 v42, v42
	v_rndne_f32_e32 v43, v43
	ds_write2_b32 v31, v14, v15 offset1:1
	ds_write2_b32 v31, v16, v17 offset0:2 offset1:3
	ds_write2_b32 v32, v20, v21 offset1:1
	ds_write2_b32 v33, v46, v47 offset1:1
	ds_write2_b32 v34, v24, v25 offset1:1
	ds_write2_b32 v35, v44, v45 offset1:1
	ds_write2_b32 v36, v50, v51 offset1:1
	ds_write2_b32 v37, v48, v49 offset1:1
	ds_write2_b32 v38, v54, v55 offset1:1
	ds_write2_b32 v39, v52, v53 offset1:1
	ds_write2_b32 v87, v58, v59 offset1:1
	ds_write2_b32 v88, v56, v57 offset1:1
	ds_write2_b32 v89, v62, v63 offset1:1
	ds_write2_b32 v90, v60, v61 offset1:1
	ds_write2_b32 v91, v40, v41 offset1:1
	ds_write2_b32 v92, v42, v43 offset1:1
	s_waitcnt lgkmcnt(0)
	ds_read2_b32 v[14:15], v30 offset1:8
	ds_read2_b32 v[16:17], v30 offset0:33 offset1:41
	ds_read2_b32 v[20:21], v30 offset0:66 offset1:74
	ds_read2_b32 v[24:25], v30 offset0:99 offset1:107
	ds_read2_b32 v[40:41], v30 offset0:132 offset1:140
	ds_read2_b32 v[42:43], v30 offset0:165 offset1:173
	ds_read2_b32 v[44:45], v30 offset0:198 offset1:206
	ds_read2_b32 v[46:47], v30 offset0:231 offset1:239
	ds_read2_b32 v[48:49], v30 offset0:16 offset1:24
	ds_read2_b32 v[50:51], v30 offset0:49 offset1:57
	ds_read2_b32 v[52:53], v30 offset0:82 offset1:90
	ds_read2_b32 v[54:55], v30 offset0:115 offset1:123
	ds_read2_b32 v[56:57], v30 offset0:148 offset1:156
	ds_read2_b32 v[58:59], v30 offset0:181 offset1:189
	ds_read2_b32 v[60:61], v30 offset0:214 offset1:222
	ds_read2_b32 v[62:63], v30 offset0:247 offset1:255
	s_waitcnt lgkmcnt(14)
	v_cvt_i32_f32_e32 v16, v16
	s_waitcnt lgkmcnt(10)
	v_cvt_i32_f32_e32 v42, v42
	v_cvt_i32_f32_e32 v14, v14
	v_cvt_i32_f32_sdwa v20, v20 dst_sel:WORD_1 dst_unused:UNUSED_PAD src0_sel:DWORD
	v_cvt_i32_f32_e32 v40, v40
	s_waitcnt lgkmcnt(9)
; #define LAS __attribute__((address_space(3)))
; #define GAS __attribute__((address_space(1)))
; #define LDS_WAIT() asm volatile("s_waitcnt lgkmcnt(0)" ::: "memory")
;     ...
;     for (int kb = 0; kb < D / 64; ++kb) {
; #pragma unroll
;         for (int i = 0; i < 8; ++i) { const int kk = 8 * i + kr; const int k = 64 * kb + kk; const f32x4 v = __builtin_nontemporal_load((const f32x4*)(W + (size_t)k * pitch)) * g[k];
;             LAS float* p = scr + kk * 33 + 4 * (lane & 7); p[0] = __builtin_rintf(v[0] * inv[0]); p[1] = __builtin_rintf(v[1] * inv[1]); p[2] = __builtin_rintf(v[2] * inv[2]); p[3] = __builtin_rintf(v[3] * inv[3]); }
;         LDS_WAIT(); asm volatile("" ::: "memory");
;         const int c = lane & 7;
; #pragma unroll
;         for (int j = 0; j < 4; ++j) { const int n = (lane >> 3) + 8 * j; const LAS float* sp = scr + (8 * c) * 33 + n;
;             u32x2 o;
;             o.x = ((unsigned)(int)sp[0 * 33] & 0xFFu) | (((unsigned)(int)sp[1 * 33] & 0xFFu) << 8) | (((unsigned)(int)sp[2 * 33] & 0xFFu) << 16) | (((unsigned)(int)sp[3 * 33] & 0xFFu) << 24);
;             o.y = ((unsigned)(int)sp[4 * 33] & 0xFFu) | (((unsigned)(int)sp[5 * 33] & 0xFFu) << 8) | (((unsigned)(int)sp[6 * 33] & 0xFFu) << 16) | (((unsigned)(int)sp[7 * 33] & 0xFFu) << 24);
;             *(GAS u32x2*)(dst + (size_t)(n0 + n) * D + 64 * kb + 8 * c) = o; }
;         LDS_WAIT(); asm volatile("" ::: "memory");
;     }
	v_cvt_i32_f32_sdwa v44, v44 dst_sel:WORD_1 dst_unused:UNUSED_PAD src0_sel:DWORD
	v_cvt_i32_f32_e32 v17, v17
	v_cvt_i32_f32_e32 v43, v43
	s_waitcnt lgkmcnt(6)
	v_cvt_i32_f32_e32 v50, v50
	s_waitcnt lgkmcnt(2)
	v_cvt_i32_f32_e32 v58, v58
	v_cvt_i32_f32_e32 v51, v51
	v_cvt_i32_f32_e32 v59, v59
	v_cvt_i32_f32_sdwa v24, v24 dst_sel:BYTE_3 dst_unused:UNUSED_PAD src0_sel:DWORD
	v_cvt_i32_f32_sdwa v46, v46 dst_sel:BYTE_3 dst_unused:UNUSED_PAD src0_sel:DWORD
	v_cvt_i32_f32_e32 v15, v15
	v_cvt_i32_f32_sdwa v21, v21 dst_sel:WORD_1 dst_unused:UNUSED_PAD src0_sel:DWORD
	v_cvt_i32_f32_e32 v41, v41
	v_cvt_i32_f32_sdwa v45, v45 dst_sel:WORD_1 dst_unused:UNUSED_PAD src0_sel:DWORD
	v_cvt_i32_f32_e32 v48, v48
	v_cvt_i32_f32_sdwa v52, v52 dst_sel:WORD_1 dst_unused:UNUSED_PAD src0_sel:DWORD
	v_cvt_i32_f32_e32 v56, v56
	s_waitcnt lgkmcnt(1)
	v_cvt_i32_f32_sdwa v60, v60 dst_sel:WORD_1 dst_unused:UNUSED_PAD src0_sel:DWORD
	v_cvt_i32_f32_e32 v49, v49
	v_cvt_i32_f32_sdwa v53, v53 dst_sel:WORD_1 dst_unused:UNUSED_PAD src0_sel:DWORD
	v_cvt_i32_f32_e32 v57, v57
	v_cvt_i32_f32_sdwa v61, v61 dst_sel:WORD_1 dst_unused:UNUSED_PAD src0_sel:DWORD
	v_cvt_i32_f32_sdwa v25, v25 dst_sel:BYTE_3 dst_unused:UNUSED_PAD src0_sel:DWORD
	v_cvt_i32_f32_sdwa v47, v47 dst_sel:BYTE_3 dst_unused:UNUSED_PAD src0_sel:DWORD
	v_cvt_i32_f32_sdwa v54, v54 dst_sel:BYTE_3 dst_unused:UNUSED_PAD src0_sel:DWORD
	s_waitcnt lgkmcnt(0)
	v_cvt_i32_f32_sdwa v62, v62 dst_sel:BYTE_3 dst_unused:UNUSED_PAD src0_sel:DWORD
	v_cvt_i32_f32_sdwa v55, v55 dst_sel:BYTE_3 dst_unused:UNUSED_PAD src0_sel:DWORD
	v_cvt_i32_f32_sdwa v63, v63 dst_sel:BYTE_3 dst_unused:UNUSED_PAD src0_sel:DWORD
	v_lshlrev_b32_e32 v16, 8, v16
	v_lshlrev_b32_e32 v42, 8, v42
	v_and_b32_e32 v20, 0xff0000, v20
	v_and_b32_e32 v44, 0xff0000, v44
	v_lshlrev_b32_e32 v17, 8, v17
	v_lshlrev_b32_e32 v43, 8, v43
	v_lshlrev_b32_e32 v50, 8, v50
	v_lshlrev_b32_e32 v58, 8, v58
	v_lshlrev_b32_e32 v51, 8, v51
	v_lshlrev_b32_e32 v59, 8, v59
	v_perm_b32 v14, v16, v14, s28
	v_perm_b32 v16, v42, v40, s28
	v_and_b32_e32 v21, 0xff0000, v21
	v_and_b32_e32 v45, 0xff0000, v45
	v_and_b32_e32 v52, 0xff0000, v52
	v_and_b32_e32 v60, 0xff0000, v60
	v_and_b32_e32 v53, 0xff0000, v53
	v_and_b32_e32 v61, 0xff0000, v61
	v_perm_b32 v17, v17, v15, s28
	v_perm_b32 v40, v43, v41, s28
	v_perm_b32 v41, v50, v48, s28
	v_perm_b32 v42, v58, v56, s28
	v_perm_b32 v43, v51, v49, s28
	v_perm_b32 v48, v59, v57, s28
	v_or3_b32 v14, v14, v20, v24
	v_or3_b32 v15, v16, v44, v46
	v_or3_b32 v16, v17, v21, v25
	v_or3_b32 v17, v40, v45, v47
	v_or3_b32 v20, v41, v52, v54
	v_or3_b32 v21, v42, v60, v62
	v_or3_b32 v24, v43, v53, v55
	v_or3_b32 v25, v48, v61, v63
	global_store_dwordx2 v[18:19], v[14:15], off
	global_store_dwordx2 v[22:23], v[16:17], off
	global_store_dwordx2 v[82:83], v[20:21], off
	global_store_dwordx2 v[84:85], v[24:25], off
	s_waitcnt lgkmcnt(0)
	v_add_u32_e32 v87, 0x14a0, v31
	v_add_u32_e32 v88, 0x14a8, v31
	v_add_u32_e32 v89, 0x18c0, v31
	v_add_u32_e32 v90, 0x18c8, v31
	v_add_u32_e32 v91, 0x1ce0, v31
	v_add_u32_e32 v92, 0x1ce8, v31
	v_lshl_add_u64 v[18:19], v[6:7], 0, v[12:13]
	v_lshl_add_u64 v[22:23], v[6:7], 0, v[10:11]
	v_lshl_add_u64 v[82:83], v[6:7], 0, v[8:9]
	v_lshl_add_u64 v[84:85], v[6:7], 0, v[4:5]
	v_lshl_add_u64 v[6:7], v[6:7], 0, 64
	s_waitcnt vmcnt(44)
	v_pk_mul_f32 v[46:47], v[176:177], v[236:237] op_sel_hi:[1,0]
	v_pk_mul_f32 v[20:21], v[174:175], v[236:237] op_sel_hi:[1,0]
	v_pk_mul_f32 v[44:45], v[180:181], v[238:239] op_sel_hi:[1,0]
	v_pk_mul_f32 v[24:25], v[178:179], v[238:239] op_sel_hi:[1,0]
	v_pk_mul_f32 v[48:49], v[184:185], v[240:241] op_sel_hi:[1,0]
	v_pk_mul_f32 v[16:17], v[172:173], v[234:235] op_sel_hi:[1,0]
	v_pk_mul_f32 v[14:15], v[170:171], v[234:235] op_sel_hi:[1,0]
	v_pk_mul_f32 v[50:51], v[182:183], v[240:241] op_sel_hi:[1,0]
	v_pk_mul_f32 v[52:53], v[188:189], v[242:243] op_sel_hi:[1,0]
	v_pk_mul_f32 v[54:55], v[186:187], v[242:243] op_sel_hi:[1,0]
	v_pk_mul_f32 v[56:57], v[192:193], v[244:245] op_sel_hi:[1,0]
	v_pk_mul_f32 v[58:59], v[190:191], v[244:245] op_sel_hi:[1,0]
	v_pk_mul_f32 v[60:61], v[196:197], v[246:247] op_sel_hi:[1,0]
	v_pk_mul_f32 v[62:63], v[194:195], v[246:247] op_sel_hi:[1,0]
	v_pk_mul_f32 v[42:43], v[200:201], v[248:249] op_sel_hi:[1,0]
	v_pk_mul_f32 v[40:41], v[198:199], v[248:249] op_sel_hi:[1,0]
	s_add_u32 s4, s4, 0x18000
	s_addc_u32 s5, s5, 0
	global_load_dwordx4 v[170:173], v250, s[4:5] nt
	global_load_dword v234, v251, s[6:7] offset:2816
	s_add_u32 s4, s4, 0x18000
	s_addc_u32 s5, s5, 0
	global_load_dwordx4 v[174:177], v250, s[4:5] nt
	global_load_dword v236, v251, s[6:7] offset:2848
	s_add_u32 s4, s4, 0x18000
	s_addc_u32 s5, s5, 0
	global_load_dwordx4 v[178:181], v250, s[4:5] nt
	global_load_dword v238, v251, s[6:7] offset:2880
	s_add_u32 s4, s4, 0x18000
	s_addc_u32 s5, s5, 0
	global_load_dwordx4 v[182:185], v250, s[4:5] nt
	global_load_dword v240, v251, s[6:7] offset:2912
	s_add_u32 s4, s4, 0x18000
	s_addc_u32 s5, s5, 0
	global_load_dwordx4 v[186:189], v250, s[4:5] nt
	global_load_dword v242, v251, s[6:7] offset:2944
	s_add_u32 s4, s4, 0x18000
	s_addc_u32 s5, s5, 0
	global_load_dwordx4 v[190:193], v250, s[4:5] nt
	global_load_dword v244, v251, s[6:7] offset:2976
	s_add_u32 s4, s4, 0x18000
	s_addc_u32 s5, s5, 0
	global_load_dwordx4 v[194:197], v250, s[4:5] nt
	global_load_dword v246, v251, s[6:7] offset:3008
	s_add_u32 s4, s4, 0x18000
	s_addc_u32 s5, s5, 0
	global_load_dwordx4 v[198:201], v250, s[4:5] nt
	global_load_dword v248, v251, s[6:7] offset:3040
	v_mul_f32_e32 v14, v26, v14
	v_mul_f32_e32 v15, v27, v15
	v_mul_f32_e32 v16, v28, v16
	v_mul_f32_e32 v17, v29, v17
	v_mul_f32_e32 v20, v26, v20
	v_mul_f32_e32 v21, v27, v21
; #define LAS __attribute__((address_space(3)))
; #define GAS __attribute__((address_space(1)))
; #define LDS_WAIT() asm volatile("s_waitcnt lgkmcnt(0)" ::: "memory")
;     ...
;         for (int i = 0; i < 8; ++i) { const int kk = 8 * i + kr; const int k = 64 * kb + kk; const f32x4 v = __builtin_nontemporal_load((const f32x4*)(W + (size_t)k * pitch)) * g[k];
;             LAS float* p = scr + kk * 33 + 4 * (lane & 7); p[0] = __builtin_rintf(v[0] * inv[0]); p[1] = __builtin_rintf(v[1] * inv[1]); p[2] = __builtin_rintf(v[2] * inv[2]); p[3] = __builtin_rintf(v[3] * inv[3]); }
;         LDS_WAIT(); asm volatile("" ::: "memory");
;         const int c = lane & 7;
; #pragma unroll
;         for (int j = 0; j < 4; ++j) { const int n = (lane >> 3) + 8 * j; const LAS float* sp = scr + (8 * c) * 33 + n;
;             u32x2 o;
;             o.x = ((unsigned)(int)sp[0 * 33] & 0xFFu) | (((unsigned)(int)sp[1 * 33] & 0xFFu) << 8) | (((unsigned)(int)sp[2 * 33] & 0xFFu) << 16) | (((unsigned)(int)sp[3 * 33] & 0xFFu) << 24);
;             o.y = ((unsigned)(int)sp[4 * 33] & 0xFFu) | (((unsigned)(int)sp[5 * 33] & 0xFFu) << 8) | (((unsigned)(int)sp[6 * 33] & 0xFFu) << 16) | (((unsigned)(int)sp[7 * 33] & 0xFFu) << 24);
;             *(GAS u32x2*)(dst + (size_t)(n0 + n) * D + 64 * kb + 8 * c) = o; }
;         LDS_WAIT(); asm volatile("" ::: "memory");
	v_mul_f32_e32 v46, v28, v46
	v_mul_f32_e32 v47, v29, v47
	v_mul_f32_e32 v24, v26, v24
	v_mul_f32_e32 v25, v27, v25
	v_mul_f32_e32 v44, v28, v44
	v_mul_f32_e32 v45, v29, v45
	v_mul_f32_e32 v50, v26, v50
	v_mul_f32_e32 v51, v27, v51
	v_mul_f32_e32 v48, v28, v48
	v_mul_f32_e32 v49, v29, v49
	v_mul_f32_e32 v54, v26, v54
	v_mul_f32_e32 v55, v27, v55
	v_mul_f32_e32 v52, v28, v52
	v_mul_f32_e32 v53, v29, v53
	v_mul_f32_e32 v58, v26, v58
	v_mul_f32_e32 v59, v27, v59
	v_mul_f32_e32 v56, v28, v56
	v_mul_f32_e32 v57, v29, v57
	v_mul_f32_e32 v62, v26, v62
	v_mul_f32_e32 v63, v27, v63
	v_mul_f32_e32 v60, v28, v60
	v_mul_f32_e32 v61, v29, v61
	v_mul_f32_e32 v40, v26, v40
	v_mul_f32_e32 v41, v27, v41
	v_mul_f32_e32 v42, v28, v42
	v_mul_f32_e32 v43, v29, v43
	v_rndne_f32_e32 v14, v14
	v_rndne_f32_e32 v15, v15
	v_rndne_f32_e32 v16, v16
	v_rndne_f32_e32 v17, v17
	v_rndne_f32_e32 v20, v20
	v_rndne_f32_e32 v21, v21
	v_rndne_f32_e32 v46, v46
	v_rndne_f32_e32 v47, v47
	v_rndne_f32_e32 v24, v24
	v_rndne_f32_e32 v25, v25
	v_rndne_f32_e32 v44, v44
	v_rndne_f32_e32 v45, v45
	v_rndne_f32_e32 v50, v50
	v_rndne_f32_e32 v51, v51
	v_rndne_f32_e32 v48, v48
	v_rndne_f32_e32 v49, v49
	v_rndne_f32_e32 v54, v54
	v_rndne_f32_e32 v55, v55
	v_rndne_f32_e32 v52, v52
	v_rndne_f32_e32 v53, v53
	v_rndne_f32_e32 v58, v58
	v_rndne_f32_e32 v59, v59
	v_rndne_f32_e32 v56, v56
	v_rndne_f32_e32 v57, v57
	v_rndne_f32_e32 v62, v62
	v_rndne_f32_e32 v63, v63
	v_rndne_f32_e32 v60, v60
	v_rndne_f32_e32 v61, v61
	v_rndne_f32_e32 v40, v40
	v_rndne_f32_e32 v41, v41
	v_rndne_f32_e32 v42, v42
	v_rndne_f32_e32 v43, v43
	ds_write2_b32 v31, v14, v15 offset1:1
	ds_write2_b32 v31, v16, v17 offset0:2 offset1:3
	ds_write2_b32 v32, v20, v21 offset1:1
	ds_write2_b32 v33, v46, v47 offset1:1
	ds_write2_b32 v34, v24, v25 offset1:1
	ds_write2_b32 v35, v44, v45 offset1:1
	ds_write2_b32 v36, v50, v51 offset1:1
	ds_write2_b32 v37, v48, v49 offset1:1
	ds_write2_b32 v38, v54, v55 offset1:1
	ds_write2_b32 v39, v52, v53 offset1:1
	ds_write2_b32 v87, v58, v59 offset1:1
	ds_write2_b32 v88, v56, v57 offset1:1
	ds_write2_b32 v89, v62, v63 offset1:1
	ds_write2_b32 v90, v60, v61 offset1:1
	ds_write2_b32 v91, v40, v41 offset1:1
	ds_write2_b32 v92, v42, v43 offset1:1
	s_waitcnt lgkmcnt(0)
	ds_read2_b32 v[14:15], v30 offset1:8
	ds_read2_b32 v[16:17], v30 offset0:33 offset1:41
	ds_read2_b32 v[20:21], v30 offset0:66 offset1:74
	ds_read2_b32 v[24:25], v30 offset0:99 offset1:107
	ds_read2_b32 v[40:41], v30 offset0:132 offset1:140
	ds_read2_b32 v[42:43], v30 offset0:165 offset1:173
	ds_read2_b32 v[44:45], v30 offset0:198 offset1:206
	ds_read2_b32 v[46:47], v30 offset0:231 offset1:239
	ds_read2_b32 v[48:49], v30 offset0:16 offset1:24
	ds_read2_b32 v[50:51], v30 offset0:49 offset1:57
	ds_read2_b32 v[52:53], v30 offset0:82 offset1:90
	ds_read2_b32 v[54:55], v30 offset0:115 offset1:123
	ds_read2_b32 v[56:57], v30 offset0:148 offset1:156
	ds_read2_b32 v[58:59], v30 offset0:181 offset1:189
	ds_read2_b32 v[60:61], v30 offset0:214 offset1:222
	ds_read2_b32 v[62:63], v30 offset0:247 offset1:255
	s_waitcnt lgkmcnt(14)
	v_cvt_i32_f32_e32 v16, v16
	s_waitcnt lgkmcnt(10)
	v_cvt_i32_f32_e32 v42, v42
	v_cvt_i32_f32_e32 v14, v14
	v_cvt_i32_f32_sdwa v20, v20 dst_sel:WORD_1 dst_unused:UNUSED_PAD src0_sel:DWORD
	v_cvt_i32_f32_e32 v40, v40
	s_waitcnt lgkmcnt(9)
	v_cvt_i32_f32_sdwa v44, v44 dst_sel:WORD_1 dst_unused:UNUSED_PAD src0_sel:DWORD
	v_cvt_i32_f32_e32 v17, v17
	v_cvt_i32_f32_e32 v43, v43
	s_waitcnt lgkmcnt(6)
	v_cvt_i32_f32_e32 v50, v50
	s_waitcnt lgkmcnt(2)
	v_cvt_i32_f32_e32 v58, v58
	v_cvt_i32_f32_e32 v51, v51
	v_cvt_i32_f32_e32 v59, v59
	v_cvt_i32_f32_sdwa v24, v24 dst_sel:BYTE_3 dst_unused:UNUSED_PAD src0_sel:DWORD
	v_cvt_i32_f32_sdwa v46, v46 dst_sel:BYTE_3 dst_unused:UNUSED_PAD src0_sel:DWORD
	v_cvt_i32_f32_e32 v15, v15
	v_cvt_i32_f32_sdwa v21, v21 dst_sel:WORD_1 dst_unused:UNUSED_PAD src0_sel:DWORD
	v_cvt_i32_f32_e32 v41, v41
	v_cvt_i32_f32_sdwa v45, v45 dst_sel:WORD_1 dst_unused:UNUSED_PAD src0_sel:DWORD
	v_cvt_i32_f32_e32 v48, v48
	v_cvt_i32_f32_sdwa v52, v52 dst_sel:WORD_1 dst_unused:UNUSED_PAD src0_sel:DWORD
	v_cvt_i32_f32_e32 v56, v56
	s_waitcnt lgkmcnt(1)
	v_cvt_i32_f32_sdwa v60, v60 dst_sel:WORD_1 dst_unused:UNUSED_PAD src0_sel:DWORD
	v_cvt_i32_f32_e32 v49, v49
	v_cvt_i32_f32_sdwa v53, v53 dst_sel:WORD_1 dst_unused:UNUSED_PAD src0_sel:DWORD
	v_cvt_i32_f32_e32 v57, v57
	v_cvt_i32_f32_sdwa v61, v61 dst_sel:WORD_1 dst_unused:UNUSED_PAD src0_sel:DWORD
	v_cvt_i32_f32_sdwa v25, v25 dst_sel:BYTE_3 dst_unused:UNUSED_PAD src0_sel:DWORD
	v_cvt_i32_f32_sdwa v47, v47 dst_sel:BYTE_3 dst_unused:UNUSED_PAD src0_sel:DWORD
	v_cvt_i32_f32_sdwa v54, v54 dst_sel:BYTE_3 dst_unused:UNUSED_PAD src0_sel:DWORD
	s_waitcnt lgkmcnt(0)
	v_cvt_i32_f32_sdwa v62, v62 dst_sel:BYTE_3 dst_unused:UNUSED_PAD src0_sel:DWORD
	v_cvt_i32_f32_sdwa v55, v55 dst_sel:BYTE_3 dst_unused:UNUSED_PAD src0_sel:DWORD
	v_cvt_i32_f32_sdwa v63, v63 dst_sel:BYTE_3 dst_unused:UNUSED_PAD src0_sel:DWORD
	v_lshlrev_b32_e32 v16, 8, v16
	v_lshlrev_b32_e32 v42, 8, v42
	v_and_b32_e32 v20, 0xff0000, v20
	v_and_b32_e32 v44, 0xff0000, v44
	v_lshlrev_b32_e32 v17, 8, v17
	v_lshlrev_b32_e32 v43, 8, v43
	v_lshlrev_b32_e32 v50, 8, v50
	v_lshlrev_b32_e32 v58, 8, v58
	v_lshlrev_b32_e32 v51, 8, v51
	v_lshlrev_b32_e32 v59, 8, v59
	v_perm_b32 v14, v16, v14, s28
	v_perm_b32 v16, v42, v40, s28
	v_and_b32_e32 v21, 0xff0000, v21
	v_and_b32_e32 v45, 0xff0000, v45
	v_and_b32_e32 v52, 0xff0000, v52
	v_and_b32_e32 v60, 0xff0000, v60
	v_and_b32_e32 v53, 0xff0000, v53
	v_and_b32_e32 v61, 0xff0000, v61
	v_perm_b32 v17, v17, v15, s28
	v_perm_b32 v40, v43, v41, s28
	v_perm_b32 v41, v50, v48, s28
	v_perm_b32 v42, v58, v56, s28
	v_perm_b32 v43, v51, v49, s28
	v_perm_b32 v48, v59, v57, s28
	v_or3_b32 v14, v14, v20, v24
	v_or3_b32 v15, v16, v44, v46
	v_or3_b32 v16, v17, v21, v25
	v_or3_b32 v17, v40, v45, v47
	v_or3_b32 v20, v41, v52, v54
	v_or3_b32 v21, v42, v60, v62
	v_or3_b32 v24, v43, v53, v55
	v_or3_b32 v25, v48, v61, v63
	global_store_dwordx2 v[18:19], v[14:15], off
	global_store_dwordx2 v[22:23], v[16:17], off
	global_store_dwordx2 v[82:83], v[20:21], off
	global_store_dwordx2 v[84:85], v[24:25], off
	s_waitcnt lgkmcnt(0)
; #define LAS __attribute__((address_space(3)))
; #define GAS __attribute__((address_space(1)))
; #define LDS_WAIT() asm volatile("s_waitcnt lgkmcnt(0)" ::: "memory")
;     ...
;     for (int kb = 0; kb < D / 64; ++kb) {
; #pragma unroll
;         for (int i = 0; i < 8; ++i) { const int kk = 8 * i + kr; const int k = 64 * kb + kk; const f32x4 v = __builtin_nontemporal_load((const f32x4*)(W + (size_t)k * pitch)) * g[k];
;             LAS float* p = scr + kk * 33 + 4 * (lane & 7); p[0] = __builtin_rintf(v[0] * inv[0]); p[1] = __builtin_rintf(v[1] * inv[1]); p[2] = __builtin_rintf(v[2] * inv[2]); p[3] = __builtin_rintf(v[3] * inv[3]); }
;         LDS_WAIT(); asm volatile("" ::: "memory");
;         const int c = lane & 7;
; #pragma unroll
;         for (int j = 0; j < 4; ++j) { const int n = (lane >> 3) + 8 * j; const LAS float* sp = scr + (8 * c) * 33 + n;
;             u32x2 o;
;             o.x = ((unsigned)(int)sp[0 * 33] & 0xFFu) | (((unsigned)(int)sp[1 * 33] & 0xFFu) << 8) | (((unsigned)(int)sp[2 * 33] & 0xFFu) << 16) | (((unsigned)(int)sp[3 * 33] & 0xFFu) << 24);
;             o.y = ((unsigned)(int)sp[4 * 33] & 0xFFu) | (((unsigned)(int)sp[5 * 33] & 0xFFu) << 8) | (((unsigned)(int)sp[6 * 33] & 0xFFu) << 16) | (((unsigned)(int)sp[7 * 33] & 0xFFu) << 24);
;             *(GAS u32x2*)(dst + (size_t)(n0 + n) * D + 64 * kb + 8 * c) = o; }
;         LDS_WAIT(); asm volatile("" ::: "memory");
	v_add_u32_e32 v87, 0x14a0, v31
	v_add_u32_e32 v88, 0x14a8, v31
	v_add_u32_e32 v89, 0x18c0, v31
	v_add_u32_e32 v90, 0x18c8, v31
	v_add_u32_e32 v91, 0x1ce0, v31
	v_add_u32_e32 v92, 0x1ce8, v31
	v_lshl_add_u64 v[18:19], v[6:7], 0, v[12:13]
	v_lshl_add_u64 v[22:23], v[6:7], 0, v[10:11]
	v_lshl_add_u64 v[82:83], v[6:7], 0, v[8:9]
	v_lshl_add_u64 v[84:85], v[6:7], 0, v[4:5]
	v_lshl_add_u64 v[6:7], v[6:7], 0, 64
	s_waitcnt vmcnt(44)
	v_pk_mul_f32 v[46:47], v[112:113], v[204:205] op_sel_hi:[1,0]
	v_pk_mul_f32 v[20:21], v[110:111], v[204:205] op_sel_hi:[1,0]
	v_pk_mul_f32 v[44:45], v[116:117], v[206:207] op_sel_hi:[1,0]
	v_pk_mul_f32 v[24:25], v[114:115], v[206:207] op_sel_hi:[1,0]
	v_pk_mul_f32 v[48:49], v[120:121], v[208:209] op_sel_hi:[1,0]
	v_pk_mul_f32 v[16:17], v[108:109], v[202:203] op_sel_hi:[1,0]
	v_pk_mul_f32 v[14:15], v[106:107], v[202:203] op_sel_hi:[1,0]
	v_pk_mul_f32 v[50:51], v[118:119], v[208:209] op_sel_hi:[1,0]
	v_pk_mul_f32 v[52:53], v[124:125], v[210:211] op_sel_hi:[1,0]
	v_pk_mul_f32 v[54:55], v[122:123], v[210:211] op_sel_hi:[1,0]
	v_pk_mul_f32 v[56:57], v[128:129], v[212:213] op_sel_hi:[1,0]
	v_pk_mul_f32 v[58:59], v[126:127], v[212:213] op_sel_hi:[1,0]
	v_pk_mul_f32 v[60:61], v[132:133], v[214:215] op_sel_hi:[1,0]
	v_pk_mul_f32 v[62:63], v[130:131], v[214:215] op_sel_hi:[1,0]
	v_pk_mul_f32 v[42:43], v[136:137], v[216:217] op_sel_hi:[1,0]
	v_pk_mul_f32 v[40:41], v[134:135], v[216:217] op_sel_hi:[1,0]
	s_add_u32 s4, s4, 0x18000
	s_addc_u32 s5, s5, 0
	global_load_dwordx4 v[106:109], v250, s[4:5] nt
	global_load_dword v202, v251, s[6:7] offset:3072
	s_add_u32 s4, s4, 0x18000
	s_addc_u32 s5, s5, 0
	global_load_dwordx4 v[110:113], v250, s[4:5] nt
	global_load_dword v204, v251, s[6:7] offset:3104
	s_add_u32 s4, s4, 0x18000
	s_addc_u32 s5, s5, 0
	global_load_dwordx4 v[114:117], v250, s[4:5] nt
	global_load_dword v206, v251, s[6:7] offset:3136
	s_add_u32 s4, s4, 0x18000
	s_addc_u32 s5, s5, 0
	global_load_dwordx4 v[118:121], v250, s[4:5] nt
	global_load_dword v208, v251, s[6:7] offset:3168
	s_add_u32 s4, s4, 0x18000
	s_addc_u32 s5, s5, 0
	global_load_dwordx4 v[122:125], v250, s[4:5] nt
	global_load_dword v210, v251, s[6:7] offset:3200
	s_add_u32 s4, s4, 0x18000
	s_addc_u32 s5, s5, 0
	global_load_dwordx4 v[126:129], v250, s[4:5] nt
	global_load_dword v212, v251, s[6:7] offset:3232
	s_add_u32 s4, s4, 0x18000
	s_addc_u32 s5, s5, 0
	global_load_dwordx4 v[130:133], v250, s[4:5] nt
	global_load_dword v214, v251, s[6:7] offset:3264
	s_add_u32 s4, s4, 0x18000
	s_addc_u32 s5, s5, 0
	global_load_dwordx4 v[134:137], v250, s[4:5] nt
	global_load_dword v216, v251, s[6:7] offset:3296
	v_mul_f32_e32 v14, v26, v14
	v_mul_f32_e32 v15, v27, v15
	v_mul_f32_e32 v16, v28, v16
	v_mul_f32_e32 v17, v29, v17
	v_mul_f32_e32 v20, v26, v20
	v_mul_f32_e32 v21, v27, v21
	v_mul_f32_e32 v46, v28, v46
	v_mul_f32_e32 v47, v29, v47
	v_mul_f32_e32 v24, v26, v24
	v_mul_f32_e32 v25, v27, v25
	v_mul_f32_e32 v44, v28, v44
	v_mul_f32_e32 v45, v29, v45
	v_mul_f32_e32 v50, v26, v50
	v_mul_f32_e32 v51, v27, v51
	v_mul_f32_e32 v48, v28, v48
	v_mul_f32_e32 v49, v29, v49
	v_mul_f32_e32 v54, v26, v54
	v_mul_f32_e32 v55, v27, v55
	v_mul_f32_e32 v52, v28, v52
	v_mul_f32_e32 v53, v29, v53
	v_mul_f32_e32 v58, v26, v58
	v_mul_f32_e32 v59, v27, v59
	v_mul_f32_e32 v56, v28, v56
	v_mul_f32_e32 v57, v29, v57
	v_mul_f32_e32 v62, v26, v62
	v_mul_f32_e32 v63, v27, v63
	v_mul_f32_e32 v60, v28, v60
	v_mul_f32_e32 v61, v29, v61
	v_mul_f32_e32 v40, v26, v40
	v_mul_f32_e32 v41, v27, v41
	v_mul_f32_e32 v42, v28, v42
	v_mul_f32_e32 v43, v29, v43
	v_rndne_f32_e32 v14, v14
	v_rndne_f32_e32 v15, v15
	v_rndne_f32_e32 v16, v16
	v_rndne_f32_e32 v17, v17
	v_rndne_f32_e32 v20, v20
	v_rndne_f32_e32 v21, v21
	v_rndne_f32_e32 v46, v46
	v_rndne_f32_e32 v47, v47
	v_rndne_f32_e32 v24, v24
	v_rndne_f32_e32 v25, v25
	v_rndne_f32_e32 v44, v44
	v_rndne_f32_e32 v45, v45
	v_rndne_f32_e32 v50, v50
	v_rndne_f32_e32 v51, v51
	v_rndne_f32_e32 v48, v48
	v_rndne_f32_e32 v49, v49
	v_rndne_f32_e32 v54, v54
	v_rndne_f32_e32 v55, v55
	v_rndne_f32_e32 v52, v52
	v_rndne_f32_e32 v53, v53
	v_rndne_f32_e32 v58, v58
	v_rndne_f32_e32 v59, v59
	v_rndne_f32_e32 v56, v56
	v_rndne_f32_e32 v57, v57
	v_rndne_f32_e32 v62, v62
	v_rndne_f32_e32 v63, v63
	v_rndne_f32_e32 v60, v60
	v_rndne_f32_e32 v61, v61
	v_rndne_f32_e32 v40, v40
	v_rndne_f32_e32 v41, v41
	v_rndne_f32_e32 v42, v42
	v_rndne_f32_e32 v43, v43
	ds_write2_b32 v31, v14, v15 offset1:1
	ds_write2_b32 v31, v16, v17 offset0:2 offset1:3
	ds_write2_b32 v32, v20, v21 offset1:1
	ds_write2_b32 v33, v46, v47 offset1:1
	ds_write2_b32 v34, v24, v25 offset1:1
	ds_write2_b32 v35, v44, v45 offset1:1
	ds_write2_b32 v36, v50, v51 offset1:1
	ds_write2_b32 v37, v48, v49 offset1:1
	ds_write2_b32 v38, v54, v55 offset1:1
	ds_write2_b32 v39, v52, v53 offset1:1
	ds_write2_b32 v87, v58, v59 offset1:1
	ds_write2_b32 v88, v56, v57 offset1:1
	ds_write2_b32 v89, v62, v63 offset1:1
	ds_write2_b32 v90, v60, v61 offset1:1
	ds_write2_b32 v91, v40, v41 offset1:1
	ds_write2_b32 v92, v42, v43 offset1:1
	s_waitcnt lgkmcnt(0)
	ds_read2_b32 v[14:15], v30 offset1:8
	ds_read2_b32 v[16:17], v30 offset0:33 offset1:41
	ds_read2_b32 v[20:21], v30 offset0:66 offset1:74
	ds_read2_b32 v[24:25], v30 offset0:99 offset1:107
	ds_read2_b32 v[40:41], v30 offset0:132 offset1:140
	ds_read2_b32 v[42:43], v30 offset0:165 offset1:173
	ds_read2_b32 v[44:45], v30 offset0:198 offset1:206
	ds_read2_b32 v[46:47], v30 offset0:231 offset1:239
	ds_read2_b32 v[48:49], v30 offset0:16 offset1:24
	ds_read2_b32 v[50:51], v30 offset0:49 offset1:57
	ds_read2_b32 v[52:53], v30 offset0:82 offset1:90
	ds_read2_b32 v[54:55], v30 offset0:115 offset1:123
	ds_read2_b32 v[56:57], v30 offset0:148 offset1:156
	ds_read2_b32 v[58:59], v30 offset0:181 offset1:189
	ds_read2_b32 v[60:61], v30 offset0:214 offset1:222
	ds_read2_b32 v[62:63], v30 offset0:247 offset1:255
	s_waitcnt lgkmcnt(14)
; #define LAS __attribute__((address_space(3)))
; #define GAS __attribute__((address_space(1)))
; #define LDS_WAIT() asm volatile("s_waitcnt lgkmcnt(0)" ::: "memory")
;     ...
;     for (int kb = 0; kb < D / 64; ++kb) {
; #pragma unroll
;         for (int i = 0; i < 8; ++i) { const int kk = 8 * i + kr; const int k = 64 * kb + kk; const f32x4 v = __builtin_nontemporal_load((const f32x4*)(W + (size_t)k * pitch)) * g[k];
;             LAS float* p = scr + kk * 33 + 4 * (lane & 7); p[0] = __builtin_rintf(v[0] * inv[0]); p[1] = __builtin_rintf(v[1] * inv[1]); p[2] = __builtin_rintf(v[2] * inv[2]); p[3] = __builtin_rintf(v[3] * inv[3]); }
;         LDS_WAIT(); asm volatile("" ::: "memory");
;         const int c = lane & 7;
; #pragma unroll
;         for (int j = 0; j < 4; ++j) { const int n = (lane >> 3) + 8 * j; const LAS float* sp = scr + (8 * c) * 33 + n;
;             u32x2 o;
;             o.x = ((unsigned)(int)sp[0 * 33] & 0xFFu) | (((unsigned)(int)sp[1 * 33] & 0xFFu) << 8) | (((unsigned)(int)sp[2 * 33] & 0xFFu) << 16) | (((unsigned)(int)sp[3 * 33] & 0xFFu) << 24);
;             o.y = ((unsigned)(int)sp[4 * 33] & 0xFFu) | (((unsigned)(int)sp[5 * 33] & 0xFFu) << 8) | (((unsigned)(int)sp[6 * 33] & 0xFFu) << 16) | (((unsigned)(int)sp[7 * 33] & 0xFFu) << 24);
;             *(GAS u32x2*)(dst + (size_t)(n0 + n) * D + 64 * kb + 8 * c) = o; }
;         LDS_WAIT(); asm volatile("" ::: "memory");
;     }
	v_cvt_i32_f32_e32 v16, v16
	s_waitcnt lgkmcnt(10)
	v_cvt_i32_f32_e32 v42, v42
	v_cvt_i32_f32_e32 v14, v14
	v_cvt_i32_f32_sdwa v20, v20 dst_sel:WORD_1 dst_unused:UNUSED_PAD src0_sel:DWORD
	v_cvt_i32_f32_e32 v40, v40
	s_waitcnt lgkmcnt(9)
	v_cvt_i32_f32_sdwa v44, v44 dst_sel:WORD_1 dst_unused:UNUSED_PAD src0_sel:DWORD
	v_cvt_i32_f32_e32 v17, v17
	v_cvt_i32_f32_e32 v43, v43
	s_waitcnt lgkmcnt(6)
	v_cvt_i32_f32_e32 v50, v50
	s_waitcnt lgkmcnt(2)
	v_cvt_i32_f32_e32 v58, v58
	v_cvt_i32_f32_e32 v51, v51
	v_cvt_i32_f32_e32 v59, v59
	v_cvt_i32_f32_sdwa v24, v24 dst_sel:BYTE_3 dst_unused:UNUSED_PAD src0_sel:DWORD
	v_cvt_i32_f32_sdwa v46, v46 dst_sel:BYTE_3 dst_unused:UNUSED_PAD src0_sel:DWORD
	v_cvt_i32_f32_e32 v15, v15
	v_cvt_i32_f32_sdwa v21, v21 dst_sel:WORD_1 dst_unused:UNUSED_PAD src0_sel:DWORD
	v_cvt_i32_f32_e32 v41, v41
	v_cvt_i32_f32_sdwa v45, v45 dst_sel:WORD_1 dst_unused:UNUSED_PAD src0_sel:DWORD
	v_cvt_i32_f32_e32 v48, v48
	v_cvt_i32_f32_sdwa v52, v52 dst_sel:WORD_1 dst_unused:UNUSED_PAD src0_sel:DWORD
	v_cvt_i32_f32_e32 v56, v56
	s_waitcnt lgkmcnt(1)
	v_cvt_i32_f32_sdwa v60, v60 dst_sel:WORD_1 dst_unused:UNUSED_PAD src0_sel:DWORD
	v_cvt_i32_f32_e32 v49, v49
	v_cvt_i32_f32_sdwa v53, v53 dst_sel:WORD_1 dst_unused:UNUSED_PAD src0_sel:DWORD
	v_cvt_i32_f32_e32 v57, v57
	v_cvt_i32_f32_sdwa v61, v61 dst_sel:WORD_1 dst_unused:UNUSED_PAD src0_sel:DWORD
	v_cvt_i32_f32_sdwa v25, v25 dst_sel:BYTE_3 dst_unused:UNUSED_PAD src0_sel:DWORD
	v_cvt_i32_f32_sdwa v47, v47 dst_sel:BYTE_3 dst_unused:UNUSED_PAD src0_sel:DWORD
	v_cvt_i32_f32_sdwa v54, v54 dst_sel:BYTE_3 dst_unused:UNUSED_PAD src0_sel:DWORD
	s_waitcnt lgkmcnt(0)
	v_cvt_i32_f32_sdwa v62, v62 dst_sel:BYTE_3 dst_unused:UNUSED_PAD src0_sel:DWORD
	v_cvt_i32_f32_sdwa v55, v55 dst_sel:BYTE_3 dst_unused:UNUSED_PAD src0_sel:DWORD
	v_cvt_i32_f32_sdwa v63, v63 dst_sel:BYTE_3 dst_unused:UNUSED_PAD src0_sel:DWORD
	v_lshlrev_b32_e32 v16, 8, v16
	v_lshlrev_b32_e32 v42, 8, v42
	v_and_b32_e32 v20, 0xff0000, v20
	v_and_b32_e32 v44, 0xff0000, v44
	v_lshlrev_b32_e32 v17, 8, v17
	v_lshlrev_b32_e32 v43, 8, v43
	v_lshlrev_b32_e32 v50, 8, v50
	v_lshlrev_b32_e32 v58, 8, v58
	v_lshlrev_b32_e32 v51, 8, v51
	v_lshlrev_b32_e32 v59, 8, v59
	v_perm_b32 v14, v16, v14, s28
	v_perm_b32 v16, v42, v40, s28
	v_and_b32_e32 v21, 0xff0000, v21
	v_and_b32_e32 v45, 0xff0000, v45
	v_and_b32_e32 v52, 0xff0000, v52
	v_and_b32_e32 v60, 0xff0000, v60
	v_and_b32_e32 v53, 0xff0000, v53
	v_and_b32_e32 v61, 0xff0000, v61
	v_perm_b32 v17, v17, v15, s28
	v_perm_b32 v40, v43, v41, s28
	v_perm_b32 v41, v50, v48, s28
	v_perm_b32 v42, v58, v56, s28
	v_perm_b32 v43, v51, v49, s28
	v_perm_b32 v48, v59, v57, s28
	v_or3_b32 v14, v14, v20, v24
	v_or3_b32 v15, v16, v44, v46
	v_or3_b32 v16, v17, v21, v25
	v_or3_b32 v17, v40, v45, v47
	v_or3_b32 v20, v41, v52, v54
	v_or3_b32 v21, v42, v60, v62
	v_or3_b32 v24, v43, v53, v55
	v_or3_b32 v25, v48, v61, v63
	global_store_dwordx2 v[18:19], v[14:15], off
	global_store_dwordx2 v[22:23], v[16:17], off
	global_store_dwordx2 v[82:83], v[20:21], off
	global_store_dwordx2 v[84:85], v[24:25], off
	s_waitcnt lgkmcnt(0)
	v_add_u32_e32 v87, 0x14a0, v31
	v_add_u32_e32 v88, 0x14a8, v31
	v_add_u32_e32 v89, 0x18c0, v31
	v_add_u32_e32 v90, 0x18c8, v31
	v_add_u32_e32 v91, 0x1ce0, v31
	v_add_u32_e32 v92, 0x1ce8, v31
	v_lshl_add_u64 v[18:19], v[6:7], 0, v[12:13]
	v_lshl_add_u64 v[22:23], v[6:7], 0, v[10:11]
	v_lshl_add_u64 v[82:83], v[6:7], 0, v[8:9]
	v_lshl_add_u64 v[84:85], v[6:7], 0, v[4:5]
	v_lshl_add_u64 v[6:7], v[6:7], 0, 64
	s_waitcnt vmcnt(44)
	v_pk_mul_f32 v[46:47], v[144:145], v[220:221] op_sel_hi:[1,0]
	v_pk_mul_f32 v[20:21], v[142:143], v[220:221] op_sel_hi:[1,0]
	v_pk_mul_f32 v[44:45], v[148:149], v[222:223] op_sel_hi:[1,0]
	v_pk_mul_f32 v[24:25], v[146:147], v[222:223] op_sel_hi:[1,0]
	v_pk_mul_f32 v[48:49], v[152:153], v[224:225] op_sel_hi:[1,0]
	v_pk_mul_f32 v[16:17], v[140:141], v[218:219] op_sel_hi:[1,0]
	v_pk_mul_f32 v[14:15], v[138:139], v[218:219] op_sel_hi:[1,0]
	v_pk_mul_f32 v[50:51], v[150:151], v[224:225] op_sel_hi:[1,0]
	v_pk_mul_f32 v[52:53], v[156:157], v[226:227] op_sel_hi:[1,0]
	v_pk_mul_f32 v[54:55], v[154:155], v[226:227] op_sel_hi:[1,0]
	v_pk_mul_f32 v[56:57], v[160:161], v[228:229] op_sel_hi:[1,0]
	v_pk_mul_f32 v[58:59], v[158:159], v[228:229] op_sel_hi:[1,0]
	v_pk_mul_f32 v[60:61], v[164:165], v[230:231] op_sel_hi:[1,0]
	v_pk_mul_f32 v[62:63], v[162:163], v[230:231] op_sel_hi:[1,0]
	v_pk_mul_f32 v[42:43], v[168:169], v[232:233] op_sel_hi:[1,0]
	v_pk_mul_f32 v[40:41], v[166:167], v[232:233] op_sel_hi:[1,0]
	s_add_u32 s4, s4, 0x18000
	s_addc_u32 s5, s5, 0
	global_load_dwordx4 v[138:141], v250, s[4:5] nt
	global_load_dword v218, v251, s[6:7] offset:3328
	s_add_u32 s4, s4, 0x18000
	s_addc_u32 s5, s5, 0
	global_load_dwordx4 v[142:145], v250, s[4:5] nt
	global_load_dword v220, v251, s[6:7] offset:3360
	s_add_u32 s4, s4, 0x18000
	s_addc_u32 s5, s5, 0
	global_load_dwordx4 v[146:149], v250, s[4:5] nt
	global_load_dword v222, v251, s[6:7] offset:3392
	s_add_u32 s4, s4, 0x18000
	s_addc_u32 s5, s5, 0
	global_load_dwordx4 v[150:153], v250, s[4:5] nt
	global_load_dword v224, v251, s[6:7] offset:3424
	s_add_u32 s4, s4, 0x18000
	s_addc_u32 s5, s5, 0
	global_load_dwordx4 v[154:157], v250, s[4:5] nt
	global_load_dword v226, v251, s[6:7] offset:3456
	s_add_u32 s4, s4, 0x18000
	s_addc_u32 s5, s5, 0
	global_load_dwordx4 v[158:161], v250, s[4:5] nt
	global_load_dword v228, v251, s[6:7] offset:3488
	s_add_u32 s4, s4, 0x18000
	s_addc_u32 s5, s5, 0
	global_load_dwordx4 v[162:165], v250, s[4:5] nt
	global_load_dword v230, v251, s[6:7] offset:3520
	s_add_u32 s4, s4, 0x18000
	s_addc_u32 s5, s5, 0
	global_load_dwordx4 v[166:169], v250, s[4:5] nt
; #define LAS __attribute__((address_space(3)))
; #define GAS __attribute__((address_space(1)))
; #define LDS_WAIT() asm volatile("s_waitcnt lgkmcnt(0)" ::: "memory")
;     ...
;         for (int i = 0; i < 8; ++i) { const int kk = 8 * i + kr; const int k = 64 * kb + kk; const f32x4 v = __builtin_nontemporal_load((const f32x4*)(W + (size_t)k * pitch)) * g[k];
;             LAS float* p = scr + kk * 33 + 4 * (lane & 7); p[0] = __builtin_rintf(v[0] * inv[0]); p[1] = __builtin_rintf(v[1] * inv[1]); p[2] = __builtin_rintf(v[2] * inv[2]); p[3] = __builtin_rintf(v[3] * inv[3]); }
;         LDS_WAIT(); asm volatile("" ::: "memory");
;         const int c = lane & 7;
; #pragma unroll
;         for (int j = 0; j < 4; ++j) { const int n = (lane >> 3) + 8 * j; const LAS float* sp = scr + (8 * c) * 33 + n;
;             u32x2 o;
;             o.x = ((unsigned)(int)sp[0 * 33] & 0xFFu) | (((unsigned)(int)sp[1 * 33] & 0xFFu) << 8) | (((unsigned)(int)sp[2 * 33] & 0xFFu) << 16) | (((unsigned)(int)sp[3 * 33] & 0xFFu) << 24);
;             o.y = ((unsigned)(int)sp[4 * 33] & 0xFFu) | (((unsigned)(int)sp[5 * 33] & 0xFFu) << 8) | (((unsigned)(int)sp[6 * 33] & 0xFFu) << 16) | (((unsigned)(int)sp[7 * 33] & 0xFFu) << 24);
;             *(GAS u32x2*)(dst + (size_t)(n0 + n) * D + 64 * kb + 8 * c) = o; }
;         LDS_WAIT(); asm volatile("" ::: "memory");
	global_load_dword v232, v251, s[6:7] offset:3552
	v_mul_f32_e32 v14, v26, v14
	v_mul_f32_e32 v15, v27, v15
	v_mul_f32_e32 v16, v28, v16
	v_mul_f32_e32 v17, v29, v17
	v_mul_f32_e32 v20, v26, v20
	v_mul_f32_e32 v21, v27, v21
	v_mul_f32_e32 v46, v28, v46
	v_mul_f32_e32 v47, v29, v47
	v_mul_f32_e32 v24, v26, v24
	v_mul_f32_e32 v25, v27, v25
	v_mul_f32_e32 v44, v28, v44
	v_mul_f32_e32 v45, v29, v45
	v_mul_f32_e32 v50, v26, v50
	v_mul_f32_e32 v51, v27, v51
	v_mul_f32_e32 v48, v28, v48
	v_mul_f32_e32 v49, v29, v49
	v_mul_f32_e32 v54, v26, v54
	v_mul_f32_e32 v55, v27, v55
	v_mul_f32_e32 v52, v28, v52
	v_mul_f32_e32 v53, v29, v53
	v_mul_f32_e32 v58, v26, v58
	v_mul_f32_e32 v59, v27, v59
	v_mul_f32_e32 v56, v28, v56
	v_mul_f32_e32 v57, v29, v57
	v_mul_f32_e32 v62, v26, v62
	v_mul_f32_e32 v63, v27, v63
	v_mul_f32_e32 v60, v28, v60
	v_mul_f32_e32 v61, v29, v61
	v_mul_f32_e32 v40, v26, v40
	v_mul_f32_e32 v41, v27, v41
	v_mul_f32_e32 v42, v28, v42
	v_mul_f32_e32 v43, v29, v43
	v_rndne_f32_e32 v14, v14
	v_rndne_f32_e32 v15, v15
	v_rndne_f32_e32 v16, v16
	v_rndne_f32_e32 v17, v17
	v_rndne_f32_e32 v20, v20
	v_rndne_f32_e32 v21, v21
	v_rndne_f32_e32 v46, v46
	v_rndne_f32_e32 v47, v47
	v_rndne_f32_e32 v24, v24
	v_rndne_f32_e32 v25, v25
	v_rndne_f32_e32 v44, v44
	v_rndne_f32_e32 v45, v45
	v_rndne_f32_e32 v50, v50
	v_rndne_f32_e32 v51, v51
	v_rndne_f32_e32 v48, v48
	v_rndne_f32_e32 v49, v49
	v_rndne_f32_e32 v54, v54
	v_rndne_f32_e32 v55, v55
	v_rndne_f32_e32 v52, v52
	v_rndne_f32_e32 v53, v53
	v_rndne_f32_e32 v58, v58
	v_rndne_f32_e32 v59, v59
	v_rndne_f32_e32 v56, v56
	v_rndne_f32_e32 v57, v57
	v_rndne_f32_e32 v62, v62
	v_rndne_f32_e32 v63, v63
	v_rndne_f32_e32 v60, v60
	v_rndne_f32_e32 v61, v61
	v_rndne_f32_e32 v40, v40
	v_rndne_f32_e32 v41, v41
	v_rndne_f32_e32 v42, v42
	v_rndne_f32_e32 v43, v43
	ds_write2_b32 v31, v14, v15 offset1:1
	ds_write2_b32 v31, v16, v17 offset0:2 offset1:3
	ds_write2_b32 v32, v20, v21 offset1:1
	ds_write2_b32 v33, v46, v47 offset1:1
	ds_write2_b32 v34, v24, v25 offset1:1
	ds_write2_b32 v35, v44, v45 offset1:1
	ds_write2_b32 v36, v50, v51 offset1:1
	ds_write2_b32 v37, v48, v49 offset1:1
	ds_write2_b32 v38, v54, v55 offset1:1
	ds_write2_b32 v39, v52, v53 offset1:1
	ds_write2_b32 v87, v58, v59 offset1:1
	ds_write2_b32 v88, v56, v57 offset1:1
	ds_write2_b32 v89, v62, v63 offset1:1
	ds_write2_b32 v90, v60, v61 offset1:1
	ds_write2_b32 v91, v40, v41 offset1:1
	ds_write2_b32 v92, v42, v43 offset1:1
	s_waitcnt lgkmcnt(0)
	ds_read2_b32 v[14:15], v30 offset1:8
	ds_read2_b32 v[16:17], v30 offset0:33 offset1:41
	ds_read2_b32 v[20:21], v30 offset0:66 offset1:74
	ds_read2_b32 v[24:25], v30 offset0:99 offset1:107
	ds_read2_b32 v[40:41], v30 offset0:132 offset1:140
	ds_read2_b32 v[42:43], v30 offset0:165 offset1:173
	ds_read2_b32 v[44:45], v30 offset0:198 offset1:206
	ds_read2_b32 v[46:47], v30 offset0:231 offset1:239
	ds_read2_b32 v[48:49], v30 offset0:16 offset1:24
	ds_read2_b32 v[50:51], v30 offset0:49 offset1:57
	ds_read2_b32 v[52:53], v30 offset0:82 offset1:90
	ds_read2_b32 v[54:55], v30 offset0:115 offset1:123
	ds_read2_b32 v[56:57], v30 offset0:148 offset1:156
	ds_read2_b32 v[58:59], v30 offset0:181 offset1:189
	ds_read2_b32 v[60:61], v30 offset0:214 offset1:222
	ds_read2_b32 v[62:63], v30 offset0:247 offset1:255
	s_waitcnt lgkmcnt(14)
	v_cvt_i32_f32_e32 v16, v16
	s_waitcnt lgkmcnt(10)
	v_cvt_i32_f32_e32 v42, v42
	v_cvt_i32_f32_e32 v14, v14
	v_cvt_i32_f32_sdwa v20, v20 dst_sel:WORD_1 dst_unused:UNUSED_PAD src0_sel:DWORD
	v_cvt_i32_f32_e32 v40, v40
	s_waitcnt lgkmcnt(9)
	v_cvt_i32_f32_sdwa v44, v44 dst_sel:WORD_1 dst_unused:UNUSED_PAD src0_sel:DWORD
	v_cvt_i32_f32_e32 v17, v17
	v_cvt_i32_f32_e32 v43, v43
	s_waitcnt lgkmcnt(6)
	v_cvt_i32_f32_e32 v50, v50
	s_waitcnt lgkmcnt(2)
	v_cvt_i32_f32_e32 v58, v58
	v_cvt_i32_f32_e32 v51, v51
	v_cvt_i32_f32_e32 v59, v59
	v_cvt_i32_f32_sdwa v24, v24 dst_sel:BYTE_3 dst_unused:UNUSED_PAD src0_sel:DWORD
	v_cvt_i32_f32_sdwa v46, v46 dst_sel:BYTE_3 dst_unused:UNUSED_PAD src0_sel:DWORD
	v_cvt_i32_f32_e32 v15, v15
	v_cvt_i32_f32_sdwa v21, v21 dst_sel:WORD_1 dst_unused:UNUSED_PAD src0_sel:DWORD
	v_cvt_i32_f32_e32 v41, v41
	v_cvt_i32_f32_sdwa v45, v45 dst_sel:WORD_1 dst_unused:UNUSED_PAD src0_sel:DWORD
	v_cvt_i32_f32_e32 v48, v48
	v_cvt_i32_f32_sdwa v52, v52 dst_sel:WORD_1 dst_unused:UNUSED_PAD src0_sel:DWORD
	v_cvt_i32_f32_e32 v56, v56
	s_waitcnt lgkmcnt(1)
	v_cvt_i32_f32_sdwa v60, v60 dst_sel:WORD_1 dst_unused:UNUSED_PAD src0_sel:DWORD
	v_cvt_i32_f32_e32 v49, v49
	v_cvt_i32_f32_sdwa v53, v53 dst_sel:WORD_1 dst_unused:UNUSED_PAD src0_sel:DWORD
	v_cvt_i32_f32_e32 v57, v57
	v_cvt_i32_f32_sdwa v61, v61 dst_sel:WORD_1 dst_unused:UNUSED_PAD src0_sel:DWORD
	v_cvt_i32_f32_sdwa v25, v25 dst_sel:BYTE_3 dst_unused:UNUSED_PAD src0_sel:DWORD
	v_cvt_i32_f32_sdwa v47, v47 dst_sel:BYTE_3 dst_unused:UNUSED_PAD src0_sel:DWORD
	v_cvt_i32_f32_sdwa v54, v54 dst_sel:BYTE_3 dst_unused:UNUSED_PAD src0_sel:DWORD
	s_waitcnt lgkmcnt(0)
; #define LAS __attribute__((address_space(3)))
; #define GAS __attribute__((address_space(1)))
; #define LDS_WAIT() asm volatile("s_waitcnt lgkmcnt(0)" ::: "memory")
;     ...
;     for (int kb = 0; kb < D / 64; ++kb) {
; #pragma unroll
;         for (int i = 0; i < 8; ++i) { const int kk = 8 * i + kr; const int k = 64 * kb + kk; const f32x4 v = __builtin_nontemporal_load((const f32x4*)(W + (size_t)k * pitch)) * g[k];
;             LAS float* p = scr + kk * 33 + 4 * (lane & 7); p[0] = __builtin_rintf(v[0] * inv[0]); p[1] = __builtin_rintf(v[1] * inv[1]); p[2] = __builtin_rintf(v[2] * inv[2]); p[3] = __builtin_rintf(v[3] * inv[3]); }
;         LDS_WAIT(); asm volatile("" ::: "memory");
;         const int c = lane & 7;
; #pragma unroll
;         for (int j = 0; j < 4; ++j) { const int n = (lane >> 3) + 8 * j; const LAS float* sp = scr + (8 * c) * 33 + n;
;             u32x2 o;
;             o.x = ((unsigned)(int)sp[0 * 33] & 0xFFu) | (((unsigned)(int)sp[1 * 33] & 0xFFu) << 8) | (((unsigned)(int)sp[2 * 33] & 0xFFu) << 16) | (((unsigned)(int)sp[3 * 33] & 0xFFu) << 24);
;             o.y = ((unsigned)(int)sp[4 * 33] & 0xFFu) | (((unsigned)(int)sp[5 * 33] & 0xFFu) << 8) | (((unsigned)(int)sp[6 * 33] & 0xFFu) << 16) | (((unsigned)(int)sp[7 * 33] & 0xFFu) << 24);
;             *(GAS u32x2*)(dst + (size_t)(n0 + n) * D + 64 * kb + 8 * c) = o; }
;         LDS_WAIT(); asm volatile("" ::: "memory");
	v_cvt_i32_f32_sdwa v62, v62 dst_sel:BYTE_3 dst_unused:UNUSED_PAD src0_sel:DWORD
	v_cvt_i32_f32_sdwa v55, v55 dst_sel:BYTE_3 dst_unused:UNUSED_PAD src0_sel:DWORD
	v_cvt_i32_f32_sdwa v63, v63 dst_sel:BYTE_3 dst_unused:UNUSED_PAD src0_sel:DWORD
	v_lshlrev_b32_e32 v16, 8, v16
	v_lshlrev_b32_e32 v42, 8, v42
	v_and_b32_e32 v20, 0xff0000, v20
	v_and_b32_e32 v44, 0xff0000, v44
	v_lshlrev_b32_e32 v17, 8, v17
	v_lshlrev_b32_e32 v43, 8, v43
	v_lshlrev_b32_e32 v50, 8, v50
	v_lshlrev_b32_e32 v58, 8, v58
	v_lshlrev_b32_e32 v51, 8, v51
	v_lshlrev_b32_e32 v59, 8, v59
	v_perm_b32 v14, v16, v14, s28
	v_perm_b32 v16, v42, v40, s28
	v_and_b32_e32 v21, 0xff0000, v21
	v_and_b32_e32 v45, 0xff0000, v45
	v_and_b32_e32 v52, 0xff0000, v52
	v_and_b32_e32 v60, 0xff0000, v60
	v_and_b32_e32 v53, 0xff0000, v53
	v_and_b32_e32 v61, 0xff0000, v61
	v_perm_b32 v17, v17, v15, s28
	v_perm_b32 v40, v43, v41, s28
	v_perm_b32 v41, v50, v48, s28
	v_perm_b32 v42, v58, v56, s28
	v_perm_b32 v43, v51, v49, s28
	v_perm_b32 v48, v59, v57, s28
	v_or3_b32 v14, v14, v20, v24
	v_or3_b32 v15, v16, v44, v46
	v_or3_b32 v16, v17, v21, v25
	v_or3_b32 v17, v40, v45, v47
	v_or3_b32 v20, v41, v52, v54
	v_or3_b32 v21, v42, v60, v62
	v_or3_b32 v24, v43, v53, v55
	v_or3_b32 v25, v48, v61, v63
	global_store_dwordx2 v[18:19], v[14:15], off
	global_store_dwordx2 v[22:23], v[16:17], off
	global_store_dwordx2 v[82:83], v[20:21], off
	global_store_dwordx2 v[84:85], v[24:25], off
	s_waitcnt lgkmcnt(0)
	v_add_u32_e32 v87, 0x14a0, v31
	v_add_u32_e32 v88, 0x14a8, v31
	v_add_u32_e32 v89, 0x18c0, v31
	v_add_u32_e32 v90, 0x18c8, v31
	v_add_u32_e32 v91, 0x1ce0, v31
	v_add_u32_e32 v92, 0x1ce8, v31
	v_lshl_add_u64 v[18:19], v[6:7], 0, v[12:13]
	v_lshl_add_u64 v[22:23], v[6:7], 0, v[10:11]
	v_lshl_add_u64 v[82:83], v[6:7], 0, v[8:9]
	v_lshl_add_u64 v[84:85], v[6:7], 0, v[4:5]
	v_lshl_add_u64 v[6:7], v[6:7], 0, 64
	s_waitcnt vmcnt(44)
	v_pk_mul_f32 v[46:47], v[176:177], v[236:237] op_sel_hi:[1,0]
	v_pk_mul_f32 v[20:21], v[174:175], v[236:237] op_sel_hi:[1,0]
	v_pk_mul_f32 v[44:45], v[180:181], v[238:239] op_sel_hi:[1,0]
	v_pk_mul_f32 v[24:25], v[178:179], v[238:239] op_sel_hi:[1,0]
	v_pk_mul_f32 v[48:49], v[184:185], v[240:241] op_sel_hi:[1,0]
	v_pk_mul_f32 v[16:17], v[172:173], v[234:235] op_sel_hi:[1,0]
	v_pk_mul_f32 v[14:15], v[170:171], v[234:235] op_sel_hi:[1,0]
	v_pk_mul_f32 v[50:51], v[182:183], v[240:241] op_sel_hi:[1,0]
	v_pk_mul_f32 v[52:53], v[188:189], v[242:243] op_sel_hi:[1,0]
	v_pk_mul_f32 v[54:55], v[186:187], v[242:243] op_sel_hi:[1,0]
	v_pk_mul_f32 v[56:57], v[192:193], v[244:245] op_sel_hi:[1,0]
	v_pk_mul_f32 v[58:59], v[190:191], v[244:245] op_sel_hi:[1,0]
	v_pk_mul_f32 v[60:61], v[196:197], v[246:247] op_sel_hi:[1,0]
	v_pk_mul_f32 v[62:63], v[194:195], v[246:247] op_sel_hi:[1,0]
	v_pk_mul_f32 v[42:43], v[200:201], v[248:249] op_sel_hi:[1,0]
	v_pk_mul_f32 v[40:41], v[198:199], v[248:249] op_sel_hi:[1,0]
	s_add_u32 s4, s4, 0x18000
	s_addc_u32 s5, s5, 0
	global_load_dwordx4 v[170:173], v250, s[4:5] nt
	global_load_dword v234, v251, s[6:7] offset:3584
	s_add_u32 s4, s4, 0x18000
	s_addc_u32 s5, s5, 0
	global_load_dwordx4 v[174:177], v250, s[4:5] nt
	global_load_dword v236, v251, s[6:7] offset:3616
	s_add_u32 s4, s4, 0x18000
	s_addc_u32 s5, s5, 0
	global_load_dwordx4 v[178:181], v250, s[4:5] nt
	global_load_dword v238, v251, s[6:7] offset:3648
	s_add_u32 s4, s4, 0x18000
	s_addc_u32 s5, s5, 0
	global_load_dwordx4 v[182:185], v250, s[4:5] nt
	global_load_dword v240, v251, s[6:7] offset:3680
	s_add_u32 s4, s4, 0x18000
	s_addc_u32 s5, s5, 0
	global_load_dwordx4 v[186:189], v250, s[4:5] nt
	global_load_dword v242, v251, s[6:7] offset:3712
	s_add_u32 s4, s4, 0x18000
	s_addc_u32 s5, s5, 0
	global_load_dwordx4 v[190:193], v250, s[4:5] nt
	global_load_dword v244, v251, s[6:7] offset:3744
	s_add_u32 s4, s4, 0x18000
	s_addc_u32 s5, s5, 0
	global_load_dwordx4 v[194:197], v250, s[4:5] nt
	global_load_dword v246, v251, s[6:7] offset:3776
	s_add_u32 s4, s4, 0x18000
	s_addc_u32 s5, s5, 0
	global_load_dwordx4 v[198:201], v250, s[4:5] nt
	global_load_dword v248, v251, s[6:7] offset:3808
	v_mul_f32_e32 v14, v26, v14
	v_mul_f32_e32 v15, v27, v15
	v_mul_f32_e32 v16, v28, v16
	v_mul_f32_e32 v17, v29, v17
	v_mul_f32_e32 v20, v26, v20
	v_mul_f32_e32 v21, v27, v21
	v_mul_f32_e32 v46, v28, v46
	v_mul_f32_e32 v47, v29, v47
	v_mul_f32_e32 v24, v26, v24
	v_mul_f32_e32 v25, v27, v25
	v_mul_f32_e32 v44, v28, v44
	v_mul_f32_e32 v45, v29, v45
	v_mul_f32_e32 v50, v26, v50
	v_mul_f32_e32 v51, v27, v51
	v_mul_f32_e32 v48, v28, v48
	v_mul_f32_e32 v49, v29, v49
	v_mul_f32_e32 v54, v26, v54
	v_mul_f32_e32 v55, v27, v55
	v_mul_f32_e32 v52, v28, v52
	v_mul_f32_e32 v53, v29, v53
	v_mul_f32_e32 v58, v26, v58
	v_mul_f32_e32 v59, v27, v59
	v_mul_f32_e32 v56, v28, v56
	v_mul_f32_e32 v57, v29, v57
	v_mul_f32_e32 v62, v26, v62
	v_mul_f32_e32 v63, v27, v63
	v_mul_f32_e32 v60, v28, v60
	v_mul_f32_e32 v61, v29, v61
	v_mul_f32_e32 v40, v26, v40
	v_mul_f32_e32 v41, v27, v41
	v_mul_f32_e32 v42, v28, v42
	v_mul_f32_e32 v43, v29, v43
	v_rndne_f32_e32 v14, v14
	v_rndne_f32_e32 v15, v15
	v_rndne_f32_e32 v16, v16
	v_rndne_f32_e32 v17, v17
	v_rndne_f32_e32 v20, v20
	v_rndne_f32_e32 v21, v21
	v_rndne_f32_e32 v46, v46
	v_rndne_f32_e32 v47, v47
	v_rndne_f32_e32 v24, v24
	v_rndne_f32_e32 v25, v25
	v_rndne_f32_e32 v44, v44
	v_rndne_f32_e32 v45, v45
	v_rndne_f32_e32 v50, v50
	v_rndne_f32_e32 v51, v51
	v_rndne_f32_e32 v48, v48
	v_rndne_f32_e32 v49, v49
	v_rndne_f32_e32 v54, v54
	v_rndne_f32_e32 v55, v55
	v_rndne_f32_e32 v52, v52
	v_rndne_f32_e32 v53, v53
	v_rndne_f32_e32 v58, v58
	v_rndne_f32_e32 v59, v59
	v_rndne_f32_e32 v56, v56
	v_rndne_f32_e32 v57, v57
	v_rndne_f32_e32 v62, v62
	v_rndne_f32_e32 v63, v63
	v_rndne_f32_e32 v60, v60
	v_rndne_f32_e32 v61, v61
	v_rndne_f32_e32 v40, v40
	v_rndne_f32_e32 v41, v41
	v_rndne_f32_e32 v42, v42
	v_rndne_f32_e32 v43, v43
	ds_write2_b32 v31, v14, v15 offset1:1
	ds_write2_b32 v31, v16, v17 offset0:2 offset1:3
	ds_write2_b32 v32, v20, v21 offset1:1
	ds_write2_b32 v33, v46, v47 offset1:1
	ds_write2_b32 v34, v24, v25 offset1:1
	ds_write2_b32 v35, v44, v45 offset1:1
	ds_write2_b32 v36, v50, v51 offset1:1
	ds_write2_b32 v37, v48, v49 offset1:1
	ds_write2_b32 v38, v54, v55 offset1:1
	ds_write2_b32 v39, v52, v53 offset1:1
	ds_write2_b32 v87, v58, v59 offset1:1
	ds_write2_b32 v88, v56, v57 offset1:1
	ds_write2_b32 v89, v62, v63 offset1:1
	ds_write2_b32 v90, v60, v61 offset1:1
	ds_write2_b32 v91, v40, v41 offset1:1
	ds_write2_b32 v92, v42, v43 offset1:1
	s_waitcnt lgkmcnt(0)
; #define LAS __attribute__((address_space(3)))
; #define GAS __attribute__((address_space(1)))
; #define LDS_WAIT() asm volatile("s_waitcnt lgkmcnt(0)" ::: "memory")
;     ...
;         LDS_WAIT(); asm volatile("" ::: "memory");
;         const int c = lane & 7;
; #pragma unroll
;         for (int j = 0; j < 4; ++j) { const int n = (lane >> 3) + 8 * j; const LAS float* sp = scr + (8 * c) * 33 + n;
;             u32x2 o;
;             o.x = ((unsigned)(int)sp[0 * 33] & 0xFFu) | (((unsigned)(int)sp[1 * 33] & 0xFFu) << 8) | (((unsigned)(int)sp[2 * 33] & 0xFFu) << 16) | (((unsigned)(int)sp[3 * 33] & 0xFFu) << 24);
;             o.y = ((unsigned)(int)sp[4 * 33] & 0xFFu) | (((unsigned)(int)sp[5 * 33] & 0xFFu) << 8) | (((unsigned)(int)sp[6 * 33] & 0xFFu) << 16) | (((unsigned)(int)sp[7 * 33] & 0xFFu) << 24);
;             *(GAS u32x2*)(dst + (size_t)(n0 + n) * D + 64 * kb + 8 * c) = o; }
;         LDS_WAIT(); asm volatile("" ::: "memory");
;     }
	ds_read2_b32 v[14:15], v30 offset1:8
	ds_read2_b32 v[16:17], v30 offset0:33 offset1:41
	ds_read2_b32 v[20:21], v30 offset0:66 offset1:74
	ds_read2_b32 v[24:25], v30 offset0:99 offset1:107
	ds_read2_b32 v[40:41], v30 offset0:132 offset1:140
	ds_read2_b32 v[42:43], v30 offset0:165 offset1:173
	ds_read2_b32 v[44:45], v30 offset0:198 offset1:206
	ds_read2_b32 v[46:47], v30 offset0:231 offset1:239
	ds_read2_b32 v[48:49], v30 offset0:16 offset1:24
	ds_read2_b32 v[50:51], v30 offset0:49 offset1:57
	ds_read2_b32 v[52:53], v30 offset0:82 offset1:90
	ds_read2_b32 v[54:55], v30 offset0:115 offset1:123
	ds_read2_b32 v[56:57], v30 offset0:148 offset1:156
	ds_read2_b32 v[58:59], v30 offset0:181 offset1:189
	ds_read2_b32 v[60:61], v30 offset0:214 offset1:222
	ds_read2_b32 v[62:63], v30 offset0:247 offset1:255
	s_waitcnt lgkmcnt(14)
	v_cvt_i32_f32_e32 v16, v16
	s_waitcnt lgkmcnt(10)
	v_cvt_i32_f32_e32 v42, v42
	v_cvt_i32_f32_e32 v14, v14
	v_cvt_i32_f32_sdwa v20, v20 dst_sel:WORD_1 dst_unused:UNUSED_PAD src0_sel:DWORD
	v_cvt_i32_f32_e32 v40, v40
	s_waitcnt lgkmcnt(9)
	v_cvt_i32_f32_sdwa v44, v44 dst_sel:WORD_1 dst_unused:UNUSED_PAD src0_sel:DWORD
	v_cvt_i32_f32_e32 v17, v17
	v_cvt_i32_f32_e32 v43, v43
	s_waitcnt lgkmcnt(6)
	v_cvt_i32_f32_e32 v50, v50
	s_waitcnt lgkmcnt(2)
	v_cvt_i32_f32_e32 v58, v58
	v_cvt_i32_f32_e32 v51, v51
	v_cvt_i32_f32_e32 v59, v59
	v_cvt_i32_f32_sdwa v24, v24 dst_sel:BYTE_3 dst_unused:UNUSED_PAD src0_sel:DWORD
	v_cvt_i32_f32_sdwa v46, v46 dst_sel:BYTE_3 dst_unused:UNUSED_PAD src0_sel:DWORD
	v_cvt_i32_f32_e32 v15, v15
	v_cvt_i32_f32_sdwa v21, v21 dst_sel:WORD_1 dst_unused:UNUSED_PAD src0_sel:DWORD
	v_cvt_i32_f32_e32 v41, v41
	v_cvt_i32_f32_sdwa v45, v45 dst_sel:WORD_1 dst_unused:UNUSED_PAD src0_sel:DWORD
	v_cvt_i32_f32_e32 v48, v48
	v_cvt_i32_f32_sdwa v52, v52 dst_sel:WORD_1 dst_unused:UNUSED_PAD src0_sel:DWORD
	v_cvt_i32_f32_e32 v56, v56
	s_waitcnt lgkmcnt(1)
	v_cvt_i32_f32_sdwa v60, v60 dst_sel:WORD_1 dst_unused:UNUSED_PAD src0_sel:DWORD
	v_cvt_i32_f32_e32 v49, v49
	v_cvt_i32_f32_sdwa v53, v53 dst_sel:WORD_1 dst_unused:UNUSED_PAD src0_sel:DWORD
	v_cvt_i32_f32_e32 v57, v57
	v_cvt_i32_f32_sdwa v61, v61 dst_sel:WORD_1 dst_unused:UNUSED_PAD src0_sel:DWORD
	v_cvt_i32_f32_sdwa v25, v25 dst_sel:BYTE_3 dst_unused:UNUSED_PAD src0_sel:DWORD
	v_cvt_i32_f32_sdwa v47, v47 dst_sel:BYTE_3 dst_unused:UNUSED_PAD src0_sel:DWORD
	v_cvt_i32_f32_sdwa v54, v54 dst_sel:BYTE_3 dst_unused:UNUSED_PAD src0_sel:DWORD
	s_waitcnt lgkmcnt(0)
	v_cvt_i32_f32_sdwa v62, v62 dst_sel:BYTE_3 dst_unused:UNUSED_PAD src0_sel:DWORD
	v_cvt_i32_f32_sdwa v55, v55 dst_sel:BYTE_3 dst_unused:UNUSED_PAD src0_sel:DWORD
	v_cvt_i32_f32_sdwa v63, v63 dst_sel:BYTE_3 dst_unused:UNUSED_PAD src0_sel:DWORD
	v_lshlrev_b32_e32 v16, 8, v16
	v_lshlrev_b32_e32 v42, 8, v42
	v_and_b32_e32 v20, 0xff0000, v20
	v_and_b32_e32 v44, 0xff0000, v44
	v_lshlrev_b32_e32 v17, 8, v17
	v_lshlrev_b32_e32 v43, 8, v43
	v_lshlrev_b32_e32 v50, 8, v50
	v_lshlrev_b32_e32 v58, 8, v58
	v_lshlrev_b32_e32 v51, 8, v51
	v_lshlrev_b32_e32 v59, 8, v59
	v_perm_b32 v14, v16, v14, s28
	v_perm_b32 v16, v42, v40, s28
	v_and_b32_e32 v21, 0xff0000, v21
	v_and_b32_e32 v45, 0xff0000, v45
	v_and_b32_e32 v52, 0xff0000, v52
	v_and_b32_e32 v60, 0xff0000, v60
	v_and_b32_e32 v53, 0xff0000, v53
	v_and_b32_e32 v61, 0xff0000, v61
	v_perm_b32 v17, v17, v15, s28
	v_perm_b32 v40, v43, v41, s28
	v_perm_b32 v41, v50, v48, s28
	v_perm_b32 v42, v58, v56, s28
	v_perm_b32 v43, v51, v49, s28
	v_perm_b32 v48, v59, v57, s28
	v_or3_b32 v14, v14, v20, v24
	v_or3_b32 v15, v16, v44, v46
	v_or3_b32 v16, v17, v21, v25
	v_or3_b32 v17, v40, v45, v47
	v_or3_b32 v20, v41, v52, v54
	v_or3_b32 v21, v42, v60, v62
	v_or3_b32 v24, v43, v53, v55
	v_or3_b32 v25, v48, v61, v63
	global_store_dwordx2 v[18:19], v[14:15], off
	global_store_dwordx2 v[22:23], v[16:17], off
	global_store_dwordx2 v[82:83], v[20:21], off
	global_store_dwordx2 v[84:85], v[24:25], off
	s_waitcnt lgkmcnt(0)
	v_add_u32_e32 v87, 0x14a0, v31
	v_add_u32_e32 v88, 0x14a8, v31
	v_add_u32_e32 v89, 0x18c0, v31
	v_add_u32_e32 v90, 0x18c8, v31
	v_add_u32_e32 v91, 0x1ce0, v31
	v_add_u32_e32 v92, 0x1ce8, v31
	v_lshl_add_u64 v[18:19], v[6:7], 0, v[12:13]
	v_lshl_add_u64 v[22:23], v[6:7], 0, v[10:11]
	v_lshl_add_u64 v[82:83], v[6:7], 0, v[8:9]
	v_lshl_add_u64 v[84:85], v[6:7], 0, v[4:5]
	v_lshl_add_u64 v[6:7], v[6:7], 0, 64
	s_waitcnt vmcnt(44)
; #define LAS __attribute__((address_space(3)))
; #define GAS __attribute__((address_space(1)))
; #define LDS_WAIT() asm volatile("s_waitcnt lgkmcnt(0)" ::: "memory")
;     ...
;     for (int kb = 0; kb < D / 64; ++kb) {
; #pragma unroll
;         for (int i = 0; i < 8; ++i) { const int kk = 8 * i + kr; const int k = 64 * kb + kk; const f32x4 v = __builtin_nontemporal_load((const f32x4*)(W + (size_t)k * pitch)) * g[k];
;             LAS float* p = scr + kk * 33 + 4 * (lane & 7); p[0] = __builtin_rintf(v[0] * inv[0]); p[1] = __builtin_rintf(v[1] * inv[1]); p[2] = __builtin_rintf(v[2] * inv[2]); p[3] = __builtin_rintf(v[3] * inv[3]); }
;         LDS_WAIT(); asm volatile("" ::: "memory");
;         const int c = lane & 7;
; #pragma unroll
;         for (int j = 0; j < 4; ++j) { const int n = (lane >> 3) + 8 * j; const LAS float* sp = scr + (8 * c) * 33 + n;
;             u32x2 o;
;             o.x = ((unsigned)(int)sp[0 * 33] & 0xFFu) | (((unsigned)(int)sp[1 * 33] & 0xFFu) << 8) | (((unsigned)(int)sp[2 * 33] & 0xFFu) << 16) | (((unsigned)(int)sp[3 * 33] & 0xFFu) << 24);
;             o.y = ((unsigned)(int)sp[4 * 33] & 0xFFu) | (((unsigned)(int)sp[5 * 33] & 0xFFu) << 8) | (((unsigned)(int)sp[6 * 33] & 0xFFu) << 16) | (((unsigned)(int)sp[7 * 33] & 0xFFu) << 24);
;             *(GAS u32x2*)(dst + (size_t)(n0 + n) * D + 64 * kb + 8 * c) = o; }
;         LDS_WAIT(); asm volatile("" ::: "memory");
	v_pk_mul_f32 v[46:47], v[112:113], v[204:205] op_sel_hi:[1,0]
	v_pk_mul_f32 v[20:21], v[110:111], v[204:205] op_sel_hi:[1,0]
	v_pk_mul_f32 v[44:45], v[116:117], v[206:207] op_sel_hi:[1,0]
	v_pk_mul_f32 v[24:25], v[114:115], v[206:207] op_sel_hi:[1,0]
	v_pk_mul_f32 v[48:49], v[120:121], v[208:209] op_sel_hi:[1,0]
	v_pk_mul_f32 v[16:17], v[108:109], v[202:203] op_sel_hi:[1,0]
	v_pk_mul_f32 v[14:15], v[106:107], v[202:203] op_sel_hi:[1,0]
	v_pk_mul_f32 v[50:51], v[118:119], v[208:209] op_sel_hi:[1,0]
	v_pk_mul_f32 v[52:53], v[124:125], v[210:211] op_sel_hi:[1,0]
	v_pk_mul_f32 v[54:55], v[122:123], v[210:211] op_sel_hi:[1,0]
	v_pk_mul_f32 v[56:57], v[128:129], v[212:213] op_sel_hi:[1,0]
	v_pk_mul_f32 v[58:59], v[126:127], v[212:213] op_sel_hi:[1,0]
	v_pk_mul_f32 v[60:61], v[132:133], v[214:215] op_sel_hi:[1,0]
	v_pk_mul_f32 v[62:63], v[130:131], v[214:215] op_sel_hi:[1,0]
	v_pk_mul_f32 v[42:43], v[136:137], v[216:217] op_sel_hi:[1,0]
	v_pk_mul_f32 v[40:41], v[134:135], v[216:217] op_sel_hi:[1,0]
	s_add_u32 s4, s4, 0x18000
	s_addc_u32 s5, s5, 0
	global_load_dwordx4 v[106:109], v250, s[4:5] nt
	global_load_dword v202, v251, s[6:7] offset:3840
	s_add_u32 s4, s4, 0x18000
	s_addc_u32 s5, s5, 0
	global_load_dwordx4 v[110:113], v250, s[4:5] nt
	global_load_dword v204, v251, s[6:7] offset:3872
	s_add_u32 s4, s4, 0x18000
	s_addc_u32 s5, s5, 0
	global_load_dwordx4 v[114:117], v250, s[4:5] nt
	global_load_dword v206, v251, s[6:7] offset:3904
	s_add_u32 s4, s4, 0x18000
	s_addc_u32 s5, s5, 0
	global_load_dwordx4 v[118:121], v250, s[4:5] nt
	global_load_dword v208, v251, s[6:7] offset:3936
	s_add_u32 s4, s4, 0x18000
	s_addc_u32 s5, s5, 0
	global_load_dwordx4 v[122:125], v250, s[4:5] nt
	global_load_dword v210, v251, s[6:7] offset:3968
	s_add_u32 s4, s4, 0x18000
	s_addc_u32 s5, s5, 0
	global_load_dwordx4 v[126:129], v250, s[4:5] nt
	global_load_dword v212, v251, s[6:7] offset:4000
	s_add_u32 s4, s4, 0x18000
	s_addc_u32 s5, s5, 0
	global_load_dwordx4 v[130:133], v250, s[4:5] nt
	global_load_dword v214, v251, s[6:7] offset:4032
	s_add_u32 s4, s4, 0x18000
	s_addc_u32 s5, s5, 0
	global_load_dwordx4 v[134:137], v250, s[4:5] nt
	global_load_dword v216, v251, s[6:7] offset:4064
	v_mul_f32_e32 v14, v26, v14
	v_mul_f32_e32 v15, v27, v15
	v_mul_f32_e32 v16, v28, v16
	v_mul_f32_e32 v17, v29, v17
	v_mul_f32_e32 v20, v26, v20
	v_mul_f32_e32 v21, v27, v21
	v_mul_f32_e32 v46, v28, v46
	v_mul_f32_e32 v47, v29, v47
	v_mul_f32_e32 v24, v26, v24
	v_mul_f32_e32 v25, v27, v25
	v_mul_f32_e32 v44, v28, v44
	v_mul_f32_e32 v45, v29, v45
	v_mul_f32_e32 v50, v26, v50
	v_mul_f32_e32 v51, v27, v51
	v_mul_f32_e32 v48, v28, v48
	v_mul_f32_e32 v49, v29, v49
	v_mul_f32_e32 v54, v26, v54
	v_mul_f32_e32 v55, v27, v55
	v_mul_f32_e32 v52, v28, v52
	v_mul_f32_e32 v53, v29, v53
	v_mul_f32_e32 v58, v26, v58
	v_mul_f32_e32 v59, v27, v59
	v_mul_f32_e32 v56, v28, v56
	v_mul_f32_e32 v57, v29, v57
	v_mul_f32_e32 v62, v26, v62
	v_mul_f32_e32 v63, v27, v63
	v_mul_f32_e32 v60, v28, v60
	v_mul_f32_e32 v61, v29, v61
	v_mul_f32_e32 v40, v26, v40
	v_mul_f32_e32 v41, v27, v41
	v_mul_f32_e32 v42, v28, v42
	v_mul_f32_e32 v43, v29, v43
	v_rndne_f32_e32 v14, v14
	v_rndne_f32_e32 v15, v15
	v_rndne_f32_e32 v16, v16
	v_rndne_f32_e32 v17, v17
	v_rndne_f32_e32 v20, v20
	v_rndne_f32_e32 v21, v21
	v_rndne_f32_e32 v46, v46
	v_rndne_f32_e32 v47, v47
	v_rndne_f32_e32 v24, v24
	v_rndne_f32_e32 v25, v25
	v_rndne_f32_e32 v44, v44
	v_rndne_f32_e32 v45, v45
	v_rndne_f32_e32 v50, v50
	v_rndne_f32_e32 v51, v51
	v_rndne_f32_e32 v48, v48
	v_rndne_f32_e32 v49, v49
	v_rndne_f32_e32 v54, v54
	v_rndne_f32_e32 v55, v55
	v_rndne_f32_e32 v52, v52
	v_rndne_f32_e32 v53, v53
	v_rndne_f32_e32 v58, v58
	v_rndne_f32_e32 v59, v59
	v_rndne_f32_e32 v56, v56
	v_rndne_f32_e32 v57, v57
	v_rndne_f32_e32 v62, v62
	v_rndne_f32_e32 v63, v63
	v_rndne_f32_e32 v60, v60
	v_rndne_f32_e32 v61, v61
	v_rndne_f32_e32 v40, v40
	v_rndne_f32_e32 v41, v41
	v_rndne_f32_e32 v42, v42
	v_rndne_f32_e32 v43, v43
	ds_write2_b32 v31, v14, v15 offset1:1
	ds_write2_b32 v31, v16, v17 offset0:2 offset1:3
	ds_write2_b32 v32, v20, v21 offset1:1
	ds_write2_b32 v33, v46, v47 offset1:1
	ds_write2_b32 v34, v24, v25 offset1:1
	ds_write2_b32 v35, v44, v45 offset1:1
	ds_write2_b32 v36, v50, v51 offset1:1
	ds_write2_b32 v37, v48, v49 offset1:1
	ds_write2_b32 v38, v54, v55 offset1:1
	ds_write2_b32 v39, v52, v53 offset1:1
	ds_write2_b32 v87, v58, v59 offset1:1
	ds_write2_b32 v88, v56, v57 offset1:1
	ds_write2_b32 v89, v62, v63 offset1:1
	ds_write2_b32 v90, v60, v61 offset1:1
	ds_write2_b32 v91, v40, v41 offset1:1
	ds_write2_b32 v92, v42, v43 offset1:1
	s_waitcnt lgkmcnt(0)
	ds_read2_b32 v[14:15], v30 offset1:8
	ds_read2_b32 v[16:17], v30 offset0:33 offset1:41
	ds_read2_b32 v[20:21], v30 offset0:66 offset1:74
	ds_read2_b32 v[24:25], v30 offset0:99 offset1:107
	ds_read2_b32 v[40:41], v30 offset0:132 offset1:140
	ds_read2_b32 v[42:43], v30 offset0:165 offset1:173
	ds_read2_b32 v[44:45], v30 offset0:198 offset1:206
	ds_read2_b32 v[46:47], v30 offset0:231 offset1:239
	ds_read2_b32 v[48:49], v30 offset0:16 offset1:24
	ds_read2_b32 v[50:51], v30 offset0:49 offset1:57
	ds_read2_b32 v[52:53], v30 offset0:82 offset1:90
	ds_read2_b32 v[54:55], v30 offset0:115 offset1:123
	ds_read2_b32 v[56:57], v30 offset0:148 offset1:156
	ds_read2_b32 v[58:59], v30 offset0:181 offset1:189
	ds_read2_b32 v[60:61], v30 offset0:214 offset1:222
	ds_read2_b32 v[62:63], v30 offset0:247 offset1:255
	s_waitcnt lgkmcnt(14)
	v_cvt_i32_f32_e32 v16, v16
	s_waitcnt lgkmcnt(10)
	v_cvt_i32_f32_e32 v42, v42
	v_cvt_i32_f32_e32 v14, v14
	v_cvt_i32_f32_sdwa v20, v20 dst_sel:WORD_1 dst_unused:UNUSED_PAD src0_sel:DWORD
	v_cvt_i32_f32_e32 v40, v40
	s_waitcnt lgkmcnt(9)
; #define LAS __attribute__((address_space(3)))
; #define GAS __attribute__((address_space(1)))
; #define LDS_WAIT() asm volatile("s_waitcnt lgkmcnt(0)" ::: "memory")
;     ...
;     for (int kb = 0; kb < D / 64; ++kb) {
; #pragma unroll
;         for (int i = 0; i < 8; ++i) { const int kk = 8 * i + kr; const int k = 64 * kb + kk; const f32x4 v = __builtin_nontemporal_load((const f32x4*)(W + (size_t)k * pitch)) * g[k];
;             LAS float* p = scr + kk * 33 + 4 * (lane & 7); p[0] = __builtin_rintf(v[0] * inv[0]); p[1] = __builtin_rintf(v[1] * inv[1]); p[2] = __builtin_rintf(v[2] * inv[2]); p[3] = __builtin_rintf(v[3] * inv[3]); }
;         LDS_WAIT(); asm volatile("" ::: "memory");
;         const int c = lane & 7;
; #pragma unroll
;         for (int j = 0; j < 4; ++j) { const int n = (lane >> 3) + 8 * j; const LAS float* sp = scr + (8 * c) * 33 + n;
;             u32x2 o;
;             o.x = ((unsigned)(int)sp[0 * 33] & 0xFFu) | (((unsigned)(int)sp[1 * 33] & 0xFFu) << 8) | (((unsigned)(int)sp[2 * 33] & 0xFFu) << 16) | (((unsigned)(int)sp[3 * 33] & 0xFFu) << 24);
;             o.y = ((unsigned)(int)sp[4 * 33] & 0xFFu) | (((unsigned)(int)sp[5 * 33] & 0xFFu) << 8) | (((unsigned)(int)sp[6 * 33] & 0xFFu) << 16) | (((unsigned)(int)sp[7 * 33] & 0xFFu) << 24);
;             *(GAS u32x2*)(dst + (size_t)(n0 + n) * D + 64 * kb + 8 * c) = o; }
;         LDS_WAIT(); asm volatile("" ::: "memory");
;     }
	v_cvt_i32_f32_sdwa v44, v44 dst_sel:WORD_1 dst_unused:UNUSED_PAD src0_sel:DWORD
	v_cvt_i32_f32_e32 v17, v17
	v_cvt_i32_f32_e32 v43, v43
	s_waitcnt lgkmcnt(6)
	v_cvt_i32_f32_e32 v50, v50
	s_waitcnt lgkmcnt(2)
	v_cvt_i32_f32_e32 v58, v58
	v_cvt_i32_f32_e32 v51, v51
	v_cvt_i32_f32_e32 v59, v59
	v_cvt_i32_f32_sdwa v24, v24 dst_sel:BYTE_3 dst_unused:UNUSED_PAD src0_sel:DWORD
	v_cvt_i32_f32_sdwa v46, v46 dst_sel:BYTE_3 dst_unused:UNUSED_PAD src0_sel:DWORD
	v_cvt_i32_f32_e32 v15, v15
	v_cvt_i32_f32_sdwa v21, v21 dst_sel:WORD_1 dst_unused:UNUSED_PAD src0_sel:DWORD
	v_cvt_i32_f32_e32 v41, v41
	v_cvt_i32_f32_sdwa v45, v45 dst_sel:WORD_1 dst_unused:UNUSED_PAD src0_sel:DWORD
	v_cvt_i32_f32_e32 v48, v48
	v_cvt_i32_f32_sdwa v52, v52 dst_sel:WORD_1 dst_unused:UNUSED_PAD src0_sel:DWORD
	v_cvt_i32_f32_e32 v56, v56
	s_waitcnt lgkmcnt(1)
	v_cvt_i32_f32_sdwa v60, v60 dst_sel:WORD_1 dst_unused:UNUSED_PAD src0_sel:DWORD
	v_cvt_i32_f32_e32 v49, v49
	v_cvt_i32_f32_sdwa v53, v53 dst_sel:WORD_1 dst_unused:UNUSED_PAD src0_sel:DWORD
	v_cvt_i32_f32_e32 v57, v57
	v_cvt_i32_f32_sdwa v61, v61 dst_sel:WORD_1 dst_unused:UNUSED_PAD src0_sel:DWORD
	v_cvt_i32_f32_sdwa v25, v25 dst_sel:BYTE_3 dst_unused:UNUSED_PAD src0_sel:DWORD
	v_cvt_i32_f32_sdwa v47, v47 dst_sel:BYTE_3 dst_unused:UNUSED_PAD src0_sel:DWORD
	v_cvt_i32_f32_sdwa v54, v54 dst_sel:BYTE_3 dst_unused:UNUSED_PAD src0_sel:DWORD
	s_waitcnt lgkmcnt(0)
	v_cvt_i32_f32_sdwa v62, v62 dst_sel:BYTE_3 dst_unused:UNUSED_PAD src0_sel:DWORD
	v_cvt_i32_f32_sdwa v55, v55 dst_sel:BYTE_3 dst_unused:UNUSED_PAD src0_sel:DWORD
	v_cvt_i32_f32_sdwa v63, v63 dst_sel:BYTE_3 dst_unused:UNUSED_PAD src0_sel:DWORD
	v_lshlrev_b32_e32 v16, 8, v16
	v_lshlrev_b32_e32 v42, 8, v42
	v_and_b32_e32 v20, 0xff0000, v20
	v_and_b32_e32 v44, 0xff0000, v44
	v_lshlrev_b32_e32 v17, 8, v17
	v_lshlrev_b32_e32 v43, 8, v43
	v_lshlrev_b32_e32 v50, 8, v50
	v_lshlrev_b32_e32 v58, 8, v58
	v_lshlrev_b32_e32 v51, 8, v51
	v_lshlrev_b32_e32 v59, 8, v59
	v_perm_b32 v14, v16, v14, s28
	v_perm_b32 v16, v42, v40, s28
	v_and_b32_e32 v21, 0xff0000, v21
	v_and_b32_e32 v45, 0xff0000, v45
	v_and_b32_e32 v52, 0xff0000, v52
	v_and_b32_e32 v60, 0xff0000, v60
	v_and_b32_e32 v53, 0xff0000, v53
	v_and_b32_e32 v61, 0xff0000, v61
	v_perm_b32 v17, v17, v15, s28
	v_perm_b32 v40, v43, v41, s28
	v_perm_b32 v41, v50, v48, s28
	v_perm_b32 v42, v58, v56, s28
	v_perm_b32 v43, v51, v49, s28
	v_perm_b32 v48, v59, v57, s28
	v_or3_b32 v14, v14, v20, v24
	v_or3_b32 v15, v16, v44, v46
	v_or3_b32 v16, v17, v21, v25
	v_or3_b32 v17, v40, v45, v47
	v_or3_b32 v20, v41, v52, v54
	v_or3_b32 v21, v42, v60, v62
	v_or3_b32 v24, v43, v53, v55
	v_or3_b32 v25, v48, v61, v63
	global_store_dwordx2 v[18:19], v[14:15], off
	global_store_dwordx2 v[22:23], v[16:17], off
	global_store_dwordx2 v[82:83], v[20:21], off
	global_store_dwordx2 v[84:85], v[24:25], off
	s_waitcnt lgkmcnt(0)
	v_add_u32_e32 v87, 0x14a0, v31
	v_add_u32_e32 v88, 0x14a8, v31
	v_add_u32_e32 v89, 0x18c0, v31
	v_add_u32_e32 v90, 0x18c8, v31
	v_add_u32_e32 v91, 0x1ce0, v31
	v_add_u32_e32 v92, 0x1ce8, v31
	v_lshl_add_u64 v[18:19], v[6:7], 0, v[12:13]
	v_lshl_add_u64 v[22:23], v[6:7], 0, v[10:11]
	v_lshl_add_u64 v[82:83], v[6:7], 0, v[8:9]
	v_lshl_add_u64 v[84:85], v[6:7], 0, v[4:5]
	v_lshl_add_u64 v[6:7], v[6:7], 0, 64
	s_waitcnt vmcnt(44)
	v_pk_mul_f32 v[46:47], v[144:145], v[220:221] op_sel_hi:[1,0]
	v_pk_mul_f32 v[20:21], v[142:143], v[220:221] op_sel_hi:[1,0]
	v_pk_mul_f32 v[44:45], v[148:149], v[222:223] op_sel_hi:[1,0]
	v_pk_mul_f32 v[24:25], v[146:147], v[222:223] op_sel_hi:[1,0]
	v_pk_mul_f32 v[48:49], v[152:153], v[224:225] op_sel_hi:[1,0]
	v_pk_mul_f32 v[16:17], v[140:141], v[218:219] op_sel_hi:[1,0]
	v_pk_mul_f32 v[14:15], v[138:139], v[218:219] op_sel_hi:[1,0]
	v_pk_mul_f32 v[50:51], v[150:151], v[224:225] op_sel_hi:[1,0]
	v_pk_mul_f32 v[52:53], v[156:157], v[226:227] op_sel_hi:[1,0]
	v_pk_mul_f32 v[54:55], v[154:155], v[226:227] op_sel_hi:[1,0]
	v_pk_mul_f32 v[56:57], v[160:161], v[228:229] op_sel_hi:[1,0]
	v_pk_mul_f32 v[58:59], v[158:159], v[228:229] op_sel_hi:[1,0]
	v_pk_mul_f32 v[60:61], v[164:165], v[230:231] op_sel_hi:[1,0]
	v_pk_mul_f32 v[62:63], v[162:163], v[230:231] op_sel_hi:[1,0]
	v_pk_mul_f32 v[42:43], v[168:169], v[232:233] op_sel_hi:[1,0]
	v_pk_mul_f32 v[40:41], v[166:167], v[232:233] op_sel_hi:[1,0]
	v_mul_f32_e32 v14, v26, v14
	v_mul_f32_e32 v15, v27, v15
	v_mul_f32_e32 v16, v28, v16
	v_mul_f32_e32 v17, v29, v17
	v_mul_f32_e32 v20, v26, v20
	v_mul_f32_e32 v21, v27, v21
	v_mul_f32_e32 v46, v28, v46
	v_mul_f32_e32 v47, v29, v47
	v_mul_f32_e32 v24, v26, v24
	v_mul_f32_e32 v25, v27, v25
	v_mul_f32_e32 v44, v28, v44
	v_mul_f32_e32 v45, v29, v45
	v_mul_f32_e32 v50, v26, v50
	v_mul_f32_e32 v51, v27, v51
	v_mul_f32_e32 v48, v28, v48
	v_mul_f32_e32 v49, v29, v49
	v_mul_f32_e32 v54, v26, v54
	v_mul_f32_e32 v55, v27, v55
	v_mul_f32_e32 v52, v28, v52
	v_mul_f32_e32 v53, v29, v53
	v_mul_f32_e32 v58, v26, v58
	v_mul_f32_e32 v59, v27, v59
	v_mul_f32_e32 v56, v28, v56
	v_mul_f32_e32 v57, v29, v57
	v_mul_f32_e32 v62, v26, v62
	v_mul_f32_e32 v63, v27, v63
	v_mul_f32_e32 v60, v28, v60
	v_mul_f32_e32 v61, v29, v61
	v_mul_f32_e32 v40, v26, v40
	v_mul_f32_e32 v41, v27, v41
	v_mul_f32_e32 v42, v28, v42
	v_mul_f32_e32 v43, v29, v43
	v_rndne_f32_e32 v14, v14
	v_rndne_f32_e32 v15, v15
	v_rndne_f32_e32 v16, v16
	v_rndne_f32_e32 v17, v17
	v_rndne_f32_e32 v20, v20
	v_rndne_f32_e32 v21, v21
	v_rndne_f32_e32 v46, v46
	v_rndne_f32_e32 v47, v47
	v_rndne_f32_e32 v24, v24
	v_rndne_f32_e32 v25, v25
	v_rndne_f32_e32 v44, v44
	v_rndne_f32_e32 v45, v45
	v_rndne_f32_e32 v50, v50
	v_rndne_f32_e32 v51, v51
	v_rndne_f32_e32 v48, v48
	v_rndne_f32_e32 v49, v49
	v_rndne_f32_e32 v54, v54
	v_rndne_f32_e32 v55, v55
	v_rndne_f32_e32 v52, v52
	v_rndne_f32_e32 v53, v53
	v_rndne_f32_e32 v58, v58
	v_rndne_f32_e32 v59, v59
	v_rndne_f32_e32 v56, v56
	v_rndne_f32_e32 v57, v57
	v_rndne_f32_e32 v62, v62
	v_rndne_f32_e32 v63, v63
	v_rndne_f32_e32 v60, v60
	v_rndne_f32_e32 v61, v61
	v_rndne_f32_e32 v40, v40
	v_rndne_f32_e32 v41, v41
	v_rndne_f32_e32 v42, v42
	v_rndne_f32_e32 v43, v43
	ds_write2_b32 v31, v14, v15 offset1:1
	ds_write2_b32 v31, v16, v17 offset0:2 offset1:3
	ds_write2_b32 v32, v20, v21 offset1:1
	ds_write2_b32 v33, v46, v47 offset1:1
	ds_write2_b32 v34, v24, v25 offset1:1
	ds_write2_b32 v35, v44, v45 offset1:1
	ds_write2_b32 v36, v50, v51 offset1:1
	ds_write2_b32 v37, v48, v49 offset1:1
	ds_write2_b32 v38, v54, v55 offset1:1
	ds_write2_b32 v39, v52, v53 offset1:1
	ds_write2_b32 v87, v58, v59 offset1:1
	ds_write2_b32 v88, v56, v57 offset1:1
	ds_write2_b32 v89, v62, v63 offset1:1
	ds_write2_b32 v90, v60, v61 offset1:1
	ds_write2_b32 v91, v40, v41 offset1:1
	ds_write2_b32 v92, v42, v43 offset1:1
	s_waitcnt lgkmcnt(0)
; #define LAS __attribute__((address_space(3)))
; #define GAS __attribute__((address_space(1)))
; #define LDS_WAIT() asm volatile("s_waitcnt lgkmcnt(0)" ::: "memory")
;     ...
;         LDS_WAIT(); asm volatile("" ::: "memory");
;         const int c = lane & 7;
; #pragma unroll
;         for (int j = 0; j < 4; ++j) { const int n = (lane >> 3) + 8 * j; const LAS float* sp = scr + (8 * c) * 33 + n;
;             u32x2 o;
;             o.x = ((unsigned)(int)sp[0 * 33] & 0xFFu) | (((unsigned)(int)sp[1 * 33] & 0xFFu) << 8) | (((unsigned)(int)sp[2 * 33] & 0xFFu) << 16) | (((unsigned)(int)sp[3 * 33] & 0xFFu) << 24);
;             o.y = ((unsigned)(int)sp[4 * 33] & 0xFFu) | (((unsigned)(int)sp[5 * 33] & 0xFFu) << 8) | (((unsigned)(int)sp[6 * 33] & 0xFFu) << 16) | (((unsigned)(int)sp[7 * 33] & 0xFFu) << 24);
;             *(GAS u32x2*)(dst + (size_t)(n0 + n) * D + 64 * kb + 8 * c) = o; }
;         LDS_WAIT(); asm volatile("" ::: "memory");
;     }
	ds_read2_b32 v[14:15], v30 offset1:8
	ds_read2_b32 v[16:17], v30 offset0:33 offset1:41
	ds_read2_b32 v[20:21], v30 offset0:66 offset1:74
	ds_read2_b32 v[24:25], v30 offset0:99 offset1:107
	ds_read2_b32 v[40:41], v30 offset0:132 offset1:140
	ds_read2_b32 v[42:43], v30 offset0:165 offset1:173
	ds_read2_b32 v[44:45], v30 offset0:198 offset1:206
	ds_read2_b32 v[46:47], v30 offset0:231 offset1:239
	ds_read2_b32 v[48:49], v30 offset0:16 offset1:24
	ds_read2_b32 v[50:51], v30 offset0:49 offset1:57
	ds_read2_b32 v[52:53], v30 offset0:82 offset1:90
	ds_read2_b32 v[54:55], v30 offset0:115 offset1:123
	ds_read2_b32 v[56:57], v30 offset0:148 offset1:156
	ds_read2_b32 v[58:59], v30 offset0:181 offset1:189
	ds_read2_b32 v[60:61], v30 offset0:214 offset1:222
	ds_read2_b32 v[62:63], v30 offset0:247 offset1:255
	s_waitcnt lgkmcnt(14)
	v_cvt_i32_f32_e32 v16, v16
	s_waitcnt lgkmcnt(10)
	v_cvt_i32_f32_e32 v42, v42
	v_cvt_i32_f32_e32 v14, v14
	v_cvt_i32_f32_sdwa v20, v20 dst_sel:WORD_1 dst_unused:UNUSED_PAD src0_sel:DWORD
	v_cvt_i32_f32_e32 v40, v40
	s_waitcnt lgkmcnt(9)
	v_cvt_i32_f32_sdwa v44, v44 dst_sel:WORD_1 dst_unused:UNUSED_PAD src0_sel:DWORD
	v_cvt_i32_f32_e32 v17, v17
	v_cvt_i32_f32_e32 v43, v43
	s_waitcnt lgkmcnt(6)
	v_cvt_i32_f32_e32 v50, v50
	s_waitcnt lgkmcnt(2)
	v_cvt_i32_f32_e32 v58, v58
	v_cvt_i32_f32_e32 v51, v51
	v_cvt_i32_f32_e32 v59, v59
	v_cvt_i32_f32_sdwa v24, v24 dst_sel:BYTE_3 dst_unused:UNUSED_PAD src0_sel:DWORD
	v_cvt_i32_f32_sdwa v46, v46 dst_sel:BYTE_3 dst_unused:UNUSED_PAD src0_sel:DWORD
	v_cvt_i32_f32_e32 v15, v15
	v_cvt_i32_f32_sdwa v21, v21 dst_sel:WORD_1 dst_unused:UNUSED_PAD src0_sel:DWORD
	v_cvt_i32_f32_e32 v41, v41
	v_cvt_i32_f32_sdwa v45, v45 dst_sel:WORD_1 dst_unused:UNUSED_PAD src0_sel:DWORD
	v_cvt_i32_f32_e32 v48, v48
	v_cvt_i32_f32_sdwa v52, v52 dst_sel:WORD_1 dst_unused:UNUSED_PAD src0_sel:DWORD
	v_cvt_i32_f32_e32 v56, v56
	s_waitcnt lgkmcnt(1)
	v_cvt_i32_f32_sdwa v60, v60 dst_sel:WORD_1 dst_unused:UNUSED_PAD src0_sel:DWORD
	v_cvt_i32_f32_e32 v49, v49
	v_cvt_i32_f32_sdwa v53, v53 dst_sel:WORD_1 dst_unused:UNUSED_PAD src0_sel:DWORD
	v_cvt_i32_f32_e32 v57, v57
	v_cvt_i32_f32_sdwa v61, v61 dst_sel:WORD_1 dst_unused:UNUSED_PAD src0_sel:DWORD
	v_cvt_i32_f32_sdwa v25, v25 dst_sel:BYTE_3 dst_unused:UNUSED_PAD src0_sel:DWORD
	v_cvt_i32_f32_sdwa v47, v47 dst_sel:BYTE_3 dst_unused:UNUSED_PAD src0_sel:DWORD
	v_cvt_i32_f32_sdwa v54, v54 dst_sel:BYTE_3 dst_unused:UNUSED_PAD src0_sel:DWORD
	s_waitcnt lgkmcnt(0)
	v_cvt_i32_f32_sdwa v62, v62 dst_sel:BYTE_3 dst_unused:UNUSED_PAD src0_sel:DWORD
	v_cvt_i32_f32_sdwa v55, v55 dst_sel:BYTE_3 dst_unused:UNUSED_PAD src0_sel:DWORD
	v_cvt_i32_f32_sdwa v63, v63 dst_sel:BYTE_3 dst_unused:UNUSED_PAD src0_sel:DWORD
	v_lshlrev_b32_e32 v16, 8, v16
	v_lshlrev_b32_e32 v42, 8, v42
	v_and_b32_e32 v20, 0xff0000, v20
	v_and_b32_e32 v44, 0xff0000, v44
	v_lshlrev_b32_e32 v17, 8, v17
	v_lshlrev_b32_e32 v43, 8, v43
	v_lshlrev_b32_e32 v50, 8, v50
	v_lshlrev_b32_e32 v58, 8, v58
	v_lshlrev_b32_e32 v51, 8, v51
	v_lshlrev_b32_e32 v59, 8, v59
	v_perm_b32 v14, v16, v14, s28
	v_perm_b32 v16, v42, v40, s28
	v_and_b32_e32 v21, 0xff0000, v21
	v_and_b32_e32 v45, 0xff0000, v45
	v_and_b32_e32 v52, 0xff0000, v52
	v_and_b32_e32 v60, 0xff0000, v60
	v_and_b32_e32 v53, 0xff0000, v53
	v_and_b32_e32 v61, 0xff0000, v61
	v_perm_b32 v17, v17, v15, s28
	v_perm_b32 v40, v43, v41, s28
	v_perm_b32 v41, v50, v48, s28
	v_perm_b32 v42, v58, v56, s28
	v_perm_b32 v43, v51, v49, s28
	v_perm_b32 v48, v59, v57, s28
	v_or3_b32 v14, v14, v20, v24
	v_or3_b32 v15, v16, v44, v46
	v_or3_b32 v16, v17, v21, v25
	v_or3_b32 v17, v40, v45, v47
	v_or3_b32 v20, v41, v52, v54
	v_or3_b32 v21, v42, v60, v62
	v_or3_b32 v24, v43, v53, v55
	v_or3_b32 v25, v48, v61, v63
	global_store_dwordx2 v[18:19], v[14:15], off
	global_store_dwordx2 v[22:23], v[16:17], off
	global_store_dwordx2 v[82:83], v[20:21], off
	global_store_dwordx2 v[84:85], v[24:25], off
	s_waitcnt lgkmcnt(0)
	v_add_u32_e32 v87, 0x14a0, v31
	v_add_u32_e32 v88, 0x14a8, v31
	v_add_u32_e32 v89, 0x18c0, v31
	v_add_u32_e32 v90, 0x18c8, v31
	v_add_u32_e32 v91, 0x1ce0, v31
	v_add_u32_e32 v92, 0x1ce8, v31
	v_lshl_add_u64 v[18:19], v[6:7], 0, v[12:13]
	v_lshl_add_u64 v[22:23], v[6:7], 0, v[10:11]
	v_lshl_add_u64 v[82:83], v[6:7], 0, v[8:9]
	v_lshl_add_u64 v[84:85], v[6:7], 0, v[4:5]
	v_lshl_add_u64 v[6:7], v[6:7], 0, 64
	s_waitcnt vmcnt(28)
; #define LAS __attribute__((address_space(3)))
; #define GAS __attribute__((address_space(1)))
; #define LDS_WAIT() asm volatile("s_waitcnt lgkmcnt(0)" ::: "memory")
;     ...
;         for (int i = 0; i < 8; ++i) { const int kk = 8 * i + kr; const int k = 64 * kb + kk; const f32x4 v = __builtin_nontemporal_load((const f32x4*)(W + (size_t)k * pitch)) * g[k];
;             LAS float* p = scr + kk * 33 + 4 * (lane & 7); p[0] = __builtin_rintf(v[0] * inv[0]); p[1] = __builtin_rintf(v[1] * inv[1]); p[2] = __builtin_rintf(v[2] * inv[2]); p[3] = __builtin_rintf(v[3] * inv[3]); }
;         LDS_WAIT(); asm volatile("" ::: "memory");
;         const int c = lane & 7;
; #pragma unroll
;         for (int j = 0; j < 4; ++j) { const int n = (lane >> 3) + 8 * j; const LAS float* sp = scr + (8 * c) * 33 + n;
;             u32x2 o;
;             o.x = ((unsigned)(int)sp[0 * 33] & 0xFFu) | (((unsigned)(int)sp[1 * 33] & 0xFFu) << 8) | (((unsigned)(int)sp[2 * 33] & 0xFFu) << 16) | (((unsigned)(int)sp[3 * 33] & 0xFFu) << 24);
;             o.y = ((unsigned)(int)sp[4 * 33] & 0xFFu) | (((unsigned)(int)sp[5 * 33] & 0xFFu) << 8) | (((unsigned)(int)sp[6 * 33] & 0xFFu) << 16) | (((unsigned)(int)sp[7 * 33] & 0xFFu) << 24);
;             *(GAS u32x2*)(dst + (size_t)(n0 + n) * D + 64 * kb + 8 * c) = o; }
;         LDS_WAIT(); asm volatile("" ::: "memory");
	v_pk_mul_f32 v[46:47], v[176:177], v[236:237] op_sel_hi:[1,0]
	v_pk_mul_f32 v[20:21], v[174:175], v[236:237] op_sel_hi:[1,0]
	v_pk_mul_f32 v[44:45], v[180:181], v[238:239] op_sel_hi:[1,0]
	v_pk_mul_f32 v[24:25], v[178:179], v[238:239] op_sel_hi:[1,0]
	v_pk_mul_f32 v[48:49], v[184:185], v[240:241] op_sel_hi:[1,0]
	v_pk_mul_f32 v[16:17], v[172:173], v[234:235] op_sel_hi:[1,0]
	v_pk_mul_f32 v[14:15], v[170:171], v[234:235] op_sel_hi:[1,0]
	v_pk_mul_f32 v[50:51], v[182:183], v[240:241] op_sel_hi:[1,0]
	v_pk_mul_f32 v[52:53], v[188:189], v[242:243] op_sel_hi:[1,0]
	v_pk_mul_f32 v[54:55], v[186:187], v[242:243] op_sel_hi:[1,0]
	v_pk_mul_f32 v[56:57], v[192:193], v[244:245] op_sel_hi:[1,0]
	v_pk_mul_f32 v[58:59], v[190:191], v[244:245] op_sel_hi:[1,0]
	v_pk_mul_f32 v[60:61], v[196:197], v[246:247] op_sel_hi:[1,0]
	v_pk_mul_f32 v[62:63], v[194:195], v[246:247] op_sel_hi:[1,0]
	v_pk_mul_f32 v[42:43], v[200:201], v[248:249] op_sel_hi:[1,0]
	v_pk_mul_f32 v[40:41], v[198:199], v[248:249] op_sel_hi:[1,0]
	v_mul_f32_e32 v14, v26, v14
	v_mul_f32_e32 v15, v27, v15
	v_mul_f32_e32 v16, v28, v16
	v_mul_f32_e32 v17, v29, v17
	v_mul_f32_e32 v20, v26, v20
	v_mul_f32_e32 v21, v27, v21
	v_mul_f32_e32 v46, v28, v46
	v_mul_f32_e32 v47, v29, v47
	v_mul_f32_e32 v24, v26, v24
	v_mul_f32_e32 v25, v27, v25
	v_mul_f32_e32 v44, v28, v44
	v_mul_f32_e32 v45, v29, v45
	v_mul_f32_e32 v50, v26, v50
	v_mul_f32_e32 v51, v27, v51
	v_mul_f32_e32 v48, v28, v48
	v_mul_f32_e32 v49, v29, v49
	v_mul_f32_e32 v54, v26, v54
	v_mul_f32_e32 v55, v27, v55
	v_mul_f32_e32 v52, v28, v52
	v_mul_f32_e32 v53, v29, v53
	v_mul_f32_e32 v58, v26, v58
	v_mul_f32_e32 v59, v27, v59
	v_mul_f32_e32 v56, v28, v56
	v_mul_f32_e32 v57, v29, v57
	v_mul_f32_e32 v62, v26, v62
	v_mul_f32_e32 v63, v27, v63
	v_mul_f32_e32 v60, v28, v60
	v_mul_f32_e32 v61, v29, v61
	v_mul_f32_e32 v40, v26, v40
	v_mul_f32_e32 v41, v27, v41
	v_mul_f32_e32 v42, v28, v42
	v_mul_f32_e32 v43, v29, v43
	v_rndne_f32_e32 v14, v14
	v_rndne_f32_e32 v15, v15
	v_rndne_f32_e32 v16, v16
	v_rndne_f32_e32 v17, v17
	v_rndne_f32_e32 v20, v20
	v_rndne_f32_e32 v21, v21
	v_rndne_f32_e32 v46, v46
	v_rndne_f32_e32 v47, v47
	v_rndne_f32_e32 v24, v24
	v_rndne_f32_e32 v25, v25
	v_rndne_f32_e32 v44, v44
	v_rndne_f32_e32 v45, v45
	v_rndne_f32_e32 v50, v50
	v_rndne_f32_e32 v51, v51
	v_rndne_f32_e32 v48, v48
	v_rndne_f32_e32 v49, v49
	v_rndne_f32_e32 v54, v54
	v_rndne_f32_e32 v55, v55
	v_rndne_f32_e32 v52, v52
	v_rndne_f32_e32 v53, v53
	v_rndne_f32_e32 v58, v58
	v_rndne_f32_e32 v59, v59
	v_rndne_f32_e32 v56, v56
	v_rndne_f32_e32 v57, v57
	v_rndne_f32_e32 v62, v62
	v_rndne_f32_e32 v63, v63
	v_rndne_f32_e32 v60, v60
	v_rndne_f32_e32 v61, v61
	v_rndne_f32_e32 v40, v40
	v_rndne_f32_e32 v41, v41
	v_rndne_f32_e32 v42, v42
	v_rndne_f32_e32 v43, v43
	ds_write2_b32 v31, v14, v15 offset1:1
	ds_write2_b32 v31, v16, v17 offset0:2 offset1:3
	ds_write2_b32 v32, v20, v21 offset1:1
	ds_write2_b32 v33, v46, v47 offset1:1
	ds_write2_b32 v34, v24, v25 offset1:1
	ds_write2_b32 v35, v44, v45 offset1:1
	ds_write2_b32 v36, v50, v51 offset1:1
	ds_write2_b32 v37, v48, v49 offset1:1
	ds_write2_b32 v38, v54, v55 offset1:1
	ds_write2_b32 v39, v52, v53 offset1:1
	ds_write2_b32 v87, v58, v59 offset1:1
	ds_write2_b32 v88, v56, v57 offset1:1
	ds_write2_b32 v89, v62, v63 offset1:1
	ds_write2_b32 v90, v60, v61 offset1:1
	ds_write2_b32 v91, v40, v41 offset1:1
	ds_write2_b32 v92, v42, v43 offset1:1
	s_waitcnt lgkmcnt(0)
	ds_read2_b32 v[14:15], v30 offset1:8
	ds_read2_b32 v[16:17], v30 offset0:33 offset1:41
	ds_read2_b32 v[20:21], v30 offset0:66 offset1:74
	ds_read2_b32 v[24:25], v30 offset0:99 offset1:107
	ds_read2_b32 v[40:41], v30 offset0:132 offset1:140
	ds_read2_b32 v[42:43], v30 offset0:165 offset1:173
	ds_read2_b32 v[44:45], v30 offset0:198 offset1:206
	ds_read2_b32 v[46:47], v30 offset0:231 offset1:239
	ds_read2_b32 v[48:49], v30 offset0:16 offset1:24
	ds_read2_b32 v[50:51], v30 offset0:49 offset1:57
	ds_read2_b32 v[52:53], v30 offset0:82 offset1:90
	ds_read2_b32 v[54:55], v30 offset0:115 offset1:123
	ds_read2_b32 v[56:57], v30 offset0:148 offset1:156
	ds_read2_b32 v[58:59], v30 offset0:181 offset1:189
	ds_read2_b32 v[60:61], v30 offset0:214 offset1:222
	ds_read2_b32 v[62:63], v30 offset0:247 offset1:255
	s_waitcnt lgkmcnt(14)
	v_cvt_i32_f32_e32 v16, v16
	s_waitcnt lgkmcnt(10)
	v_cvt_i32_f32_e32 v42, v42
	v_cvt_i32_f32_e32 v14, v14
	v_cvt_i32_f32_sdwa v20, v20 dst_sel:WORD_1 dst_unused:UNUSED_PAD src0_sel:DWORD
	v_cvt_i32_f32_e32 v40, v40
	s_waitcnt lgkmcnt(9)
	v_cvt_i32_f32_sdwa v44, v44 dst_sel:WORD_1 dst_unused:UNUSED_PAD src0_sel:DWORD
	v_cvt_i32_f32_e32 v17, v17
	v_cvt_i32_f32_e32 v43, v43
	s_waitcnt lgkmcnt(6)
	v_cvt_i32_f32_e32 v50, v50
	s_waitcnt lgkmcnt(2)
	v_cvt_i32_f32_e32 v58, v58
	v_cvt_i32_f32_e32 v51, v51
	v_cvt_i32_f32_e32 v59, v59
	v_cvt_i32_f32_sdwa v24, v24 dst_sel:BYTE_3 dst_unused:UNUSED_PAD src0_sel:DWORD
	v_cvt_i32_f32_sdwa v46, v46 dst_sel:BYTE_3 dst_unused:UNUSED_PAD src0_sel:DWORD
	v_cvt_i32_f32_e32 v15, v15
	v_cvt_i32_f32_sdwa v21, v21 dst_sel:WORD_1 dst_unused:UNUSED_PAD src0_sel:DWORD
	v_cvt_i32_f32_e32 v41, v41
	v_cvt_i32_f32_sdwa v45, v45 dst_sel:WORD_1 dst_unused:UNUSED_PAD src0_sel:DWORD
	v_cvt_i32_f32_e32 v48, v48
	v_cvt_i32_f32_sdwa v52, v52 dst_sel:WORD_1 dst_unused:UNUSED_PAD src0_sel:DWORD
	v_cvt_i32_f32_e32 v56, v56
	s_waitcnt lgkmcnt(1)
	v_cvt_i32_f32_sdwa v60, v60 dst_sel:WORD_1 dst_unused:UNUSED_PAD src0_sel:DWORD
	v_cvt_i32_f32_e32 v49, v49
	v_cvt_i32_f32_sdwa v53, v53 dst_sel:WORD_1 dst_unused:UNUSED_PAD src0_sel:DWORD
	v_cvt_i32_f32_e32 v57, v57
	v_cvt_i32_f32_sdwa v61, v61 dst_sel:WORD_1 dst_unused:UNUSED_PAD src0_sel:DWORD
	v_cvt_i32_f32_sdwa v25, v25 dst_sel:BYTE_3 dst_unused:UNUSED_PAD src0_sel:DWORD
	v_cvt_i32_f32_sdwa v47, v47 dst_sel:BYTE_3 dst_unused:UNUSED_PAD src0_sel:DWORD
	v_cvt_i32_f32_sdwa v54, v54 dst_sel:BYTE_3 dst_unused:UNUSED_PAD src0_sel:DWORD
	s_waitcnt lgkmcnt(0)
; #define LAS __attribute__((address_space(3)))
; #define GAS __attribute__((address_space(1)))
; #define LDS_WAIT() asm volatile("s_waitcnt lgkmcnt(0)" ::: "memory")
;     ...
;     for (int kb = 0; kb < D / 64; ++kb) {
; #pragma unroll
;         for (int i = 0; i < 8; ++i) { const int kk = 8 * i + kr; const int k = 64 * kb + kk; const f32x4 v = __builtin_nontemporal_load((const f32x4*)(W + (size_t)k * pitch)) * g[k];
;             LAS float* p = scr + kk * 33 + 4 * (lane & 7); p[0] = __builtin_rintf(v[0] * inv[0]); p[1] = __builtin_rintf(v[1] * inv[1]); p[2] = __builtin_rintf(v[2] * inv[2]); p[3] = __builtin_rintf(v[3] * inv[3]); }
;         LDS_WAIT(); asm volatile("" ::: "memory");
;         const int c = lane & 7;
; #pragma unroll
;         for (int j = 0; j < 4; ++j) { const int n = (lane >> 3) + 8 * j; const LAS float* sp = scr + (8 * c) * 33 + n;
;             u32x2 o;
;             o.x = ((unsigned)(int)sp[0 * 33] & 0xFFu) | (((unsigned)(int)sp[1 * 33] & 0xFFu) << 8) | (((unsigned)(int)sp[2 * 33] & 0xFFu) << 16) | (((unsigned)(int)sp[3 * 33] & 0xFFu) << 24);
;             o.y = ((unsigned)(int)sp[4 * 33] & 0xFFu) | (((unsigned)(int)sp[5 * 33] & 0xFFu) << 8) | (((unsigned)(int)sp[6 * 33] & 0xFFu) << 16) | (((unsigned)(int)sp[7 * 33] & 0xFFu) << 24);
;             *(GAS u32x2*)(dst + (size_t)(n0 + n) * D + 64 * kb + 8 * c) = o; }
;         LDS_WAIT(); asm volatile("" ::: "memory");
;     }
	v_cvt_i32_f32_sdwa v62, v62 dst_sel:BYTE_3 dst_unused:UNUSED_PAD src0_sel:DWORD
	v_cvt_i32_f32_sdwa v55, v55 dst_sel:BYTE_3 dst_unused:UNUSED_PAD src0_sel:DWORD
	v_cvt_i32_f32_sdwa v63, v63 dst_sel:BYTE_3 dst_unused:UNUSED_PAD src0_sel:DWORD
	v_lshlrev_b32_e32 v16, 8, v16
	v_lshlrev_b32_e32 v42, 8, v42
	v_and_b32_e32 v20, 0xff0000, v20
	v_and_b32_e32 v44, 0xff0000, v44
	v_lshlrev_b32_e32 v17, 8, v17
	v_lshlrev_b32_e32 v43, 8, v43
	v_lshlrev_b32_e32 v50, 8, v50
	v_lshlrev_b32_e32 v58, 8, v58
	v_lshlrev_b32_e32 v51, 8, v51
	v_lshlrev_b32_e32 v59, 8, v59
	v_perm_b32 v14, v16, v14, s28
	v_perm_b32 v16, v42, v40, s28
	v_and_b32_e32 v21, 0xff0000, v21
	v_and_b32_e32 v45, 0xff0000, v45
	v_and_b32_e32 v52, 0xff0000, v52
	v_and_b32_e32 v60, 0xff0000, v60
	v_and_b32_e32 v53, 0xff0000, v53
	v_and_b32_e32 v61, 0xff0000, v61
	v_perm_b32 v17, v17, v15, s28
	v_perm_b32 v40, v43, v41, s28
	v_perm_b32 v41, v50, v48, s28
	v_perm_b32 v42, v58, v56, s28
	v_perm_b32 v43, v51, v49, s28
	v_perm_b32 v48, v59, v57, s28
	v_or3_b32 v14, v14, v20, v24
	v_or3_b32 v15, v16, v44, v46
	v_or3_b32 v16, v17, v21, v25
	v_or3_b32 v17, v40, v45, v47
	v_or3_b32 v20, v41, v52, v54
	v_or3_b32 v21, v42, v60, v62
	v_or3_b32 v24, v43, v53, v55
	v_or3_b32 v25, v48, v61, v63
	global_store_dwordx2 v[18:19], v[14:15], off
	global_store_dwordx2 v[22:23], v[16:17], off
	global_store_dwordx2 v[82:83], v[20:21], off
	global_store_dwordx2 v[84:85], v[24:25], off
	s_waitcnt lgkmcnt(0)
	v_add_u32_e32 v87, 0x14a0, v31
	v_add_u32_e32 v88, 0x14a8, v31
	v_add_u32_e32 v89, 0x18c0, v31
	v_add_u32_e32 v90, 0x18c8, v31
	v_add_u32_e32 v91, 0x1ce0, v31
	v_add_u32_e32 v92, 0x1ce8, v31
	v_lshl_add_u64 v[18:19], v[6:7], 0, v[12:13]
	v_lshl_add_u64 v[22:23], v[6:7], 0, v[10:11]
	v_lshl_add_u64 v[82:83], v[6:7], 0, v[8:9]
	v_lshl_add_u64 v[84:85], v[6:7], 0, v[4:5]
	v_lshl_add_u64 v[6:7], v[6:7], 0, 64
	s_waitcnt vmcnt(12)
	v_pk_mul_f32 v[46:47], v[112:113], v[204:205] op_sel_hi:[1,0]
	v_pk_mul_f32 v[20:21], v[110:111], v[204:205] op_sel_hi:[1,0]
	v_pk_mul_f32 v[44:45], v[116:117], v[206:207] op_sel_hi:[1,0]
	v_pk_mul_f32 v[24:25], v[114:115], v[206:207] op_sel_hi:[1,0]
	v_pk_mul_f32 v[48:49], v[120:121], v[208:209] op_sel_hi:[1,0]
	v_pk_mul_f32 v[16:17], v[108:109], v[202:203] op_sel_hi:[1,0]
	v_pk_mul_f32 v[14:15], v[106:107], v[202:203] op_sel_hi:[1,0]
	v_pk_mul_f32 v[50:51], v[118:119], v[208:209] op_sel_hi:[1,0]
	v_pk_mul_f32 v[52:53], v[124:125], v[210:211] op_sel_hi:[1,0]
	v_pk_mul_f32 v[54:55], v[122:123], v[210:211] op_sel_hi:[1,0]
	v_pk_mul_f32 v[56:57], v[128:129], v[212:213] op_sel_hi:[1,0]
	v_pk_mul_f32 v[58:59], v[126:127], v[212:213] op_sel_hi:[1,0]
	v_pk_mul_f32 v[60:61], v[132:133], v[214:215] op_sel_hi:[1,0]
	v_pk_mul_f32 v[62:63], v[130:131], v[214:215] op_sel_hi:[1,0]
	v_pk_mul_f32 v[42:43], v[136:137], v[216:217] op_sel_hi:[1,0]
	v_pk_mul_f32 v[40:41], v[134:135], v[216:217] op_sel_hi:[1,0]
	v_mul_f32_e32 v14, v26, v14
	v_mul_f32_e32 v15, v27, v15
	v_mul_f32_e32 v16, v28, v16
	v_mul_f32_e32 v17, v29, v17
	v_mul_f32_e32 v20, v26, v20
	v_mul_f32_e32 v21, v27, v21
	v_mul_f32_e32 v46, v28, v46
	v_mul_f32_e32 v47, v29, v47
	v_mul_f32_e32 v24, v26, v24
	v_mul_f32_e32 v25, v27, v25
	v_mul_f32_e32 v44, v28, v44
	v_mul_f32_e32 v45, v29, v45
	v_mul_f32_e32 v50, v26, v50
	v_mul_f32_e32 v51, v27, v51
	v_mul_f32_e32 v48, v28, v48
	v_mul_f32_e32 v49, v29, v49
	v_mul_f32_e32 v54, v26, v54
	v_mul_f32_e32 v55, v27, v55
	v_mul_f32_e32 v52, v28, v52
	v_mul_f32_e32 v53, v29, v53
	v_mul_f32_e32 v58, v26, v58
	v_mul_f32_e32 v59, v27, v59
	v_mul_f32_e32 v56, v28, v56
	v_mul_f32_e32 v57, v29, v57
	v_mul_f32_e32 v62, v26, v62
	v_mul_f32_e32 v63, v27, v63
	v_mul_f32_e32 v60, v28, v60
	v_mul_f32_e32 v61, v29, v61
	v_mul_f32_e32 v40, v26, v40
	v_mul_f32_e32 v41, v27, v41
	v_mul_f32_e32 v42, v28, v42
	v_mul_f32_e32 v43, v29, v43
	v_rndne_f32_e32 v14, v14
	v_rndne_f32_e32 v15, v15
	v_rndne_f32_e32 v16, v16
	v_rndne_f32_e32 v17, v17
	v_rndne_f32_e32 v20, v20
	v_rndne_f32_e32 v21, v21
	v_rndne_f32_e32 v46, v46
	v_rndne_f32_e32 v47, v47
	v_rndne_f32_e32 v24, v24
	v_rndne_f32_e32 v25, v25
	v_rndne_f32_e32 v44, v44
	v_rndne_f32_e32 v45, v45
	v_rndne_f32_e32 v50, v50
	v_rndne_f32_e32 v51, v51
	v_rndne_f32_e32 v48, v48
	v_rndne_f32_e32 v49, v49
	v_rndne_f32_e32 v54, v54
	v_rndne_f32_e32 v55, v55
	v_rndne_f32_e32 v52, v52
	v_rndne_f32_e32 v53, v53
	v_rndne_f32_e32 v58, v58
	v_rndne_f32_e32 v59, v59
	v_rndne_f32_e32 v56, v56
	v_rndne_f32_e32 v57, v57
	v_rndne_f32_e32 v62, v62
	v_rndne_f32_e32 v63, v63
	v_rndne_f32_e32 v60, v60
	v_rndne_f32_e32 v61, v61
	v_rndne_f32_e32 v40, v40
	v_rndne_f32_e32 v41, v41
	v_rndne_f32_e32 v42, v42
	v_rndne_f32_e32 v43, v43
	ds_write2_b32 v31, v14, v15 offset1:1
	ds_write2_b32 v31, v16, v17 offset0:2 offset1:3
	ds_write2_b32 v32, v20, v21 offset1:1
	ds_write2_b32 v33, v46, v47 offset1:1
	ds_write2_b32 v34, v24, v25 offset1:1
	ds_write2_b32 v35, v44, v45 offset1:1
	ds_write2_b32 v36, v50, v51 offset1:1
	ds_write2_b32 v37, v48, v49 offset1:1
	ds_write2_b32 v38, v54, v55 offset1:1
	ds_write2_b32 v39, v52, v53 offset1:1
	ds_write2_b32 v87, v58, v59 offset1:1
	ds_write2_b32 v88, v56, v57 offset1:1
	ds_write2_b32 v89, v62, v63 offset1:1
	ds_write2_b32 v90, v60, v61 offset1:1
	ds_write2_b32 v91, v40, v41 offset1:1
	ds_write2_b32 v92, v42, v43 offset1:1
	s_waitcnt lgkmcnt(0)
; #define LAS __attribute__((address_space(3)))
; #define GAS __attribute__((address_space(1)))
; #define LDS_WAIT() asm volatile("s_waitcnt lgkmcnt(0)" ::: "memory")
;     ...
;         LDS_WAIT(); asm volatile("" ::: "memory");
;         const int c = lane & 7;
; #pragma unroll
;         for (int j = 0; j < 4; ++j) { const int n = (lane >> 3) + 8 * j; const LAS float* sp = scr + (8 * c) * 33 + n;
;             u32x2 o;
;             o.x = ((unsigned)(int)sp[0 * 33] & 0xFFu) | (((unsigned)(int)sp[1 * 33] & 0xFFu) << 8) | (((unsigned)(int)sp[2 * 33] & 0xFFu) << 16) | (((unsigned)(int)sp[3 * 33] & 0xFFu) << 24);
;             o.y = ((unsigned)(int)sp[4 * 33] & 0xFFu) | (((unsigned)(int)sp[5 * 33] & 0xFFu) << 8) | (((unsigned)(int)sp[6 * 33] & 0xFFu) << 16) | (((unsigned)(int)sp[7 * 33] & 0xFFu) << 24);
;             *(GAS u32x2*)(dst + (size_t)(n0 + n) * D + 64 * kb + 8 * c) = o; }
;         LDS_WAIT(); asm volatile("" ::: "memory");
;     }
	ds_read2_b32 v[14:15], v30 offset1:8
	ds_read2_b32 v[16:17], v30 offset0:33 offset1:41
	ds_read2_b32 v[20:21], v30 offset0:66 offset1:74
	ds_read2_b32 v[24:25], v30 offset0:99 offset1:107
	ds_read2_b32 v[40:41], v30 offset0:132 offset1:140
	ds_read2_b32 v[42:43], v30 offset0:165 offset1:173
	ds_read2_b32 v[44:45], v30 offset0:198 offset1:206
	ds_read2_b32 v[46:47], v30 offset0:231 offset1:239
	ds_read2_b32 v[48:49], v30 offset0:16 offset1:24
	ds_read2_b32 v[50:51], v30 offset0:49 offset1:57
	ds_read2_b32 v[52:53], v30 offset0:82 offset1:90
	ds_read2_b32 v[54:55], v30 offset0:115 offset1:123
	ds_read2_b32 v[56:57], v30 offset0:148 offset1:156
	ds_read2_b32 v[58:59], v30 offset0:181 offset1:189
	ds_read2_b32 v[60:61], v30 offset0:214 offset1:222
	ds_read2_b32 v[62:63], v30 offset0:247 offset1:255
	s_waitcnt lgkmcnt(14)
	v_cvt_i32_f32_e32 v16, v16
	s_waitcnt lgkmcnt(10)
	v_cvt_i32_f32_e32 v42, v42
	v_cvt_i32_f32_e32 v14, v14
	v_cvt_i32_f32_sdwa v20, v20 dst_sel:WORD_1 dst_unused:UNUSED_PAD src0_sel:DWORD
	v_cvt_i32_f32_e32 v40, v40
	s_waitcnt lgkmcnt(9)
	v_cvt_i32_f32_sdwa v44, v44 dst_sel:WORD_1 dst_unused:UNUSED_PAD src0_sel:DWORD
	v_cvt_i32_f32_e32 v17, v17
	v_cvt_i32_f32_e32 v43, v43
	s_waitcnt lgkmcnt(6)
	v_cvt_i32_f32_e32 v50, v50
	s_waitcnt lgkmcnt(2)
	v_cvt_i32_f32_e32 v58, v58
	v_cvt_i32_f32_e32 v51, v51
	v_cvt_i32_f32_e32 v59, v59
	v_cvt_i32_f32_sdwa v24, v24 dst_sel:BYTE_3 dst_unused:UNUSED_PAD src0_sel:DWORD
	v_cvt_i32_f32_sdwa v46, v46 dst_sel:BYTE_3 dst_unused:UNUSED_PAD src0_sel:DWORD
	v_cvt_i32_f32_e32 v15, v15
	v_cvt_i32_f32_sdwa v21, v21 dst_sel:WORD_1 dst_unused:UNUSED_PAD src0_sel:DWORD
	v_cvt_i32_f32_e32 v41, v41
	v_cvt_i32_f32_sdwa v45, v45 dst_sel:WORD_1 dst_unused:UNUSED_PAD src0_sel:DWORD
	v_cvt_i32_f32_e32 v48, v48
	v_cvt_i32_f32_sdwa v52, v52 dst_sel:WORD_1 dst_unused:UNUSED_PAD src0_sel:DWORD
	v_cvt_i32_f32_e32 v56, v56
	s_waitcnt lgkmcnt(1)
	v_cvt_i32_f32_sdwa v60, v60 dst_sel:WORD_1 dst_unused:UNUSED_PAD src0_sel:DWORD
	v_cvt_i32_f32_e32 v49, v49
	v_cvt_i32_f32_sdwa v53, v53 dst_sel:WORD_1 dst_unused:UNUSED_PAD src0_sel:DWORD
	v_cvt_i32_f32_e32 v57, v57
	v_cvt_i32_f32_sdwa v61, v61 dst_sel:WORD_1 dst_unused:UNUSED_PAD src0_sel:DWORD
	v_cvt_i32_f32_sdwa v25, v25 dst_sel:BYTE_3 dst_unused:UNUSED_PAD src0_sel:DWORD
	v_cvt_i32_f32_sdwa v47, v47 dst_sel:BYTE_3 dst_unused:UNUSED_PAD src0_sel:DWORD
	v_cvt_i32_f32_sdwa v54, v54 dst_sel:BYTE_3 dst_unused:UNUSED_PAD src0_sel:DWORD
	s_waitcnt lgkmcnt(0)
	v_cvt_i32_f32_sdwa v62, v62 dst_sel:BYTE_3 dst_unused:UNUSED_PAD src0_sel:DWORD
	v_cvt_i32_f32_sdwa v55, v55 dst_sel:BYTE_3 dst_unused:UNUSED_PAD src0_sel:DWORD
	v_cvt_i32_f32_sdwa v63, v63 dst_sel:BYTE_3 dst_unused:UNUSED_PAD src0_sel:DWORD
	v_lshlrev_b32_e32 v16, 8, v16
	v_lshlrev_b32_e32 v42, 8, v42
	v_and_b32_e32 v20, 0xff0000, v20
	v_and_b32_e32 v44, 0xff0000, v44
	v_lshlrev_b32_e32 v17, 8, v17
	v_lshlrev_b32_e32 v43, 8, v43
	v_lshlrev_b32_e32 v50, 8, v50
	v_lshlrev_b32_e32 v58, 8, v58
	v_lshlrev_b32_e32 v51, 8, v51
	v_lshlrev_b32_e32 v59, 8, v59
	v_perm_b32 v14, v16, v14, s28
	v_perm_b32 v16, v42, v40, s28
	v_and_b32_e32 v21, 0xff0000, v21
	v_and_b32_e32 v45, 0xff0000, v45
	v_and_b32_e32 v52, 0xff0000, v52
	v_and_b32_e32 v60, 0xff0000, v60
	v_and_b32_e32 v53, 0xff0000, v53
	v_and_b32_e32 v61, 0xff0000, v61
	v_perm_b32 v17, v17, v15, s28
	v_perm_b32 v40, v43, v41, s28
	v_perm_b32 v41, v50, v48, s28
	v_perm_b32 v42, v58, v56, s28
	v_perm_b32 v43, v51, v49, s28
	v_perm_b32 v48, v59, v57, s28
	v_or3_b32 v14, v14, v20, v24
	v_or3_b32 v15, v16, v44, v46
	v_or3_b32 v16, v17, v21, v25
	v_or3_b32 v17, v40, v45, v47
	v_or3_b32 v20, v41, v52, v54
	v_or3_b32 v21, v42, v60, v62
	v_or3_b32 v24, v43, v53, v55
	v_or3_b32 v25, v48, v61, v63
	global_store_dwordx2 v[18:19], v[14:15], off
	global_store_dwordx2 v[22:23], v[16:17], off
	global_store_dwordx2 v[82:83], v[20:21], off
	global_store_dwordx2 v[84:85], v[24:25], off
	s_waitcnt lgkmcnt(0)
	s_mov_b64 s[4:5], 0

;     const int kr = lane >> 3;
;     f32x4 mx = {0.f, 0.f, 0.f, 0.f};
; #pragma unroll 2
;     for (int kb = 0; kb < D / 64; ++kb) {
; #pragma unroll
;         for (int i = 0; i < 8; ++i) { const int k = 64 * kb + 8 * i + kr; const f32x4 v = __builtin_nontemporal_load((const f32x4*)(W + (size_t)k * pitch)) * g[k];
;             mx[0] = __builtin_fmaxf(mx[0], __builtin_fabsf(v[0])); mx[1] = __builtin_fmaxf(mx[1], __builtin_fabsf(v[1])); mx[2] = __builtin_fmaxf(mx[2], __builtin_fabsf(v[2])); mx[3] = __builtin_fmaxf(mx[3], __builtin_fabsf(v[3])); } }
.LBB0_135:
	v_readfirstlane_b32 s6, v2
	v_readfirstlane_b32 s7, v3
	v_readfirstlane_b32 s8, v4
	v_readfirstlane_b32 s9, v5
	s_nop 1
	v_subrev_u32_e32 v250, s6, v2
	v_subrev_u32_e32 v251, s8, v4
	s_nop 4
	global_load_dwordx4 v[106:109], v250, s[6:7] nt
	global_load_dword v202, v251, s[8:9] offset:-480
	s_add_u32 s6, s6, 0x16000
	s_addc_u32 s7, s7, 0
	global_load_dwordx4 v[110:113], v250, s[6:7] nt
	global_load_dword v204, v251, s[8:9] offset:-448
	s_add_u32 s6, s6, 0x16000
	s_addc_u32 s7, s7, 0
	global_load_dwordx4 v[114:117], v250, s[6:7] nt
	global_load_dword v206, v251, s[8:9] offset:-416
	s_add_u32 s6, s6, 0x16000
	s_addc_u32 s7, s7, 0
	global_load_dwordx4 v[118:121], v250, s[6:7] nt
	global_load_dword v208, v251, s[8:9] offset:-384
	s_add_u32 s6, s6, 0x16000
	s_addc_u32 s7, s7, 0
	global_load_dwordx4 v[122:125], v250, s[6:7] nt
	global_load_dword v210, v251, s[8:9] offset:-352
	s_add_u32 s6, s6, 0x16000
	s_addc_u32 s7, s7, 0
	global_load_dwordx4 v[126:129], v250, s[6:7] nt
	global_load_dword v212, v251, s[8:9] offset:-320
	s_add_u32 s6, s6, 0x16000
	s_addc_u32 s7, s7, 0
	global_load_dwordx4 v[130:133], v250, s[6:7] nt
	global_load_dword v214, v251, s[8:9] offset:-288
	s_add_u32 s6, s6, 0x16000
	s_addc_u32 s7, s7, 0
	global_load_dwordx4 v[134:137], v250, s[6:7] nt
	global_load_dword v216, v251, s[8:9] offset:-256
	s_add_u32 s6, s6, 0x16000
	s_addc_u32 s7, s7, 0
	global_load_dwordx4 v[138:141], v250, s[6:7] nt
	global_load_dword v218, v251, s[8:9] offset:-224
	s_add_u32 s6, s6, 0x16000
	s_addc_u32 s7, s7, 0
	global_load_dwordx4 v[142:145], v250, s[6:7] nt
	global_load_dword v220, v251, s[8:9] offset:-192
	s_add_u32 s6, s6, 0x16000
	s_addc_u32 s7, s7, 0
	global_load_dwordx4 v[146:149], v250, s[6:7] nt
	global_load_dword v222, v251, s[8:9] offset:-160
	s_add_u32 s6, s6, 0x16000
	s_addc_u32 s7, s7, 0
	global_load_dwordx4 v[150:153], v250, s[6:7] nt
	global_load_dword v224, v251, s[8:9] offset:-128
	s_add_u32 s6, s6, 0x16000
	s_addc_u32 s7, s7, 0
	global_load_dwordx4 v[154:157], v250, s[6:7] nt
	global_load_dword v226, v251, s[8:9] offset:-96
	s_add_u32 s6, s6, 0x16000
	s_addc_u32 s7, s7, 0
	global_load_dwordx4 v[158:161], v250, s[6:7] nt
	global_load_dword v228, v251, s[8:9] offset:-64
	s_add_u32 s6, s6, 0x16000
	s_addc_u32 s7, s7, 0
	global_load_dwordx4 v[162:165], v250, s[6:7] nt
	global_load_dword v230, v251, s[8:9] offset:-32
	s_add_u32 s6, s6, 0x16000
	s_addc_u32 s7, s7, 0
	global_load_dwordx4 v[166:169], v250, s[6:7] nt
	global_load_dword v232, v251, s[8:9]
	s_add_u32 s6, s6, 0x16000
	s_addc_u32 s7, s7, 0
	global_load_dwordx4 v[170:173], v250, s[6:7] nt
	global_load_dword v234, v251, s[8:9] offset:32
	s_add_u32 s6, s6, 0x16000
	s_addc_u32 s7, s7, 0
	global_load_dwordx4 v[174:177], v250, s[6:7] nt
	global_load_dword v236, v251, s[8:9] offset:64
	s_add_u32 s6, s6, 0x16000
	s_addc_u32 s7, s7, 0
	global_load_dwordx4 v[178:181], v250, s[6:7] nt
	global_load_dword v238, v251, s[8:9] offset:96
	s_add_u32 s6, s6, 0x16000
	s_addc_u32 s7, s7, 0
	global_load_dwordx4 v[182:185], v250, s[6:7] nt
	global_load_dword v240, v251, s[8:9] offset:128
	s_add_u32 s6, s6, 0x16000
	s_addc_u32 s7, s7, 0
	global_load_dwordx4 v[186:189], v250, s[6:7] nt
	global_load_dword v242, v251, s[8:9] offset:160
	s_add_u32 s6, s6, 0x16000
	s_addc_u32 s7, s7, 0
	global_load_dwordx4 v[190:193], v250, s[6:7] nt
	global_load_dword v244, v251, s[8:9] offset:192
	s_add_u32 s6, s6, 0x16000
	s_addc_u32 s7, s7, 0
	global_load_dwordx4 v[194:197], v250, s[6:7] nt
	global_load_dword v246, v251, s[8:9] offset:224
	s_add_u32 s6, s6, 0x16000
	s_addc_u32 s7, s7, 0
	global_load_dwordx4 v[198:201], v250, s[6:7] nt
	global_load_dword v248, v251, s[8:9] offset:256
	s_waitcnt vmcnt(44)
	v_pk_mul_f32 v[16:17], v[106:107], v[202:203] op_sel_hi:[1,0]
	v_pk_mul_f32 v[18:19], v[108:109], v[202:203] op_sel_hi:[1,0]
	v_pk_mul_f32 v[20:21], v[110:111], v[204:205] op_sel_hi:[1,0]
	v_pk_mul_f32 v[22:23], v[112:113], v[204:205] op_sel_hi:[1,0]
	v_max3_f32 v15, v15, |v16|, |v20|
	v_max3_f32 v13, v13, |v17|, |v21|
	v_max3_f32 v9, v9, |v18|, |v22|
	v_max3_f32 v7, v7, |v19|, |v23|
	s_add_u32 s6, s6, 0x16000
	s_addc_u32 s7, s7, 0
	global_load_dwordx4 v[106:109], v250, s[6:7] nt
	global_load_dword v202, v251, s[8:9] offset:288
	s_add_u32 s6, s6, 0x16000
	s_addc_u32 s7, s7, 0
	global_load_dwordx4 v[110:113], v250, s[6:7] nt
	global_load_dword v204, v251, s[8:9] offset:320
	s_waitcnt vmcnt(44)
	v_pk_mul_f32 v[16:17], v[114:115], v[206:207] op_sel_hi:[1,0]
	v_pk_mul_f32 v[18:19], v[116:117], v[206:207] op_sel_hi:[1,0]
	v_pk_mul_f32 v[20:21], v[118:119], v[208:209] op_sel_hi:[1,0]
	v_pk_mul_f32 v[22:23], v[120:121], v[208:209] op_sel_hi:[1,0]
	v_max3_f32 v15, v15, |v16|, |v20|
	v_max3_f32 v13, v13, |v17|, |v21|
	v_max3_f32 v9, v9, |v18|, |v22|
	v_max3_f32 v7, v7, |v19|, |v23|
	s_add_u32 s6, s6, 0x16000
	s_addc_u32 s7, s7, 0
	global_load_dwordx4 v[114:117], v250, s[6:7] nt
	global_load_dword v206, v251, s[8:9] offset:352
	s_add_u32 s6, s6, 0x16000
	s_addc_u32 s7, s7, 0
	global_load_dwordx4 v[118:121], v250, s[6:7] nt
	global_load_dword v208, v251, s[8:9] offset:384
	s_waitcnt vmcnt(44)
	v_pk_mul_f32 v[16:17], v[122:123], v[210:211] op_sel_hi:[1,0]
	v_pk_mul_f32 v[18:19], v[124:125], v[210:211] op_sel_hi:[1,0]
	v_pk_mul_f32 v[20:21], v[126:127], v[212:213] op_sel_hi:[1,0]
	v_pk_mul_f32 v[22:23], v[128:129], v[212:213] op_sel_hi:[1,0]
	v_max3_f32 v15, v15, |v16|, |v20|
	v_max3_f32 v13, v13, |v17|, |v21|
	v_max3_f32 v9, v9, |v18|, |v22|
	v_max3_f32 v7, v7, |v19|, |v23|
	s_add_u32 s6, s6, 0x16000
	s_addc_u32 s7, s7, 0
	global_load_dwordx4 v[122:125], v250, s[6:7] nt
	global_load_dword v210, v251, s[8:9] offset:416
	s_add_u32 s6, s6, 0x16000
	s_addc_u32 s7, s7, 0
	global_load_dwordx4 v[126:129], v250, s[6:7] nt
	global_load_dword v212, v251, s[8:9] offset:448
	s_waitcnt vmcnt(44)
;     ...
;     for (int kb = 0; kb < D / 64; ++kb) {
; #pragma unroll
;         for (int i = 0; i < 8; ++i) { const int k = 64 * kb + 8 * i + kr; const f32x4 v = __builtin_nontemporal_load((const f32x4*)(W + (size_t)k * pitch)) * g[k];
;             mx[0] = __builtin_fmaxf(mx[0], __builtin_fabsf(v[0])); mx[1] = __builtin_fmaxf(mx[1], __builtin_fabsf(v[1])); mx[2] = __builtin_fmaxf(mx[2], __builtin_fabsf(v[2])); mx[3] = __builtin_fmaxf(mx[3], __builtin_fabsf(v[3])); } }
	v_pk_mul_f32 v[16:17], v[130:131], v[214:215] op_sel_hi:[1,0]
	v_pk_mul_f32 v[18:19], v[132:133], v[214:215] op_sel_hi:[1,0]
	v_pk_mul_f32 v[20:21], v[134:135], v[216:217] op_sel_hi:[1,0]
	v_pk_mul_f32 v[22:23], v[136:137], v[216:217] op_sel_hi:[1,0]
	v_max3_f32 v15, v15, |v16|, |v20|
	v_max3_f32 v13, v13, |v17|, |v21|
	v_max3_f32 v9, v9, |v18|, |v22|
	v_max3_f32 v7, v7, |v19|, |v23|
	s_add_u32 s6, s6, 0x16000
	s_addc_u32 s7, s7, 0
	global_load_dwordx4 v[130:133], v250, s[6:7] nt
	global_load_dword v214, v251, s[8:9] offset:480
	s_add_u32 s6, s6, 0x16000
	s_addc_u32 s7, s7, 0
	global_load_dwordx4 v[134:137], v250, s[6:7] nt
	global_load_dword v216, v251, s[8:9] offset:512
	s_waitcnt vmcnt(44)
	v_pk_mul_f32 v[16:17], v[138:139], v[218:219] op_sel_hi:[1,0]
	v_pk_mul_f32 v[18:19], v[140:141], v[218:219] op_sel_hi:[1,0]
	v_pk_mul_f32 v[20:21], v[142:143], v[220:221] op_sel_hi:[1,0]
	v_pk_mul_f32 v[22:23], v[144:145], v[220:221] op_sel_hi:[1,0]
	v_max3_f32 v15, v15, |v16|, |v20|
	v_max3_f32 v13, v13, |v17|, |v21|
	v_max3_f32 v9, v9, |v18|, |v22|
	v_max3_f32 v7, v7, |v19|, |v23|
	s_add_u32 s6, s6, 0x16000
	s_addc_u32 s7, s7, 0
	global_load_dwordx4 v[138:141], v250, s[6:7] nt
	global_load_dword v218, v251, s[8:9] offset:544
	s_add_u32 s6, s6, 0x16000
	s_addc_u32 s7, s7, 0
	global_load_dwordx4 v[142:145], v250, s[6:7] nt
	global_load_dword v220, v251, s[8:9] offset:576
	s_waitcnt vmcnt(44)
	v_pk_mul_f32 v[16:17], v[146:147], v[222:223] op_sel_hi:[1,0]
	v_pk_mul_f32 v[18:19], v[148:149], v[222:223] op_sel_hi:[1,0]
	v_pk_mul_f32 v[20:21], v[150:151], v[224:225] op_sel_hi:[1,0]
	v_pk_mul_f32 v[22:23], v[152:153], v[224:225] op_sel_hi:[1,0]
	v_max3_f32 v15, v15, |v16|, |v20|
	v_max3_f32 v13, v13, |v17|, |v21|
	v_max3_f32 v9, v9, |v18|, |v22|
	v_max3_f32 v7, v7, |v19|, |v23|
	s_add_u32 s6, s6, 0x16000
	s_addc_u32 s7, s7, 0
	global_load_dwordx4 v[146:149], v250, s[6:7] nt
	global_load_dword v222, v251, s[8:9] offset:608
	s_add_u32 s6, s6, 0x16000
	s_addc_u32 s7, s7, 0
	global_load_dwordx4 v[150:153], v250, s[6:7] nt
	global_load_dword v224, v251, s[8:9] offset:640
	s_waitcnt vmcnt(44)
	v_pk_mul_f32 v[16:17], v[154:155], v[226:227] op_sel_hi:[1,0]
	v_pk_mul_f32 v[18:19], v[156:157], v[226:227] op_sel_hi:[1,0]
	v_pk_mul_f32 v[20:21], v[158:159], v[228:229] op_sel_hi:[1,0]
	v_pk_mul_f32 v[22:23], v[160:161], v[228:229] op_sel_hi:[1,0]
	v_max3_f32 v15, v15, |v16|, |v20|
	v_max3_f32 v13, v13, |v17|, |v21|
	v_max3_f32 v9, v9, |v18|, |v22|
	v_max3_f32 v7, v7, |v19|, |v23|
	s_add_u32 s6, s6, 0x16000
	s_addc_u32 s7, s7, 0
	global_load_dwordx4 v[154:157], v250, s[6:7] nt
	global_load_dword v226, v251, s[8:9] offset:672
	s_add_u32 s6, s6, 0x16000
	s_addc_u32 s7, s7, 0
	global_load_dwordx4 v[158:161], v250, s[6:7] nt
	global_load_dword v228, v251, s[8:9] offset:704
	s_waitcnt vmcnt(44)
	v_pk_mul_f32 v[16:17], v[162:163], v[230:231] op_sel_hi:[1,0]
	v_pk_mul_f32 v[18:19], v[164:165], v[230:231] op_sel_hi:[1,0]
	v_pk_mul_f32 v[20:21], v[166:167], v[232:233] op_sel_hi:[1,0]
	v_pk_mul_f32 v[22:23], v[168:169], v[232:233] op_sel_hi:[1,0]
	v_max3_f32 v15, v15, |v16|, |v20|
	v_max3_f32 v13, v13, |v17|, |v21|
	v_max3_f32 v9, v9, |v18|, |v22|
	v_max3_f32 v7, v7, |v19|, |v23|
	s_add_u32 s6, s6, 0x16000
	s_addc_u32 s7, s7, 0
	global_load_dwordx4 v[162:165], v250, s[6:7] nt
	global_load_dword v230, v251, s[8:9] offset:736
	s_add_u32 s6, s6, 0x16000
	s_addc_u32 s7, s7, 0
	global_load_dwordx4 v[166:169], v250, s[6:7] nt
	global_load_dword v232, v251, s[8:9] offset:768
	s_waitcnt vmcnt(44)
	v_pk_mul_f32 v[16:17], v[170:171], v[234:235] op_sel_hi:[1,0]
	v_pk_mul_f32 v[18:19], v[172:173], v[234:235] op_sel_hi:[1,0]
	v_pk_mul_f32 v[20:21], v[174:175], v[236:237] op_sel_hi:[1,0]
	v_pk_mul_f32 v[22:23], v[176:177], v[236:237] op_sel_hi:[1,0]
	v_max3_f32 v15, v15, |v16|, |v20|
	v_max3_f32 v13, v13, |v17|, |v21|
	v_max3_f32 v9, v9, |v18|, |v22|
	v_max3_f32 v7, v7, |v19|, |v23|
	s_add_u32 s6, s6, 0x16000
	s_addc_u32 s7, s7, 0
	global_load_dwordx4 v[170:173], v250, s[6:7] nt
	global_load_dword v234, v251, s[8:9] offset:800
	s_add_u32 s6, s6, 0x16000
	s_addc_u32 s7, s7, 0
	global_load_dwordx4 v[174:177], v250, s[6:7] nt
	global_load_dword v236, v251, s[8:9] offset:832
	s_waitcnt vmcnt(44)
	v_pk_mul_f32 v[16:17], v[178:179], v[238:239] op_sel_hi:[1,0]
	v_pk_mul_f32 v[18:19], v[180:181], v[238:239] op_sel_hi:[1,0]
	v_pk_mul_f32 v[20:21], v[182:183], v[240:241] op_sel_hi:[1,0]
	v_pk_mul_f32 v[22:23], v[184:185], v[240:241] op_sel_hi:[1,0]
	v_max3_f32 v15, v15, |v16|, |v20|
	v_max3_f32 v13, v13, |v17|, |v21|
	v_max3_f32 v9, v9, |v18|, |v22|
	v_max3_f32 v7, v7, |v19|, |v23|
	s_add_u32 s6, s6, 0x16000
	s_addc_u32 s7, s7, 0
	global_load_dwordx4 v[178:181], v250, s[6:7] nt
	global_load_dword v238, v251, s[8:9] offset:864
	s_add_u32 s6, s6, 0x16000
	s_addc_u32 s7, s7, 0
	global_load_dwordx4 v[182:185], v250, s[6:7] nt
	global_load_dword v240, v251, s[8:9] offset:896
	s_waitcnt vmcnt(44)
	v_pk_mul_f32 v[16:17], v[186:187], v[242:243] op_sel_hi:[1,0]
	v_pk_mul_f32 v[18:19], v[188:189], v[242:243] op_sel_hi:[1,0]
	v_pk_mul_f32 v[20:21], v[190:191], v[244:245] op_sel_hi:[1,0]
	v_pk_mul_f32 v[22:23], v[192:193], v[244:245] op_sel_hi:[1,0]
	v_max3_f32 v15, v15, |v16|, |v20|
	v_max3_f32 v13, v13, |v17|, |v21|
	v_max3_f32 v9, v9, |v18|, |v22|
	v_max3_f32 v7, v7, |v19|, |v23|
	s_add_u32 s6, s6, 0x16000
	s_addc_u32 s7, s7, 0
	global_load_dwordx4 v[186:189], v250, s[6:7] nt
	global_load_dword v242, v251, s[8:9] offset:928
	s_add_u32 s6, s6, 0x16000
	s_addc_u32 s7, s7, 0
	global_load_dwordx4 v[190:193], v250, s[6:7] nt
	global_load_dword v244, v251, s[8:9] offset:960
	s_waitcnt vmcnt(44)
;     ...
;     for (int kb = 0; kb < D / 64; ++kb) {
; #pragma unroll
;         for (int i = 0; i < 8; ++i) { const int k = 64 * kb + 8 * i + kr; const f32x4 v = __builtin_nontemporal_load((const f32x4*)(W + (size_t)k * pitch)) * g[k];
;             mx[0] = __builtin_fmaxf(mx[0], __builtin_fabsf(v[0])); mx[1] = __builtin_fmaxf(mx[1], __builtin_fabsf(v[1])); mx[2] = __builtin_fmaxf(mx[2], __builtin_fabsf(v[2])); mx[3] = __builtin_fmaxf(mx[3], __builtin_fabsf(v[3])); } }
	v_pk_mul_f32 v[16:17], v[194:195], v[246:247] op_sel_hi:[1,0]
	v_pk_mul_f32 v[18:19], v[196:197], v[246:247] op_sel_hi:[1,0]
	v_pk_mul_f32 v[20:21], v[198:199], v[248:249] op_sel_hi:[1,0]
	v_pk_mul_f32 v[22:23], v[200:201], v[248:249] op_sel_hi:[1,0]
	v_max3_f32 v15, v15, |v16|, |v20|
	v_max3_f32 v13, v13, |v17|, |v21|
	v_max3_f32 v9, v9, |v18|, |v22|
	v_max3_f32 v7, v7, |v19|, |v23|
	s_add_u32 s6, s6, 0x16000
	s_addc_u32 s7, s7, 0
	global_load_dwordx4 v[194:197], v250, s[6:7] nt
	global_load_dword v246, v251, s[8:9] offset:992
	s_add_u32 s6, s6, 0x16000
	s_addc_u32 s7, s7, 0
	global_load_dwordx4 v[198:201], v250, s[6:7] nt
	global_load_dword v248, v251, s[8:9] offset:1024
	s_waitcnt vmcnt(44)
	v_pk_mul_f32 v[16:17], v[106:107], v[202:203] op_sel_hi:[1,0]
	v_pk_mul_f32 v[18:19], v[108:109], v[202:203] op_sel_hi:[1,0]
	v_pk_mul_f32 v[20:21], v[110:111], v[204:205] op_sel_hi:[1,0]
	v_pk_mul_f32 v[22:23], v[112:113], v[204:205] op_sel_hi:[1,0]
	v_max3_f32 v15, v15, |v16|, |v20|
	v_max3_f32 v13, v13, |v17|, |v21|
	v_max3_f32 v9, v9, |v18|, |v22|
	v_max3_f32 v7, v7, |v19|, |v23|
	s_add_u32 s6, s6, 0x16000
	s_addc_u32 s7, s7, 0
	global_load_dwordx4 v[106:109], v250, s[6:7] nt
	global_load_dword v202, v251, s[8:9] offset:1056
	s_add_u32 s6, s6, 0x16000
	s_addc_u32 s7, s7, 0
	global_load_dwordx4 v[110:113], v250, s[6:7] nt
	global_load_dword v204, v251, s[8:9] offset:1088
	s_waitcnt vmcnt(44)
	v_pk_mul_f32 v[16:17], v[114:115], v[206:207] op_sel_hi:[1,0]
	v_pk_mul_f32 v[18:19], v[116:117], v[206:207] op_sel_hi:[1,0]
	v_pk_mul_f32 v[20:21], v[118:119], v[208:209] op_sel_hi:[1,0]
	v_pk_mul_f32 v[22:23], v[120:121], v[208:209] op_sel_hi:[1,0]
	v_max3_f32 v15, v15, |v16|, |v20|
	v_max3_f32 v13, v13, |v17|, |v21|
	v_max3_f32 v9, v9, |v18|, |v22|
	v_max3_f32 v7, v7, |v19|, |v23|
	s_add_u32 s6, s6, 0x16000
	s_addc_u32 s7, s7, 0
	global_load_dwordx4 v[114:117], v250, s[6:7] nt
	global_load_dword v206, v251, s[8:9] offset:1120
	s_add_u32 s6, s6, 0x16000
	s_addc_u32 s7, s7, 0
	global_load_dwordx4 v[118:121], v250, s[6:7] nt
	global_load_dword v208, v251, s[8:9] offset:1152
	s_waitcnt vmcnt(44)
	v_pk_mul_f32 v[16:17], v[122:123], v[210:211] op_sel_hi:[1,0]
	v_pk_mul_f32 v[18:19], v[124:125], v[210:211] op_sel_hi:[1,0]
	v_pk_mul_f32 v[20:21], v[126:127], v[212:213] op_sel_hi:[1,0]
	v_pk_mul_f32 v[22:23], v[128:129], v[212:213] op_sel_hi:[1,0]
	v_max3_f32 v15, v15, |v16|, |v20|
	v_max3_f32 v13, v13, |v17|, |v21|
	v_max3_f32 v9, v9, |v18|, |v22|
	v_max3_f32 v7, v7, |v19|, |v23|
	s_add_u32 s6, s6, 0x16000
	s_addc_u32 s7, s7, 0
	global_load_dwordx4 v[122:125], v250, s[6:7] nt
	global_load_dword v210, v251, s[8:9] offset:1184
	s_add_u32 s6, s6, 0x16000
	s_addc_u32 s7, s7, 0
	global_load_dwordx4 v[126:129], v250, s[6:7] nt
	global_load_dword v212, v251, s[8:9] offset:1216
	s_waitcnt vmcnt(44)
	v_pk_mul_f32 v[16:17], v[130:131], v[214:215] op_sel_hi:[1,0]
	v_pk_mul_f32 v[18:19], v[132:133], v[214:215] op_sel_hi:[1,0]
	v_pk_mul_f32 v[20:21], v[134:135], v[216:217] op_sel_hi:[1,0]
	v_pk_mul_f32 v[22:23], v[136:137], v[216:217] op_sel_hi:[1,0]
	v_max3_f32 v15, v15, |v16|, |v20|
	v_max3_f32 v13, v13, |v17|, |v21|
	v_max3_f32 v9, v9, |v18|, |v22|
	v_max3_f32 v7, v7, |v19|, |v23|
	s_add_u32 s6, s6, 0x16000
	s_addc_u32 s7, s7, 0
	global_load_dwordx4 v[130:133], v250, s[6:7] nt
	global_load_dword v214, v251, s[8:9] offset:1248
	s_add_u32 s6, s6, 0x16000
	s_addc_u32 s7, s7, 0
	global_load_dwordx4 v[134:137], v250, s[6:7] nt
	global_load_dword v216, v251, s[8:9] offset:1280
	s_waitcnt vmcnt(44)
	v_pk_mul_f32 v[16:17], v[138:139], v[218:219] op_sel_hi:[1,0]
	v_pk_mul_f32 v[18:19], v[140:141], v[218:219] op_sel_hi:[1,0]
	v_pk_mul_f32 v[20:21], v[142:143], v[220:221] op_sel_hi:[1,0]
	v_pk_mul_f32 v[22:23], v[144:145], v[220:221] op_sel_hi:[1,0]
	v_max3_f32 v15, v15, |v16|, |v20|
	v_max3_f32 v13, v13, |v17|, |v21|
	v_max3_f32 v9, v9, |v18|, |v22|
	v_max3_f32 v7, v7, |v19|, |v23|
	s_add_u32 s6, s6, 0x16000
	s_addc_u32 s7, s7, 0
	global_load_dwordx4 v[138:141], v250, s[6:7] nt
	global_load_dword v218, v251, s[8:9] offset:1312
	s_add_u32 s6, s6, 0x16000
	s_addc_u32 s7, s7, 0
	global_load_dwordx4 v[142:145], v250, s[6:7] nt
	global_load_dword v220, v251, s[8:9] offset:1344
	s_waitcnt vmcnt(44)
	v_pk_mul_f32 v[16:17], v[146:147], v[222:223] op_sel_hi:[1,0]
	v_pk_mul_f32 v[18:19], v[148:149], v[222:223] op_sel_hi:[1,0]
	v_pk_mul_f32 v[20:21], v[150:151], v[224:225] op_sel_hi:[1,0]
	v_pk_mul_f32 v[22:23], v[152:153], v[224:225] op_sel_hi:[1,0]
	v_max3_f32 v15, v15, |v16|, |v20|
	v_max3_f32 v13, v13, |v17|, |v21|
	v_max3_f32 v9, v9, |v18|, |v22|
	v_max3_f32 v7, v7, |v19|, |v23|
	s_add_u32 s6, s6, 0x16000
	s_addc_u32 s7, s7, 0
	global_load_dwordx4 v[146:149], v250, s[6:7] nt
	global_load_dword v222, v251, s[8:9] offset:1376
	s_add_u32 s6, s6, 0x16000
	s_addc_u32 s7, s7, 0
	global_load_dwordx4 v[150:153], v250, s[6:7] nt
	global_load_dword v224, v251, s[8:9] offset:1408
	s_waitcnt vmcnt(44)
	v_pk_mul_f32 v[16:17], v[154:155], v[226:227] op_sel_hi:[1,0]
	v_pk_mul_f32 v[18:19], v[156:157], v[226:227] op_sel_hi:[1,0]
	v_pk_mul_f32 v[20:21], v[158:159], v[228:229] op_sel_hi:[1,0]
	v_pk_mul_f32 v[22:23], v[160:161], v[228:229] op_sel_hi:[1,0]
	v_max3_f32 v15, v15, |v16|, |v20|
	v_max3_f32 v13, v13, |v17|, |v21|
	v_max3_f32 v9, v9, |v18|, |v22|
	v_max3_f32 v7, v7, |v19|, |v23|
	s_add_u32 s6, s6, 0x16000
	s_addc_u32 s7, s7, 0
	global_load_dwordx4 v[154:157], v250, s[6:7] nt
	global_load_dword v226, v251, s[8:9] offset:1440
	s_add_u32 s6, s6, 0x16000
	s_addc_u32 s7, s7, 0
	global_load_dwordx4 v[158:161], v250, s[6:7] nt
	global_load_dword v228, v251, s[8:9] offset:1472
	s_waitcnt vmcnt(44)
;     ...
;     for (int kb = 0; kb < D / 64; ++kb) {
; #pragma unroll
;         for (int i = 0; i < 8; ++i) { const int k = 64 * kb + 8 * i + kr; const f32x4 v = __builtin_nontemporal_load((const f32x4*)(W + (size_t)k * pitch)) * g[k];
;             mx[0] = __builtin_fmaxf(mx[0], __builtin_fabsf(v[0])); mx[1] = __builtin_fmaxf(mx[1], __builtin_fabsf(v[1])); mx[2] = __builtin_fmaxf(mx[2], __builtin_fabsf(v[2])); mx[3] = __builtin_fmaxf(mx[3], __builtin_fabsf(v[3])); } }
	v_pk_mul_f32 v[16:17], v[162:163], v[230:231] op_sel_hi:[1,0]
	v_pk_mul_f32 v[18:19], v[164:165], v[230:231] op_sel_hi:[1,0]
	v_pk_mul_f32 v[20:21], v[166:167], v[232:233] op_sel_hi:[1,0]
	v_pk_mul_f32 v[22:23], v[168:169], v[232:233] op_sel_hi:[1,0]
	v_max3_f32 v15, v15, |v16|, |v20|
	v_max3_f32 v13, v13, |v17|, |v21|
	v_max3_f32 v9, v9, |v18|, |v22|
	v_max3_f32 v7, v7, |v19|, |v23|
	s_add_u32 s6, s6, 0x16000
	s_addc_u32 s7, s7, 0
	global_load_dwordx4 v[162:165], v250, s[6:7] nt
	global_load_dword v230, v251, s[8:9] offset:1504
	s_add_u32 s6, s6, 0x16000
	s_addc_u32 s7, s7, 0
	global_load_dwordx4 v[166:169], v250, s[6:7] nt
	global_load_dword v232, v251, s[8:9] offset:1536
	s_waitcnt vmcnt(44)
	v_pk_mul_f32 v[16:17], v[170:171], v[234:235] op_sel_hi:[1,0]
	v_pk_mul_f32 v[18:19], v[172:173], v[234:235] op_sel_hi:[1,0]
	v_pk_mul_f32 v[20:21], v[174:175], v[236:237] op_sel_hi:[1,0]
	v_pk_mul_f32 v[22:23], v[176:177], v[236:237] op_sel_hi:[1,0]
	v_max3_f32 v15, v15, |v16|, |v20|
	v_max3_f32 v13, v13, |v17|, |v21|
	v_max3_f32 v9, v9, |v18|, |v22|
	v_max3_f32 v7, v7, |v19|, |v23|
	s_add_u32 s6, s6, 0x16000
	s_addc_u32 s7, s7, 0
	global_load_dwordx4 v[170:173], v250, s[6:7] nt
	global_load_dword v234, v251, s[8:9] offset:1568
	s_add_u32 s6, s6, 0x16000
	s_addc_u32 s7, s7, 0
	global_load_dwordx4 v[174:177], v250, s[6:7] nt
	global_load_dword v236, v251, s[8:9] offset:1600
	s_waitcnt vmcnt(44)
	v_pk_mul_f32 v[16:17], v[178:179], v[238:239] op_sel_hi:[1,0]
	v_pk_mul_f32 v[18:19], v[180:181], v[238:239] op_sel_hi:[1,0]
	v_pk_mul_f32 v[20:21], v[182:183], v[240:241] op_sel_hi:[1,0]
	v_pk_mul_f32 v[22:23], v[184:185], v[240:241] op_sel_hi:[1,0]
	v_max3_f32 v15, v15, |v16|, |v20|
	v_max3_f32 v13, v13, |v17|, |v21|
	v_max3_f32 v9, v9, |v18|, |v22|
	v_max3_f32 v7, v7, |v19|, |v23|
	s_add_u32 s6, s6, 0x16000
	s_addc_u32 s7, s7, 0
	global_load_dwordx4 v[178:181], v250, s[6:7] nt
	global_load_dword v238, v251, s[8:9] offset:1632
	s_add_u32 s6, s6, 0x16000
	s_addc_u32 s7, s7, 0
	global_load_dwordx4 v[182:185], v250, s[6:7] nt
	global_load_dword v240, v251, s[8:9] offset:1664
	s_waitcnt vmcnt(44)
	v_pk_mul_f32 v[16:17], v[186:187], v[242:243] op_sel_hi:[1,0]
	v_pk_mul_f32 v[18:19], v[188:189], v[242:243] op_sel_hi:[1,0]
	v_pk_mul_f32 v[20:21], v[190:191], v[244:245] op_sel_hi:[1,0]
	v_pk_mul_f32 v[22:23], v[192:193], v[244:245] op_sel_hi:[1,0]
	v_max3_f32 v15, v15, |v16|, |v20|
	v_max3_f32 v13, v13, |v17|, |v21|
	v_max3_f32 v9, v9, |v18|, |v22|
	v_max3_f32 v7, v7, |v19|, |v23|
	s_add_u32 s6, s6, 0x16000
	s_addc_u32 s7, s7, 0
	global_load_dwordx4 v[186:189], v250, s[6:7] nt
	global_load_dword v242, v251, s[8:9] offset:1696
	s_add_u32 s6, s6, 0x16000
	s_addc_u32 s7, s7, 0
	global_load_dwordx4 v[190:193], v250, s[6:7] nt
	global_load_dword v244, v251, s[8:9] offset:1728
	s_waitcnt vmcnt(44)
	v_pk_mul_f32 v[16:17], v[194:195], v[246:247] op_sel_hi:[1,0]
	v_pk_mul_f32 v[18:19], v[196:197], v[246:247] op_sel_hi:[1,0]
	v_pk_mul_f32 v[20:21], v[198:199], v[248:249] op_sel_hi:[1,0]
	v_pk_mul_f32 v[22:23], v[200:201], v[248:249] op_sel_hi:[1,0]
	v_max3_f32 v15, v15, |v16|, |v20|
	v_max3_f32 v13, v13, |v17|, |v21|
	v_max3_f32 v9, v9, |v18|, |v22|
	v_max3_f32 v7, v7, |v19|, |v23|
	s_add_u32 s6, s6, 0x16000
	s_addc_u32 s7, s7, 0
	global_load_dwordx4 v[194:197], v250, s[6:7] nt
	global_load_dword v246, v251, s[8:9] offset:1760
	s_add_u32 s6, s6, 0x16000
	s_addc_u32 s7, s7, 0
	global_load_dwordx4 v[198:201], v250, s[6:7] nt
	global_load_dword v248, v251, s[8:9] offset:1792
	s_waitcnt vmcnt(44)
	v_pk_mul_f32 v[16:17], v[106:107], v[202:203] op_sel_hi:[1,0]
	v_pk_mul_f32 v[18:19], v[108:109], v[202:203] op_sel_hi:[1,0]
	v_pk_mul_f32 v[20:21], v[110:111], v[204:205] op_sel_hi:[1,0]
	v_pk_mul_f32 v[22:23], v[112:113], v[204:205] op_sel_hi:[1,0]
	v_max3_f32 v15, v15, |v16|, |v20|
	v_max3_f32 v13, v13, |v17|, |v21|
	v_max3_f32 v9, v9, |v18|, |v22|
	v_max3_f32 v7, v7, |v19|, |v23|
	s_add_u32 s6, s6, 0x16000
	s_addc_u32 s7, s7, 0
	global_load_dwordx4 v[106:109], v250, s[6:7] nt
	global_load_dword v202, v251, s[8:9] offset:1824
	s_add_u32 s6, s6, 0x16000
	s_addc_u32 s7, s7, 0
	global_load_dwordx4 v[110:113], v250, s[6:7] nt
	global_load_dword v204, v251, s[8:9] offset:1856
	s_waitcnt vmcnt(44)
	v_pk_mul_f32 v[16:17], v[114:115], v[206:207] op_sel_hi:[1,0]
	v_pk_mul_f32 v[18:19], v[116:117], v[206:207] op_sel_hi:[1,0]
	v_pk_mul_f32 v[20:21], v[118:119], v[208:209] op_sel_hi:[1,0]
	v_pk_mul_f32 v[22:23], v[120:121], v[208:209] op_sel_hi:[1,0]
	v_max3_f32 v15, v15, |v16|, |v20|
	v_max3_f32 v13, v13, |v17|, |v21|
	v_max3_f32 v9, v9, |v18|, |v22|
	v_max3_f32 v7, v7, |v19|, |v23|
	s_add_u32 s6, s6, 0x16000
	s_addc_u32 s7, s7, 0
	global_load_dwordx4 v[114:117], v250, s[6:7] nt
	global_load_dword v206, v251, s[8:9] offset:1888
	s_add_u32 s6, s6, 0x16000
	s_addc_u32 s7, s7, 0
	global_load_dwordx4 v[118:121], v250, s[6:7] nt
	global_load_dword v208, v251, s[8:9] offset:1920
	s_waitcnt vmcnt(44)
	v_pk_mul_f32 v[16:17], v[122:123], v[210:211] op_sel_hi:[1,0]
	v_pk_mul_f32 v[18:19], v[124:125], v[210:211] op_sel_hi:[1,0]
	v_pk_mul_f32 v[20:21], v[126:127], v[212:213] op_sel_hi:[1,0]
	v_pk_mul_f32 v[22:23], v[128:129], v[212:213] op_sel_hi:[1,0]
	v_max3_f32 v15, v15, |v16|, |v20|
	v_max3_f32 v13, v13, |v17|, |v21|
	v_max3_f32 v9, v9, |v18|, |v22|
	v_max3_f32 v7, v7, |v19|, |v23|
	s_add_u32 s6, s6, 0x16000
	s_addc_u32 s7, s7, 0
	global_load_dwordx4 v[122:125], v250, s[6:7] nt
	global_load_dword v210, v251, s[8:9] offset:1952
	s_add_u32 s6, s6, 0x16000
	s_addc_u32 s7, s7, 0
	global_load_dwordx4 v[126:129], v250, s[6:7] nt
	global_load_dword v212, v251, s[8:9] offset:1984
	s_waitcnt vmcnt(44)
;     ...
;     for (int kb = 0; kb < D / 64; ++kb) {
; #pragma unroll
;         for (int i = 0; i < 8; ++i) { const int k = 64 * kb + 8 * i + kr; const f32x4 v = __builtin_nontemporal_load((const f32x4*)(W + (size_t)k * pitch)) * g[k];
;             mx[0] = __builtin_fmaxf(mx[0], __builtin_fabsf(v[0])); mx[1] = __builtin_fmaxf(mx[1], __builtin_fabsf(v[1])); mx[2] = __builtin_fmaxf(mx[2], __builtin_fabsf(v[2])); mx[3] = __builtin_fmaxf(mx[3], __builtin_fabsf(v[3])); } }
	v_pk_mul_f32 v[16:17], v[130:131], v[214:215] op_sel_hi:[1,0]
	v_pk_mul_f32 v[18:19], v[132:133], v[214:215] op_sel_hi:[1,0]
	v_pk_mul_f32 v[20:21], v[134:135], v[216:217] op_sel_hi:[1,0]
	v_pk_mul_f32 v[22:23], v[136:137], v[216:217] op_sel_hi:[1,0]
	v_max3_f32 v15, v15, |v16|, |v20|
	v_max3_f32 v13, v13, |v17|, |v21|
	v_max3_f32 v9, v9, |v18|, |v22|
	v_max3_f32 v7, v7, |v19|, |v23|
	s_add_u32 s6, s6, 0x16000
	s_addc_u32 s7, s7, 0
	global_load_dwordx4 v[130:133], v250, s[6:7] nt
	global_load_dword v214, v251, s[8:9] offset:2016
	s_add_u32 s6, s6, 0x16000
	s_addc_u32 s7, s7, 0
	global_load_dwordx4 v[134:137], v250, s[6:7] nt
	global_load_dword v216, v251, s[8:9] offset:2048
	s_waitcnt vmcnt(44)
	v_pk_mul_f32 v[16:17], v[138:139], v[218:219] op_sel_hi:[1,0]
	v_pk_mul_f32 v[18:19], v[140:141], v[218:219] op_sel_hi:[1,0]
	v_pk_mul_f32 v[20:21], v[142:143], v[220:221] op_sel_hi:[1,0]
	v_pk_mul_f32 v[22:23], v[144:145], v[220:221] op_sel_hi:[1,0]
	v_max3_f32 v15, v15, |v16|, |v20|
	v_max3_f32 v13, v13, |v17|, |v21|
	v_max3_f32 v9, v9, |v18|, |v22|
	v_max3_f32 v7, v7, |v19|, |v23|
	s_add_u32 s6, s6, 0x16000
	s_addc_u32 s7, s7, 0
	global_load_dwordx4 v[138:141], v250, s[6:7] nt
	global_load_dword v218, v251, s[8:9] offset:2080
	s_add_u32 s6, s6, 0x16000
	s_addc_u32 s7, s7, 0
	global_load_dwordx4 v[142:145], v250, s[6:7] nt
	global_load_dword v220, v251, s[8:9] offset:2112
	s_waitcnt vmcnt(44)
	v_pk_mul_f32 v[16:17], v[146:147], v[222:223] op_sel_hi:[1,0]
	v_pk_mul_f32 v[18:19], v[148:149], v[222:223] op_sel_hi:[1,0]
	v_pk_mul_f32 v[20:21], v[150:151], v[224:225] op_sel_hi:[1,0]
	v_pk_mul_f32 v[22:23], v[152:153], v[224:225] op_sel_hi:[1,0]
	v_max3_f32 v15, v15, |v16|, |v20|
	v_max3_f32 v13, v13, |v17|, |v21|
	v_max3_f32 v9, v9, |v18|, |v22|
	v_max3_f32 v7, v7, |v19|, |v23|
	s_add_u32 s6, s6, 0x16000
	s_addc_u32 s7, s7, 0
	global_load_dwordx4 v[146:149], v250, s[6:7] nt
	global_load_dword v222, v251, s[8:9] offset:2144
	s_add_u32 s6, s6, 0x16000
	s_addc_u32 s7, s7, 0
	global_load_dwordx4 v[150:153], v250, s[6:7] nt
	global_load_dword v224, v251, s[8:9] offset:2176
	s_waitcnt vmcnt(44)
	v_pk_mul_f32 v[16:17], v[154:155], v[226:227] op_sel_hi:[1,0]
	v_pk_mul_f32 v[18:19], v[156:157], v[226:227] op_sel_hi:[1,0]
	v_pk_mul_f32 v[20:21], v[158:159], v[228:229] op_sel_hi:[1,0]
	v_pk_mul_f32 v[22:23], v[160:161], v[228:229] op_sel_hi:[1,0]
	v_max3_f32 v15, v15, |v16|, |v20|
	v_max3_f32 v13, v13, |v17|, |v21|
	v_max3_f32 v9, v9, |v18|, |v22|
	v_max3_f32 v7, v7, |v19|, |v23|
	s_add_u32 s6, s6, 0x16000
	s_addc_u32 s7, s7, 0
	global_load_dwordx4 v[154:157], v250, s[6:7] nt
	global_load_dword v226, v251, s[8:9] offset:2208
	s_add_u32 s6, s6, 0x16000
	s_addc_u32 s7, s7, 0
	global_load_dwordx4 v[158:161], v250, s[6:7] nt
	global_load_dword v228, v251, s[8:9] offset:2240
	s_waitcnt vmcnt(44)
	v_pk_mul_f32 v[16:17], v[162:163], v[230:231] op_sel_hi:[1,0]
	v_pk_mul_f32 v[18:19], v[164:165], v[230:231] op_sel_hi:[1,0]
	v_pk_mul_f32 v[20:21], v[166:167], v[232:233] op_sel_hi:[1,0]
	v_pk_mul_f32 v[22:23], v[168:169], v[232:233] op_sel_hi:[1,0]
	v_max3_f32 v15, v15, |v16|, |v20|
	v_max3_f32 v13, v13, |v17|, |v21|
	v_max3_f32 v9, v9, |v18|, |v22|
	v_max3_f32 v7, v7, |v19|, |v23|
	s_add_u32 s6, s6, 0x16000
	s_addc_u32 s7, s7, 0
	global_load_dwordx4 v[162:165], v250, s[6:7] nt
	global_load_dword v230, v251, s[8:9] offset:2272
	s_add_u32 s6, s6, 0x16000
	s_addc_u32 s7, s7, 0
	global_load_dwordx4 v[166:169], v250, s[6:7] nt
	global_load_dword v232, v251, s[8:9] offset:2304
	s_waitcnt vmcnt(44)
	v_pk_mul_f32 v[16:17], v[170:171], v[234:235] op_sel_hi:[1,0]
	v_pk_mul_f32 v[18:19], v[172:173], v[234:235] op_sel_hi:[1,0]
	v_pk_mul_f32 v[20:21], v[174:175], v[236:237] op_sel_hi:[1,0]
	v_pk_mul_f32 v[22:23], v[176:177], v[236:237] op_sel_hi:[1,0]
	v_max3_f32 v15, v15, |v16|, |v20|
	v_max3_f32 v13, v13, |v17|, |v21|
	v_max3_f32 v9, v9, |v18|, |v22|
	v_max3_f32 v7, v7, |v19|, |v23|
	s_add_u32 s6, s6, 0x16000
	s_addc_u32 s7, s7, 0
	global_load_dwordx4 v[170:173], v250, s[6:7] nt
	global_load_dword v234, v251, s[8:9] offset:2336
	s_add_u32 s6, s6, 0x16000
	s_addc_u32 s7, s7, 0
	global_load_dwordx4 v[174:177], v250, s[6:7] nt
	global_load_dword v236, v251, s[8:9] offset:2368
	s_waitcnt vmcnt(44)
	v_pk_mul_f32 v[16:17], v[178:179], v[238:239] op_sel_hi:[1,0]
	v_pk_mul_f32 v[18:19], v[180:181], v[238:239] op_sel_hi:[1,0]
	v_pk_mul_f32 v[20:21], v[182:183], v[240:241] op_sel_hi:[1,0]
	v_pk_mul_f32 v[22:23], v[184:185], v[240:241] op_sel_hi:[1,0]
	v_max3_f32 v15, v15, |v16|, |v20|
	v_max3_f32 v13, v13, |v17|, |v21|
	v_max3_f32 v9, v9, |v18|, |v22|
	v_max3_f32 v7, v7, |v19|, |v23|
	s_add_u32 s6, s6, 0x16000
	s_addc_u32 s7, s7, 0
	global_load_dwordx4 v[178:181], v250, s[6:7] nt
	global_load_dword v238, v251, s[8:9] offset:2400
	s_add_u32 s6, s6, 0x16000
	s_addc_u32 s7, s7, 0
	global_load_dwordx4 v[182:185], v250, s[6:7] nt
	global_load_dword v240, v251, s[8:9] offset:2432
	s_waitcnt vmcnt(44)
	v_pk_mul_f32 v[16:17], v[186:187], v[242:243] op_sel_hi:[1,0]
	v_pk_mul_f32 v[18:19], v[188:189], v[242:243] op_sel_hi:[1,0]
	v_pk_mul_f32 v[20:21], v[190:191], v[244:245] op_sel_hi:[1,0]
	v_pk_mul_f32 v[22:23], v[192:193], v[244:245] op_sel_hi:[1,0]
	v_max3_f32 v15, v15, |v16|, |v20|
	v_max3_f32 v13, v13, |v17|, |v21|
	v_max3_f32 v9, v9, |v18|, |v22|
	v_max3_f32 v7, v7, |v19|, |v23|
	s_add_u32 s6, s6, 0x16000
	s_addc_u32 s7, s7, 0
	global_load_dwordx4 v[186:189], v250, s[6:7] nt
	global_load_dword v242, v251, s[8:9] offset:2464
	s_add_u32 s6, s6, 0x16000
	s_addc_u32 s7, s7, 0
	global_load_dwordx4 v[190:193], v250, s[6:7] nt
	global_load_dword v244, v251, s[8:9] offset:2496
	s_waitcnt vmcnt(44)
;     ...
;     for (int kb = 0; kb < D / 64; ++kb) {
; #pragma unroll
;         for (int i = 0; i < 8; ++i) { const int k = 64 * kb + 8 * i + kr; const f32x4 v = __builtin_nontemporal_load((const f32x4*)(W + (size_t)k * pitch)) * g[k];
;             mx[0] = __builtin_fmaxf(mx[0], __builtin_fabsf(v[0])); mx[1] = __builtin_fmaxf(mx[1], __builtin_fabsf(v[1])); mx[2] = __builtin_fmaxf(mx[2], __builtin_fabsf(v[2])); mx[3] = __builtin_fmaxf(mx[3], __builtin_fabsf(v[3])); } }
	v_pk_mul_f32 v[16:17], v[194:195], v[246:247] op_sel_hi:[1,0]
	v_pk_mul_f32 v[18:19], v[196:197], v[246:247] op_sel_hi:[1,0]
	v_pk_mul_f32 v[20:21], v[198:199], v[248:249] op_sel_hi:[1,0]
	v_pk_mul_f32 v[22:23], v[200:201], v[248:249] op_sel_hi:[1,0]
	v_max3_f32 v15, v15, |v16|, |v20|
	v_max3_f32 v13, v13, |v17|, |v21|
	v_max3_f32 v9, v9, |v18|, |v22|
	v_max3_f32 v7, v7, |v19|, |v23|
	s_add_u32 s6, s6, 0x16000
	s_addc_u32 s7, s7, 0
	global_load_dwordx4 v[194:197], v250, s[6:7] nt
	global_load_dword v246, v251, s[8:9] offset:2528
	s_add_u32 s6, s6, 0x16000
	s_addc_u32 s7, s7, 0
	global_load_dwordx4 v[198:201], v250, s[6:7] nt
	global_load_dword v248, v251, s[8:9] offset:2560
	s_waitcnt vmcnt(44)
	v_pk_mul_f32 v[16:17], v[106:107], v[202:203] op_sel_hi:[1,0]
	v_pk_mul_f32 v[18:19], v[108:109], v[202:203] op_sel_hi:[1,0]
	v_pk_mul_f32 v[20:21], v[110:111], v[204:205] op_sel_hi:[1,0]
	v_pk_mul_f32 v[22:23], v[112:113], v[204:205] op_sel_hi:[1,0]
	v_max3_f32 v15, v15, |v16|, |v20|
	v_max3_f32 v13, v13, |v17|, |v21|
	v_max3_f32 v9, v9, |v18|, |v22|
	v_max3_f32 v7, v7, |v19|, |v23|
	s_add_u32 s6, s6, 0x16000
	s_addc_u32 s7, s7, 0
	global_load_dwordx4 v[106:109], v250, s[6:7] nt
	global_load_dword v202, v251, s[8:9] offset:2592
	s_add_u32 s6, s6, 0x16000
	s_addc_u32 s7, s7, 0
	global_load_dwordx4 v[110:113], v250, s[6:7] nt
	global_load_dword v204, v251, s[8:9] offset:2624
	s_waitcnt vmcnt(44)
	v_pk_mul_f32 v[16:17], v[114:115], v[206:207] op_sel_hi:[1,0]
	v_pk_mul_f32 v[18:19], v[116:117], v[206:207] op_sel_hi:[1,0]
	v_pk_mul_f32 v[20:21], v[118:119], v[208:209] op_sel_hi:[1,0]
	v_pk_mul_f32 v[22:23], v[120:121], v[208:209] op_sel_hi:[1,0]
	v_max3_f32 v15, v15, |v16|, |v20|
	v_max3_f32 v13, v13, |v17|, |v21|
	v_max3_f32 v9, v9, |v18|, |v22|
	v_max3_f32 v7, v7, |v19|, |v23|
	s_add_u32 s6, s6, 0x16000
	s_addc_u32 s7, s7, 0
	global_load_dwordx4 v[114:117], v250, s[6:7] nt
	global_load_dword v206, v251, s[8:9] offset:2656
	s_add_u32 s6, s6, 0x16000
	s_addc_u32 s7, s7, 0
	global_load_dwordx4 v[118:121], v250, s[6:7] nt
	global_load_dword v208, v251, s[8:9] offset:2688
	s_waitcnt vmcnt(44)
	v_pk_mul_f32 v[16:17], v[122:123], v[210:211] op_sel_hi:[1,0]
	v_pk_mul_f32 v[18:19], v[124:125], v[210:211] op_sel_hi:[1,0]
	v_pk_mul_f32 v[20:21], v[126:127], v[212:213] op_sel_hi:[1,0]
	v_pk_mul_f32 v[22:23], v[128:129], v[212:213] op_sel_hi:[1,0]
	v_max3_f32 v15, v15, |v16|, |v20|
	v_max3_f32 v13, v13, |v17|, |v21|
	v_max3_f32 v9, v9, |v18|, |v22|
	v_max3_f32 v7, v7, |v19|, |v23|
	s_add_u32 s6, s6, 0x16000
	s_addc_u32 s7, s7, 0
	global_load_dwordx4 v[122:125], v250, s[6:7] nt
	global_load_dword v210, v251, s[8:9] offset:2720
	s_add_u32 s6, s6, 0x16000
	s_addc_u32 s7, s7, 0
	global_load_dwordx4 v[126:129], v250, s[6:7] nt
	global_load_dword v212, v251, s[8:9] offset:2752
	s_waitcnt vmcnt(44)
	v_pk_mul_f32 v[16:17], v[130:131], v[214:215] op_sel_hi:[1,0]
	v_pk_mul_f32 v[18:19], v[132:133], v[214:215] op_sel_hi:[1,0]
	v_pk_mul_f32 v[20:21], v[134:135], v[216:217] op_sel_hi:[1,0]
	v_pk_mul_f32 v[22:23], v[136:137], v[216:217] op_sel_hi:[1,0]
	v_max3_f32 v15, v15, |v16|, |v20|
	v_max3_f32 v13, v13, |v17|, |v21|
	v_max3_f32 v9, v9, |v18|, |v22|
	v_max3_f32 v7, v7, |v19|, |v23|
	s_add_u32 s6, s6, 0x16000
	s_addc_u32 s7, s7, 0
	global_load_dwordx4 v[130:133], v250, s[6:7] nt
	global_load_dword v214, v251, s[8:9] offset:2784
	s_add_u32 s6, s6, 0x16000
	s_addc_u32 s7, s7, 0
	global_load_dwordx4 v[134:137], v250, s[6:7] nt
	global_load_dword v216, v251, s[8:9] offset:2816
	s_waitcnt vmcnt(44)
	v_pk_mul_f32 v[16:17], v[138:139], v[218:219] op_sel_hi:[1,0]
	v_pk_mul_f32 v[18:19], v[140:141], v[218:219] op_sel_hi:[1,0]
	v_pk_mul_f32 v[20:21], v[142:143], v[220:221] op_sel_hi:[1,0]
	v_pk_mul_f32 v[22:23], v[144:145], v[220:221] op_sel_hi:[1,0]
	v_max3_f32 v15, v15, |v16|, |v20|
	v_max3_f32 v13, v13, |v17|, |v21|
	v_max3_f32 v9, v9, |v18|, |v22|
	v_max3_f32 v7, v7, |v19|, |v23|
	s_add_u32 s6, s6, 0x16000
	s_addc_u32 s7, s7, 0
	global_load_dwordx4 v[138:141], v250, s[6:7] nt
	global_load_dword v218, v251, s[8:9] offset:2848
	s_add_u32 s6, s6, 0x16000
	s_addc_u32 s7, s7, 0
	global_load_dwordx4 v[142:145], v250, s[6:7] nt
	global_load_dword v220, v251, s[8:9] offset:2880
	s_waitcnt vmcnt(44)
	v_pk_mul_f32 v[16:17], v[146:147], v[222:223] op_sel_hi:[1,0]
	v_pk_mul_f32 v[18:19], v[148:149], v[222:223] op_sel_hi:[1,0]
	v_pk_mul_f32 v[20:21], v[150:151], v[224:225] op_sel_hi:[1,0]
	v_pk_mul_f32 v[22:23], v[152:153], v[224:225] op_sel_hi:[1,0]
	v_max3_f32 v15, v15, |v16|, |v20|
	v_max3_f32 v13, v13, |v17|, |v21|
	v_max3_f32 v9, v9, |v18|, |v22|
	v_max3_f32 v7, v7, |v19|, |v23|
	s_add_u32 s6, s6, 0x16000
	s_addc_u32 s7, s7, 0
	global_load_dwordx4 v[146:149], v250, s[6:7] nt
	global_load_dword v222, v251, s[8:9] offset:2912
	s_add_u32 s6, s6, 0x16000
	s_addc_u32 s7, s7, 0
	global_load_dwordx4 v[150:153], v250, s[6:7] nt
	global_load_dword v224, v251, s[8:9] offset:2944
	s_waitcnt vmcnt(44)
	v_pk_mul_f32 v[16:17], v[154:155], v[226:227] op_sel_hi:[1,0]
	v_pk_mul_f32 v[18:19], v[156:157], v[226:227] op_sel_hi:[1,0]
	v_pk_mul_f32 v[20:21], v[158:159], v[228:229] op_sel_hi:[1,0]
	v_pk_mul_f32 v[22:23], v[160:161], v[228:229] op_sel_hi:[1,0]
	v_max3_f32 v15, v15, |v16|, |v20|
	v_max3_f32 v13, v13, |v17|, |v21|
	v_max3_f32 v9, v9, |v18|, |v22|
	v_max3_f32 v7, v7, |v19|, |v23|
	s_add_u32 s6, s6, 0x16000
	s_addc_u32 s7, s7, 0
	global_load_dwordx4 v[154:157], v250, s[6:7] nt
	global_load_dword v226, v251, s[8:9] offset:2976
	s_add_u32 s6, s6, 0x16000
	s_addc_u32 s7, s7, 0
	global_load_dwordx4 v[158:161], v250, s[6:7] nt
	global_load_dword v228, v251, s[8:9] offset:3008
	s_waitcnt vmcnt(44)
;     ...
;     for (int kb = 0; kb < D / 64; ++kb) {
; #pragma unroll
;         for (int i = 0; i < 8; ++i) { const int k = 64 * kb + 8 * i + kr; const f32x4 v = __builtin_nontemporal_load((const f32x4*)(W + (size_t)k * pitch)) * g[k];
;             mx[0] = __builtin_fmaxf(mx[0], __builtin_fabsf(v[0])); mx[1] = __builtin_fmaxf(mx[1], __builtin_fabsf(v[1])); mx[2] = __builtin_fmaxf(mx[2], __builtin_fabsf(v[2])); mx[3] = __builtin_fmaxf(mx[3], __builtin_fabsf(v[3])); } }
	v_pk_mul_f32 v[16:17], v[162:163], v[230:231] op_sel_hi:[1,0]
	v_pk_mul_f32 v[18:19], v[164:165], v[230:231] op_sel_hi:[1,0]
	v_pk_mul_f32 v[20:21], v[166:167], v[232:233] op_sel_hi:[1,0]
	v_pk_mul_f32 v[22:23], v[168:169], v[232:233] op_sel_hi:[1,0]
	v_max3_f32 v15, v15, |v16|, |v20|
	v_max3_f32 v13, v13, |v17|, |v21|
	v_max3_f32 v9, v9, |v18|, |v22|
	v_max3_f32 v7, v7, |v19|, |v23|
	s_add_u32 s6, s6, 0x16000
	s_addc_u32 s7, s7, 0
	global_load_dwordx4 v[162:165], v250, s[6:7] nt
	global_load_dword v230, v251, s[8:9] offset:3040
	s_add_u32 s6, s6, 0x16000
	s_addc_u32 s7, s7, 0
	global_load_dwordx4 v[166:169], v250, s[6:7] nt
	global_load_dword v232, v251, s[8:9] offset:3072
	s_waitcnt vmcnt(44)
	v_pk_mul_f32 v[16:17], v[170:171], v[234:235] op_sel_hi:[1,0]
	v_pk_mul_f32 v[18:19], v[172:173], v[234:235] op_sel_hi:[1,0]
	v_pk_mul_f32 v[20:21], v[174:175], v[236:237] op_sel_hi:[1,0]
	v_pk_mul_f32 v[22:23], v[176:177], v[236:237] op_sel_hi:[1,0]
	v_max3_f32 v15, v15, |v16|, |v20|
	v_max3_f32 v13, v13, |v17|, |v21|
	v_max3_f32 v9, v9, |v18|, |v22|
	v_max3_f32 v7, v7, |v19|, |v23|
	s_add_u32 s6, s6, 0x16000
	s_addc_u32 s7, s7, 0
	global_load_dwordx4 v[170:173], v250, s[6:7] nt
	global_load_dword v234, v251, s[8:9] offset:3104
	s_add_u32 s6, s6, 0x16000
	s_addc_u32 s7, s7, 0
	global_load_dwordx4 v[174:177], v250, s[6:7] nt
	global_load_dword v236, v251, s[8:9] offset:3136
	s_waitcnt vmcnt(44)
	v_pk_mul_f32 v[16:17], v[178:179], v[238:239] op_sel_hi:[1,0]
	v_pk_mul_f32 v[18:19], v[180:181], v[238:239] op_sel_hi:[1,0]
	v_pk_mul_f32 v[20:21], v[182:183], v[240:241] op_sel_hi:[1,0]
	v_pk_mul_f32 v[22:23], v[184:185], v[240:241] op_sel_hi:[1,0]
	v_max3_f32 v15, v15, |v16|, |v20|
	v_max3_f32 v13, v13, |v17|, |v21|
	v_max3_f32 v9, v9, |v18|, |v22|
	v_max3_f32 v7, v7, |v19|, |v23|
	s_add_u32 s6, s6, 0x16000
	s_addc_u32 s7, s7, 0
	global_load_dwordx4 v[178:181], v250, s[6:7] nt
	global_load_dword v238, v251, s[8:9] offset:3168
	s_add_u32 s6, s6, 0x16000
	s_addc_u32 s7, s7, 0
	global_load_dwordx4 v[182:185], v250, s[6:7] nt
	global_load_dword v240, v251, s[8:9] offset:3200
	s_waitcnt vmcnt(44)
	v_pk_mul_f32 v[16:17], v[186:187], v[242:243] op_sel_hi:[1,0]
	v_pk_mul_f32 v[18:19], v[188:189], v[242:243] op_sel_hi:[1,0]
	v_pk_mul_f32 v[20:21], v[190:191], v[244:245] op_sel_hi:[1,0]
	v_pk_mul_f32 v[22:23], v[192:193], v[244:245] op_sel_hi:[1,0]
	v_max3_f32 v15, v15, |v16|, |v20|
	v_max3_f32 v13, v13, |v17|, |v21|
	v_max3_f32 v9, v9, |v18|, |v22|
	v_max3_f32 v7, v7, |v19|, |v23|
	s_add_u32 s6, s6, 0x16000
	s_addc_u32 s7, s7, 0
	global_load_dwordx4 v[186:189], v250, s[6:7] nt
	global_load_dword v242, v251, s[8:9] offset:3232
	s_add_u32 s6, s6, 0x16000
	s_addc_u32 s7, s7, 0
	global_load_dwordx4 v[190:193], v250, s[6:7] nt
	global_load_dword v244, v251, s[8:9] offset:3264
	s_waitcnt vmcnt(44)
	v_pk_mul_f32 v[16:17], v[194:195], v[246:247] op_sel_hi:[1,0]
	v_pk_mul_f32 v[18:19], v[196:197], v[246:247] op_sel_hi:[1,0]
	v_pk_mul_f32 v[20:21], v[198:199], v[248:249] op_sel_hi:[1,0]
	v_pk_mul_f32 v[22:23], v[200:201], v[248:249] op_sel_hi:[1,0]
	v_max3_f32 v15, v15, |v16|, |v20|
	v_max3_f32 v13, v13, |v17|, |v21|
	v_max3_f32 v9, v9, |v18|, |v22|
	v_max3_f32 v7, v7, |v19|, |v23|
	s_add_u32 s6, s6, 0x16000
	s_addc_u32 s7, s7, 0
	global_load_dwordx4 v[194:197], v250, s[6:7] nt
	global_load_dword v246, v251, s[8:9] offset:3296
	s_add_u32 s6, s6, 0x16000
	s_addc_u32 s7, s7, 0
	global_load_dwordx4 v[198:201], v250, s[6:7] nt
	global_load_dword v248, v251, s[8:9] offset:3328
	s_waitcnt vmcnt(44)
	v_pk_mul_f32 v[16:17], v[106:107], v[202:203] op_sel_hi:[1,0]
	v_pk_mul_f32 v[18:19], v[108:109], v[202:203] op_sel_hi:[1,0]
	v_pk_mul_f32 v[20:21], v[110:111], v[204:205] op_sel_hi:[1,0]
	v_pk_mul_f32 v[22:23], v[112:113], v[204:205] op_sel_hi:[1,0]
	v_max3_f32 v15, v15, |v16|, |v20|
	v_max3_f32 v13, v13, |v17|, |v21|
	v_max3_f32 v9, v9, |v18|, |v22|
	v_max3_f32 v7, v7, |v19|, |v23|
	s_add_u32 s6, s6, 0x16000
	s_addc_u32 s7, s7, 0
	global_load_dwordx4 v[106:109], v250, s[6:7] nt
	global_load_dword v202, v251, s[8:9] offset:3360
	s_add_u32 s6, s6, 0x16000
	s_addc_u32 s7, s7, 0
	global_load_dwordx4 v[110:113], v250, s[6:7] nt
	global_load_dword v204, v251, s[8:9] offset:3392
	s_waitcnt vmcnt(44)
	v_pk_mul_f32 v[16:17], v[114:115], v[206:207] op_sel_hi:[1,0]
	v_pk_mul_f32 v[18:19], v[116:117], v[206:207] op_sel_hi:[1,0]
	v_pk_mul_f32 v[20:21], v[118:119], v[208:209] op_sel_hi:[1,0]
	v_pk_mul_f32 v[22:23], v[120:121], v[208:209] op_sel_hi:[1,0]
	v_max3_f32 v15, v15, |v16|, |v20|
	v_max3_f32 v13, v13, |v17|, |v21|
	v_max3_f32 v9, v9, |v18|, |v22|
	v_max3_f32 v7, v7, |v19|, |v23|
	s_add_u32 s6, s6, 0x16000
	s_addc_u32 s7, s7, 0
	global_load_dwordx4 v[114:117], v250, s[6:7] nt
	global_load_dword v206, v251, s[8:9] offset:3424
	s_add_u32 s6, s6, 0x16000
	s_addc_u32 s7, s7, 0
	global_load_dwordx4 v[118:121], v250, s[6:7] nt
	global_load_dword v208, v251, s[8:9] offset:3456
	s_waitcnt vmcnt(44)
	v_pk_mul_f32 v[16:17], v[122:123], v[210:211] op_sel_hi:[1,0]
	v_pk_mul_f32 v[18:19], v[124:125], v[210:211] op_sel_hi:[1,0]
	v_pk_mul_f32 v[20:21], v[126:127], v[212:213] op_sel_hi:[1,0]
	v_pk_mul_f32 v[22:23], v[128:129], v[212:213] op_sel_hi:[1,0]
	v_max3_f32 v15, v15, |v16|, |v20|
	v_max3_f32 v13, v13, |v17|, |v21|
	v_max3_f32 v9, v9, |v18|, |v22|
	v_max3_f32 v7, v7, |v19|, |v23|
	s_add_u32 s6, s6, 0x16000
	s_addc_u32 s7, s7, 0
	global_load_dwordx4 v[122:125], v250, s[6:7] nt
	global_load_dword v210, v251, s[8:9] offset:3488
	s_add_u32 s6, s6, 0x16000
	s_addc_u32 s7, s7, 0
	global_load_dwordx4 v[126:129], v250, s[6:7] nt
	global_load_dword v212, v251, s[8:9] offset:3520
	s_waitcnt vmcnt(44)
;     ...
;     for (int kb = 0; kb < D / 64; ++kb) {
; #pragma unroll
;         for (int i = 0; i < 8; ++i) { const int k = 64 * kb + 8 * i + kr; const f32x4 v = __builtin_nontemporal_load((const f32x4*)(W + (size_t)k * pitch)) * g[k];
;             mx[0] = __builtin_fmaxf(mx[0], __builtin_fabsf(v[0])); mx[1] = __builtin_fmaxf(mx[1], __builtin_fabsf(v[1])); mx[2] = __builtin_fmaxf(mx[2], __builtin_fabsf(v[2])); mx[3] = __builtin_fmaxf(mx[3], __builtin_fabsf(v[3])); } }
	v_pk_mul_f32 v[16:17], v[130:131], v[214:215] op_sel_hi:[1,0]
	v_pk_mul_f32 v[18:19], v[132:133], v[214:215] op_sel_hi:[1,0]
	v_pk_mul_f32 v[20:21], v[134:135], v[216:217] op_sel_hi:[1,0]
	v_pk_mul_f32 v[22:23], v[136:137], v[216:217] op_sel_hi:[1,0]
	v_max3_f32 v15, v15, |v16|, |v20|
	v_max3_f32 v13, v13, |v17|, |v21|
	v_max3_f32 v9, v9, |v18|, |v22|
	v_max3_f32 v7, v7, |v19|, |v23|
	s_add_u32 s6, s6, 0x16000
	s_addc_u32 s7, s7, 0
	global_load_dwordx4 v[130:133], v250, s[6:7] nt
	global_load_dword v214, v251, s[8:9] offset:3552
	s_add_u32 s6, s6, 0x16000
	s_addc_u32 s7, s7, 0
	global_load_dwordx4 v[134:137], v250, s[6:7] nt
	global_load_dword v216, v251, s[8:9] offset:3584
	s_waitcnt vmcnt(44)
	v_pk_mul_f32 v[16:17], v[138:139], v[218:219] op_sel_hi:[1,0]
	v_pk_mul_f32 v[18:19], v[140:141], v[218:219] op_sel_hi:[1,0]
	v_pk_mul_f32 v[20:21], v[142:143], v[220:221] op_sel_hi:[1,0]
	v_pk_mul_f32 v[22:23], v[144:145], v[220:221] op_sel_hi:[1,0]
	v_max3_f32 v15, v15, |v16|, |v20|
	v_max3_f32 v13, v13, |v17|, |v21|
	v_max3_f32 v9, v9, |v18|, |v22|
	v_max3_f32 v7, v7, |v19|, |v23|
	s_waitcnt vmcnt(40)
	v_pk_mul_f32 v[16:17], v[146:147], v[222:223] op_sel_hi:[1,0]
	v_pk_mul_f32 v[18:19], v[148:149], v[222:223] op_sel_hi:[1,0]
	v_pk_mul_f32 v[20:21], v[150:151], v[224:225] op_sel_hi:[1,0]
	v_pk_mul_f32 v[22:23], v[152:153], v[224:225] op_sel_hi:[1,0]
	v_max3_f32 v15, v15, |v16|, |v20|
	v_max3_f32 v13, v13, |v17|, |v21|
	v_max3_f32 v9, v9, |v18|, |v22|
	v_max3_f32 v7, v7, |v19|, |v23|
	s_waitcnt vmcnt(36)
	v_pk_mul_f32 v[16:17], v[154:155], v[226:227] op_sel_hi:[1,0]
	v_pk_mul_f32 v[18:19], v[156:157], v[226:227] op_sel_hi:[1,0]
	v_pk_mul_f32 v[20:21], v[158:159], v[228:229] op_sel_hi:[1,0]
	v_pk_mul_f32 v[22:23], v[160:161], v[228:229] op_sel_hi:[1,0]
	v_max3_f32 v15, v15, |v16|, |v20|
	v_max3_f32 v13, v13, |v17|, |v21|
	v_max3_f32 v9, v9, |v18|, |v22|
	v_max3_f32 v7, v7, |v19|, |v23|
	s_waitcnt vmcnt(32)
	v_pk_mul_f32 v[16:17], v[162:163], v[230:231] op_sel_hi:[1,0]
	v_pk_mul_f32 v[18:19], v[164:165], v[230:231] op_sel_hi:[1,0]
	v_pk_mul_f32 v[20:21], v[166:167], v[232:233] op_sel_hi:[1,0]
	v_pk_mul_f32 v[22:23], v[168:169], v[232:233] op_sel_hi:[1,0]
	v_max3_f32 v15, v15, |v16|, |v20|
	v_max3_f32 v13, v13, |v17|, |v21|
	v_max3_f32 v9, v9, |v18|, |v22|
	v_max3_f32 v7, v7, |v19|, |v23|
	s_waitcnt vmcnt(28)
	v_pk_mul_f32 v[16:17], v[170:171], v[234:235] op_sel_hi:[1,0]
	v_pk_mul_f32 v[18:19], v[172:173], v[234:235] op_sel_hi:[1,0]
	v_pk_mul_f32 v[20:21], v[174:175], v[236:237] op_sel_hi:[1,0]
	v_pk_mul_f32 v[22:23], v[176:177], v[236:237] op_sel_hi:[1,0]
	v_max3_f32 v15, v15, |v16|, |v20|
	v_max3_f32 v13, v13, |v17|, |v21|
	v_max3_f32 v9, v9, |v18|, |v22|
	v_max3_f32 v7, v7, |v19|, |v23|
	s_waitcnt vmcnt(24)
	v_pk_mul_f32 v[16:17], v[178:179], v[238:239] op_sel_hi:[1,0]
	v_pk_mul_f32 v[18:19], v[180:181], v[238:239] op_sel_hi:[1,0]
	v_pk_mul_f32 v[20:21], v[182:183], v[240:241] op_sel_hi:[1,0]
	v_pk_mul_f32 v[22:23], v[184:185], v[240:241] op_sel_hi:[1,0]
	v_max3_f32 v15, v15, |v16|, |v20|
	v_max3_f32 v13, v13, |v17|, |v21|
	v_max3_f32 v9, v9, |v18|, |v22|
	v_max3_f32 v7, v7, |v19|, |v23|
	s_waitcnt vmcnt(20)
	v_pk_mul_f32 v[16:17], v[186:187], v[242:243] op_sel_hi:[1,0]
	v_pk_mul_f32 v[18:19], v[188:189], v[242:243] op_sel_hi:[1,0]
	v_pk_mul_f32 v[20:21], v[190:191], v[244:245] op_sel_hi:[1,0]
	v_pk_mul_f32 v[22:23], v[192:193], v[244:245] op_sel_hi:[1,0]
	v_max3_f32 v15, v15, |v16|, |v20|
	v_max3_f32 v13, v13, |v17|, |v21|
	v_max3_f32 v9, v9, |v18|, |v22|
	v_max3_f32 v7, v7, |v19|, |v23|
	s_waitcnt vmcnt(16)
	v_pk_mul_f32 v[16:17], v[194:195], v[246:247] op_sel_hi:[1,0]
	v_pk_mul_f32 v[18:19], v[196:197], v[246:247] op_sel_hi:[1,0]
	v_pk_mul_f32 v[20:21], v[198:199], v[248:249] op_sel_hi:[1,0]
	v_pk_mul_f32 v[22:23], v[200:201], v[248:249] op_sel_hi:[1,0]
	v_max3_f32 v15, v15, |v16|, |v20|
	v_max3_f32 v13, v13, |v17|, |v21|
	v_max3_f32 v9, v9, |v18|, |v22|
	v_max3_f32 v7, v7, |v19|, |v23|
	s_waitcnt vmcnt(12)
; __device__ __forceinline__ float shfl_xor_f(float v, int mask, int lane) { return __int_as_float(__builtin_amdgcn_ds_bpermute((lane ^ mask) << 2, __float_as_int(v))); }
;     ...
;         for (int i = 0; i < 8; ++i) { const int k = 64 * kb + 8 * i + kr; const f32x4 v = __builtin_nontemporal_load((const f32x4*)(W + (size_t)k * pitch)) * g[k];
;             mx[0] = __builtin_fmaxf(mx[0], __builtin_fabsf(v[0])); mx[1] = __builtin_fmaxf(mx[1], __builtin_fabsf(v[1])); mx[2] = __builtin_fmaxf(mx[2], __builtin_fabsf(v[2])); mx[3] = __builtin_fmaxf(mx[3], __builtin_fabsf(v[3])); } }
; #pragma unroll
;     for (int c = 0; c < 4; ++c) { float m = mx[c]; m = __builtin_fmaxf(m, shfl_xor_f(m, 8, lane)); m = __builtin_fmaxf(m, shfl_xor_f(m, 16, lane)); m = __builtin_fmaxf(m, shfl_xor_f(m, 32, lane)); mx[c] = m; }
;     f32x4 inv, step;
; #pragma unroll
;     for (int c = 0; c < 4; ++c) { step[c] = mx[c] > 0.f ? mx[c] * (1.0f / 127.0f) : 1.0f; inv[c] = mx[c] > 0.f ? 127.0f / mx[c] : 0.f; }
;     if (lane < 8) *(f32x4*)(sw + n0 + 4 * lane) = step * swm;
	v_pk_mul_f32 v[16:17], v[106:107], v[202:203] op_sel_hi:[1,0]
	v_pk_mul_f32 v[18:19], v[108:109], v[202:203] op_sel_hi:[1,0]
	v_pk_mul_f32 v[20:21], v[110:111], v[204:205] op_sel_hi:[1,0]
	v_pk_mul_f32 v[22:23], v[112:113], v[204:205] op_sel_hi:[1,0]
	v_max3_f32 v15, v15, |v16|, |v20|
	v_max3_f32 v13, v13, |v17|, |v21|
	v_max3_f32 v9, v9, |v18|, |v22|
	v_max3_f32 v7, v7, |v19|, |v23|
	s_waitcnt vmcnt(8)
	v_pk_mul_f32 v[16:17], v[114:115], v[206:207] op_sel_hi:[1,0]
	v_pk_mul_f32 v[18:19], v[116:117], v[206:207] op_sel_hi:[1,0]
	v_pk_mul_f32 v[20:21], v[118:119], v[208:209] op_sel_hi:[1,0]
	v_pk_mul_f32 v[22:23], v[120:121], v[208:209] op_sel_hi:[1,0]
	v_max3_f32 v15, v15, |v16|, |v20|
	v_max3_f32 v13, v13, |v17|, |v21|
	v_max3_f32 v9, v9, |v18|, |v22|
	v_max3_f32 v7, v7, |v19|, |v23|
	s_waitcnt vmcnt(4)
	v_pk_mul_f32 v[16:17], v[122:123], v[210:211] op_sel_hi:[1,0]
	v_pk_mul_f32 v[18:19], v[124:125], v[210:211] op_sel_hi:[1,0]
	v_pk_mul_f32 v[20:21], v[126:127], v[212:213] op_sel_hi:[1,0]
	v_pk_mul_f32 v[22:23], v[128:129], v[212:213] op_sel_hi:[1,0]
	v_max3_f32 v15, v15, |v16|, |v20|
	v_max3_f32 v13, v13, |v17|, |v21|
	v_max3_f32 v9, v9, |v18|, |v22|
	v_max3_f32 v7, v7, |v19|, |v23|
	s_waitcnt vmcnt(0)
	v_pk_mul_f32 v[16:17], v[130:131], v[214:215] op_sel_hi:[1,0]
	v_pk_mul_f32 v[18:19], v[132:133], v[214:215] op_sel_hi:[1,0]
	v_pk_mul_f32 v[20:21], v[134:135], v[216:217] op_sel_hi:[1,0]
	v_pk_mul_f32 v[22:23], v[136:137], v[216:217] op_sel_hi:[1,0]
	v_max3_f32 v15, v15, |v16|, |v20|
	v_max3_f32 v13, v13, |v17|, |v21|
	v_max3_f32 v9, v9, |v18|, |v22|
	v_max3_f32 v7, v7, |v19|, |v23|
	v_lshlrev_b32_e32 v2, 2, v68
	v_xor_b32_e32 v3, 32, v2
	ds_bpermute_b32 v4, v3, v15
	v_max_f32_e32 v5, v15, v15
	v_xor_b32_e32 v8, 64, v2
	ds_bpermute_b32 v10, v3, v13
	v_max_f32_e32 v6, v13, v13
	s_waitcnt lgkmcnt(1)
	v_max_f32_e32 v4, v4, v4
	v_max_f32_e32 v4, v5, v4
	ds_bpermute_b32 v5, v8, v4
	s_waitcnt lgkmcnt(1)
	v_max_f32_e32 v10, v10, v10
	v_xor_b32_e32 v11, 0x80, v2
	v_max_f32_e32 v6, v6, v10
	ds_bpermute_b32 v10, v8, v6
	s_waitcnt lgkmcnt(1)
	v_max_f32_e32 v5, v5, v5
	v_max_f32_e32 v4, v4, v5
	ds_bpermute_b32 v5, v11, v4
	ds_bpermute_b32 v12, v3, v9
	ds_bpermute_b32 v3, v3, v7
	s_waitcnt lgkmcnt(3)
	v_max_f32_e32 v10, v10, v10
	v_max_f32_e32 v10, v6, v10
	s_waitcnt lgkmcnt(2)
	v_max_f32_e32 v5, v5, v5
	v_max_f32_e32 v6, v4, v5
	s_waitcnt lgkmcnt(1)
	v_max_f32_e32 v4, v12, v12
	v_max_f32_e32 v5, v9, v9
	v_max_f32_e32 v4, v5, v4
	s_waitcnt lgkmcnt(0)
	v_max_f32_e32 v3, v3, v3
	v_max_f32_e32 v7, v7, v7
	ds_bpermute_b32 v5, v8, v4
	v_max_f32_e32 v3, v7, v3
	ds_bpermute_b32 v7, v8, v3
	ds_bpermute_b32 v8, v11, v10
	v_cmp_lt_f32_e64 s[12:13], 0, v6
	s_waitcnt lgkmcnt(2)
	v_max_f32_e32 v5, v5, v5
	v_max_f32_e32 v4, v4, v5
	s_waitcnt lgkmcnt(1)
	v_max_f32_e32 v5, v7, v7
	v_max_f32_e32 v3, v3, v5
	ds_bpermute_b32 v9, v11, v4
	ds_bpermute_b32 v7, v11, v3
	s_waitcnt lgkmcnt(2)
	v_max_f32_e32 v5, v8, v8
	v_max_f32_e32 v5, v10, v5
	v_cmp_lt_f32_e64 s[10:11], 0, v5
	s_waitcnt lgkmcnt(1)
	v_max_f32_e32 v8, v9, v9
	s_waitcnt lgkmcnt(0)
	v_max_f32_e32 v7, v7, v7
	v_max_f32_e32 v4, v4, v8
	v_max_f32_e32 v3, v3, v7
	v_cmp_lt_f32_e64 s[8:9], 0, v4
	v_cmp_lt_f32_e64 s[6:7], 0, v3
	v_cmp_gt_u32_e32 vcc, 8, v68
	s_and_saveexec_b64 s[40:41], vcc
	s_cbranch_execz .LBB0_138
	s_mul_i32 s43, s28, 0x5800
	s_mul_hi_i32 s39, s28, 0x5800
	s_add_u32 s43, s14, s43
	v_mov_b32_e32 v7, 0x3f317218
	v_mov_b32_e32 v8, 0x3fb8aa3b
	s_addc_u32 s44, s15, s39
	v_cndmask_b32_e64 v8, v7, v8, s[4:5]
	v_mul_f32_e32 v7, 0x3c010204, v6
	s_ashr_i32 s39, s38, 31
	v_cndmask_b32_e64 v12, 1.0, v7, s[12:13]
	v_mul_f32_e32 v7, 0x3c010204, v5
	s_lshl_b64 s[4:5], s[38:39], 2
	v_cndmask_b32_e64 v13, 1.0, v7, s[10:11]
	v_mul_f32_e32 v7, 0x3c010204, v4
	s_add_u32 s4, s43, s4
	v_cndmask_b32_e64 v10, 1.0, v7, s[8:9]
	v_mul_f32_e32 v7, 0x3c010204, v3
	s_addc_u32 s5, s44, s5
	v_lshlrev_b32_e32 v14, 2, v2
	v_mov_b32_e32 v15, 0
	v_cndmask_b32_e64 v11, 1.0, v7, s[6:7]
	v_lshl_add_u64 v[14:15], s[4:5], 0, v[14:15]
	v_pk_mul_f32 v[10:11], v[8:9], v[10:11] op_sel_hi:[0,1]
	v_pk_mul_f32 v[8:9], v[8:9], v[12:13] op_sel_hi:[0,1]
	v_add_co_u32_e32 v12, vcc, 0x40000, v14
	s_nop 1
	v_addc_co_u32_e32 v13, vcc, 0, v15, vcc
	global_store_dwordx4 v[12:13], v[8:11], off

;     ...
;     for (int kb = 0; kb < D / 64; ++kb) {
; #pragma unroll
;         for (int i = 0; i < 8; ++i) { const int kk = 8 * i + kr; const int k = 64 * kb + kk; const f32x4 v = __builtin_nontemporal_load((const f32x4*)(W + (size_t)k * pitch)) * g[k];
.LBB0_139:
	v_readfirstlane_b32 s4, v0
	v_readfirstlane_b32 s5, v1
	v_readfirstlane_b32 s6, v2
	v_readfirstlane_b32 s7, v3
	s_nop 1
	v_subrev_u32_e32 v250, s4, v0
	v_subrev_u32_e32 v251, s6, v2
	s_add_u32 s4, s4, s26
	s_addc_u32 s5, s5, s27
	s_nop 4
	global_load_dwordx4 v[106:109], v250, s[4:5] nt
	global_load_dword v202, v251, s[6:7]
	s_add_u32 s4, s4, 0x16000
	s_addc_u32 s5, s5, 0
	global_load_dwordx4 v[110:113], v250, s[4:5] nt
	global_load_dword v204, v251, s[6:7] offset:32
	s_add_u32 s4, s4, 0x16000
	s_addc_u32 s5, s5, 0
	global_load_dwordx4 v[114:117], v250, s[4:5] nt
	global_load_dword v206, v251, s[6:7] offset:64
	s_add_u32 s4, s4, 0x16000
	s_addc_u32 s5, s5, 0
	global_load_dwordx4 v[118:121], v250, s[4:5] nt
	global_load_dword v208, v251, s[6:7] offset:96
	s_add_u32 s4, s4, 0x16000
	s_addc_u32 s5, s5, 0
	global_load_dwordx4 v[122:125], v250, s[4:5] nt
	global_load_dword v210, v251, s[6:7] offset:128
	s_add_u32 s4, s4, 0x16000
	s_addc_u32 s5, s5, 0
	global_load_dwordx4 v[126:129], v250, s[4:5] nt
	global_load_dword v212, v251, s[6:7] offset:160
	s_add_u32 s4, s4, 0x16000
	s_addc_u32 s5, s5, 0
	global_load_dwordx4 v[130:133], v250, s[4:5] nt
	global_load_dword v214, v251, s[6:7] offset:192
	s_add_u32 s4, s4, 0x16000
	s_addc_u32 s5, s5, 0
	global_load_dwordx4 v[134:137], v250, s[4:5] nt
	global_load_dword v216, v251, s[6:7] offset:224
	s_add_u32 s4, s4, 0x16000
	s_addc_u32 s5, s5, 0
	global_load_dwordx4 v[138:141], v250, s[4:5] nt
	global_load_dword v218, v251, s[6:7] offset:256
	s_add_u32 s4, s4, 0x16000
	s_addc_u32 s5, s5, 0
	global_load_dwordx4 v[142:145], v250, s[4:5] nt
	global_load_dword v220, v251, s[6:7] offset:288
	s_add_u32 s4, s4, 0x16000
	s_addc_u32 s5, s5, 0
	global_load_dwordx4 v[146:149], v250, s[4:5] nt
	global_load_dword v222, v251, s[6:7] offset:320
	s_add_u32 s4, s4, 0x16000
	s_addc_u32 s5, s5, 0
	global_load_dwordx4 v[150:153], v250, s[4:5] nt
	global_load_dword v224, v251, s[6:7] offset:352
	s_add_u32 s4, s4, 0x16000
	s_addc_u32 s5, s5, 0
	global_load_dwordx4 v[154:157], v250, s[4:5] nt
	global_load_dword v226, v251, s[6:7] offset:384
	s_add_u32 s4, s4, 0x16000
	s_addc_u32 s5, s5, 0
	global_load_dwordx4 v[158:161], v250, s[4:5] nt
	global_load_dword v228, v251, s[6:7] offset:416
	s_add_u32 s4, s4, 0x16000
	s_addc_u32 s5, s5, 0
	global_load_dwordx4 v[162:165], v250, s[4:5] nt
	global_load_dword v230, v251, s[6:7] offset:448
	s_add_u32 s4, s4, 0x16000
	s_addc_u32 s5, s5, 0
	global_load_dwordx4 v[166:169], v250, s[4:5] nt
	global_load_dword v232, v251, s[6:7] offset:480
	s_add_u32 s4, s4, 0x16000
	s_addc_u32 s5, s5, 0
	global_load_dwordx4 v[170:173], v250, s[4:5] nt
	global_load_dword v234, v251, s[6:7] offset:512
	s_add_u32 s4, s4, 0x16000
	s_addc_u32 s5, s5, 0
	global_load_dwordx4 v[174:177], v250, s[4:5] nt
	global_load_dword v236, v251, s[6:7] offset:544
	s_add_u32 s4, s4, 0x16000
	s_addc_u32 s5, s5, 0
	global_load_dwordx4 v[178:181], v250, s[4:5] nt
	global_load_dword v238, v251, s[6:7] offset:576
	s_add_u32 s4, s4, 0x16000
	s_addc_u32 s5, s5, 0
	global_load_dwordx4 v[182:185], v250, s[4:5] nt
	global_load_dword v240, v251, s[6:7] offset:608
	s_add_u32 s4, s4, 0x16000
	s_addc_u32 s5, s5, 0
	global_load_dwordx4 v[186:189], v250, s[4:5] nt
	global_load_dword v242, v251, s[6:7] offset:640
	s_add_u32 s4, s4, 0x16000
	s_addc_u32 s5, s5, 0
	global_load_dwordx4 v[190:193], v250, s[4:5] nt
	global_load_dword v244, v251, s[6:7] offset:672
	s_add_u32 s4, s4, 0x16000
	s_addc_u32 s5, s5, 0
	global_load_dwordx4 v[194:197], v250, s[4:5] nt
	global_load_dword v246, v251, s[6:7] offset:704
	s_add_u32 s4, s4, 0x16000
	s_addc_u32 s5, s5, 0
	global_load_dwordx4 v[198:201], v250, s[4:5] nt
	global_load_dword v248, v251, s[6:7] offset:736
	v_add_u32_e32 v77, 0x420, v25
	v_add_u32_e32 v79, 0x428, v25
	v_add_u32_e32 v81, 0x840, v25
	v_add_u32_e32 v83, 0x848, v25
	v_add_u32_e32 v85, 0xc60, v25
	v_add_u32_e32 v87, 0xc68, v25
	v_add_u32_e32 v89, 0x1080, v25
	v_add_u32_e32 v91, 0x1088, v25
	v_add_u32_e32 v92, 0x14a0, v25
	v_add_u32_e32 v93, 0x14a8, v25
	v_add_u32_e32 v94, 0x18c0, v25
	v_add_u32_e32 v95, 0x18c8, v25
	v_add_u32_e32 v96, 0x1ce0, v25
	v_add_u32_e32 v97, 0x1ce8, v25
	v_lshl_add_u64 v[16:17], v[10:11], 0, s[26:27]
	v_lshl_add_u64 v[18:19], v[8:9], 0, s[26:27]
	v_lshl_add_u64 v[58:59], v[6:7], 0, s[26:27]
	v_lshl_add_u64 v[60:61], v[4:5], 0, s[26:27]
	v_lshl_add_u64 v[4:5], v[4:5], 0, 64
	v_lshl_add_u64 v[6:7], v[6:7], 0, 64
	v_lshl_add_u64 v[8:9], v[8:9], 0, 64
	v_lshl_add_u64 v[10:11], v[10:11], 0, 64
	s_waitcnt vmcnt(32)
; #define LAS __attribute__((address_space(3)))
; #define GAS __attribute__((address_space(1)))
; #define LDS_WAIT() asm volatile("s_waitcnt lgkmcnt(0)" ::: "memory")
;     ...
;     for (int kb = 0; kb < D / 64; ++kb) {
; #pragma unroll
;         for (int i = 0; i < 8; ++i) { const int kk = 8 * i + kr; const int k = 64 * kb + kk; const f32x4 v = __builtin_nontemporal_load((const f32x4*)(W + (size_t)k * pitch)) * g[k];
;             LAS float* p = scr + kk * 33 + 4 * (lane & 7); p[0] = __builtin_rintf(v[0] * inv[0]); p[1] = __builtin_rintf(v[1] * inv[1]); p[2] = __builtin_rintf(v[2] * inv[2]); p[3] = __builtin_rintf(v[3] * inv[3]); }
;         LDS_WAIT(); asm volatile("" ::: "memory");
;         const int c = lane & 7;
; #pragma unroll
;         for (int j = 0; j < 4; ++j) { const int n = (lane >> 3) + 8 * j; const LAS float* sp = scr + (8 * c) * 33 + n;
;             u32x2 o;
;             o.x = ((unsigned)(int)sp[0 * 33] & 0xFFu) | (((unsigned)(int)sp[1 * 33] & 0xFFu) << 8) | (((unsigned)(int)sp[2 * 33] & 0xFFu) << 16) | (((unsigned)(int)sp[3 * 33] & 0xFFu) << 24);
;             o.y = ((unsigned)(int)sp[4 * 33] & 0xFFu) | (((unsigned)(int)sp[5 * 33] & 0xFFu) << 8) | (((unsigned)(int)sp[6 * 33] & 0xFFu) << 16) | (((unsigned)(int)sp[7 * 33] & 0xFFu) << 24);
;             *(GAS u32x2*)(dst + (size_t)(n0 + n) * D + 64 * kb + 8 * c) = o; }
;         LDS_WAIT(); asm volatile("" ::: "memory");
	v_pk_mul_f32 v[14:15], v[106:107], v[202:203] op_sel_hi:[1,0]
	v_pk_mul_f32 v[12:13], v[108:109], v[202:203] op_sel_hi:[1,0]
	v_mul_f32_e32 v62, v20, v14
	v_mul_f32_e32 v63, v21, v15
	v_mul_f32_e32 v64, v22, v12
	v_mul_f32_e32 v65, v23, v13
	v_pk_mul_f32 v[14:15], v[110:111], v[204:205] op_sel_hi:[1,0]
	v_pk_mul_f32 v[12:13], v[112:113], v[204:205] op_sel_hi:[1,0]
	v_pk_mul_f32 v[26:27], v[116:117], v[206:207] op_sel_hi:[1,0]
	v_pk_mul_f32 v[28:29], v[114:115], v[206:207] op_sel_hi:[1,0]
	v_pk_mul_f32 v[30:31], v[120:121], v[208:209] op_sel_hi:[1,0]
	v_pk_mul_f32 v[32:33], v[118:119], v[208:209] op_sel_hi:[1,0]
	v_pk_mul_f32 v[34:35], v[124:125], v[210:211] op_sel_hi:[1,0]
	v_pk_mul_f32 v[36:37], v[122:123], v[210:211] op_sel_hi:[1,0]
	v_pk_mul_f32 v[38:39], v[128:129], v[212:213] op_sel_hi:[1,0]
	v_pk_mul_f32 v[40:41], v[126:127], v[212:213] op_sel_hi:[1,0]
	v_pk_mul_f32 v[42:43], v[132:133], v[214:215] op_sel_hi:[1,0]
	v_pk_mul_f32 v[44:45], v[130:131], v[214:215] op_sel_hi:[1,0]
	v_pk_mul_f32 v[46:47], v[136:137], v[216:217] op_sel_hi:[1,0]
	v_pk_mul_f32 v[48:49], v[134:135], v[216:217] op_sel_hi:[1,0]
	s_add_u32 s4, s4, 0x16000
	s_addc_u32 s5, s5, 0
	global_load_dwordx4 v[106:109], v250, s[4:5] nt
	global_load_dword v202, v251, s[6:7] offset:768
	s_add_u32 s4, s4, 0x16000
	s_addc_u32 s5, s5, 0
	global_load_dwordx4 v[110:113], v250, s[4:5] nt
	global_load_dword v204, v251, s[6:7] offset:800
	s_add_u32 s4, s4, 0x16000
	s_addc_u32 s5, s5, 0
	global_load_dwordx4 v[114:117], v250, s[4:5] nt
	global_load_dword v206, v251, s[6:7] offset:832
	s_add_u32 s4, s4, 0x16000
	s_addc_u32 s5, s5, 0
	global_load_dwordx4 v[118:121], v250, s[4:5] nt
	global_load_dword v208, v251, s[6:7] offset:864
	s_add_u32 s4, s4, 0x16000
	s_addc_u32 s5, s5, 0
	global_load_dwordx4 v[122:125], v250, s[4:5] nt
	global_load_dword v210, v251, s[6:7] offset:896
	s_add_u32 s4, s4, 0x16000
	s_addc_u32 s5, s5, 0
	global_load_dwordx4 v[126:129], v250, s[4:5] nt
	global_load_dword v212, v251, s[6:7] offset:928
	s_add_u32 s4, s4, 0x16000
	s_addc_u32 s5, s5, 0
	global_load_dwordx4 v[130:133], v250, s[4:5] nt
	global_load_dword v214, v251, s[6:7] offset:960
	s_add_u32 s4, s4, 0x16000
	s_addc_u32 s5, s5, 0
	global_load_dwordx4 v[134:137], v250, s[4:5] nt
	global_load_dword v216, v251, s[6:7] offset:992
	v_mul_f32_e32 v14, v20, v14
	v_mul_f32_e32 v15, v21, v15
	v_rndne_f32_e32 v50, v62
	v_rndne_f32_e32 v51, v63
	v_mul_f32_e32 v12, v22, v12
	v_mul_f32_e32 v13, v23, v13
	v_mul_f32_e32 v28, v20, v28
	v_mul_f32_e32 v29, v21, v29
	v_mul_f32_e32 v26, v22, v26
	v_mul_f32_e32 v27, v23, v27
	v_mul_f32_e32 v32, v20, v32
	v_mul_f32_e32 v33, v21, v33
	v_mul_f32_e32 v30, v22, v30
	v_mul_f32_e32 v31, v23, v31
	v_mul_f32_e32 v36, v20, v36
	v_mul_f32_e32 v37, v21, v37
	v_mul_f32_e32 v34, v22, v34
	v_mul_f32_e32 v35, v23, v35
	v_mul_f32_e32 v40, v20, v40
	v_mul_f32_e32 v41, v21, v41
	v_mul_f32_e32 v38, v22, v38
	v_mul_f32_e32 v39, v23, v39
	v_mul_f32_e32 v44, v20, v44
	v_mul_f32_e32 v45, v21, v45
	v_mul_f32_e32 v42, v22, v42
	v_mul_f32_e32 v43, v23, v43
	v_mul_f32_e32 v48, v20, v48
	v_mul_f32_e32 v49, v21, v49
	v_mul_f32_e32 v46, v22, v46
	v_mul_f32_e32 v47, v23, v47
	v_rndne_f32_e32 v14, v14
	v_rndne_f32_e32 v15, v15
	v_rndne_f32_e32 v52, v64
	v_rndne_f32_e32 v53, v65
	ds_write2_b32 v25, v50, v51 offset1:1
	ds_write2_b32 v25, v52, v53 offset0:2 offset1:3
	v_rndne_f32_e32 v12, v12
	v_rndne_f32_e32 v13, v13
	v_rndne_f32_e32 v28, v28
	v_rndne_f32_e32 v29, v29
	v_rndne_f32_e32 v26, v26
	v_rndne_f32_e32 v27, v27
	v_rndne_f32_e32 v32, v32
	v_rndne_f32_e32 v33, v33
	v_rndne_f32_e32 v30, v30
	v_rndne_f32_e32 v31, v31
	v_rndne_f32_e32 v36, v36
	v_rndne_f32_e32 v37, v37
	v_rndne_f32_e32 v34, v34
	v_rndne_f32_e32 v35, v35
	v_rndne_f32_e32 v40, v40
	v_rndne_f32_e32 v41, v41
	v_rndne_f32_e32 v38, v38
	v_rndne_f32_e32 v39, v39
	v_rndne_f32_e32 v44, v44
	v_rndne_f32_e32 v45, v45
	v_rndne_f32_e32 v42, v42
	v_rndne_f32_e32 v43, v43
	v_rndne_f32_e32 v48, v48
	v_rndne_f32_e32 v49, v49
	v_rndne_f32_e32 v46, v46
	v_rndne_f32_e32 v47, v47
	ds_write2_b32 v77, v14, v15 offset1:1
	ds_write2_b32 v79, v12, v13 offset1:1
	ds_write2_b32 v81, v28, v29 offset1:1
	ds_write2_b32 v83, v26, v27 offset1:1
	ds_write2_b32 v85, v32, v33 offset1:1
	ds_write2_b32 v87, v30, v31 offset1:1
	ds_write2_b32 v89, v36, v37 offset1:1
	ds_write2_b32 v91, v34, v35 offset1:1
	ds_write2_b32 v92, v40, v41 offset1:1
	ds_write2_b32 v93, v38, v39 offset1:1
	ds_write2_b32 v94, v44, v45 offset1:1
	ds_write2_b32 v95, v42, v43 offset1:1
	ds_write2_b32 v96, v48, v49 offset1:1
	ds_write2_b32 v97, v46, v47 offset1:1
	s_waitcnt lgkmcnt(0)
	ds_read2_b32 v[12:13], v24 offset1:8
	ds_read2_b32 v[14:15], v24 offset0:33 offset1:41
	ds_read2_b32 v[26:27], v24 offset0:66 offset1:74
	ds_read2_b32 v[28:29], v24 offset0:99 offset1:107
	ds_read2_b32 v[30:31], v24 offset0:132 offset1:140
	ds_read2_b32 v[32:33], v24 offset0:165 offset1:173
	ds_read2_b32 v[34:35], v24 offset0:198 offset1:206
	ds_read2_b32 v[36:37], v24 offset0:231 offset1:239
	ds_read2_b32 v[38:39], v24 offset0:16 offset1:24
	ds_read2_b32 v[40:41], v24 offset0:49 offset1:57
	ds_read2_b32 v[42:43], v24 offset0:82 offset1:90
	ds_read2_b32 v[44:45], v24 offset0:115 offset1:123
	ds_read2_b32 v[46:47], v24 offset0:148 offset1:156
	ds_read2_b32 v[48:49], v24 offset0:181 offset1:189
	ds_read2_b32 v[50:51], v24 offset0:214 offset1:222
	ds_read2_b32 v[52:53], v24 offset0:247 offset1:255
	s_waitcnt lgkmcnt(14)
	v_cvt_i32_f32_e32 v14, v14
	s_waitcnt lgkmcnt(10)
	v_cvt_i32_f32_e32 v32, v32
	v_cvt_i32_f32_e32 v12, v12
	v_cvt_i32_f32_sdwa v26, v26 dst_sel:WORD_1 dst_unused:UNUSED_PAD src0_sel:DWORD
	v_cvt_i32_f32_e32 v30, v30
	s_waitcnt lgkmcnt(9)
; #define LAS __attribute__((address_space(3)))
; #define GAS __attribute__((address_space(1)))
; #define LDS_WAIT() asm volatile("s_waitcnt lgkmcnt(0)" ::: "memory")
;     ...
;     for (int kb = 0; kb < D / 64; ++kb) {
; #pragma unroll
;         for (int i = 0; i < 8; ++i) { const int kk = 8 * i + kr; const int k = 64 * kb + kk; const f32x4 v = __builtin_nontemporal_load((const f32x4*)(W + (size_t)k * pitch)) * g[k];
;     ...
;         LDS_WAIT(); asm volatile("" ::: "memory");
;         const int c = lane & 7;
; #pragma unroll
;         for (int j = 0; j < 4; ++j) { const int n = (lane >> 3) + 8 * j; const LAS float* sp = scr + (8 * c) * 33 + n;
;             u32x2 o;
;             o.x = ((unsigned)(int)sp[0 * 33] & 0xFFu) | (((unsigned)(int)sp[1 * 33] & 0xFFu) << 8) | (((unsigned)(int)sp[2 * 33] & 0xFFu) << 16) | (((unsigned)(int)sp[3 * 33] & 0xFFu) << 24);
;             o.y = ((unsigned)(int)sp[4 * 33] & 0xFFu) | (((unsigned)(int)sp[5 * 33] & 0xFFu) << 8) | (((unsigned)(int)sp[6 * 33] & 0xFFu) << 16) | (((unsigned)(int)sp[7 * 33] & 0xFFu) << 24);
;             *(GAS u32x2*)(dst + (size_t)(n0 + n) * D + 64 * kb + 8 * c) = o; }
;         LDS_WAIT(); asm volatile("" ::: "memory");
	v_cvt_i32_f32_sdwa v34, v34 dst_sel:WORD_1 dst_unused:UNUSED_PAD src0_sel:DWORD
	v_cvt_i32_f32_e32 v15, v15
	v_cvt_i32_f32_e32 v33, v33
	s_waitcnt lgkmcnt(6)
	v_cvt_i32_f32_e32 v40, v40
	s_waitcnt lgkmcnt(2)
	v_cvt_i32_f32_e32 v48, v48
	v_cvt_i32_f32_e32 v41, v41
	v_cvt_i32_f32_e32 v49, v49
	v_cvt_i32_f32_sdwa v28, v28 dst_sel:BYTE_3 dst_unused:UNUSED_PAD src0_sel:DWORD
	v_cvt_i32_f32_sdwa v36, v36 dst_sel:BYTE_3 dst_unused:UNUSED_PAD src0_sel:DWORD
	v_cvt_i32_f32_e32 v13, v13
	v_cvt_i32_f32_sdwa v27, v27 dst_sel:WORD_1 dst_unused:UNUSED_PAD src0_sel:DWORD
	v_cvt_i32_f32_e32 v31, v31
	v_cvt_i32_f32_sdwa v35, v35 dst_sel:WORD_1 dst_unused:UNUSED_PAD src0_sel:DWORD
	v_cvt_i32_f32_e32 v38, v38
	v_cvt_i32_f32_sdwa v42, v42 dst_sel:WORD_1 dst_unused:UNUSED_PAD src0_sel:DWORD
	v_cvt_i32_f32_e32 v46, v46
	s_waitcnt lgkmcnt(1)
	v_cvt_i32_f32_sdwa v50, v50 dst_sel:WORD_1 dst_unused:UNUSED_PAD src0_sel:DWORD
	v_cvt_i32_f32_e32 v39, v39
	v_cvt_i32_f32_sdwa v43, v43 dst_sel:WORD_1 dst_unused:UNUSED_PAD src0_sel:DWORD
	v_cvt_i32_f32_e32 v47, v47
	v_cvt_i32_f32_sdwa v51, v51 dst_sel:WORD_1 dst_unused:UNUSED_PAD src0_sel:DWORD
	v_cvt_i32_f32_sdwa v29, v29 dst_sel:BYTE_3 dst_unused:UNUSED_PAD src0_sel:DWORD
	v_cvt_i32_f32_sdwa v37, v37 dst_sel:BYTE_3 dst_unused:UNUSED_PAD src0_sel:DWORD
	v_cvt_i32_f32_sdwa v44, v44 dst_sel:BYTE_3 dst_unused:UNUSED_PAD src0_sel:DWORD
	s_waitcnt lgkmcnt(0)
	v_cvt_i32_f32_sdwa v52, v52 dst_sel:BYTE_3 dst_unused:UNUSED_PAD src0_sel:DWORD
	v_cvt_i32_f32_sdwa v45, v45 dst_sel:BYTE_3 dst_unused:UNUSED_PAD src0_sel:DWORD
	v_cvt_i32_f32_sdwa v53, v53 dst_sel:BYTE_3 dst_unused:UNUSED_PAD src0_sel:DWORD
	v_lshlrev_b32_e32 v14, 8, v14
	v_lshlrev_b32_e32 v32, 8, v32
	v_and_b32_e32 v26, 0xff0000, v26
	v_and_b32_e32 v34, 0xff0000, v34
	v_lshlrev_b32_e32 v15, 8, v15
	v_lshlrev_b32_e32 v33, 8, v33
	v_lshlrev_b32_e32 v40, 8, v40
	v_lshlrev_b32_e32 v48, 8, v48
	v_lshlrev_b32_e32 v41, 8, v41
	v_lshlrev_b32_e32 v49, 8, v49
	v_perm_b32 v12, v14, v12, s28
	v_perm_b32 v14, v32, v30, s28
	v_and_b32_e32 v27, 0xff0000, v27
	v_and_b32_e32 v35, 0xff0000, v35
	v_and_b32_e32 v42, 0xff0000, v42
	v_and_b32_e32 v50, 0xff0000, v50
	v_and_b32_e32 v43, 0xff0000, v43
	v_and_b32_e32 v51, 0xff0000, v51
	v_perm_b32 v15, v15, v13, s28
	v_perm_b32 v30, v33, v31, s28
	v_perm_b32 v31, v40, v38, s28
	v_perm_b32 v32, v48, v46, s28
	v_perm_b32 v33, v41, v39, s28
	v_perm_b32 v38, v49, v47, s28
	v_or3_b32 v12, v12, v26, v28
	v_or3_b32 v13, v14, v34, v36
	v_or3_b32 v14, v15, v27, v29
	v_or3_b32 v15, v30, v35, v37
	v_or3_b32 v26, v31, v42, v44
	v_or3_b32 v27, v32, v50, v52
	v_or3_b32 v28, v33, v43, v45
	v_or3_b32 v29, v38, v51, v53
	global_store_dwordx2 v[16:17], v[12:13], off
	global_store_dwordx2 v[18:19], v[14:15], off
	global_store_dwordx2 v[58:59], v[26:27], off
	global_store_dwordx2 v[60:61], v[28:29], off
	s_waitcnt lgkmcnt(0)
	v_add_u32_e32 v77, 0x420, v25
	v_add_u32_e32 v79, 0x428, v25
	v_add_u32_e32 v81, 0x840, v25
	v_add_u32_e32 v83, 0x848, v25
	v_add_u32_e32 v85, 0xc60, v25
	v_add_u32_e32 v87, 0xc68, v25
	v_add_u32_e32 v89, 0x1080, v25
	v_add_u32_e32 v91, 0x1088, v25
	v_add_u32_e32 v92, 0x14a0, v25
	v_add_u32_e32 v93, 0x14a8, v25
	v_add_u32_e32 v94, 0x18c0, v25
	v_add_u32_e32 v95, 0x18c8, v25
	v_add_u32_e32 v96, 0x1ce0, v25
	v_add_u32_e32 v97, 0x1ce8, v25
	v_lshl_add_u64 v[16:17], v[10:11], 0, s[26:27]
	v_lshl_add_u64 v[18:19], v[8:9], 0, s[26:27]
	v_lshl_add_u64 v[58:59], v[6:7], 0, s[26:27]
	v_lshl_add_u64 v[60:61], v[4:5], 0, s[26:27]
	v_lshl_add_u64 v[4:5], v[4:5], 0, 64
	v_lshl_add_u64 v[6:7], v[6:7], 0, 64
	v_lshl_add_u64 v[8:9], v[8:9], 0, 64
	v_lshl_add_u64 v[10:11], v[10:11], 0, 64
	s_waitcnt vmcnt(36)
	v_pk_mul_f32 v[14:15], v[138:139], v[218:219] op_sel_hi:[1,0]
	v_pk_mul_f32 v[12:13], v[140:141], v[218:219] op_sel_hi:[1,0]
	v_mul_f32_e32 v62, v20, v14
	v_mul_f32_e32 v63, v21, v15
	v_mul_f32_e32 v64, v22, v12
	v_mul_f32_e32 v65, v23, v13
	v_pk_mul_f32 v[14:15], v[142:143], v[220:221] op_sel_hi:[1,0]
	v_pk_mul_f32 v[12:13], v[144:145], v[220:221] op_sel_hi:[1,0]
	v_pk_mul_f32 v[26:27], v[148:149], v[222:223] op_sel_hi:[1,0]
	v_pk_mul_f32 v[28:29], v[146:147], v[222:223] op_sel_hi:[1,0]
	v_pk_mul_f32 v[30:31], v[152:153], v[224:225] op_sel_hi:[1,0]
	v_pk_mul_f32 v[32:33], v[150:151], v[224:225] op_sel_hi:[1,0]
	v_pk_mul_f32 v[34:35], v[156:157], v[226:227] op_sel_hi:[1,0]
	v_pk_mul_f32 v[36:37], v[154:155], v[226:227] op_sel_hi:[1,0]
	v_pk_mul_f32 v[38:39], v[160:161], v[228:229] op_sel_hi:[1,0]
	v_pk_mul_f32 v[40:41], v[158:159], v[228:229] op_sel_hi:[1,0]
	v_pk_mul_f32 v[42:43], v[164:165], v[230:231] op_sel_hi:[1,0]
	v_pk_mul_f32 v[44:45], v[162:163], v[230:231] op_sel_hi:[1,0]
	v_pk_mul_f32 v[46:47], v[168:169], v[232:233] op_sel_hi:[1,0]
	v_pk_mul_f32 v[48:49], v[166:167], v[232:233] op_sel_hi:[1,0]
	s_add_u32 s4, s4, 0x16000
	s_addc_u32 s5, s5, 0
	global_load_dwordx4 v[138:141], v250, s[4:5] nt
	global_load_dword v218, v251, s[6:7] offset:1024
	s_add_u32 s4, s4, 0x16000
	s_addc_u32 s5, s5, 0
	global_load_dwordx4 v[142:145], v250, s[4:5] nt
	global_load_dword v220, v251, s[6:7] offset:1056
	s_add_u32 s4, s4, 0x16000
	s_addc_u32 s5, s5, 0
	global_load_dwordx4 v[146:149], v250, s[4:5] nt
	global_load_dword v222, v251, s[6:7] offset:1088
	s_add_u32 s4, s4, 0x16000
	s_addc_u32 s5, s5, 0
	global_load_dwordx4 v[150:153], v250, s[4:5] nt
	global_load_dword v224, v251, s[6:7] offset:1120
	s_add_u32 s4, s4, 0x16000
	s_addc_u32 s5, s5, 0
	global_load_dwordx4 v[154:157], v250, s[4:5] nt
	global_load_dword v226, v251, s[6:7] offset:1152
	s_add_u32 s4, s4, 0x16000
	s_addc_u32 s5, s5, 0
	global_load_dwordx4 v[158:161], v250, s[4:5] nt
; #define LAS __attribute__((address_space(3)))
; #define GAS __attribute__((address_space(1)))
; #define LDS_WAIT() asm volatile("s_waitcnt lgkmcnt(0)" ::: "memory")
;     ...
;     for (int kb = 0; kb < D / 64; ++kb) {
; #pragma unroll
;         for (int i = 0; i < 8; ++i) { const int kk = 8 * i + kr; const int k = 64 * kb + kk; const f32x4 v = __builtin_nontemporal_load((const f32x4*)(W + (size_t)k * pitch)) * g[k];
;             LAS float* p = scr + kk * 33 + 4 * (lane & 7); p[0] = __builtin_rintf(v[0] * inv[0]); p[1] = __builtin_rintf(v[1] * inv[1]); p[2] = __builtin_rintf(v[2] * inv[2]); p[3] = __builtin_rintf(v[3] * inv[3]); }
;         LDS_WAIT(); asm volatile("" ::: "memory");
;         const int c = lane & 7;
; #pragma unroll
;         for (int j = 0; j < 4; ++j) { const int n = (lane >> 3) + 8 * j; const LAS float* sp = scr + (8 * c) * 33 + n;
;             u32x2 o;
;             o.x = ((unsigned)(int)sp[0 * 33] & 0xFFu) | (((unsigned)(int)sp[1 * 33] & 0xFFu) << 8) | (((unsigned)(int)sp[2 * 33] & 0xFFu) << 16) | (((unsigned)(int)sp[3 * 33] & 0xFFu) << 24);
;             o.y = ((unsigned)(int)sp[4 * 33] & 0xFFu) | (((unsigned)(int)sp[5 * 33] & 0xFFu) << 8) | (((unsigned)(int)sp[6 * 33] & 0xFFu) << 16) | (((unsigned)(int)sp[7 * 33] & 0xFFu) << 24);
;             *(GAS u32x2*)(dst + (size_t)(n0 + n) * D + 64 * kb + 8 * c) = o; }
;         LDS_WAIT(); asm volatile("" ::: "memory");
	global_load_dword v228, v251, s[6:7] offset:1184
	s_add_u32 s4, s4, 0x16000
	s_addc_u32 s5, s5, 0
	global_load_dwordx4 v[162:165], v250, s[4:5] nt
	global_load_dword v230, v251, s[6:7] offset:1216
	s_add_u32 s4, s4, 0x16000
	s_addc_u32 s5, s5, 0
	global_load_dwordx4 v[166:169], v250, s[4:5] nt
	global_load_dword v232, v251, s[6:7] offset:1248
	v_mul_f32_e32 v14, v20, v14
	v_mul_f32_e32 v15, v21, v15
	v_rndne_f32_e32 v50, v62
	v_rndne_f32_e32 v51, v63
	v_mul_f32_e32 v12, v22, v12
	v_mul_f32_e32 v13, v23, v13
	v_mul_f32_e32 v28, v20, v28
	v_mul_f32_e32 v29, v21, v29
	v_mul_f32_e32 v26, v22, v26
	v_mul_f32_e32 v27, v23, v27
	v_mul_f32_e32 v32, v20, v32
	v_mul_f32_e32 v33, v21, v33
	v_mul_f32_e32 v30, v22, v30
	v_mul_f32_e32 v31, v23, v31
	v_mul_f32_e32 v36, v20, v36
	v_mul_f32_e32 v37, v21, v37
	v_mul_f32_e32 v34, v22, v34
	v_mul_f32_e32 v35, v23, v35
	v_mul_f32_e32 v40, v20, v40
	v_mul_f32_e32 v41, v21, v41
	v_mul_f32_e32 v38, v22, v38
	v_mul_f32_e32 v39, v23, v39
	v_mul_f32_e32 v44, v20, v44
	v_mul_f32_e32 v45, v21, v45
	v_mul_f32_e32 v42, v22, v42
	v_mul_f32_e32 v43, v23, v43
	v_mul_f32_e32 v48, v20, v48
	v_mul_f32_e32 v49, v21, v49
	v_mul_f32_e32 v46, v22, v46
	v_mul_f32_e32 v47, v23, v47
	v_rndne_f32_e32 v14, v14
	v_rndne_f32_e32 v15, v15
	v_rndne_f32_e32 v52, v64
	v_rndne_f32_e32 v53, v65
	ds_write2_b32 v25, v50, v51 offset1:1
	ds_write2_b32 v25, v52, v53 offset0:2 offset1:3
	v_rndne_f32_e32 v12, v12
	v_rndne_f32_e32 v13, v13
	v_rndne_f32_e32 v28, v28
	v_rndne_f32_e32 v29, v29
	v_rndne_f32_e32 v26, v26
	v_rndne_f32_e32 v27, v27
	v_rndne_f32_e32 v32, v32
	v_rndne_f32_e32 v33, v33
	v_rndne_f32_e32 v30, v30
	v_rndne_f32_e32 v31, v31
	v_rndne_f32_e32 v36, v36
	v_rndne_f32_e32 v37, v37
	v_rndne_f32_e32 v34, v34
	v_rndne_f32_e32 v35, v35
	v_rndne_f32_e32 v40, v40
	v_rndne_f32_e32 v41, v41
	v_rndne_f32_e32 v38, v38
	v_rndne_f32_e32 v39, v39
	v_rndne_f32_e32 v44, v44
	v_rndne_f32_e32 v45, v45
	v_rndne_f32_e32 v42, v42
	v_rndne_f32_e32 v43, v43
	v_rndne_f32_e32 v48, v48
	v_rndne_f32_e32 v49, v49
	v_rndne_f32_e32 v46, v46
	v_rndne_f32_e32 v47, v47
	ds_write2_b32 v77, v14, v15 offset1:1
	ds_write2_b32 v79, v12, v13 offset1:1
	ds_write2_b32 v81, v28, v29 offset1:1
	ds_write2_b32 v83, v26, v27 offset1:1
	ds_write2_b32 v85, v32, v33 offset1:1
	ds_write2_b32 v87, v30, v31 offset1:1
	ds_write2_b32 v89, v36, v37 offset1:1
	ds_write2_b32 v91, v34, v35 offset1:1
	ds_write2_b32 v92, v40, v41 offset1:1
	ds_write2_b32 v93, v38, v39 offset1:1
	ds_write2_b32 v94, v44, v45 offset1:1
	ds_write2_b32 v95, v42, v43 offset1:1
	ds_write2_b32 v96, v48, v49 offset1:1
	ds_write2_b32 v97, v46, v47 offset1:1
	s_waitcnt lgkmcnt(0)
	ds_read2_b32 v[12:13], v24 offset1:8
	ds_read2_b32 v[14:15], v24 offset0:33 offset1:41
	ds_read2_b32 v[26:27], v24 offset0:66 offset1:74
	ds_read2_b32 v[28:29], v24 offset0:99 offset1:107
	ds_read2_b32 v[30:31], v24 offset0:132 offset1:140
	ds_read2_b32 v[32:33], v24 offset0:165 offset1:173
	ds_read2_b32 v[34:35], v24 offset0:198 offset1:206
	ds_read2_b32 v[36:37], v24 offset0:231 offset1:239
	ds_read2_b32 v[38:39], v24 offset0:16 offset1:24
	ds_read2_b32 v[40:41], v24 offset0:49 offset1:57
	ds_read2_b32 v[42:43], v24 offset0:82 offset1:90
	ds_read2_b32 v[44:45], v24 offset0:115 offset1:123
	ds_read2_b32 v[46:47], v24 offset0:148 offset1:156
	ds_read2_b32 v[48:49], v24 offset0:181 offset1:189
	ds_read2_b32 v[50:51], v24 offset0:214 offset1:222
	ds_read2_b32 v[52:53], v24 offset0:247 offset1:255
	s_waitcnt lgkmcnt(14)
	v_cvt_i32_f32_e32 v14, v14
	s_waitcnt lgkmcnt(10)
	v_cvt_i32_f32_e32 v32, v32
	v_cvt_i32_f32_e32 v12, v12
	v_cvt_i32_f32_sdwa v26, v26 dst_sel:WORD_1 dst_unused:UNUSED_PAD src0_sel:DWORD
	v_cvt_i32_f32_e32 v30, v30
	s_waitcnt lgkmcnt(9)
	v_cvt_i32_f32_sdwa v34, v34 dst_sel:WORD_1 dst_unused:UNUSED_PAD src0_sel:DWORD
	v_cvt_i32_f32_e32 v15, v15
	v_cvt_i32_f32_e32 v33, v33
	s_waitcnt lgkmcnt(6)
	v_cvt_i32_f32_e32 v40, v40
	s_waitcnt lgkmcnt(2)
	v_cvt_i32_f32_e32 v48, v48
	v_cvt_i32_f32_e32 v41, v41
	v_cvt_i32_f32_e32 v49, v49
	v_cvt_i32_f32_sdwa v28, v28 dst_sel:BYTE_3 dst_unused:UNUSED_PAD src0_sel:DWORD
	v_cvt_i32_f32_sdwa v36, v36 dst_sel:BYTE_3 dst_unused:UNUSED_PAD src0_sel:DWORD
	v_cvt_i32_f32_e32 v13, v13
	v_cvt_i32_f32_sdwa v27, v27 dst_sel:WORD_1 dst_unused:UNUSED_PAD src0_sel:DWORD
	v_cvt_i32_f32_e32 v31, v31
	v_cvt_i32_f32_sdwa v35, v35 dst_sel:WORD_1 dst_unused:UNUSED_PAD src0_sel:DWORD
	v_cvt_i32_f32_e32 v38, v38
	v_cvt_i32_f32_sdwa v42, v42 dst_sel:WORD_1 dst_unused:UNUSED_PAD src0_sel:DWORD
	v_cvt_i32_f32_e32 v46, v46
	s_waitcnt lgkmcnt(1)
	v_cvt_i32_f32_sdwa v50, v50 dst_sel:WORD_1 dst_unused:UNUSED_PAD src0_sel:DWORD
	v_cvt_i32_f32_e32 v39, v39
	v_cvt_i32_f32_sdwa v43, v43 dst_sel:WORD_1 dst_unused:UNUSED_PAD src0_sel:DWORD
	v_cvt_i32_f32_e32 v47, v47
	v_cvt_i32_f32_sdwa v51, v51 dst_sel:WORD_1 dst_unused:UNUSED_PAD src0_sel:DWORD
	v_cvt_i32_f32_sdwa v29, v29 dst_sel:BYTE_3 dst_unused:UNUSED_PAD src0_sel:DWORD
	v_cvt_i32_f32_sdwa v37, v37 dst_sel:BYTE_3 dst_unused:UNUSED_PAD src0_sel:DWORD
	v_cvt_i32_f32_sdwa v44, v44 dst_sel:BYTE_3 dst_unused:UNUSED_PAD src0_sel:DWORD
	s_waitcnt lgkmcnt(0)
; #define LAS __attribute__((address_space(3)))
; #define GAS __attribute__((address_space(1)))
; #define LDS_WAIT() asm volatile("s_waitcnt lgkmcnt(0)" ::: "memory")
;     ...
;     for (int kb = 0; kb < D / 64; ++kb) {
; #pragma unroll
;         for (int i = 0; i < 8; ++i) { const int kk = 8 * i + kr; const int k = 64 * kb + kk; const f32x4 v = __builtin_nontemporal_load((const f32x4*)(W + (size_t)k * pitch)) * g[k];
;             LAS float* p = scr + kk * 33 + 4 * (lane & 7); p[0] = __builtin_rintf(v[0] * inv[0]); p[1] = __builtin_rintf(v[1] * inv[1]); p[2] = __builtin_rintf(v[2] * inv[2]); p[3] = __builtin_rintf(v[3] * inv[3]); }
;         LDS_WAIT(); asm volatile("" ::: "memory");
;         const int c = lane & 7;
; #pragma unroll
;         for (int j = 0; j < 4; ++j) { const int n = (lane >> 3) + 8 * j; const LAS float* sp = scr + (8 * c) * 33 + n;
;             u32x2 o;
;             o.x = ((unsigned)(int)sp[0 * 33] & 0xFFu) | (((unsigned)(int)sp[1 * 33] & 0xFFu) << 8) | (((unsigned)(int)sp[2 * 33] & 0xFFu) << 16) | (((unsigned)(int)sp[3 * 33] & 0xFFu) << 24);
;             o.y = ((unsigned)(int)sp[4 * 33] & 0xFFu) | (((unsigned)(int)sp[5 * 33] & 0xFFu) << 8) | (((unsigned)(int)sp[6 * 33] & 0xFFu) << 16) | (((unsigned)(int)sp[7 * 33] & 0xFFu) << 24);
;             *(GAS u32x2*)(dst + (size_t)(n0 + n) * D + 64 * kb + 8 * c) = o; }
;         LDS_WAIT(); asm volatile("" ::: "memory");
	v_cvt_i32_f32_sdwa v52, v52 dst_sel:BYTE_3 dst_unused:UNUSED_PAD src0_sel:DWORD
	v_cvt_i32_f32_sdwa v45, v45 dst_sel:BYTE_3 dst_unused:UNUSED_PAD src0_sel:DWORD
	v_cvt_i32_f32_sdwa v53, v53 dst_sel:BYTE_3 dst_unused:UNUSED_PAD src0_sel:DWORD
	v_lshlrev_b32_e32 v14, 8, v14
	v_lshlrev_b32_e32 v32, 8, v32
	v_and_b32_e32 v26, 0xff0000, v26
	v_and_b32_e32 v34, 0xff0000, v34
	v_lshlrev_b32_e32 v15, 8, v15
	v_lshlrev_b32_e32 v33, 8, v33
	v_lshlrev_b32_e32 v40, 8, v40
	v_lshlrev_b32_e32 v48, 8, v48
	v_lshlrev_b32_e32 v41, 8, v41
	v_lshlrev_b32_e32 v49, 8, v49
	v_perm_b32 v12, v14, v12, s28
	v_perm_b32 v14, v32, v30, s28
	v_and_b32_e32 v27, 0xff0000, v27
	v_and_b32_e32 v35, 0xff0000, v35
	v_and_b32_e32 v42, 0xff0000, v42
	v_and_b32_e32 v50, 0xff0000, v50
	v_and_b32_e32 v43, 0xff0000, v43
	v_and_b32_e32 v51, 0xff0000, v51
	v_perm_b32 v15, v15, v13, s28
	v_perm_b32 v30, v33, v31, s28
	v_perm_b32 v31, v40, v38, s28
	v_perm_b32 v32, v48, v46, s28
	v_perm_b32 v33, v41, v39, s28
	v_perm_b32 v38, v49, v47, s28
	v_or3_b32 v12, v12, v26, v28
	v_or3_b32 v13, v14, v34, v36
	v_or3_b32 v14, v15, v27, v29
	v_or3_b32 v15, v30, v35, v37
	v_or3_b32 v26, v31, v42, v44
	v_or3_b32 v27, v32, v50, v52
	v_or3_b32 v28, v33, v43, v45
	v_or3_b32 v29, v38, v51, v53
	global_store_dwordx2 v[16:17], v[12:13], off
	global_store_dwordx2 v[18:19], v[14:15], off
	global_store_dwordx2 v[58:59], v[26:27], off
	global_store_dwordx2 v[60:61], v[28:29], off
	s_waitcnt lgkmcnt(0)
	v_add_u32_e32 v77, 0x420, v25
	v_add_u32_e32 v79, 0x428, v25
	v_add_u32_e32 v81, 0x840, v25
	v_add_u32_e32 v83, 0x848, v25
	v_add_u32_e32 v85, 0xc60, v25
	v_add_u32_e32 v87, 0xc68, v25
	v_add_u32_e32 v89, 0x1080, v25
	v_add_u32_e32 v91, 0x1088, v25
	v_add_u32_e32 v92, 0x14a0, v25
	v_add_u32_e32 v93, 0x14a8, v25
	v_add_u32_e32 v94, 0x18c0, v25
	v_add_u32_e32 v95, 0x18c8, v25
	v_add_u32_e32 v96, 0x1ce0, v25
	v_add_u32_e32 v97, 0x1ce8, v25
	v_lshl_add_u64 v[16:17], v[10:11], 0, s[26:27]
	v_lshl_add_u64 v[18:19], v[8:9], 0, s[26:27]
	v_lshl_add_u64 v[58:59], v[6:7], 0, s[26:27]
	v_lshl_add_u64 v[60:61], v[4:5], 0, s[26:27]
	v_lshl_add_u64 v[4:5], v[4:5], 0, 64
	v_lshl_add_u64 v[6:7], v[6:7], 0, 64
	v_lshl_add_u64 v[8:9], v[8:9], 0, 64
	v_lshl_add_u64 v[10:11], v[10:11], 0, 64
	s_waitcnt vmcnt(40)
	v_pk_mul_f32 v[14:15], v[170:171], v[234:235] op_sel_hi:[1,0]
	v_pk_mul_f32 v[12:13], v[172:173], v[234:235] op_sel_hi:[1,0]
	v_mul_f32_e32 v62, v20, v14
	v_mul_f32_e32 v63, v21, v15
	v_mul_f32_e32 v64, v22, v12
	v_mul_f32_e32 v65, v23, v13
	v_pk_mul_f32 v[14:15], v[174:175], v[236:237] op_sel_hi:[1,0]
	v_pk_mul_f32 v[12:13], v[176:177], v[236:237] op_sel_hi:[1,0]
	v_pk_mul_f32 v[26:27], v[180:181], v[238:239] op_sel_hi:[1,0]
	v_pk_mul_f32 v[28:29], v[178:179], v[238:239] op_sel_hi:[1,0]
	v_pk_mul_f32 v[30:31], v[184:185], v[240:241] op_sel_hi:[1,0]
	v_pk_mul_f32 v[32:33], v[182:183], v[240:241] op_sel_hi:[1,0]
	v_pk_mul_f32 v[34:35], v[188:189], v[242:243] op_sel_hi:[1,0]
	v_pk_mul_f32 v[36:37], v[186:187], v[242:243] op_sel_hi:[1,0]
	v_pk_mul_f32 v[38:39], v[192:193], v[244:245] op_sel_hi:[1,0]
	v_pk_mul_f32 v[40:41], v[190:191], v[244:245] op_sel_hi:[1,0]
	v_pk_mul_f32 v[42:43], v[196:197], v[246:247] op_sel_hi:[1,0]
	v_pk_mul_f32 v[44:45], v[194:195], v[246:247] op_sel_hi:[1,0]
	v_pk_mul_f32 v[46:47], v[200:201], v[248:249] op_sel_hi:[1,0]
	v_pk_mul_f32 v[48:49], v[198:199], v[248:249] op_sel_hi:[1,0]
	s_add_u32 s4, s4, 0x16000
	s_addc_u32 s5, s5, 0
	global_load_dwordx4 v[170:173], v250, s[4:5] nt
	global_load_dword v234, v251, s[6:7] offset:1280
	s_add_u32 s4, s4, 0x16000
	s_addc_u32 s5, s5, 0
	global_load_dwordx4 v[174:177], v250, s[4:5] nt
	global_load_dword v236, v251, s[6:7] offset:1312
	s_add_u32 s4, s4, 0x16000
	s_addc_u32 s5, s5, 0
	global_load_dwordx4 v[178:181], v250, s[4:5] nt
	global_load_dword v238, v251, s[6:7] offset:1344
	s_add_u32 s4, s4, 0x16000
	s_addc_u32 s5, s5, 0
	global_load_dwordx4 v[182:185], v250, s[4:5] nt
	global_load_dword v240, v251, s[6:7] offset:1376
	s_add_u32 s4, s4, 0x16000
	s_addc_u32 s5, s5, 0
	global_load_dwordx4 v[186:189], v250, s[4:5] nt
	global_load_dword v242, v251, s[6:7] offset:1408
	s_add_u32 s4, s4, 0x16000
	s_addc_u32 s5, s5, 0
	global_load_dwordx4 v[190:193], v250, s[4:5] nt
	global_load_dword v244, v251, s[6:7] offset:1440
	s_add_u32 s4, s4, 0x16000
	s_addc_u32 s5, s5, 0
	global_load_dwordx4 v[194:197], v250, s[4:5] nt
	global_load_dword v246, v251, s[6:7] offset:1472
	s_add_u32 s4, s4, 0x16000
	s_addc_u32 s5, s5, 0
	global_load_dwordx4 v[198:201], v250, s[4:5] nt
	global_load_dword v248, v251, s[6:7] offset:1504
	v_mul_f32_e32 v14, v20, v14
	v_mul_f32_e32 v15, v21, v15
	v_rndne_f32_e32 v50, v62
	v_rndne_f32_e32 v51, v63
	v_mul_f32_e32 v12, v22, v12
	v_mul_f32_e32 v13, v23, v13
	v_mul_f32_e32 v28, v20, v28
	v_mul_f32_e32 v29, v21, v29
	v_mul_f32_e32 v26, v22, v26
	v_mul_f32_e32 v27, v23, v27
	v_mul_f32_e32 v32, v20, v32
	v_mul_f32_e32 v33, v21, v33
	v_mul_f32_e32 v30, v22, v30
	v_mul_f32_e32 v31, v23, v31
	v_mul_f32_e32 v36, v20, v36
	v_mul_f32_e32 v37, v21, v37
	v_mul_f32_e32 v34, v22, v34
	v_mul_f32_e32 v35, v23, v35
	v_mul_f32_e32 v40, v20, v40
	v_mul_f32_e32 v41, v21, v41
	v_mul_f32_e32 v38, v22, v38
	v_mul_f32_e32 v39, v23, v39
	v_mul_f32_e32 v44, v20, v44
	v_mul_f32_e32 v45, v21, v45
	v_mul_f32_e32 v42, v22, v42
	v_mul_f32_e32 v43, v23, v43
	v_mul_f32_e32 v48, v20, v48
	v_mul_f32_e32 v49, v21, v49
	v_mul_f32_e32 v46, v22, v46
	v_mul_f32_e32 v47, v23, v47
	v_rndne_f32_e32 v14, v14
	v_rndne_f32_e32 v15, v15
	v_rndne_f32_e32 v52, v64
	v_rndne_f32_e32 v53, v65
	ds_write2_b32 v25, v50, v51 offset1:1
	ds_write2_b32 v25, v52, v53 offset0:2 offset1:3
	v_rndne_f32_e32 v12, v12
	v_rndne_f32_e32 v13, v13
	v_rndne_f32_e32 v28, v28
	v_rndne_f32_e32 v29, v29
	v_rndne_f32_e32 v26, v26
	v_rndne_f32_e32 v27, v27
	v_rndne_f32_e32 v32, v32
	v_rndne_f32_e32 v33, v33
	v_rndne_f32_e32 v30, v30
	v_rndne_f32_e32 v31, v31
	v_rndne_f32_e32 v36, v36
	v_rndne_f32_e32 v37, v37
	v_rndne_f32_e32 v34, v34
	v_rndne_f32_e32 v35, v35
	v_rndne_f32_e32 v40, v40
	v_rndne_f32_e32 v41, v41
	v_rndne_f32_e32 v38, v38
	v_rndne_f32_e32 v39, v39
	v_rndne_f32_e32 v44, v44
	v_rndne_f32_e32 v45, v45
	v_rndne_f32_e32 v42, v42
	v_rndne_f32_e32 v43, v43
	v_rndne_f32_e32 v48, v48
	v_rndne_f32_e32 v49, v49
	v_rndne_f32_e32 v46, v46
	v_rndne_f32_e32 v47, v47
	ds_write2_b32 v77, v14, v15 offset1:1
	ds_write2_b32 v79, v12, v13 offset1:1
	ds_write2_b32 v81, v28, v29 offset1:1
	ds_write2_b32 v83, v26, v27 offset1:1
	ds_write2_b32 v85, v32, v33 offset1:1
	ds_write2_b32 v87, v30, v31 offset1:1
	ds_write2_b32 v89, v36, v37 offset1:1
	ds_write2_b32 v91, v34, v35 offset1:1
	ds_write2_b32 v92, v40, v41 offset1:1
	ds_write2_b32 v93, v38, v39 offset1:1
	ds_write2_b32 v94, v44, v45 offset1:1
	ds_write2_b32 v95, v42, v43 offset1:1
	ds_write2_b32 v96, v48, v49 offset1:1
	ds_write2_b32 v97, v46, v47 offset1:1
	s_waitcnt lgkmcnt(0)
; #define LAS __attribute__((address_space(3)))
; #define GAS __attribute__((address_space(1)))
; #define LDS_WAIT() asm volatile("s_waitcnt lgkmcnt(0)" ::: "memory")
;     ...
;     for (int kb = 0; kb < D / 64; ++kb) {
; #pragma unroll
;         for (int i = 0; i < 8; ++i) { const int kk = 8 * i + kr; const int k = 64 * kb + kk; const f32x4 v = __builtin_nontemporal_load((const f32x4*)(W + (size_t)k * pitch)) * g[k];
;             LAS float* p = scr + kk * 33 + 4 * (lane & 7); p[0] = __builtin_rintf(v[0] * inv[0]); p[1] = __builtin_rintf(v[1] * inv[1]); p[2] = __builtin_rintf(v[2] * inv[2]); p[3] = __builtin_rintf(v[3] * inv[3]); }
;         LDS_WAIT(); asm volatile("" ::: "memory");
;         const int c = lane & 7;
; #pragma unroll
;         for (int j = 0; j < 4; ++j) { const int n = (lane >> 3) + 8 * j; const LAS float* sp = scr + (8 * c) * 33 + n;
;             u32x2 o;
;             o.x = ((unsigned)(int)sp[0 * 33] & 0xFFu) | (((unsigned)(int)sp[1 * 33] & 0xFFu) << 8) | (((unsigned)(int)sp[2 * 33] & 0xFFu) << 16) | (((unsigned)(int)sp[3 * 33] & 0xFFu) << 24);
;             o.y = ((unsigned)(int)sp[4 * 33] & 0xFFu) | (((unsigned)(int)sp[5 * 33] & 0xFFu) << 8) | (((unsigned)(int)sp[6 * 33] & 0xFFu) << 16) | (((unsigned)(int)sp[7 * 33] & 0xFFu) << 24);
;             *(GAS u32x2*)(dst + (size_t)(n0 + n) * D + 64 * kb + 8 * c) = o; }
;         LDS_WAIT(); asm volatile("" ::: "memory");
	ds_read2_b32 v[12:13], v24 offset1:8
	ds_read2_b32 v[14:15], v24 offset0:33 offset1:41
	ds_read2_b32 v[26:27], v24 offset0:66 offset1:74
	ds_read2_b32 v[28:29], v24 offset0:99 offset1:107
	ds_read2_b32 v[30:31], v24 offset0:132 offset1:140
	ds_read2_b32 v[32:33], v24 offset0:165 offset1:173
	ds_read2_b32 v[34:35], v24 offset0:198 offset1:206
	ds_read2_b32 v[36:37], v24 offset0:231 offset1:239
	ds_read2_b32 v[38:39], v24 offset0:16 offset1:24
	ds_read2_b32 v[40:41], v24 offset0:49 offset1:57
	ds_read2_b32 v[42:43], v24 offset0:82 offset1:90
	ds_read2_b32 v[44:45], v24 offset0:115 offset1:123
	ds_read2_b32 v[46:47], v24 offset0:148 offset1:156
	ds_read2_b32 v[48:49], v24 offset0:181 offset1:189
	ds_read2_b32 v[50:51], v24 offset0:214 offset1:222
	ds_read2_b32 v[52:53], v24 offset0:247 offset1:255
	s_waitcnt lgkmcnt(14)
	v_cvt_i32_f32_e32 v14, v14
	s_waitcnt lgkmcnt(10)
	v_cvt_i32_f32_e32 v32, v32
	v_cvt_i32_f32_e32 v12, v12
	v_cvt_i32_f32_sdwa v26, v26 dst_sel:WORD_1 dst_unused:UNUSED_PAD src0_sel:DWORD
	v_cvt_i32_f32_e32 v30, v30
	s_waitcnt lgkmcnt(9)
	v_cvt_i32_f32_sdwa v34, v34 dst_sel:WORD_1 dst_unused:UNUSED_PAD src0_sel:DWORD
	v_cvt_i32_f32_e32 v15, v15
	v_cvt_i32_f32_e32 v33, v33
	s_waitcnt lgkmcnt(6)
	v_cvt_i32_f32_e32 v40, v40
	s_waitcnt lgkmcnt(2)
	v_cvt_i32_f32_e32 v48, v48
	v_cvt_i32_f32_e32 v41, v41
	v_cvt_i32_f32_e32 v49, v49
	v_cvt_i32_f32_sdwa v28, v28 dst_sel:BYTE_3 dst_unused:UNUSED_PAD src0_sel:DWORD
	v_cvt_i32_f32_sdwa v36, v36 dst_sel:BYTE_3 dst_unused:UNUSED_PAD src0_sel:DWORD
	v_cvt_i32_f32_e32 v13, v13
	v_cvt_i32_f32_sdwa v27, v27 dst_sel:WORD_1 dst_unused:UNUSED_PAD src0_sel:DWORD
	v_cvt_i32_f32_e32 v31, v31
	v_cvt_i32_f32_sdwa v35, v35 dst_sel:WORD_1 dst_unused:UNUSED_PAD src0_sel:DWORD
	v_cvt_i32_f32_e32 v38, v38
	v_cvt_i32_f32_sdwa v42, v42 dst_sel:WORD_1 dst_unused:UNUSED_PAD src0_sel:DWORD
	v_cvt_i32_f32_e32 v46, v46
	s_waitcnt lgkmcnt(1)
	v_cvt_i32_f32_sdwa v50, v50 dst_sel:WORD_1 dst_unused:UNUSED_PAD src0_sel:DWORD
	v_cvt_i32_f32_e32 v39, v39
	v_cvt_i32_f32_sdwa v43, v43 dst_sel:WORD_1 dst_unused:UNUSED_PAD src0_sel:DWORD
	v_cvt_i32_f32_e32 v47, v47
	v_cvt_i32_f32_sdwa v51, v51 dst_sel:WORD_1 dst_unused:UNUSED_PAD src0_sel:DWORD
	v_cvt_i32_f32_sdwa v29, v29 dst_sel:BYTE_3 dst_unused:UNUSED_PAD src0_sel:DWORD
	v_cvt_i32_f32_sdwa v37, v37 dst_sel:BYTE_3 dst_unused:UNUSED_PAD src0_sel:DWORD
	v_cvt_i32_f32_sdwa v44, v44 dst_sel:BYTE_3 dst_unused:UNUSED_PAD src0_sel:DWORD
	s_waitcnt lgkmcnt(0)
	v_cvt_i32_f32_sdwa v52, v52 dst_sel:BYTE_3 dst_unused:UNUSED_PAD src0_sel:DWORD
	v_cvt_i32_f32_sdwa v45, v45 dst_sel:BYTE_3 dst_unused:UNUSED_PAD src0_sel:DWORD
	v_cvt_i32_f32_sdwa v53, v53 dst_sel:BYTE_3 dst_unused:UNUSED_PAD src0_sel:DWORD
	v_lshlrev_b32_e32 v14, 8, v14
	v_lshlrev_b32_e32 v32, 8, v32
	v_and_b32_e32 v26, 0xff0000, v26
	v_and_b32_e32 v34, 0xff0000, v34
	v_lshlrev_b32_e32 v15, 8, v15
	v_lshlrev_b32_e32 v33, 8, v33
	v_lshlrev_b32_e32 v40, 8, v40
	v_lshlrev_b32_e32 v48, 8, v48
	v_lshlrev_b32_e32 v41, 8, v41
	v_lshlrev_b32_e32 v49, 8, v49
	v_perm_b32 v12, v14, v12, s28
	v_perm_b32 v14, v32, v30, s28
	v_and_b32_e32 v27, 0xff0000, v27
	v_and_b32_e32 v35, 0xff0000, v35
	v_and_b32_e32 v42, 0xff0000, v42
	v_and_b32_e32 v50, 0xff0000, v50
	v_and_b32_e32 v43, 0xff0000, v43
	v_and_b32_e32 v51, 0xff0000, v51
	v_perm_b32 v15, v15, v13, s28
	v_perm_b32 v30, v33, v31, s28
	v_perm_b32 v31, v40, v38, s28
	v_perm_b32 v32, v48, v46, s28
	v_perm_b32 v33, v41, v39, s28
	v_perm_b32 v38, v49, v47, s28
	v_or3_b32 v12, v12, v26, v28
	v_or3_b32 v13, v14, v34, v36
	v_or3_b32 v14, v15, v27, v29
	v_or3_b32 v15, v30, v35, v37
	v_or3_b32 v26, v31, v42, v44
	v_or3_b32 v27, v32, v50, v52
	v_or3_b32 v28, v33, v43, v45
	v_or3_b32 v29, v38, v51, v53
	global_store_dwordx2 v[16:17], v[12:13], off
	global_store_dwordx2 v[18:19], v[14:15], off
	global_store_dwordx2 v[58:59], v[26:27], off
	global_store_dwordx2 v[60:61], v[28:29], off
	s_waitcnt lgkmcnt(0)
	v_add_u32_e32 v77, 0x420, v25
	v_add_u32_e32 v79, 0x428, v25
	v_add_u32_e32 v81, 0x840, v25
	v_add_u32_e32 v83, 0x848, v25
	v_add_u32_e32 v85, 0xc60, v25
	v_add_u32_e32 v87, 0xc68, v25
	v_add_u32_e32 v89, 0x1080, v25
	v_add_u32_e32 v91, 0x1088, v25
	v_add_u32_e32 v92, 0x14a0, v25
	v_add_u32_e32 v93, 0x14a8, v25
	v_add_u32_e32 v94, 0x18c0, v25
	v_add_u32_e32 v95, 0x18c8, v25
	v_add_u32_e32 v96, 0x1ce0, v25
	v_add_u32_e32 v97, 0x1ce8, v25
	v_lshl_add_u64 v[16:17], v[10:11], 0, s[26:27]
	v_lshl_add_u64 v[18:19], v[8:9], 0, s[26:27]
	v_lshl_add_u64 v[58:59], v[6:7], 0, s[26:27]
	v_lshl_add_u64 v[60:61], v[4:5], 0, s[26:27]
	v_lshl_add_u64 v[4:5], v[4:5], 0, 64
	v_lshl_add_u64 v[6:7], v[6:7], 0, 64
	v_lshl_add_u64 v[8:9], v[8:9], 0, 64
	v_lshl_add_u64 v[10:11], v[10:11], 0, 64
	s_waitcnt vmcnt(44)
; #define LAS __attribute__((address_space(3)))
; #define GAS __attribute__((address_space(1)))
; #define LDS_WAIT() asm volatile("s_waitcnt lgkmcnt(0)" ::: "memory")
;     ...
;     for (int kb = 0; kb < D / 64; ++kb) {
; #pragma unroll
;         for (int i = 0; i < 8; ++i) { const int kk = 8 * i + kr; const int k = 64 * kb + kk; const f32x4 v = __builtin_nontemporal_load((const f32x4*)(W + (size_t)k * pitch)) * g[k];
;             LAS float* p = scr + kk * 33 + 4 * (lane & 7); p[0] = __builtin_rintf(v[0] * inv[0]); p[1] = __builtin_rintf(v[1] * inv[1]); p[2] = __builtin_rintf(v[2] * inv[2]); p[3] = __builtin_rintf(v[3] * inv[3]); }
;         LDS_WAIT(); asm volatile("" ::: "memory");
;         const int c = lane & 7;
; #pragma unroll
;         for (int j = 0; j < 4; ++j) { const int n = (lane >> 3) + 8 * j; const LAS float* sp = scr + (8 * c) * 33 + n;
;             u32x2 o;
;             o.x = ((unsigned)(int)sp[0 * 33] & 0xFFu) | (((unsigned)(int)sp[1 * 33] & 0xFFu) << 8) | (((unsigned)(int)sp[2 * 33] & 0xFFu) << 16) | (((unsigned)(int)sp[3 * 33] & 0xFFu) << 24);
;             o.y = ((unsigned)(int)sp[4 * 33] & 0xFFu) | (((unsigned)(int)sp[5 * 33] & 0xFFu) << 8) | (((unsigned)(int)sp[6 * 33] & 0xFFu) << 16) | (((unsigned)(int)sp[7 * 33] & 0xFFu) << 24);
;             *(GAS u32x2*)(dst + (size_t)(n0 + n) * D + 64 * kb + 8 * c) = o; }
;         LDS_WAIT(); asm volatile("" ::: "memory");
	v_pk_mul_f32 v[14:15], v[106:107], v[202:203] op_sel_hi:[1,0]
	v_pk_mul_f32 v[12:13], v[108:109], v[202:203] op_sel_hi:[1,0]
	v_mul_f32_e32 v62, v20, v14
	v_mul_f32_e32 v63, v21, v15
	v_mul_f32_e32 v64, v22, v12
	v_mul_f32_e32 v65, v23, v13
	v_pk_mul_f32 v[14:15], v[110:111], v[204:205] op_sel_hi:[1,0]
	v_pk_mul_f32 v[12:13], v[112:113], v[204:205] op_sel_hi:[1,0]
	v_pk_mul_f32 v[26:27], v[116:117], v[206:207] op_sel_hi:[1,0]
	v_pk_mul_f32 v[28:29], v[114:115], v[206:207] op_sel_hi:[1,0]
	v_pk_mul_f32 v[30:31], v[120:121], v[208:209] op_sel_hi:[1,0]
	v_pk_mul_f32 v[32:33], v[118:119], v[208:209] op_sel_hi:[1,0]
	v_pk_mul_f32 v[34:35], v[124:125], v[210:211] op_sel_hi:[1,0]
	v_pk_mul_f32 v[36:37], v[122:123], v[210:211] op_sel_hi:[1,0]
	v_pk_mul_f32 v[38:39], v[128:129], v[212:213] op_sel_hi:[1,0]
	v_pk_mul_f32 v[40:41], v[126:127], v[212:213] op_sel_hi:[1,0]
	v_pk_mul_f32 v[42:43], v[132:133], v[214:215] op_sel_hi:[1,0]
	v_pk_mul_f32 v[44:45], v[130:131], v[214:215] op_sel_hi:[1,0]
	v_pk_mul_f32 v[46:47], v[136:137], v[216:217] op_sel_hi:[1,0]
	v_pk_mul_f32 v[48:49], v[134:135], v[216:217] op_sel_hi:[1,0]
	s_add_u32 s4, s4, 0x16000
	s_addc_u32 s5, s5, 0
	global_load_dwordx4 v[106:109], v250, s[4:5] nt
	global_load_dword v202, v251, s[6:7] offset:1536
	s_add_u32 s4, s4, 0x16000
	s_addc_u32 s5, s5, 0
	global_load_dwordx4 v[110:113], v250, s[4:5] nt
	global_load_dword v204, v251, s[6:7] offset:1568
	s_add_u32 s4, s4, 0x16000
	s_addc_u32 s5, s5, 0
	global_load_dwordx4 v[114:117], v250, s[4:5] nt
	global_load_dword v206, v251, s[6:7] offset:1600
	s_add_u32 s4, s4, 0x16000
	s_addc_u32 s5, s5, 0
	global_load_dwordx4 v[118:121], v250, s[4:5] nt
	global_load_dword v208, v251, s[6:7] offset:1632
	s_add_u32 s4, s4, 0x16000
	s_addc_u32 s5, s5, 0
	global_load_dwordx4 v[122:125], v250, s[4:5] nt
	global_load_dword v210, v251, s[6:7] offset:1664
	s_add_u32 s4, s4, 0x16000
	s_addc_u32 s5, s5, 0
	global_load_dwordx4 v[126:129], v250, s[4:5] nt
	global_load_dword v212, v251, s[6:7] offset:1696
	s_add_u32 s4, s4, 0x16000
	s_addc_u32 s5, s5, 0
	global_load_dwordx4 v[130:133], v250, s[4:5] nt
	global_load_dword v214, v251, s[6:7] offset:1728
	s_add_u32 s4, s4, 0x16000
	s_addc_u32 s5, s5, 0
	global_load_dwordx4 v[134:137], v250, s[4:5] nt
	global_load_dword v216, v251, s[6:7] offset:1760
	v_mul_f32_e32 v14, v20, v14
	v_mul_f32_e32 v15, v21, v15
	v_rndne_f32_e32 v50, v62
	v_rndne_f32_e32 v51, v63
	v_mul_f32_e32 v12, v22, v12
	v_mul_f32_e32 v13, v23, v13
	v_mul_f32_e32 v28, v20, v28
	v_mul_f32_e32 v29, v21, v29
	v_mul_f32_e32 v26, v22, v26
	v_mul_f32_e32 v27, v23, v27
	v_mul_f32_e32 v32, v20, v32
	v_mul_f32_e32 v33, v21, v33
	v_mul_f32_e32 v30, v22, v30
	v_mul_f32_e32 v31, v23, v31
	v_mul_f32_e32 v36, v20, v36
	v_mul_f32_e32 v37, v21, v37
	v_mul_f32_e32 v34, v22, v34
	v_mul_f32_e32 v35, v23, v35
	v_mul_f32_e32 v40, v20, v40
	v_mul_f32_e32 v41, v21, v41
	v_mul_f32_e32 v38, v22, v38
	v_mul_f32_e32 v39, v23, v39
	v_mul_f32_e32 v44, v20, v44
	v_mul_f32_e32 v45, v21, v45
	v_mul_f32_e32 v42, v22, v42
	v_mul_f32_e32 v43, v23, v43
	v_mul_f32_e32 v48, v20, v48
	v_mul_f32_e32 v49, v21, v49
	v_mul_f32_e32 v46, v22, v46
	v_mul_f32_e32 v47, v23, v47
	v_rndne_f32_e32 v14, v14
	v_rndne_f32_e32 v15, v15
	v_rndne_f32_e32 v52, v64
	v_rndne_f32_e32 v53, v65
	ds_write2_b32 v25, v50, v51 offset1:1
	ds_write2_b32 v25, v52, v53 offset0:2 offset1:3
	v_rndne_f32_e32 v12, v12
	v_rndne_f32_e32 v13, v13
	v_rndne_f32_e32 v28, v28
	v_rndne_f32_e32 v29, v29
	v_rndne_f32_e32 v26, v26
	v_rndne_f32_e32 v27, v27
	v_rndne_f32_e32 v32, v32
	v_rndne_f32_e32 v33, v33
	v_rndne_f32_e32 v30, v30
	v_rndne_f32_e32 v31, v31
	v_rndne_f32_e32 v36, v36
	v_rndne_f32_e32 v37, v37
	v_rndne_f32_e32 v34, v34
	v_rndne_f32_e32 v35, v35
	v_rndne_f32_e32 v40, v40
	v_rndne_f32_e32 v41, v41
	v_rndne_f32_e32 v38, v38
	v_rndne_f32_e32 v39, v39
	v_rndne_f32_e32 v44, v44
	v_rndne_f32_e32 v45, v45
	v_rndne_f32_e32 v42, v42
	v_rndne_f32_e32 v43, v43
	v_rndne_f32_e32 v48, v48
	v_rndne_f32_e32 v49, v49
	v_rndne_f32_e32 v46, v46
	v_rndne_f32_e32 v47, v47
	ds_write2_b32 v77, v14, v15 offset1:1
	ds_write2_b32 v79, v12, v13 offset1:1
	ds_write2_b32 v81, v28, v29 offset1:1
	ds_write2_b32 v83, v26, v27 offset1:1
	ds_write2_b32 v85, v32, v33 offset1:1
	ds_write2_b32 v87, v30, v31 offset1:1
	ds_write2_b32 v89, v36, v37 offset1:1
	ds_write2_b32 v91, v34, v35 offset1:1
	ds_write2_b32 v92, v40, v41 offset1:1
	ds_write2_b32 v93, v38, v39 offset1:1
	ds_write2_b32 v94, v44, v45 offset1:1
	ds_write2_b32 v95, v42, v43 offset1:1
	ds_write2_b32 v96, v48, v49 offset1:1
	ds_write2_b32 v97, v46, v47 offset1:1
	s_waitcnt lgkmcnt(0)
	ds_read2_b32 v[12:13], v24 offset1:8
	ds_read2_b32 v[14:15], v24 offset0:33 offset1:41
	ds_read2_b32 v[26:27], v24 offset0:66 offset1:74
	ds_read2_b32 v[28:29], v24 offset0:99 offset1:107
	ds_read2_b32 v[30:31], v24 offset0:132 offset1:140
	ds_read2_b32 v[32:33], v24 offset0:165 offset1:173
	ds_read2_b32 v[34:35], v24 offset0:198 offset1:206
	ds_read2_b32 v[36:37], v24 offset0:231 offset1:239
	ds_read2_b32 v[38:39], v24 offset0:16 offset1:24
	ds_read2_b32 v[40:41], v24 offset0:49 offset1:57
	ds_read2_b32 v[42:43], v24 offset0:82 offset1:90
	ds_read2_b32 v[44:45], v24 offset0:115 offset1:123
	ds_read2_b32 v[46:47], v24 offset0:148 offset1:156
	ds_read2_b32 v[48:49], v24 offset0:181 offset1:189
	ds_read2_b32 v[50:51], v24 offset0:214 offset1:222
	ds_read2_b32 v[52:53], v24 offset0:247 offset1:255
	s_waitcnt lgkmcnt(14)
	v_cvt_i32_f32_e32 v14, v14
	s_waitcnt lgkmcnt(10)
	v_cvt_i32_f32_e32 v32, v32
	v_cvt_i32_f32_e32 v12, v12
	v_cvt_i32_f32_sdwa v26, v26 dst_sel:WORD_1 dst_unused:UNUSED_PAD src0_sel:DWORD
	v_cvt_i32_f32_e32 v30, v30
	s_waitcnt lgkmcnt(9)
; #define LAS __attribute__((address_space(3)))
; #define GAS __attribute__((address_space(1)))
; #define LDS_WAIT() asm volatile("s_waitcnt lgkmcnt(0)" ::: "memory")
;     ...
;     for (int kb = 0; kb < D / 64; ++kb) {
; #pragma unroll
;         for (int i = 0; i < 8; ++i) { const int kk = 8 * i + kr; const int k = 64 * kb + kk; const f32x4 v = __builtin_nontemporal_load((const f32x4*)(W + (size_t)k * pitch)) * g[k];
;             LAS float* p = scr + kk * 33 + 4 * (lane & 7); p[0] = __builtin_rintf(v[0] * inv[0]); p[1] = __builtin_rintf(v[1] * inv[1]); p[2] = __builtin_rintf(v[2] * inv[2]); p[3] = __builtin_rintf(v[3] * inv[3]); }
;         LDS_WAIT(); asm volatile("" ::: "memory");
;         const int c = lane & 7;
; #pragma unroll
;         for (int j = 0; j < 4; ++j) { const int n = (lane >> 3) + 8 * j; const LAS float* sp = scr + (8 * c) * 33 + n;
;             u32x2 o;
;             o.x = ((unsigned)(int)sp[0 * 33] & 0xFFu) | (((unsigned)(int)sp[1 * 33] & 0xFFu) << 8) | (((unsigned)(int)sp[2 * 33] & 0xFFu) << 16) | (((unsigned)(int)sp[3 * 33] & 0xFFu) << 24);
;             o.y = ((unsigned)(int)sp[4 * 33] & 0xFFu) | (((unsigned)(int)sp[5 * 33] & 0xFFu) << 8) | (((unsigned)(int)sp[6 * 33] & 0xFFu) << 16) | (((unsigned)(int)sp[7 * 33] & 0xFFu) << 24);
;             *(GAS u32x2*)(dst + (size_t)(n0 + n) * D + 64 * kb + 8 * c) = o; }
;         LDS_WAIT(); asm volatile("" ::: "memory");
	v_cvt_i32_f32_sdwa v34, v34 dst_sel:WORD_1 dst_unused:UNUSED_PAD src0_sel:DWORD
	v_cvt_i32_f32_e32 v15, v15
	v_cvt_i32_f32_e32 v33, v33
	s_waitcnt lgkmcnt(6)
	v_cvt_i32_f32_e32 v40, v40
	s_waitcnt lgkmcnt(2)
	v_cvt_i32_f32_e32 v48, v48
	v_cvt_i32_f32_e32 v41, v41
	v_cvt_i32_f32_e32 v49, v49
	v_cvt_i32_f32_sdwa v28, v28 dst_sel:BYTE_3 dst_unused:UNUSED_PAD src0_sel:DWORD
	v_cvt_i32_f32_sdwa v36, v36 dst_sel:BYTE_3 dst_unused:UNUSED_PAD src0_sel:DWORD
	v_cvt_i32_f32_e32 v13, v13
	v_cvt_i32_f32_sdwa v27, v27 dst_sel:WORD_1 dst_unused:UNUSED_PAD src0_sel:DWORD
	v_cvt_i32_f32_e32 v31, v31
	v_cvt_i32_f32_sdwa v35, v35 dst_sel:WORD_1 dst_unused:UNUSED_PAD src0_sel:DWORD
	v_cvt_i32_f32_e32 v38, v38
	v_cvt_i32_f32_sdwa v42, v42 dst_sel:WORD_1 dst_unused:UNUSED_PAD src0_sel:DWORD
	v_cvt_i32_f32_e32 v46, v46
	s_waitcnt lgkmcnt(1)
	v_cvt_i32_f32_sdwa v50, v50 dst_sel:WORD_1 dst_unused:UNUSED_PAD src0_sel:DWORD
	v_cvt_i32_f32_e32 v39, v39
	v_cvt_i32_f32_sdwa v43, v43 dst_sel:WORD_1 dst_unused:UNUSED_PAD src0_sel:DWORD
	v_cvt_i32_f32_e32 v47, v47
	v_cvt_i32_f32_sdwa v51, v51 dst_sel:WORD_1 dst_unused:UNUSED_PAD src0_sel:DWORD
	v_cvt_i32_f32_sdwa v29, v29 dst_sel:BYTE_3 dst_unused:UNUSED_PAD src0_sel:DWORD
	v_cvt_i32_f32_sdwa v37, v37 dst_sel:BYTE_3 dst_unused:UNUSED_PAD src0_sel:DWORD
	v_cvt_i32_f32_sdwa v44, v44 dst_sel:BYTE_3 dst_unused:UNUSED_PAD src0_sel:DWORD
	s_waitcnt lgkmcnt(0)
	v_cvt_i32_f32_sdwa v52, v52 dst_sel:BYTE_3 dst_unused:UNUSED_PAD src0_sel:DWORD
	v_cvt_i32_f32_sdwa v45, v45 dst_sel:BYTE_3 dst_unused:UNUSED_PAD src0_sel:DWORD
	v_cvt_i32_f32_sdwa v53, v53 dst_sel:BYTE_3 dst_unused:UNUSED_PAD src0_sel:DWORD
	v_lshlrev_b32_e32 v14, 8, v14
	v_lshlrev_b32_e32 v32, 8, v32
	v_and_b32_e32 v26, 0xff0000, v26
	v_and_b32_e32 v34, 0xff0000, v34
	v_lshlrev_b32_e32 v15, 8, v15
	v_lshlrev_b32_e32 v33, 8, v33
	v_lshlrev_b32_e32 v40, 8, v40
	v_lshlrev_b32_e32 v48, 8, v48
	v_lshlrev_b32_e32 v41, 8, v41
	v_lshlrev_b32_e32 v49, 8, v49
	v_perm_b32 v12, v14, v12, s28
	v_perm_b32 v14, v32, v30, s28
	v_and_b32_e32 v27, 0xff0000, v27
	v_and_b32_e32 v35, 0xff0000, v35
	v_and_b32_e32 v42, 0xff0000, v42
	v_and_b32_e32 v50, 0xff0000, v50
	v_and_b32_e32 v43, 0xff0000, v43
	v_and_b32_e32 v51, 0xff0000, v51
	v_perm_b32 v15, v15, v13, s28
	v_perm_b32 v30, v33, v31, s28
	v_perm_b32 v31, v40, v38, s28
	v_perm_b32 v32, v48, v46, s28
	v_perm_b32 v33, v41, v39, s28
	v_perm_b32 v38, v49, v47, s28
	v_or3_b32 v12, v12, v26, v28
	v_or3_b32 v13, v14, v34, v36
	v_or3_b32 v14, v15, v27, v29
	v_or3_b32 v15, v30, v35, v37
	v_or3_b32 v26, v31, v42, v44
	v_or3_b32 v27, v32, v50, v52
	v_or3_b32 v28, v33, v43, v45
	v_or3_b32 v29, v38, v51, v53
	global_store_dwordx2 v[16:17], v[12:13], off
	global_store_dwordx2 v[18:19], v[14:15], off
	global_store_dwordx2 v[58:59], v[26:27], off
	global_store_dwordx2 v[60:61], v[28:29], off
	s_waitcnt lgkmcnt(0)
	v_add_u32_e32 v77, 0x420, v25
	v_add_u32_e32 v79, 0x428, v25
	v_add_u32_e32 v81, 0x840, v25
	v_add_u32_e32 v83, 0x848, v25
	v_add_u32_e32 v85, 0xc60, v25
	v_add_u32_e32 v87, 0xc68, v25
	v_add_u32_e32 v89, 0x1080, v25
	v_add_u32_e32 v91, 0x1088, v25
	v_add_u32_e32 v92, 0x14a0, v25
	v_add_u32_e32 v93, 0x14a8, v25
	v_add_u32_e32 v94, 0x18c0, v25
	v_add_u32_e32 v95, 0x18c8, v25
	v_add_u32_e32 v96, 0x1ce0, v25
	v_add_u32_e32 v97, 0x1ce8, v25
	v_lshl_add_u64 v[16:17], v[10:11], 0, s[26:27]
	v_lshl_add_u64 v[18:19], v[8:9], 0, s[26:27]
	v_lshl_add_u64 v[58:59], v[6:7], 0, s[26:27]
	v_lshl_add_u64 v[60:61], v[4:5], 0, s[26:27]
	v_lshl_add_u64 v[4:5], v[4:5], 0, 64
	v_lshl_add_u64 v[6:7], v[6:7], 0, 64
	v_lshl_add_u64 v[8:9], v[8:9], 0, 64
	v_lshl_add_u64 v[10:11], v[10:11], 0, 64
	s_waitcnt vmcnt(44)
	v_pk_mul_f32 v[14:15], v[138:139], v[218:219] op_sel_hi:[1,0]
	v_pk_mul_f32 v[12:13], v[140:141], v[218:219] op_sel_hi:[1,0]
	v_mul_f32_e32 v62, v20, v14
	v_mul_f32_e32 v63, v21, v15
	v_mul_f32_e32 v64, v22, v12
	v_mul_f32_e32 v65, v23, v13
	v_pk_mul_f32 v[14:15], v[142:143], v[220:221] op_sel_hi:[1,0]
	v_pk_mul_f32 v[12:13], v[144:145], v[220:221] op_sel_hi:[1,0]
	v_pk_mul_f32 v[26:27], v[148:149], v[222:223] op_sel_hi:[1,0]
	v_pk_mul_f32 v[28:29], v[146:147], v[222:223] op_sel_hi:[1,0]
	v_pk_mul_f32 v[30:31], v[152:153], v[224:225] op_sel_hi:[1,0]
	v_pk_mul_f32 v[32:33], v[150:151], v[224:225] op_sel_hi:[1,0]
	v_pk_mul_f32 v[34:35], v[156:157], v[226:227] op_sel_hi:[1,0]
	v_pk_mul_f32 v[36:37], v[154:155], v[226:227] op_sel_hi:[1,0]
	v_pk_mul_f32 v[38:39], v[160:161], v[228:229] op_sel_hi:[1,0]
	v_pk_mul_f32 v[40:41], v[158:159], v[228:229] op_sel_hi:[1,0]
	v_pk_mul_f32 v[42:43], v[164:165], v[230:231] op_sel_hi:[1,0]
	v_pk_mul_f32 v[44:45], v[162:163], v[230:231] op_sel_hi:[1,0]
	v_pk_mul_f32 v[46:47], v[168:169], v[232:233] op_sel_hi:[1,0]
	v_pk_mul_f32 v[48:49], v[166:167], v[232:233] op_sel_hi:[1,0]
	s_add_u32 s4, s4, 0x16000
	s_addc_u32 s5, s5, 0
	global_load_dwordx4 v[138:141], v250, s[4:5] nt
	global_load_dword v218, v251, s[6:7] offset:1792
	s_add_u32 s4, s4, 0x16000
	s_addc_u32 s5, s5, 0
	global_load_dwordx4 v[142:145], v250, s[4:5] nt
	global_load_dword v220, v251, s[6:7] offset:1824
	s_add_u32 s4, s4, 0x16000
	s_addc_u32 s5, s5, 0
	global_load_dwordx4 v[146:149], v250, s[4:5] nt
	global_load_dword v222, v251, s[6:7] offset:1856
	s_add_u32 s4, s4, 0x16000
	s_addc_u32 s5, s5, 0
	global_load_dwordx4 v[150:153], v250, s[4:5] nt
	global_load_dword v224, v251, s[6:7] offset:1888
	s_add_u32 s4, s4, 0x16000
	s_addc_u32 s5, s5, 0
	global_load_dwordx4 v[154:157], v250, s[4:5] nt
	global_load_dword v226, v251, s[6:7] offset:1920
	s_add_u32 s4, s4, 0x16000
	s_addc_u32 s5, s5, 0
	global_load_dwordx4 v[158:161], v250, s[4:5] nt
; #define LAS __attribute__((address_space(3)))
; #define GAS __attribute__((address_space(1)))
; #define LDS_WAIT() asm volatile("s_waitcnt lgkmcnt(0)" ::: "memory")
;     ...
;     for (int kb = 0; kb < D / 64; ++kb) {
; #pragma unroll
;         for (int i = 0; i < 8; ++i) { const int kk = 8 * i + kr; const int k = 64 * kb + kk; const f32x4 v = __builtin_nontemporal_load((const f32x4*)(W + (size_t)k * pitch)) * g[k];
;             LAS float* p = scr + kk * 33 + 4 * (lane & 7); p[0] = __builtin_rintf(v[0] * inv[0]); p[1] = __builtin_rintf(v[1] * inv[1]); p[2] = __builtin_rintf(v[2] * inv[2]); p[3] = __builtin_rintf(v[3] * inv[3]); }
;         LDS_WAIT(); asm volatile("" ::: "memory");
;         const int c = lane & 7;
; #pragma unroll
;         for (int j = 0; j < 4; ++j) { const int n = (lane >> 3) + 8 * j; const LAS float* sp = scr + (8 * c) * 33 + n;
;             u32x2 o;
;             o.x = ((unsigned)(int)sp[0 * 33] & 0xFFu) | (((unsigned)(int)sp[1 * 33] & 0xFFu) << 8) | (((unsigned)(int)sp[2 * 33] & 0xFFu) << 16) | (((unsigned)(int)sp[3 * 33] & 0xFFu) << 24);
;             o.y = ((unsigned)(int)sp[4 * 33] & 0xFFu) | (((unsigned)(int)sp[5 * 33] & 0xFFu) << 8) | (((unsigned)(int)sp[6 * 33] & 0xFFu) << 16) | (((unsigned)(int)sp[7 * 33] & 0xFFu) << 24);
;             *(GAS u32x2*)(dst + (size_t)(n0 + n) * D + 64 * kb + 8 * c) = o; }
;         LDS_WAIT(); asm volatile("" ::: "memory");
	global_load_dword v228, v251, s[6:7] offset:1952
	s_add_u32 s4, s4, 0x16000
	s_addc_u32 s5, s5, 0
	global_load_dwordx4 v[162:165], v250, s[4:5] nt
	global_load_dword v230, v251, s[6:7] offset:1984
	s_add_u32 s4, s4, 0x16000
	s_addc_u32 s5, s5, 0
	global_load_dwordx4 v[166:169], v250, s[4:5] nt
	global_load_dword v232, v251, s[6:7] offset:2016
	v_mul_f32_e32 v14, v20, v14
	v_mul_f32_e32 v15, v21, v15
	v_rndne_f32_e32 v50, v62
	v_rndne_f32_e32 v51, v63
	v_mul_f32_e32 v12, v22, v12
	v_mul_f32_e32 v13, v23, v13
	v_mul_f32_e32 v28, v20, v28
	v_mul_f32_e32 v29, v21, v29
	v_mul_f32_e32 v26, v22, v26
	v_mul_f32_e32 v27, v23, v27
	v_mul_f32_e32 v32, v20, v32
	v_mul_f32_e32 v33, v21, v33
	v_mul_f32_e32 v30, v22, v30
	v_mul_f32_e32 v31, v23, v31
	v_mul_f32_e32 v36, v20, v36
	v_mul_f32_e32 v37, v21, v37
	v_mul_f32_e32 v34, v22, v34
	v_mul_f32_e32 v35, v23, v35
	v_mul_f32_e32 v40, v20, v40
	v_mul_f32_e32 v41, v21, v41
	v_mul_f32_e32 v38, v22, v38
	v_mul_f32_e32 v39, v23, v39
	v_mul_f32_e32 v44, v20, v44
	v_mul_f32_e32 v45, v21, v45
	v_mul_f32_e32 v42, v22, v42
	v_mul_f32_e32 v43, v23, v43
	v_mul_f32_e32 v48, v20, v48
	v_mul_f32_e32 v49, v21, v49
	v_mul_f32_e32 v46, v22, v46
	v_mul_f32_e32 v47, v23, v47
	v_rndne_f32_e32 v14, v14
	v_rndne_f32_e32 v15, v15
	v_rndne_f32_e32 v52, v64
	v_rndne_f32_e32 v53, v65
	ds_write2_b32 v25, v50, v51 offset1:1
	ds_write2_b32 v25, v52, v53 offset0:2 offset1:3
	v_rndne_f32_e32 v12, v12
	v_rndne_f32_e32 v13, v13
	v_rndne_f32_e32 v28, v28
	v_rndne_f32_e32 v29, v29
	v_rndne_f32_e32 v26, v26
	v_rndne_f32_e32 v27, v27
	v_rndne_f32_e32 v32, v32
	v_rndne_f32_e32 v33, v33
	v_rndne_f32_e32 v30, v30
	v_rndne_f32_e32 v31, v31
	v_rndne_f32_e32 v36, v36
	v_rndne_f32_e32 v37, v37
	v_rndne_f32_e32 v34, v34
	v_rndne_f32_e32 v35, v35
	v_rndne_f32_e32 v40, v40
	v_rndne_f32_e32 v41, v41
	v_rndne_f32_e32 v38, v38
	v_rndne_f32_e32 v39, v39
	v_rndne_f32_e32 v44, v44
	v_rndne_f32_e32 v45, v45
	v_rndne_f32_e32 v42, v42
	v_rndne_f32_e32 v43, v43
	v_rndne_f32_e32 v48, v48
	v_rndne_f32_e32 v49, v49
	v_rndne_f32_e32 v46, v46
	v_rndne_f32_e32 v47, v47
	ds_write2_b32 v77, v14, v15 offset1:1
	ds_write2_b32 v79, v12, v13 offset1:1
	ds_write2_b32 v81, v28, v29 offset1:1
	ds_write2_b32 v83, v26, v27 offset1:1
	ds_write2_b32 v85, v32, v33 offset1:1
	ds_write2_b32 v87, v30, v31 offset1:1
	ds_write2_b32 v89, v36, v37 offset1:1
	ds_write2_b32 v91, v34, v35 offset1:1
	ds_write2_b32 v92, v40, v41 offset1:1
	ds_write2_b32 v93, v38, v39 offset1:1
	ds_write2_b32 v94, v44, v45 offset1:1
	ds_write2_b32 v95, v42, v43 offset1:1
	ds_write2_b32 v96, v48, v49 offset1:1
	ds_write2_b32 v97, v46, v47 offset1:1
	s_waitcnt lgkmcnt(0)
	ds_read2_b32 v[12:13], v24 offset1:8
	ds_read2_b32 v[14:15], v24 offset0:33 offset1:41
	ds_read2_b32 v[26:27], v24 offset0:66 offset1:74
	ds_read2_b32 v[28:29], v24 offset0:99 offset1:107
	ds_read2_b32 v[30:31], v24 offset0:132 offset1:140
	ds_read2_b32 v[32:33], v24 offset0:165 offset1:173
	ds_read2_b32 v[34:35], v24 offset0:198 offset1:206
	ds_read2_b32 v[36:37], v24 offset0:231 offset1:239
	ds_read2_b32 v[38:39], v24 offset0:16 offset1:24
	ds_read2_b32 v[40:41], v24 offset0:49 offset1:57
	ds_read2_b32 v[42:43], v24 offset0:82 offset1:90
	ds_read2_b32 v[44:45], v24 offset0:115 offset1:123
	ds_read2_b32 v[46:47], v24 offset0:148 offset1:156
	ds_read2_b32 v[48:49], v24 offset0:181 offset1:189
	ds_read2_b32 v[50:51], v24 offset0:214 offset1:222
	ds_read2_b32 v[52:53], v24 offset0:247 offset1:255
	s_waitcnt lgkmcnt(14)
	v_cvt_i32_f32_e32 v14, v14
	s_waitcnt lgkmcnt(10)
	v_cvt_i32_f32_e32 v32, v32
	v_cvt_i32_f32_e32 v12, v12
	v_cvt_i32_f32_sdwa v26, v26 dst_sel:WORD_1 dst_unused:UNUSED_PAD src0_sel:DWORD
	v_cvt_i32_f32_e32 v30, v30
	s_waitcnt lgkmcnt(9)
	v_cvt_i32_f32_sdwa v34, v34 dst_sel:WORD_1 dst_unused:UNUSED_PAD src0_sel:DWORD
	v_cvt_i32_f32_e32 v15, v15
	v_cvt_i32_f32_e32 v33, v33
	s_waitcnt lgkmcnt(6)
	v_cvt_i32_f32_e32 v40, v40
	s_waitcnt lgkmcnt(2)
	v_cvt_i32_f32_e32 v48, v48
	v_cvt_i32_f32_e32 v41, v41
	v_cvt_i32_f32_e32 v49, v49
	v_cvt_i32_f32_sdwa v28, v28 dst_sel:BYTE_3 dst_unused:UNUSED_PAD src0_sel:DWORD
	v_cvt_i32_f32_sdwa v36, v36 dst_sel:BYTE_3 dst_unused:UNUSED_PAD src0_sel:DWORD
	v_cvt_i32_f32_e32 v13, v13
	v_cvt_i32_f32_sdwa v27, v27 dst_sel:WORD_1 dst_unused:UNUSED_PAD src0_sel:DWORD
	v_cvt_i32_f32_e32 v31, v31
	v_cvt_i32_f32_sdwa v35, v35 dst_sel:WORD_1 dst_unused:UNUSED_PAD src0_sel:DWORD
	v_cvt_i32_f32_e32 v38, v38
	v_cvt_i32_f32_sdwa v42, v42 dst_sel:WORD_1 dst_unused:UNUSED_PAD src0_sel:DWORD
	v_cvt_i32_f32_e32 v46, v46
	s_waitcnt lgkmcnt(1)
	v_cvt_i32_f32_sdwa v50, v50 dst_sel:WORD_1 dst_unused:UNUSED_PAD src0_sel:DWORD
	v_cvt_i32_f32_e32 v39, v39
	v_cvt_i32_f32_sdwa v43, v43 dst_sel:WORD_1 dst_unused:UNUSED_PAD src0_sel:DWORD
	v_cvt_i32_f32_e32 v47, v47
	v_cvt_i32_f32_sdwa v51, v51 dst_sel:WORD_1 dst_unused:UNUSED_PAD src0_sel:DWORD
	v_cvt_i32_f32_sdwa v29, v29 dst_sel:BYTE_3 dst_unused:UNUSED_PAD src0_sel:DWORD
	v_cvt_i32_f32_sdwa v37, v37 dst_sel:BYTE_3 dst_unused:UNUSED_PAD src0_sel:DWORD
	v_cvt_i32_f32_sdwa v44, v44 dst_sel:BYTE_3 dst_unused:UNUSED_PAD src0_sel:DWORD
	s_waitcnt lgkmcnt(0)
; #define LAS __attribute__((address_space(3)))
; #define GAS __attribute__((address_space(1)))
; #define LDS_WAIT() asm volatile("s_waitcnt lgkmcnt(0)" ::: "memory")
;     ...
;     for (int kb = 0; kb < D / 64; ++kb) {
; #pragma unroll
;         for (int i = 0; i < 8; ++i) { const int kk = 8 * i + kr; const int k = 64 * kb + kk; const f32x4 v = __builtin_nontemporal_load((const f32x4*)(W + (size_t)k * pitch)) * g[k];
;             LAS float* p = scr + kk * 33 + 4 * (lane & 7); p[0] = __builtin_rintf(v[0] * inv[0]); p[1] = __builtin_rintf(v[1] * inv[1]); p[2] = __builtin_rintf(v[2] * inv[2]); p[3] = __builtin_rintf(v[3] * inv[3]); }
;         LDS_WAIT(); asm volatile("" ::: "memory");
;         const int c = lane & 7;
; #pragma unroll
;         for (int j = 0; j < 4; ++j) { const int n = (lane >> 3) + 8 * j; const LAS float* sp = scr + (8 * c) * 33 + n;
;             u32x2 o;
;             o.x = ((unsigned)(int)sp[0 * 33] & 0xFFu) | (((unsigned)(int)sp[1 * 33] & 0xFFu) << 8) | (((unsigned)(int)sp[2 * 33] & 0xFFu) << 16) | (((unsigned)(int)sp[3 * 33] & 0xFFu) << 24);
;             o.y = ((unsigned)(int)sp[4 * 33] & 0xFFu) | (((unsigned)(int)sp[5 * 33] & 0xFFu) << 8) | (((unsigned)(int)sp[6 * 33] & 0xFFu) << 16) | (((unsigned)(int)sp[7 * 33] & 0xFFu) << 24);
;             *(GAS u32x2*)(dst + (size_t)(n0 + n) * D + 64 * kb + 8 * c) = o; }
;         LDS_WAIT(); asm volatile("" ::: "memory");
	v_cvt_i32_f32_sdwa v52, v52 dst_sel:BYTE_3 dst_unused:UNUSED_PAD src0_sel:DWORD
	v_cvt_i32_f32_sdwa v45, v45 dst_sel:BYTE_3 dst_unused:UNUSED_PAD src0_sel:DWORD
	v_cvt_i32_f32_sdwa v53, v53 dst_sel:BYTE_3 dst_unused:UNUSED_PAD src0_sel:DWORD
	v_lshlrev_b32_e32 v14, 8, v14
	v_lshlrev_b32_e32 v32, 8, v32
	v_and_b32_e32 v26, 0xff0000, v26
	v_and_b32_e32 v34, 0xff0000, v34
	v_lshlrev_b32_e32 v15, 8, v15
	v_lshlrev_b32_e32 v33, 8, v33
	v_lshlrev_b32_e32 v40, 8, v40
	v_lshlrev_b32_e32 v48, 8, v48
	v_lshlrev_b32_e32 v41, 8, v41
	v_lshlrev_b32_e32 v49, 8, v49
	v_perm_b32 v12, v14, v12, s28
	v_perm_b32 v14, v32, v30, s28
	v_and_b32_e32 v27, 0xff0000, v27
	v_and_b32_e32 v35, 0xff0000, v35
	v_and_b32_e32 v42, 0xff0000, v42
	v_and_b32_e32 v50, 0xff0000, v50
	v_and_b32_e32 v43, 0xff0000, v43
	v_and_b32_e32 v51, 0xff0000, v51
	v_perm_b32 v15, v15, v13, s28
	v_perm_b32 v30, v33, v31, s28
	v_perm_b32 v31, v40, v38, s28
	v_perm_b32 v32, v48, v46, s28
	v_perm_b32 v33, v41, v39, s28
	v_perm_b32 v38, v49, v47, s28
	v_or3_b32 v12, v12, v26, v28
	v_or3_b32 v13, v14, v34, v36
	v_or3_b32 v14, v15, v27, v29
	v_or3_b32 v15, v30, v35, v37
	v_or3_b32 v26, v31, v42, v44
	v_or3_b32 v27, v32, v50, v52
	v_or3_b32 v28, v33, v43, v45
	v_or3_b32 v29, v38, v51, v53
	global_store_dwordx2 v[16:17], v[12:13], off
	global_store_dwordx2 v[18:19], v[14:15], off
	global_store_dwordx2 v[58:59], v[26:27], off
	global_store_dwordx2 v[60:61], v[28:29], off
	s_waitcnt lgkmcnt(0)
	v_add_u32_e32 v77, 0x420, v25
	v_add_u32_e32 v79, 0x428, v25
	v_add_u32_e32 v81, 0x840, v25
	v_add_u32_e32 v83, 0x848, v25
	v_add_u32_e32 v85, 0xc60, v25
	v_add_u32_e32 v87, 0xc68, v25
	v_add_u32_e32 v89, 0x1080, v25
	v_add_u32_e32 v91, 0x1088, v25
	v_add_u32_e32 v92, 0x14a0, v25
	v_add_u32_e32 v93, 0x14a8, v25
	v_add_u32_e32 v94, 0x18c0, v25
	v_add_u32_e32 v95, 0x18c8, v25
	v_add_u32_e32 v96, 0x1ce0, v25
	v_add_u32_e32 v97, 0x1ce8, v25
	v_lshl_add_u64 v[16:17], v[10:11], 0, s[26:27]
	v_lshl_add_u64 v[18:19], v[8:9], 0, s[26:27]
	v_lshl_add_u64 v[58:59], v[6:7], 0, s[26:27]
	v_lshl_add_u64 v[60:61], v[4:5], 0, s[26:27]
	v_lshl_add_u64 v[4:5], v[4:5], 0, 64
	v_lshl_add_u64 v[6:7], v[6:7], 0, 64
	v_lshl_add_u64 v[8:9], v[8:9], 0, 64
	v_lshl_add_u64 v[10:11], v[10:11], 0, 64
	s_waitcnt vmcnt(44)
	v_pk_mul_f32 v[14:15], v[170:171], v[234:235] op_sel_hi:[1,0]
	v_pk_mul_f32 v[12:13], v[172:173], v[234:235] op_sel_hi:[1,0]
	v_mul_f32_e32 v62, v20, v14
	v_mul_f32_e32 v63, v21, v15
	v_mul_f32_e32 v64, v22, v12
	v_mul_f32_e32 v65, v23, v13
	v_pk_mul_f32 v[14:15], v[174:175], v[236:237] op_sel_hi:[1,0]
	v_pk_mul_f32 v[12:13], v[176:177], v[236:237] op_sel_hi:[1,0]
	v_pk_mul_f32 v[26:27], v[180:181], v[238:239] op_sel_hi:[1,0]
	v_pk_mul_f32 v[28:29], v[178:179], v[238:239] op_sel_hi:[1,0]
	v_pk_mul_f32 v[30:31], v[184:185], v[240:241] op_sel_hi:[1,0]
	v_pk_mul_f32 v[32:33], v[182:183], v[240:241] op_sel_hi:[1,0]
	v_pk_mul_f32 v[34:35], v[188:189], v[242:243] op_sel_hi:[1,0]
	v_pk_mul_f32 v[36:37], v[186:187], v[242:243] op_sel_hi:[1,0]
	v_pk_mul_f32 v[38:39], v[192:193], v[244:245] op_sel_hi:[1,0]
	v_pk_mul_f32 v[40:41], v[190:191], v[244:245] op_sel_hi:[1,0]
	v_pk_mul_f32 v[42:43], v[196:197], v[246:247] op_sel_hi:[1,0]
	v_pk_mul_f32 v[44:45], v[194:195], v[246:247] op_sel_hi:[1,0]
	v_pk_mul_f32 v[46:47], v[200:201], v[248:249] op_sel_hi:[1,0]
	v_pk_mul_f32 v[48:49], v[198:199], v[248:249] op_sel_hi:[1,0]
	s_add_u32 s4, s4, 0x16000
	s_addc_u32 s5, s5, 0
	global_load_dwordx4 v[170:173], v250, s[4:5] nt
	global_load_dword v234, v251, s[6:7] offset:2048
	s_add_u32 s4, s4, 0x16000
	s_addc_u32 s5, s5, 0
	global_load_dwordx4 v[174:177], v250, s[4:5] nt
	global_load_dword v236, v251, s[6:7] offset:2080
	s_add_u32 s4, s4, 0x16000
	s_addc_u32 s5, s5, 0
	global_load_dwordx4 v[178:181], v250, s[4:5] nt
	global_load_dword v238, v251, s[6:7] offset:2112
	s_add_u32 s4, s4, 0x16000
	s_addc_u32 s5, s5, 0
	global_load_dwordx4 v[182:185], v250, s[4:5] nt
	global_load_dword v240, v251, s[6:7] offset:2144
	s_add_u32 s4, s4, 0x16000
	s_addc_u32 s5, s5, 0
	global_load_dwordx4 v[186:189], v250, s[4:5] nt
	global_load_dword v242, v251, s[6:7] offset:2176
	s_add_u32 s4, s4, 0x16000
	s_addc_u32 s5, s5, 0
	global_load_dwordx4 v[190:193], v250, s[4:5] nt
	global_load_dword v244, v251, s[6:7] offset:2208
	s_add_u32 s4, s4, 0x16000
	s_addc_u32 s5, s5, 0
	global_load_dwordx4 v[194:197], v250, s[4:5] nt
	global_load_dword v246, v251, s[6:7] offset:2240
	s_add_u32 s4, s4, 0x16000
	s_addc_u32 s5, s5, 0
	global_load_dwordx4 v[198:201], v250, s[4:5] nt
	global_load_dword v248, v251, s[6:7] offset:2272
	v_mul_f32_e32 v14, v20, v14
	v_mul_f32_e32 v15, v21, v15
	v_rndne_f32_e32 v50, v62
	v_rndne_f32_e32 v51, v63
	v_mul_f32_e32 v12, v22, v12
	v_mul_f32_e32 v13, v23, v13
	v_mul_f32_e32 v28, v20, v28
	v_mul_f32_e32 v29, v21, v29
	v_mul_f32_e32 v26, v22, v26
	v_mul_f32_e32 v27, v23, v27
	v_mul_f32_e32 v32, v20, v32
	v_mul_f32_e32 v33, v21, v33
	v_mul_f32_e32 v30, v22, v30
	v_mul_f32_e32 v31, v23, v31
	v_mul_f32_e32 v36, v20, v36
	v_mul_f32_e32 v37, v21, v37
	v_mul_f32_e32 v34, v22, v34
	v_mul_f32_e32 v35, v23, v35
	v_mul_f32_e32 v40, v20, v40
	v_mul_f32_e32 v41, v21, v41
	v_mul_f32_e32 v38, v22, v38
	v_mul_f32_e32 v39, v23, v39
	v_mul_f32_e32 v44, v20, v44
	v_mul_f32_e32 v45, v21, v45
	v_mul_f32_e32 v42, v22, v42
	v_mul_f32_e32 v43, v23, v43
	v_mul_f32_e32 v48, v20, v48
	v_mul_f32_e32 v49, v21, v49
	v_mul_f32_e32 v46, v22, v46
	v_mul_f32_e32 v47, v23, v47
	v_rndne_f32_e32 v14, v14
	v_rndne_f32_e32 v15, v15
	v_rndne_f32_e32 v52, v64
	v_rndne_f32_e32 v53, v65
	ds_write2_b32 v25, v50, v51 offset1:1
	ds_write2_b32 v25, v52, v53 offset0:2 offset1:3
	v_rndne_f32_e32 v12, v12
	v_rndne_f32_e32 v13, v13
	v_rndne_f32_e32 v28, v28
	v_rndne_f32_e32 v29, v29
	v_rndne_f32_e32 v26, v26
	v_rndne_f32_e32 v27, v27
	v_rndne_f32_e32 v32, v32
	v_rndne_f32_e32 v33, v33
	v_rndne_f32_e32 v30, v30
	v_rndne_f32_e32 v31, v31
	v_rndne_f32_e32 v36, v36
	v_rndne_f32_e32 v37, v37
	v_rndne_f32_e32 v34, v34
	v_rndne_f32_e32 v35, v35
	v_rndne_f32_e32 v40, v40
	v_rndne_f32_e32 v41, v41
	v_rndne_f32_e32 v38, v38
	v_rndne_f32_e32 v39, v39
	v_rndne_f32_e32 v44, v44
	v_rndne_f32_e32 v45, v45
	v_rndne_f32_e32 v42, v42
	v_rndne_f32_e32 v43, v43
	v_rndne_f32_e32 v48, v48
	v_rndne_f32_e32 v49, v49
	v_rndne_f32_e32 v46, v46
	v_rndne_f32_e32 v47, v47
	ds_write2_b32 v77, v14, v15 offset1:1
	ds_write2_b32 v79, v12, v13 offset1:1
	ds_write2_b32 v81, v28, v29 offset1:1
	ds_write2_b32 v83, v26, v27 offset1:1
	ds_write2_b32 v85, v32, v33 offset1:1
	ds_write2_b32 v87, v30, v31 offset1:1
	ds_write2_b32 v89, v36, v37 offset1:1
	ds_write2_b32 v91, v34, v35 offset1:1
	ds_write2_b32 v92, v40, v41 offset1:1
	ds_write2_b32 v93, v38, v39 offset1:1
	ds_write2_b32 v94, v44, v45 offset1:1
	ds_write2_b32 v95, v42, v43 offset1:1
	ds_write2_b32 v96, v48, v49 offset1:1
	ds_write2_b32 v97, v46, v47 offset1:1
	s_waitcnt lgkmcnt(0)
; #define LAS __attribute__((address_space(3)))
; #define GAS __attribute__((address_space(1)))
; #define LDS_WAIT() asm volatile("s_waitcnt lgkmcnt(0)" ::: "memory")
;     ...
;     for (int kb = 0; kb < D / 64; ++kb) {
; #pragma unroll
;         for (int i = 0; i < 8; ++i) { const int kk = 8 * i + kr; const int k = 64 * kb + kk; const f32x4 v = __builtin_nontemporal_load((const f32x4*)(W + (size_t)k * pitch)) * g[k];
;             LAS float* p = scr + kk * 33 + 4 * (lane & 7); p[0] = __builtin_rintf(v[0] * inv[0]); p[1] = __builtin_rintf(v[1] * inv[1]); p[2] = __builtin_rintf(v[2] * inv[2]); p[3] = __builtin_rintf(v[3] * inv[3]); }
;         LDS_WAIT(); asm volatile("" ::: "memory");
;         const int c = lane & 7;
; #pragma unroll
;         for (int j = 0; j < 4; ++j) { const int n = (lane >> 3) + 8 * j; const LAS float* sp = scr + (8 * c) * 33 + n;
;             u32x2 o;
;             o.x = ((unsigned)(int)sp[0 * 33] & 0xFFu) | (((unsigned)(int)sp[1 * 33] & 0xFFu) << 8) | (((unsigned)(int)sp[2 * 33] & 0xFFu) << 16) | (((unsigned)(int)sp[3 * 33] & 0xFFu) << 24);
;             o.y = ((unsigned)(int)sp[4 * 33] & 0xFFu) | (((unsigned)(int)sp[5 * 33] & 0xFFu) << 8) | (((unsigned)(int)sp[6 * 33] & 0xFFu) << 16) | (((unsigned)(int)sp[7 * 33] & 0xFFu) << 24);
;             *(GAS u32x2*)(dst + (size_t)(n0 + n) * D + 64 * kb + 8 * c) = o; }
;         LDS_WAIT(); asm volatile("" ::: "memory");
	ds_read2_b32 v[12:13], v24 offset1:8
	ds_read2_b32 v[14:15], v24 offset0:33 offset1:41
	ds_read2_b32 v[26:27], v24 offset0:66 offset1:74
	ds_read2_b32 v[28:29], v24 offset0:99 offset1:107
	ds_read2_b32 v[30:31], v24 offset0:132 offset1:140
	ds_read2_b32 v[32:33], v24 offset0:165 offset1:173
	ds_read2_b32 v[34:35], v24 offset0:198 offset1:206
	ds_read2_b32 v[36:37], v24 offset0:231 offset1:239
	ds_read2_b32 v[38:39], v24 offset0:16 offset1:24
	ds_read2_b32 v[40:41], v24 offset0:49 offset1:57
	ds_read2_b32 v[42:43], v24 offset0:82 offset1:90
	ds_read2_b32 v[44:45], v24 offset0:115 offset1:123
	ds_read2_b32 v[46:47], v24 offset0:148 offset1:156
	ds_read2_b32 v[48:49], v24 offset0:181 offset1:189
	ds_read2_b32 v[50:51], v24 offset0:214 offset1:222
	ds_read2_b32 v[52:53], v24 offset0:247 offset1:255
	s_waitcnt lgkmcnt(14)
	v_cvt_i32_f32_e32 v14, v14
	s_waitcnt lgkmcnt(10)
	v_cvt_i32_f32_e32 v32, v32
	v_cvt_i32_f32_e32 v12, v12
	v_cvt_i32_f32_sdwa v26, v26 dst_sel:WORD_1 dst_unused:UNUSED_PAD src0_sel:DWORD
	v_cvt_i32_f32_e32 v30, v30
	s_waitcnt lgkmcnt(9)
	v_cvt_i32_f32_sdwa v34, v34 dst_sel:WORD_1 dst_unused:UNUSED_PAD src0_sel:DWORD
	v_cvt_i32_f32_e32 v15, v15
	v_cvt_i32_f32_e32 v33, v33
	s_waitcnt lgkmcnt(6)
	v_cvt_i32_f32_e32 v40, v40
	s_waitcnt lgkmcnt(2)
	v_cvt_i32_f32_e32 v48, v48
	v_cvt_i32_f32_e32 v41, v41
	v_cvt_i32_f32_e32 v49, v49
	v_cvt_i32_f32_sdwa v28, v28 dst_sel:BYTE_3 dst_unused:UNUSED_PAD src0_sel:DWORD
	v_cvt_i32_f32_sdwa v36, v36 dst_sel:BYTE_3 dst_unused:UNUSED_PAD src0_sel:DWORD
	v_cvt_i32_f32_e32 v13, v13
	v_cvt_i32_f32_sdwa v27, v27 dst_sel:WORD_1 dst_unused:UNUSED_PAD src0_sel:DWORD
	v_cvt_i32_f32_e32 v31, v31
	v_cvt_i32_f32_sdwa v35, v35 dst_sel:WORD_1 dst_unused:UNUSED_PAD src0_sel:DWORD
	v_cvt_i32_f32_e32 v38, v38
	v_cvt_i32_f32_sdwa v42, v42 dst_sel:WORD_1 dst_unused:UNUSED_PAD src0_sel:DWORD
	v_cvt_i32_f32_e32 v46, v46
	s_waitcnt lgkmcnt(1)
	v_cvt_i32_f32_sdwa v50, v50 dst_sel:WORD_1 dst_unused:UNUSED_PAD src0_sel:DWORD
	v_cvt_i32_f32_e32 v39, v39
	v_cvt_i32_f32_sdwa v43, v43 dst_sel:WORD_1 dst_unused:UNUSED_PAD src0_sel:DWORD
	v_cvt_i32_f32_e32 v47, v47
	v_cvt_i32_f32_sdwa v51, v51 dst_sel:WORD_1 dst_unused:UNUSED_PAD src0_sel:DWORD
	v_cvt_i32_f32_sdwa v29, v29 dst_sel:BYTE_3 dst_unused:UNUSED_PAD src0_sel:DWORD
	v_cvt_i32_f32_sdwa v37, v37 dst_sel:BYTE_3 dst_unused:UNUSED_PAD src0_sel:DWORD
	v_cvt_i32_f32_sdwa v44, v44 dst_sel:BYTE_3 dst_unused:UNUSED_PAD src0_sel:DWORD
	s_waitcnt lgkmcnt(0)
	v_cvt_i32_f32_sdwa v52, v52 dst_sel:BYTE_3 dst_unused:UNUSED_PAD src0_sel:DWORD
	v_cvt_i32_f32_sdwa v45, v45 dst_sel:BYTE_3 dst_unused:UNUSED_PAD src0_sel:DWORD
	v_cvt_i32_f32_sdwa v53, v53 dst_sel:BYTE_3 dst_unused:UNUSED_PAD src0_sel:DWORD
	v_lshlrev_b32_e32 v14, 8, v14
	v_lshlrev_b32_e32 v32, 8, v32
	v_and_b32_e32 v26, 0xff0000, v26
	v_and_b32_e32 v34, 0xff0000, v34
	v_lshlrev_b32_e32 v15, 8, v15
	v_lshlrev_b32_e32 v33, 8, v33
	v_lshlrev_b32_e32 v40, 8, v40
	v_lshlrev_b32_e32 v48, 8, v48
	v_lshlrev_b32_e32 v41, 8, v41
	v_lshlrev_b32_e32 v49, 8, v49
	v_perm_b32 v12, v14, v12, s28
	v_perm_b32 v14, v32, v30, s28
	v_and_b32_e32 v27, 0xff0000, v27
	v_and_b32_e32 v35, 0xff0000, v35
	v_and_b32_e32 v42, 0xff0000, v42
	v_and_b32_e32 v50, 0xff0000, v50
	v_and_b32_e32 v43, 0xff0000, v43
	v_and_b32_e32 v51, 0xff0000, v51
	v_perm_b32 v15, v15, v13, s28
	v_perm_b32 v30, v33, v31, s28
	v_perm_b32 v31, v40, v38, s28
	v_perm_b32 v32, v48, v46, s28
	v_perm_b32 v33, v41, v39, s28
	v_perm_b32 v38, v49, v47, s28
	v_or3_b32 v12, v12, v26, v28
	v_or3_b32 v13, v14, v34, v36
	v_or3_b32 v14, v15, v27, v29
	v_or3_b32 v15, v30, v35, v37
	v_or3_b32 v26, v31, v42, v44
	v_or3_b32 v27, v32, v50, v52
	v_or3_b32 v28, v33, v43, v45
	v_or3_b32 v29, v38, v51, v53
	global_store_dwordx2 v[16:17], v[12:13], off
	global_store_dwordx2 v[18:19], v[14:15], off
	global_store_dwordx2 v[58:59], v[26:27], off
	global_store_dwordx2 v[60:61], v[28:29], off
	s_waitcnt lgkmcnt(0)
	v_add_u32_e32 v77, 0x420, v25
	v_add_u32_e32 v79, 0x428, v25
	v_add_u32_e32 v81, 0x840, v25
	v_add_u32_e32 v83, 0x848, v25
	v_add_u32_e32 v85, 0xc60, v25
	v_add_u32_e32 v87, 0xc68, v25
	v_add_u32_e32 v89, 0x1080, v25
	v_add_u32_e32 v91, 0x1088, v25
	v_add_u32_e32 v92, 0x14a0, v25
	v_add_u32_e32 v93, 0x14a8, v25
	v_add_u32_e32 v94, 0x18c0, v25
	v_add_u32_e32 v95, 0x18c8, v25
	v_add_u32_e32 v96, 0x1ce0, v25
	v_add_u32_e32 v97, 0x1ce8, v25
	v_lshl_add_u64 v[16:17], v[10:11], 0, s[26:27]
	v_lshl_add_u64 v[18:19], v[8:9], 0, s[26:27]
	v_lshl_add_u64 v[58:59], v[6:7], 0, s[26:27]
	v_lshl_add_u64 v[60:61], v[4:5], 0, s[26:27]
	v_lshl_add_u64 v[4:5], v[4:5], 0, 64
	v_lshl_add_u64 v[6:7], v[6:7], 0, 64
	v_lshl_add_u64 v[8:9], v[8:9], 0, 64
	v_lshl_add_u64 v[10:11], v[10:11], 0, 64
	s_waitcnt vmcnt(44)
; #define LAS __attribute__((address_space(3)))
; #define GAS __attribute__((address_space(1)))
; #define LDS_WAIT() asm volatile("s_waitcnt lgkmcnt(0)" ::: "memory")
;     ...
;     for (int kb = 0; kb < D / 64; ++kb) {
; #pragma unroll
;         for (int i = 0; i < 8; ++i) { const int kk = 8 * i + kr; const int k = 64 * kb + kk; const f32x4 v = __builtin_nontemporal_load((const f32x4*)(W + (size_t)k * pitch)) * g[k];
;             LAS float* p = scr + kk * 33 + 4 * (lane & 7); p[0] = __builtin_rintf(v[0] * inv[0]); p[1] = __builtin_rintf(v[1] * inv[1]); p[2] = __builtin_rintf(v[2] * inv[2]); p[3] = __builtin_rintf(v[3] * inv[3]); }
;         LDS_WAIT(); asm volatile("" ::: "memory");
;         const int c = lane & 7;
; #pragma unroll
;         for (int j = 0; j < 4; ++j) { const int n = (lane >> 3) + 8 * j; const LAS float* sp = scr + (8 * c) * 33 + n;
;             u32x2 o;
;             o.x = ((unsigned)(int)sp[0 * 33] & 0xFFu) | (((unsigned)(int)sp[1 * 33] & 0xFFu) << 8) | (((unsigned)(int)sp[2 * 33] & 0xFFu) << 16) | (((unsigned)(int)sp[3 * 33] & 0xFFu) << 24);
;             o.y = ((unsigned)(int)sp[4 * 33] & 0xFFu) | (((unsigned)(int)sp[5 * 33] & 0xFFu) << 8) | (((unsigned)(int)sp[6 * 33] & 0xFFu) << 16) | (((unsigned)(int)sp[7 * 33] & 0xFFu) << 24);
;             *(GAS u32x2*)(dst + (size_t)(n0 + n) * D + 64 * kb + 8 * c) = o; }
;         LDS_WAIT(); asm volatile("" ::: "memory");
	v_pk_mul_f32 v[14:15], v[106:107], v[202:203] op_sel_hi:[1,0]
	v_pk_mul_f32 v[12:13], v[108:109], v[202:203] op_sel_hi:[1,0]
	v_mul_f32_e32 v62, v20, v14
	v_mul_f32_e32 v63, v21, v15
	v_mul_f32_e32 v64, v22, v12
	v_mul_f32_e32 v65, v23, v13
	v_pk_mul_f32 v[14:15], v[110:111], v[204:205] op_sel_hi:[1,0]
	v_pk_mul_f32 v[12:13], v[112:113], v[204:205] op_sel_hi:[1,0]
	v_pk_mul_f32 v[26:27], v[116:117], v[206:207] op_sel_hi:[1,0]
	v_pk_mul_f32 v[28:29], v[114:115], v[206:207] op_sel_hi:[1,0]
	v_pk_mul_f32 v[30:31], v[120:121], v[208:209] op_sel_hi:[1,0]
	v_pk_mul_f32 v[32:33], v[118:119], v[208:209] op_sel_hi:[1,0]
	v_pk_mul_f32 v[34:35], v[124:125], v[210:211] op_sel_hi:[1,0]
	v_pk_mul_f32 v[36:37], v[122:123], v[210:211] op_sel_hi:[1,0]
	v_pk_mul_f32 v[38:39], v[128:129], v[212:213] op_sel_hi:[1,0]
	v_pk_mul_f32 v[40:41], v[126:127], v[212:213] op_sel_hi:[1,0]
	v_pk_mul_f32 v[42:43], v[132:133], v[214:215] op_sel_hi:[1,0]
	v_pk_mul_f32 v[44:45], v[130:131], v[214:215] op_sel_hi:[1,0]
	v_pk_mul_f32 v[46:47], v[136:137], v[216:217] op_sel_hi:[1,0]
	v_pk_mul_f32 v[48:49], v[134:135], v[216:217] op_sel_hi:[1,0]
	s_add_u32 s4, s4, 0x16000
	s_addc_u32 s5, s5, 0
	global_load_dwordx4 v[106:109], v250, s[4:5] nt
	global_load_dword v202, v251, s[6:7] offset:2304
	s_add_u32 s4, s4, 0x16000
	s_addc_u32 s5, s5, 0
	global_load_dwordx4 v[110:113], v250, s[4:5] nt
	global_load_dword v204, v251, s[6:7] offset:2336
	s_add_u32 s4, s4, 0x16000
	s_addc_u32 s5, s5, 0
	global_load_dwordx4 v[114:117], v250, s[4:5] nt
	global_load_dword v206, v251, s[6:7] offset:2368
	s_add_u32 s4, s4, 0x16000
	s_addc_u32 s5, s5, 0
	global_load_dwordx4 v[118:121], v250, s[4:5] nt
	global_load_dword v208, v251, s[6:7] offset:2400
	s_add_u32 s4, s4, 0x16000
	s_addc_u32 s5, s5, 0
	global_load_dwordx4 v[122:125], v250, s[4:5] nt
	global_load_dword v210, v251, s[6:7] offset:2432
	s_add_u32 s4, s4, 0x16000
	s_addc_u32 s5, s5, 0
	global_load_dwordx4 v[126:129], v250, s[4:5] nt
	global_load_dword v212, v251, s[6:7] offset:2464
	s_add_u32 s4, s4, 0x16000
	s_addc_u32 s5, s5, 0
	global_load_dwordx4 v[130:133], v250, s[4:5] nt
	global_load_dword v214, v251, s[6:7] offset:2496
	s_add_u32 s4, s4, 0x16000
	s_addc_u32 s5, s5, 0
	global_load_dwordx4 v[134:137], v250, s[4:5] nt
	global_load_dword v216, v251, s[6:7] offset:2528
	v_mul_f32_e32 v14, v20, v14
	v_mul_f32_e32 v15, v21, v15
	v_rndne_f32_e32 v50, v62
	v_rndne_f32_e32 v51, v63
	v_mul_f32_e32 v12, v22, v12
	v_mul_f32_e32 v13, v23, v13
	v_mul_f32_e32 v28, v20, v28
	v_mul_f32_e32 v29, v21, v29
	v_mul_f32_e32 v26, v22, v26
	v_mul_f32_e32 v27, v23, v27
	v_mul_f32_e32 v32, v20, v32
	v_mul_f32_e32 v33, v21, v33
	v_mul_f32_e32 v30, v22, v30
	v_mul_f32_e32 v31, v23, v31
	v_mul_f32_e32 v36, v20, v36
	v_mul_f32_e32 v37, v21, v37
	v_mul_f32_e32 v34, v22, v34
	v_mul_f32_e32 v35, v23, v35
	v_mul_f32_e32 v40, v20, v40
	v_mul_f32_e32 v41, v21, v41
	v_mul_f32_e32 v38, v22, v38
	v_mul_f32_e32 v39, v23, v39
	v_mul_f32_e32 v44, v20, v44
	v_mul_f32_e32 v45, v21, v45
	v_mul_f32_e32 v42, v22, v42
	v_mul_f32_e32 v43, v23, v43
	v_mul_f32_e32 v48, v20, v48
	v_mul_f32_e32 v49, v21, v49
	v_mul_f32_e32 v46, v22, v46
	v_mul_f32_e32 v47, v23, v47
	v_rndne_f32_e32 v14, v14
	v_rndne_f32_e32 v15, v15
	v_rndne_f32_e32 v52, v64
	v_rndne_f32_e32 v53, v65
	ds_write2_b32 v25, v50, v51 offset1:1
	ds_write2_b32 v25, v52, v53 offset0:2 offset1:3
	v_rndne_f32_e32 v12, v12
	v_rndne_f32_e32 v13, v13
	v_rndne_f32_e32 v28, v28
	v_rndne_f32_e32 v29, v29
	v_rndne_f32_e32 v26, v26
	v_rndne_f32_e32 v27, v27
	v_rndne_f32_e32 v32, v32
	v_rndne_f32_e32 v33, v33
	v_rndne_f32_e32 v30, v30
	v_rndne_f32_e32 v31, v31
	v_rndne_f32_e32 v36, v36
	v_rndne_f32_e32 v37, v37
	v_rndne_f32_e32 v34, v34
	v_rndne_f32_e32 v35, v35
	v_rndne_f32_e32 v40, v40
	v_rndne_f32_e32 v41, v41
	v_rndne_f32_e32 v38, v38
	v_rndne_f32_e32 v39, v39
	v_rndne_f32_e32 v44, v44
	v_rndne_f32_e32 v45, v45
	v_rndne_f32_e32 v42, v42
	v_rndne_f32_e32 v43, v43
	v_rndne_f32_e32 v48, v48
	v_rndne_f32_e32 v49, v49
	v_rndne_f32_e32 v46, v46
	v_rndne_f32_e32 v47, v47
	ds_write2_b32 v77, v14, v15 offset1:1
	ds_write2_b32 v79, v12, v13 offset1:1
	ds_write2_b32 v81, v28, v29 offset1:1
	ds_write2_b32 v83, v26, v27 offset1:1
	ds_write2_b32 v85, v32, v33 offset1:1
	ds_write2_b32 v87, v30, v31 offset1:1
	ds_write2_b32 v89, v36, v37 offset1:1
	ds_write2_b32 v91, v34, v35 offset1:1
	ds_write2_b32 v92, v40, v41 offset1:1
	ds_write2_b32 v93, v38, v39 offset1:1
	ds_write2_b32 v94, v44, v45 offset1:1
	ds_write2_b32 v95, v42, v43 offset1:1
	ds_write2_b32 v96, v48, v49 offset1:1
	ds_write2_b32 v97, v46, v47 offset1:1
	s_waitcnt lgkmcnt(0)
	ds_read2_b32 v[12:13], v24 offset1:8
	ds_read2_b32 v[14:15], v24 offset0:33 offset1:41
	ds_read2_b32 v[26:27], v24 offset0:66 offset1:74
	ds_read2_b32 v[28:29], v24 offset0:99 offset1:107
	ds_read2_b32 v[30:31], v24 offset0:132 offset1:140
	ds_read2_b32 v[32:33], v24 offset0:165 offset1:173
	ds_read2_b32 v[34:35], v24 offset0:198 offset1:206
	ds_read2_b32 v[36:37], v24 offset0:231 offset1:239
	ds_read2_b32 v[38:39], v24 offset0:16 offset1:24
	ds_read2_b32 v[40:41], v24 offset0:49 offset1:57
	ds_read2_b32 v[42:43], v24 offset0:82 offset1:90
	ds_read2_b32 v[44:45], v24 offset0:115 offset1:123
	ds_read2_b32 v[46:47], v24 offset0:148 offset1:156
	ds_read2_b32 v[48:49], v24 offset0:181 offset1:189
	ds_read2_b32 v[50:51], v24 offset0:214 offset1:222
	ds_read2_b32 v[52:53], v24 offset0:247 offset1:255
	s_waitcnt lgkmcnt(14)
	v_cvt_i32_f32_e32 v14, v14
	s_waitcnt lgkmcnt(10)
	v_cvt_i32_f32_e32 v32, v32
	v_cvt_i32_f32_e32 v12, v12
	v_cvt_i32_f32_sdwa v26, v26 dst_sel:WORD_1 dst_unused:UNUSED_PAD src0_sel:DWORD
	v_cvt_i32_f32_e32 v30, v30
	s_waitcnt lgkmcnt(9)
; #define LAS __attribute__((address_space(3)))
; #define GAS __attribute__((address_space(1)))
; #define LDS_WAIT() asm volatile("s_waitcnt lgkmcnt(0)" ::: "memory")
;     ...
;     for (int kb = 0; kb < D / 64; ++kb) {
; #pragma unroll
;         for (int i = 0; i < 8; ++i) { const int kk = 8 * i + kr; const int k = 64 * kb + kk; const f32x4 v = __builtin_nontemporal_load((const f32x4*)(W + (size_t)k * pitch)) * g[k];
;             LAS float* p = scr + kk * 33 + 4 * (lane & 7); p[0] = __builtin_rintf(v[0] * inv[0]); p[1] = __builtin_rintf(v[1] * inv[1]); p[2] = __builtin_rintf(v[2] * inv[2]); p[3] = __builtin_rintf(v[3] * inv[3]); }
;         LDS_WAIT(); asm volatile("" ::: "memory");
;         const int c = lane & 7;
; #pragma unroll
;         for (int j = 0; j < 4; ++j) { const int n = (lane >> 3) + 8 * j; const LAS float* sp = scr + (8 * c) * 33 + n;
;             u32x2 o;
;             o.x = ((unsigned)(int)sp[0 * 33] & 0xFFu) | (((unsigned)(int)sp[1 * 33] & 0xFFu) << 8) | (((unsigned)(int)sp[2 * 33] & 0xFFu) << 16) | (((unsigned)(int)sp[3 * 33] & 0xFFu) << 24);
;             o.y = ((unsigned)(int)sp[4 * 33] & 0xFFu) | (((unsigned)(int)sp[5 * 33] & 0xFFu) << 8) | (((unsigned)(int)sp[6 * 33] & 0xFFu) << 16) | (((unsigned)(int)sp[7 * 33] & 0xFFu) << 24);
;             *(GAS u32x2*)(dst + (size_t)(n0 + n) * D + 64 * kb + 8 * c) = o; }
;         LDS_WAIT(); asm volatile("" ::: "memory");
	v_cvt_i32_f32_sdwa v34, v34 dst_sel:WORD_1 dst_unused:UNUSED_PAD src0_sel:DWORD
	v_cvt_i32_f32_e32 v15, v15
	v_cvt_i32_f32_e32 v33, v33
	s_waitcnt lgkmcnt(6)
	v_cvt_i32_f32_e32 v40, v40
	s_waitcnt lgkmcnt(2)
	v_cvt_i32_f32_e32 v48, v48
	v_cvt_i32_f32_e32 v41, v41
	v_cvt_i32_f32_e32 v49, v49
	v_cvt_i32_f32_sdwa v28, v28 dst_sel:BYTE_3 dst_unused:UNUSED_PAD src0_sel:DWORD
	v_cvt_i32_f32_sdwa v36, v36 dst_sel:BYTE_3 dst_unused:UNUSED_PAD src0_sel:DWORD
	v_cvt_i32_f32_e32 v13, v13
	v_cvt_i32_f32_sdwa v27, v27 dst_sel:WORD_1 dst_unused:UNUSED_PAD src0_sel:DWORD
	v_cvt_i32_f32_e32 v31, v31
	v_cvt_i32_f32_sdwa v35, v35 dst_sel:WORD_1 dst_unused:UNUSED_PAD src0_sel:DWORD
	v_cvt_i32_f32_e32 v38, v38
	v_cvt_i32_f32_sdwa v42, v42 dst_sel:WORD_1 dst_unused:UNUSED_PAD src0_sel:DWORD
	v_cvt_i32_f32_e32 v46, v46
	s_waitcnt lgkmcnt(1)
	v_cvt_i32_f32_sdwa v50, v50 dst_sel:WORD_1 dst_unused:UNUSED_PAD src0_sel:DWORD
	v_cvt_i32_f32_e32 v39, v39
	v_cvt_i32_f32_sdwa v43, v43 dst_sel:WORD_1 dst_unused:UNUSED_PAD src0_sel:DWORD
	v_cvt_i32_f32_e32 v47, v47
	v_cvt_i32_f32_sdwa v51, v51 dst_sel:WORD_1 dst_unused:UNUSED_PAD src0_sel:DWORD
	v_cvt_i32_f32_sdwa v29, v29 dst_sel:BYTE_3 dst_unused:UNUSED_PAD src0_sel:DWORD
	v_cvt_i32_f32_sdwa v37, v37 dst_sel:BYTE_3 dst_unused:UNUSED_PAD src0_sel:DWORD
	v_cvt_i32_f32_sdwa v44, v44 dst_sel:BYTE_3 dst_unused:UNUSED_PAD src0_sel:DWORD
	s_waitcnt lgkmcnt(0)
	v_cvt_i32_f32_sdwa v52, v52 dst_sel:BYTE_3 dst_unused:UNUSED_PAD src0_sel:DWORD
	v_cvt_i32_f32_sdwa v45, v45 dst_sel:BYTE_3 dst_unused:UNUSED_PAD src0_sel:DWORD
	v_cvt_i32_f32_sdwa v53, v53 dst_sel:BYTE_3 dst_unused:UNUSED_PAD src0_sel:DWORD
	v_lshlrev_b32_e32 v14, 8, v14
	v_lshlrev_b32_e32 v32, 8, v32
	v_and_b32_e32 v26, 0xff0000, v26
	v_and_b32_e32 v34, 0xff0000, v34
	v_lshlrev_b32_e32 v15, 8, v15
	v_lshlrev_b32_e32 v33, 8, v33
	v_lshlrev_b32_e32 v40, 8, v40
	v_lshlrev_b32_e32 v48, 8, v48
	v_lshlrev_b32_e32 v41, 8, v41
	v_lshlrev_b32_e32 v49, 8, v49
	v_perm_b32 v12, v14, v12, s28
	v_perm_b32 v14, v32, v30, s28
	v_and_b32_e32 v27, 0xff0000, v27
	v_and_b32_e32 v35, 0xff0000, v35
	v_and_b32_e32 v42, 0xff0000, v42
	v_and_b32_e32 v50, 0xff0000, v50
	v_and_b32_e32 v43, 0xff0000, v43
	v_and_b32_e32 v51, 0xff0000, v51
	v_perm_b32 v15, v15, v13, s28
	v_perm_b32 v30, v33, v31, s28
	v_perm_b32 v31, v40, v38, s28
	v_perm_b32 v32, v48, v46, s28
	v_perm_b32 v33, v41, v39, s28
	v_perm_b32 v38, v49, v47, s28
	v_or3_b32 v12, v12, v26, v28
	v_or3_b32 v13, v14, v34, v36
	v_or3_b32 v14, v15, v27, v29
	v_or3_b32 v15, v30, v35, v37
	v_or3_b32 v26, v31, v42, v44
	v_or3_b32 v27, v32, v50, v52
	v_or3_b32 v28, v33, v43, v45
	v_or3_b32 v29, v38, v51, v53
	global_store_dwordx2 v[16:17], v[12:13], off
	global_store_dwordx2 v[18:19], v[14:15], off
	global_store_dwordx2 v[58:59], v[26:27], off
	global_store_dwordx2 v[60:61], v[28:29], off
	s_waitcnt lgkmcnt(0)
	v_add_u32_e32 v77, 0x420, v25
	v_add_u32_e32 v79, 0x428, v25
	v_add_u32_e32 v81, 0x840, v25
	v_add_u32_e32 v83, 0x848, v25
	v_add_u32_e32 v85, 0xc60, v25
	v_add_u32_e32 v87, 0xc68, v25
	v_add_u32_e32 v89, 0x1080, v25
	v_add_u32_e32 v91, 0x1088, v25
	v_add_u32_e32 v92, 0x14a0, v25
	v_add_u32_e32 v93, 0x14a8, v25
	v_add_u32_e32 v94, 0x18c0, v25
	v_add_u32_e32 v95, 0x18c8, v25
	v_add_u32_e32 v96, 0x1ce0, v25
	v_add_u32_e32 v97, 0x1ce8, v25
	v_lshl_add_u64 v[16:17], v[10:11], 0, s[26:27]
	v_lshl_add_u64 v[18:19], v[8:9], 0, s[26:27]
	v_lshl_add_u64 v[58:59], v[6:7], 0, s[26:27]
	v_lshl_add_u64 v[60:61], v[4:5], 0, s[26:27]
	v_lshl_add_u64 v[4:5], v[4:5], 0, 64
	v_lshl_add_u64 v[6:7], v[6:7], 0, 64
	v_lshl_add_u64 v[8:9], v[8:9], 0, 64
	v_lshl_add_u64 v[10:11], v[10:11], 0, 64
	s_waitcnt vmcnt(44)
	v_pk_mul_f32 v[14:15], v[138:139], v[218:219] op_sel_hi:[1,0]
	v_pk_mul_f32 v[12:13], v[140:141], v[218:219] op_sel_hi:[1,0]
	v_mul_f32_e32 v62, v20, v14
	v_mul_f32_e32 v63, v21, v15
	v_mul_f32_e32 v64, v22, v12
	v_mul_f32_e32 v65, v23, v13
	v_pk_mul_f32 v[14:15], v[142:143], v[220:221] op_sel_hi:[1,0]
	v_pk_mul_f32 v[12:13], v[144:145], v[220:221] op_sel_hi:[1,0]
	v_pk_mul_f32 v[26:27], v[148:149], v[222:223] op_sel_hi:[1,0]
	v_pk_mul_f32 v[28:29], v[146:147], v[222:223] op_sel_hi:[1,0]
	v_pk_mul_f32 v[30:31], v[152:153], v[224:225] op_sel_hi:[1,0]
	v_pk_mul_f32 v[32:33], v[150:151], v[224:225] op_sel_hi:[1,0]
	v_pk_mul_f32 v[34:35], v[156:157], v[226:227] op_sel_hi:[1,0]
	v_pk_mul_f32 v[36:37], v[154:155], v[226:227] op_sel_hi:[1,0]
	v_pk_mul_f32 v[38:39], v[160:161], v[228:229] op_sel_hi:[1,0]
	v_pk_mul_f32 v[40:41], v[158:159], v[228:229] op_sel_hi:[1,0]
	v_pk_mul_f32 v[42:43], v[164:165], v[230:231] op_sel_hi:[1,0]
	v_pk_mul_f32 v[44:45], v[162:163], v[230:231] op_sel_hi:[1,0]
	v_pk_mul_f32 v[46:47], v[168:169], v[232:233] op_sel_hi:[1,0]
	v_pk_mul_f32 v[48:49], v[166:167], v[232:233] op_sel_hi:[1,0]
	s_add_u32 s4, s4, 0x16000
	s_addc_u32 s5, s5, 0
	global_load_dwordx4 v[138:141], v250, s[4:5] nt
	global_load_dword v218, v251, s[6:7] offset:2560
	s_add_u32 s4, s4, 0x16000
	s_addc_u32 s5, s5, 0
	global_load_dwordx4 v[142:145], v250, s[4:5] nt
	global_load_dword v220, v251, s[6:7] offset:2592
	s_add_u32 s4, s4, 0x16000
	s_addc_u32 s5, s5, 0
	global_load_dwordx4 v[146:149], v250, s[4:5] nt
	global_load_dword v222, v251, s[6:7] offset:2624
	s_add_u32 s4, s4, 0x16000
	s_addc_u32 s5, s5, 0
	global_load_dwordx4 v[150:153], v250, s[4:5] nt
	global_load_dword v224, v251, s[6:7] offset:2656
	s_add_u32 s4, s4, 0x16000
	s_addc_u32 s5, s5, 0
	global_load_dwordx4 v[154:157], v250, s[4:5] nt
	global_load_dword v226, v251, s[6:7] offset:2688
	s_add_u32 s4, s4, 0x16000
	s_addc_u32 s5, s5, 0
	global_load_dwordx4 v[158:161], v250, s[4:5] nt
; #define LAS __attribute__((address_space(3)))
; #define GAS __attribute__((address_space(1)))
; #define LDS_WAIT() asm volatile("s_waitcnt lgkmcnt(0)" ::: "memory")
;     ...
;     for (int kb = 0; kb < D / 64; ++kb) {
; #pragma unroll
;         for (int i = 0; i < 8; ++i) { const int kk = 8 * i + kr; const int k = 64 * kb + kk; const f32x4 v = __builtin_nontemporal_load((const f32x4*)(W + (size_t)k * pitch)) * g[k];
;             LAS float* p = scr + kk * 33 + 4 * (lane & 7); p[0] = __builtin_rintf(v[0] * inv[0]); p[1] = __builtin_rintf(v[1] * inv[1]); p[2] = __builtin_rintf(v[2] * inv[2]); p[3] = __builtin_rintf(v[3] * inv[3]); }
;         LDS_WAIT(); asm volatile("" ::: "memory");
;         const int c = lane & 7;
; #pragma unroll
;         for (int j = 0; j < 4; ++j) { const int n = (lane >> 3) + 8 * j; const LAS float* sp = scr + (8 * c) * 33 + n;
;             u32x2 o;
;             o.x = ((unsigned)(int)sp[0 * 33] & 0xFFu) | (((unsigned)(int)sp[1 * 33] & 0xFFu) << 8) | (((unsigned)(int)sp[2 * 33] & 0xFFu) << 16) | (((unsigned)(int)sp[3 * 33] & 0xFFu) << 24);
;             o.y = ((unsigned)(int)sp[4 * 33] & 0xFFu) | (((unsigned)(int)sp[5 * 33] & 0xFFu) << 8) | (((unsigned)(int)sp[6 * 33] & 0xFFu) << 16) | (((unsigned)(int)sp[7 * 33] & 0xFFu) << 24);
;             *(GAS u32x2*)(dst + (size_t)(n0 + n) * D + 64 * kb + 8 * c) = o; }
;         LDS_WAIT(); asm volatile("" ::: "memory");
	global_load_dword v228, v251, s[6:7] offset:2720
	s_add_u32 s4, s4, 0x16000
	s_addc_u32 s5, s5, 0
	global_load_dwordx4 v[162:165], v250, s[4:5] nt
	global_load_dword v230, v251, s[6:7] offset:2752
	s_add_u32 s4, s4, 0x16000
	s_addc_u32 s5, s5, 0
	global_load_dwordx4 v[166:169], v250, s[4:5] nt
	global_load_dword v232, v251, s[6:7] offset:2784
	v_mul_f32_e32 v14, v20, v14
	v_mul_f32_e32 v15, v21, v15
	v_rndne_f32_e32 v50, v62
	v_rndne_f32_e32 v51, v63
	v_mul_f32_e32 v12, v22, v12
	v_mul_f32_e32 v13, v23, v13
	v_mul_f32_e32 v28, v20, v28
	v_mul_f32_e32 v29, v21, v29
	v_mul_f32_e32 v26, v22, v26
	v_mul_f32_e32 v27, v23, v27
	v_mul_f32_e32 v32, v20, v32
	v_mul_f32_e32 v33, v21, v33
	v_mul_f32_e32 v30, v22, v30
	v_mul_f32_e32 v31, v23, v31
	v_mul_f32_e32 v36, v20, v36
	v_mul_f32_e32 v37, v21, v37
	v_mul_f32_e32 v34, v22, v34
	v_mul_f32_e32 v35, v23, v35
	v_mul_f32_e32 v40, v20, v40
	v_mul_f32_e32 v41, v21, v41
	v_mul_f32_e32 v38, v22, v38
	v_mul_f32_e32 v39, v23, v39
	v_mul_f32_e32 v44, v20, v44
	v_mul_f32_e32 v45, v21, v45
	v_mul_f32_e32 v42, v22, v42
	v_mul_f32_e32 v43, v23, v43
	v_mul_f32_e32 v48, v20, v48
	v_mul_f32_e32 v49, v21, v49
	v_mul_f32_e32 v46, v22, v46
	v_mul_f32_e32 v47, v23, v47
	v_rndne_f32_e32 v14, v14
	v_rndne_f32_e32 v15, v15
	v_rndne_f32_e32 v52, v64
	v_rndne_f32_e32 v53, v65
	ds_write2_b32 v25, v50, v51 offset1:1
	ds_write2_b32 v25, v52, v53 offset0:2 offset1:3
	v_rndne_f32_e32 v12, v12
	v_rndne_f32_e32 v13, v13
	v_rndne_f32_e32 v28, v28
	v_rndne_f32_e32 v29, v29
	v_rndne_f32_e32 v26, v26
	v_rndne_f32_e32 v27, v27
	v_rndne_f32_e32 v32, v32
	v_rndne_f32_e32 v33, v33
	v_rndne_f32_e32 v30, v30
	v_rndne_f32_e32 v31, v31
	v_rndne_f32_e32 v36, v36
	v_rndne_f32_e32 v37, v37
	v_rndne_f32_e32 v34, v34
	v_rndne_f32_e32 v35, v35
	v_rndne_f32_e32 v40, v40
	v_rndne_f32_e32 v41, v41
	v_rndne_f32_e32 v38, v38
	v_rndne_f32_e32 v39, v39
	v_rndne_f32_e32 v44, v44
	v_rndne_f32_e32 v45, v45
	v_rndne_f32_e32 v42, v42
	v_rndne_f32_e32 v43, v43
	v_rndne_f32_e32 v48, v48
	v_rndne_f32_e32 v49, v49
	v_rndne_f32_e32 v46, v46
	v_rndne_f32_e32 v47, v47
	ds_write2_b32 v77, v14, v15 offset1:1
	ds_write2_b32 v79, v12, v13 offset1:1
	ds_write2_b32 v81, v28, v29 offset1:1
	ds_write2_b32 v83, v26, v27 offset1:1
	ds_write2_b32 v85, v32, v33 offset1:1
	ds_write2_b32 v87, v30, v31 offset1:1
	ds_write2_b32 v89, v36, v37 offset1:1
	ds_write2_b32 v91, v34, v35 offset1:1
	ds_write2_b32 v92, v40, v41 offset1:1
	ds_write2_b32 v93, v38, v39 offset1:1
	ds_write2_b32 v94, v44, v45 offset1:1
	ds_write2_b32 v95, v42, v43 offset1:1
	ds_write2_b32 v96, v48, v49 offset1:1
	ds_write2_b32 v97, v46, v47 offset1:1
	s_waitcnt lgkmcnt(0)
	ds_read2_b32 v[12:13], v24 offset1:8
	ds_read2_b32 v[14:15], v24 offset0:33 offset1:41
	ds_read2_b32 v[26:27], v24 offset0:66 offset1:74
	ds_read2_b32 v[28:29], v24 offset0:99 offset1:107
	ds_read2_b32 v[30:31], v24 offset0:132 offset1:140
	ds_read2_b32 v[32:33], v24 offset0:165 offset1:173
	ds_read2_b32 v[34:35], v24 offset0:198 offset1:206
	ds_read2_b32 v[36:37], v24 offset0:231 offset1:239
	ds_read2_b32 v[38:39], v24 offset0:16 offset1:24
	ds_read2_b32 v[40:41], v24 offset0:49 offset1:57
	ds_read2_b32 v[42:43], v24 offset0:82 offset1:90
	ds_read2_b32 v[44:45], v24 offset0:115 offset1:123
	ds_read2_b32 v[46:47], v24 offset0:148 offset1:156
	ds_read2_b32 v[48:49], v24 offset0:181 offset1:189
	ds_read2_b32 v[50:51], v24 offset0:214 offset1:222
	ds_read2_b32 v[52:53], v24 offset0:247 offset1:255
	s_waitcnt lgkmcnt(14)
	v_cvt_i32_f32_e32 v14, v14
	s_waitcnt lgkmcnt(10)
	v_cvt_i32_f32_e32 v32, v32
	v_cvt_i32_f32_e32 v12, v12
	v_cvt_i32_f32_sdwa v26, v26 dst_sel:WORD_1 dst_unused:UNUSED_PAD src0_sel:DWORD
	v_cvt_i32_f32_e32 v30, v30
	s_waitcnt lgkmcnt(9)
	v_cvt_i32_f32_sdwa v34, v34 dst_sel:WORD_1 dst_unused:UNUSED_PAD src0_sel:DWORD
	v_cvt_i32_f32_e32 v15, v15
	v_cvt_i32_f32_e32 v33, v33
	s_waitcnt lgkmcnt(6)
	v_cvt_i32_f32_e32 v40, v40
	s_waitcnt lgkmcnt(2)
	v_cvt_i32_f32_e32 v48, v48
	v_cvt_i32_f32_e32 v41, v41
	v_cvt_i32_f32_e32 v49, v49
	v_cvt_i32_f32_sdwa v28, v28 dst_sel:BYTE_3 dst_unused:UNUSED_PAD src0_sel:DWORD
	v_cvt_i32_f32_sdwa v36, v36 dst_sel:BYTE_3 dst_unused:UNUSED_PAD src0_sel:DWORD
	v_cvt_i32_f32_e32 v13, v13
	v_cvt_i32_f32_sdwa v27, v27 dst_sel:WORD_1 dst_unused:UNUSED_PAD src0_sel:DWORD
	v_cvt_i32_f32_e32 v31, v31
	v_cvt_i32_f32_sdwa v35, v35 dst_sel:WORD_1 dst_unused:UNUSED_PAD src0_sel:DWORD
	v_cvt_i32_f32_e32 v38, v38
	v_cvt_i32_f32_sdwa v42, v42 dst_sel:WORD_1 dst_unused:UNUSED_PAD src0_sel:DWORD
	v_cvt_i32_f32_e32 v46, v46
	s_waitcnt lgkmcnt(1)
	v_cvt_i32_f32_sdwa v50, v50 dst_sel:WORD_1 dst_unused:UNUSED_PAD src0_sel:DWORD
	v_cvt_i32_f32_e32 v39, v39
	v_cvt_i32_f32_sdwa v43, v43 dst_sel:WORD_1 dst_unused:UNUSED_PAD src0_sel:DWORD
	v_cvt_i32_f32_e32 v47, v47
	v_cvt_i32_f32_sdwa v51, v51 dst_sel:WORD_1 dst_unused:UNUSED_PAD src0_sel:DWORD
	v_cvt_i32_f32_sdwa v29, v29 dst_sel:BYTE_3 dst_unused:UNUSED_PAD src0_sel:DWORD
	v_cvt_i32_f32_sdwa v37, v37 dst_sel:BYTE_3 dst_unused:UNUSED_PAD src0_sel:DWORD
	v_cvt_i32_f32_sdwa v44, v44 dst_sel:BYTE_3 dst_unused:UNUSED_PAD src0_sel:DWORD
	s_waitcnt lgkmcnt(0)
; #define LAS __attribute__((address_space(3)))
; #define GAS __attribute__((address_space(1)))
; #define LDS_WAIT() asm volatile("s_waitcnt lgkmcnt(0)" ::: "memory")
;     ...
;     for (int kb = 0; kb < D / 64; ++kb) {
; #pragma unroll
;         for (int i = 0; i < 8; ++i) { const int kk = 8 * i + kr; const int k = 64 * kb + kk; const f32x4 v = __builtin_nontemporal_load((const f32x4*)(W + (size_t)k * pitch)) * g[k];
;             LAS float* p = scr + kk * 33 + 4 * (lane & 7); p[0] = __builtin_rintf(v[0] * inv[0]); p[1] = __builtin_rintf(v[1] * inv[1]); p[2] = __builtin_rintf(v[2] * inv[2]); p[3] = __builtin_rintf(v[3] * inv[3]); }
;         LDS_WAIT(); asm volatile("" ::: "memory");
;         const int c = lane & 7;
; #pragma unroll
;         for (int j = 0; j < 4; ++j) { const int n = (lane >> 3) + 8 * j; const LAS float* sp = scr + (8 * c) * 33 + n;
;             u32x2 o;
;             o.x = ((unsigned)(int)sp[0 * 33] & 0xFFu) | (((unsigned)(int)sp[1 * 33] & 0xFFu) << 8) | (((unsigned)(int)sp[2 * 33] & 0xFFu) << 16) | (((unsigned)(int)sp[3 * 33] & 0xFFu) << 24);
;             o.y = ((unsigned)(int)sp[4 * 33] & 0xFFu) | (((unsigned)(int)sp[5 * 33] & 0xFFu) << 8) | (((unsigned)(int)sp[6 * 33] & 0xFFu) << 16) | (((unsigned)(int)sp[7 * 33] & 0xFFu) << 24);
;             *(GAS u32x2*)(dst + (size_t)(n0 + n) * D + 64 * kb + 8 * c) = o; }
;         LDS_WAIT(); asm volatile("" ::: "memory");
	v_cvt_i32_f32_sdwa v52, v52 dst_sel:BYTE_3 dst_unused:UNUSED_PAD src0_sel:DWORD
	v_cvt_i32_f32_sdwa v45, v45 dst_sel:BYTE_3 dst_unused:UNUSED_PAD src0_sel:DWORD
	v_cvt_i32_f32_sdwa v53, v53 dst_sel:BYTE_3 dst_unused:UNUSED_PAD src0_sel:DWORD
	v_lshlrev_b32_e32 v14, 8, v14
	v_lshlrev_b32_e32 v32, 8, v32
	v_and_b32_e32 v26, 0xff0000, v26
	v_and_b32_e32 v34, 0xff0000, v34
	v_lshlrev_b32_e32 v15, 8, v15
	v_lshlrev_b32_e32 v33, 8, v33
	v_lshlrev_b32_e32 v40, 8, v40
	v_lshlrev_b32_e32 v48, 8, v48
	v_lshlrev_b32_e32 v41, 8, v41
	v_lshlrev_b32_e32 v49, 8, v49
	v_perm_b32 v12, v14, v12, s28
	v_perm_b32 v14, v32, v30, s28
	v_and_b32_e32 v27, 0xff0000, v27
	v_and_b32_e32 v35, 0xff0000, v35
	v_and_b32_e32 v42, 0xff0000, v42
	v_and_b32_e32 v50, 0xff0000, v50
	v_and_b32_e32 v43, 0xff0000, v43
	v_and_b32_e32 v51, 0xff0000, v51
	v_perm_b32 v15, v15, v13, s28
	v_perm_b32 v30, v33, v31, s28
	v_perm_b32 v31, v40, v38, s28
	v_perm_b32 v32, v48, v46, s28
	v_perm_b32 v33, v41, v39, s28
	v_perm_b32 v38, v49, v47, s28
	v_or3_b32 v12, v12, v26, v28
	v_or3_b32 v13, v14, v34, v36
	v_or3_b32 v14, v15, v27, v29
	v_or3_b32 v15, v30, v35, v37
	v_or3_b32 v26, v31, v42, v44
	v_or3_b32 v27, v32, v50, v52
	v_or3_b32 v28, v33, v43, v45
	v_or3_b32 v29, v38, v51, v53
	global_store_dwordx2 v[16:17], v[12:13], off
	global_store_dwordx2 v[18:19], v[14:15], off
	global_store_dwordx2 v[58:59], v[26:27], off
	global_store_dwordx2 v[60:61], v[28:29], off
	s_waitcnt lgkmcnt(0)
	v_add_u32_e32 v77, 0x420, v25
	v_add_u32_e32 v79, 0x428, v25
	v_add_u32_e32 v81, 0x840, v25
	v_add_u32_e32 v83, 0x848, v25
	v_add_u32_e32 v85, 0xc60, v25
	v_add_u32_e32 v87, 0xc68, v25
	v_add_u32_e32 v89, 0x1080, v25
	v_add_u32_e32 v91, 0x1088, v25
	v_add_u32_e32 v92, 0x14a0, v25
	v_add_u32_e32 v93, 0x14a8, v25
	v_add_u32_e32 v94, 0x18c0, v25
	v_add_u32_e32 v95, 0x18c8, v25
	v_add_u32_e32 v96, 0x1ce0, v25
	v_add_u32_e32 v97, 0x1ce8, v25
	v_lshl_add_u64 v[16:17], v[10:11], 0, s[26:27]
	v_lshl_add_u64 v[18:19], v[8:9], 0, s[26:27]
	v_lshl_add_u64 v[58:59], v[6:7], 0, s[26:27]
	v_lshl_add_u64 v[60:61], v[4:5], 0, s[26:27]
	v_lshl_add_u64 v[4:5], v[4:5], 0, 64
	v_lshl_add_u64 v[6:7], v[6:7], 0, 64
	v_lshl_add_u64 v[8:9], v[8:9], 0, 64
	v_lshl_add_u64 v[10:11], v[10:11], 0, 64
	s_waitcnt vmcnt(44)
	v_pk_mul_f32 v[14:15], v[170:171], v[234:235] op_sel_hi:[1,0]
	v_pk_mul_f32 v[12:13], v[172:173], v[234:235] op_sel_hi:[1,0]
	v_mul_f32_e32 v62, v20, v14
	v_mul_f32_e32 v63, v21, v15
	v_mul_f32_e32 v64, v22, v12
	v_mul_f32_e32 v65, v23, v13
	v_pk_mul_f32 v[14:15], v[174:175], v[236:237] op_sel_hi:[1,0]
	v_pk_mul_f32 v[12:13], v[176:177], v[236:237] op_sel_hi:[1,0]
	v_pk_mul_f32 v[26:27], v[180:181], v[238:239] op_sel_hi:[1,0]
	v_pk_mul_f32 v[28:29], v[178:179], v[238:239] op_sel_hi:[1,0]
	v_pk_mul_f32 v[30:31], v[184:185], v[240:241] op_sel_hi:[1,0]
	v_pk_mul_f32 v[32:33], v[182:183], v[240:241] op_sel_hi:[1,0]
	v_pk_mul_f32 v[34:35], v[188:189], v[242:243] op_sel_hi:[1,0]
	v_pk_mul_f32 v[36:37], v[186:187], v[242:243] op_sel_hi:[1,0]
	v_pk_mul_f32 v[38:39], v[192:193], v[244:245] op_sel_hi:[1,0]
	v_pk_mul_f32 v[40:41], v[190:191], v[244:245] op_sel_hi:[1,0]
	v_pk_mul_f32 v[42:43], v[196:197], v[246:247] op_sel_hi:[1,0]
	v_pk_mul_f32 v[44:45], v[194:195], v[246:247] op_sel_hi:[1,0]
	v_pk_mul_f32 v[46:47], v[200:201], v[248:249] op_sel_hi:[1,0]
	v_pk_mul_f32 v[48:49], v[198:199], v[248:249] op_sel_hi:[1,0]
	s_add_u32 s4, s4, 0x16000
	s_addc_u32 s5, s5, 0
	global_load_dwordx4 v[170:173], v250, s[4:5] nt
	global_load_dword v234, v251, s[6:7] offset:2816
	s_add_u32 s4, s4, 0x16000
	s_addc_u32 s5, s5, 0
	global_load_dwordx4 v[174:177], v250, s[4:5] nt
	global_load_dword v236, v251, s[6:7] offset:2848
	s_add_u32 s4, s4, 0x16000
	s_addc_u32 s5, s5, 0
	global_load_dwordx4 v[178:181], v250, s[4:5] nt
	global_load_dword v238, v251, s[6:7] offset:2880
	s_add_u32 s4, s4, 0x16000
	s_addc_u32 s5, s5, 0
	global_load_dwordx4 v[182:185], v250, s[4:5] nt
	global_load_dword v240, v251, s[6:7] offset:2912
	s_add_u32 s4, s4, 0x16000
	s_addc_u32 s5, s5, 0
	global_load_dwordx4 v[186:189], v250, s[4:5] nt
	global_load_dword v242, v251, s[6:7] offset:2944
	s_add_u32 s4, s4, 0x16000
	s_addc_u32 s5, s5, 0
	global_load_dwordx4 v[190:193], v250, s[4:5] nt
	global_load_dword v244, v251, s[6:7] offset:2976
	s_add_u32 s4, s4, 0x16000
	s_addc_u32 s5, s5, 0
	global_load_dwordx4 v[194:197], v250, s[4:5] nt
	global_load_dword v246, v251, s[6:7] offset:3008
	s_add_u32 s4, s4, 0x16000
	s_addc_u32 s5, s5, 0
	global_load_dwordx4 v[198:201], v250, s[4:5] nt
	global_load_dword v248, v251, s[6:7] offset:3040
	v_mul_f32_e32 v14, v20, v14
	v_mul_f32_e32 v15, v21, v15
	v_rndne_f32_e32 v50, v62
	v_rndne_f32_e32 v51, v63
	v_mul_f32_e32 v12, v22, v12
	v_mul_f32_e32 v13, v23, v13
	v_mul_f32_e32 v28, v20, v28
	v_mul_f32_e32 v29, v21, v29
	v_mul_f32_e32 v26, v22, v26
	v_mul_f32_e32 v27, v23, v27
	v_mul_f32_e32 v32, v20, v32
	v_mul_f32_e32 v33, v21, v33
	v_mul_f32_e32 v30, v22, v30
	v_mul_f32_e32 v31, v23, v31
	v_mul_f32_e32 v36, v20, v36
	v_mul_f32_e32 v37, v21, v37
	v_mul_f32_e32 v34, v22, v34
	v_mul_f32_e32 v35, v23, v35
	v_mul_f32_e32 v40, v20, v40
	v_mul_f32_e32 v41, v21, v41
	v_mul_f32_e32 v38, v22, v38
	v_mul_f32_e32 v39, v23, v39
	v_mul_f32_e32 v44, v20, v44
	v_mul_f32_e32 v45, v21, v45
	v_mul_f32_e32 v42, v22, v42
	v_mul_f32_e32 v43, v23, v43
	v_mul_f32_e32 v48, v20, v48
	v_mul_f32_e32 v49, v21, v49
	v_mul_f32_e32 v46, v22, v46
	v_mul_f32_e32 v47, v23, v47
	v_rndne_f32_e32 v14, v14
	v_rndne_f32_e32 v15, v15
	v_rndne_f32_e32 v52, v64
	v_rndne_f32_e32 v53, v65
	ds_write2_b32 v25, v50, v51 offset1:1
	ds_write2_b32 v25, v52, v53 offset0:2 offset1:3
	v_rndne_f32_e32 v12, v12
	v_rndne_f32_e32 v13, v13
	v_rndne_f32_e32 v28, v28
	v_rndne_f32_e32 v29, v29
	v_rndne_f32_e32 v26, v26
	v_rndne_f32_e32 v27, v27
	v_rndne_f32_e32 v32, v32
	v_rndne_f32_e32 v33, v33
	v_rndne_f32_e32 v30, v30
	v_rndne_f32_e32 v31, v31
	v_rndne_f32_e32 v36, v36
	v_rndne_f32_e32 v37, v37
	v_rndne_f32_e32 v34, v34
	v_rndne_f32_e32 v35, v35
	v_rndne_f32_e32 v40, v40
	v_rndne_f32_e32 v41, v41
	v_rndne_f32_e32 v38, v38
	v_rndne_f32_e32 v39, v39
	v_rndne_f32_e32 v44, v44
	v_rndne_f32_e32 v45, v45
	v_rndne_f32_e32 v42, v42
	v_rndne_f32_e32 v43, v43
	v_rndne_f32_e32 v48, v48
	v_rndne_f32_e32 v49, v49
	v_rndne_f32_e32 v46, v46
	v_rndne_f32_e32 v47, v47
	ds_write2_b32 v77, v14, v15 offset1:1
	ds_write2_b32 v79, v12, v13 offset1:1
	ds_write2_b32 v81, v28, v29 offset1:1
	ds_write2_b32 v83, v26, v27 offset1:1
	ds_write2_b32 v85, v32, v33 offset1:1
	ds_write2_b32 v87, v30, v31 offset1:1
	ds_write2_b32 v89, v36, v37 offset1:1
	ds_write2_b32 v91, v34, v35 offset1:1
	ds_write2_b32 v92, v40, v41 offset1:1
	ds_write2_b32 v93, v38, v39 offset1:1
	ds_write2_b32 v94, v44, v45 offset1:1
	ds_write2_b32 v95, v42, v43 offset1:1
	ds_write2_b32 v96, v48, v49 offset1:1
	ds_write2_b32 v97, v46, v47 offset1:1
	s_waitcnt lgkmcnt(0)
; #define LAS __attribute__((address_space(3)))
; #define GAS __attribute__((address_space(1)))
; #define LDS_WAIT() asm volatile("s_waitcnt lgkmcnt(0)" ::: "memory")
;     ...
;     for (int kb = 0; kb < D / 64; ++kb) {
; #pragma unroll
;         for (int i = 0; i < 8; ++i) { const int kk = 8 * i + kr; const int k = 64 * kb + kk; const f32x4 v = __builtin_nontemporal_load((const f32x4*)(W + (size_t)k * pitch)) * g[k];
;             LAS float* p = scr + kk * 33 + 4 * (lane & 7); p[0] = __builtin_rintf(v[0] * inv[0]); p[1] = __builtin_rintf(v[1] * inv[1]); p[2] = __builtin_rintf(v[2] * inv[2]); p[3] = __builtin_rintf(v[3] * inv[3]); }
;         LDS_WAIT(); asm volatile("" ::: "memory");
;         const int c = lane & 7;
; #pragma unroll
;         for (int j = 0; j < 4; ++j) { const int n = (lane >> 3) + 8 * j; const LAS float* sp = scr + (8 * c) * 33 + n;
;             u32x2 o;
;             o.x = ((unsigned)(int)sp[0 * 33] & 0xFFu) | (((unsigned)(int)sp[1 * 33] & 0xFFu) << 8) | (((unsigned)(int)sp[2 * 33] & 0xFFu) << 16) | (((unsigned)(int)sp[3 * 33] & 0xFFu) << 24);
;             o.y = ((unsigned)(int)sp[4 * 33] & 0xFFu) | (((unsigned)(int)sp[5 * 33] & 0xFFu) << 8) | (((unsigned)(int)sp[6 * 33] & 0xFFu) << 16) | (((unsigned)(int)sp[7 * 33] & 0xFFu) << 24);
;             *(GAS u32x2*)(dst + (size_t)(n0 + n) * D + 64 * kb + 8 * c) = o; }
;         LDS_WAIT(); asm volatile("" ::: "memory");
;     }
	ds_read2_b32 v[12:13], v24 offset1:8
	ds_read2_b32 v[14:15], v24 offset0:33 offset1:41
	ds_read2_b32 v[26:27], v24 offset0:66 offset1:74
	ds_read2_b32 v[28:29], v24 offset0:99 offset1:107
	ds_read2_b32 v[30:31], v24 offset0:132 offset1:140
	ds_read2_b32 v[32:33], v24 offset0:165 offset1:173
	ds_read2_b32 v[34:35], v24 offset0:198 offset1:206
	ds_read2_b32 v[36:37], v24 offset0:231 offset1:239
	ds_read2_b32 v[38:39], v24 offset0:16 offset1:24
	ds_read2_b32 v[40:41], v24 offset0:49 offset1:57
	ds_read2_b32 v[42:43], v24 offset0:82 offset1:90
	ds_read2_b32 v[44:45], v24 offset0:115 offset1:123
	ds_read2_b32 v[46:47], v24 offset0:148 offset1:156
	ds_read2_b32 v[48:49], v24 offset0:181 offset1:189
	ds_read2_b32 v[50:51], v24 offset0:214 offset1:222
	ds_read2_b32 v[52:53], v24 offset0:247 offset1:255
	s_waitcnt lgkmcnt(14)
	v_cvt_i32_f32_e32 v14, v14
	s_waitcnt lgkmcnt(10)
	v_cvt_i32_f32_e32 v32, v32
	v_cvt_i32_f32_e32 v12, v12
	v_cvt_i32_f32_sdwa v26, v26 dst_sel:WORD_1 dst_unused:UNUSED_PAD src0_sel:DWORD
	v_cvt_i32_f32_e32 v30, v30
	s_waitcnt lgkmcnt(9)
	v_cvt_i32_f32_sdwa v34, v34 dst_sel:WORD_1 dst_unused:UNUSED_PAD src0_sel:DWORD
	v_cvt_i32_f32_e32 v15, v15
	v_cvt_i32_f32_e32 v33, v33
	s_waitcnt lgkmcnt(6)
	v_cvt_i32_f32_e32 v40, v40
	s_waitcnt lgkmcnt(2)
	v_cvt_i32_f32_e32 v48, v48
	v_cvt_i32_f32_e32 v41, v41
	v_cvt_i32_f32_e32 v49, v49
	v_cvt_i32_f32_sdwa v28, v28 dst_sel:BYTE_3 dst_unused:UNUSED_PAD src0_sel:DWORD
	v_cvt_i32_f32_sdwa v36, v36 dst_sel:BYTE_3 dst_unused:UNUSED_PAD src0_sel:DWORD
	v_cvt_i32_f32_e32 v13, v13
	v_cvt_i32_f32_sdwa v27, v27 dst_sel:WORD_1 dst_unused:UNUSED_PAD src0_sel:DWORD
	v_cvt_i32_f32_e32 v31, v31
	v_cvt_i32_f32_sdwa v35, v35 dst_sel:WORD_1 dst_unused:UNUSED_PAD src0_sel:DWORD
	v_cvt_i32_f32_e32 v38, v38
	v_cvt_i32_f32_sdwa v42, v42 dst_sel:WORD_1 dst_unused:UNUSED_PAD src0_sel:DWORD
	v_cvt_i32_f32_e32 v46, v46
	s_waitcnt lgkmcnt(1)
	v_cvt_i32_f32_sdwa v50, v50 dst_sel:WORD_1 dst_unused:UNUSED_PAD src0_sel:DWORD
	v_cvt_i32_f32_e32 v39, v39
	v_cvt_i32_f32_sdwa v43, v43 dst_sel:WORD_1 dst_unused:UNUSED_PAD src0_sel:DWORD
	v_cvt_i32_f32_e32 v47, v47
	v_cvt_i32_f32_sdwa v51, v51 dst_sel:WORD_1 dst_unused:UNUSED_PAD src0_sel:DWORD
	v_cvt_i32_f32_sdwa v29, v29 dst_sel:BYTE_3 dst_unused:UNUSED_PAD src0_sel:DWORD
	v_cvt_i32_f32_sdwa v37, v37 dst_sel:BYTE_3 dst_unused:UNUSED_PAD src0_sel:DWORD
	v_cvt_i32_f32_sdwa v44, v44 dst_sel:BYTE_3 dst_unused:UNUSED_PAD src0_sel:DWORD
	s_waitcnt lgkmcnt(0)
	v_cvt_i32_f32_sdwa v52, v52 dst_sel:BYTE_3 dst_unused:UNUSED_PAD src0_sel:DWORD
	v_cvt_i32_f32_sdwa v45, v45 dst_sel:BYTE_3 dst_unused:UNUSED_PAD src0_sel:DWORD
	v_cvt_i32_f32_sdwa v53, v53 dst_sel:BYTE_3 dst_unused:UNUSED_PAD src0_sel:DWORD
	v_lshlrev_b32_e32 v14, 8, v14
	v_lshlrev_b32_e32 v32, 8, v32
	v_and_b32_e32 v26, 0xff0000, v26
	v_and_b32_e32 v34, 0xff0000, v34
	v_lshlrev_b32_e32 v15, 8, v15
	v_lshlrev_b32_e32 v33, 8, v33
	v_lshlrev_b32_e32 v40, 8, v40
	v_lshlrev_b32_e32 v48, 8, v48
	v_lshlrev_b32_e32 v41, 8, v41
	v_lshlrev_b32_e32 v49, 8, v49
	v_perm_b32 v12, v14, v12, s28
	v_perm_b32 v14, v32, v30, s28
	v_and_b32_e32 v27, 0xff0000, v27
	v_and_b32_e32 v35, 0xff0000, v35
	v_and_b32_e32 v42, 0xff0000, v42
	v_and_b32_e32 v50, 0xff0000, v50
	v_and_b32_e32 v43, 0xff0000, v43
	v_and_b32_e32 v51, 0xff0000, v51
	v_perm_b32 v15, v15, v13, s28
	v_perm_b32 v30, v33, v31, s28
	v_perm_b32 v31, v40, v38, s28
	v_perm_b32 v32, v48, v46, s28
	v_perm_b32 v33, v41, v39, s28
	v_perm_b32 v38, v49, v47, s28
	v_or3_b32 v12, v12, v26, v28
	v_or3_b32 v13, v14, v34, v36
	v_or3_b32 v14, v15, v27, v29
	v_or3_b32 v15, v30, v35, v37
	v_or3_b32 v26, v31, v42, v44
	v_or3_b32 v27, v32, v50, v52
	v_or3_b32 v28, v33, v43, v45
	v_or3_b32 v29, v38, v51, v53
	global_store_dwordx2 v[16:17], v[12:13], off
	global_store_dwordx2 v[18:19], v[14:15], off
	global_store_dwordx2 v[58:59], v[26:27], off
	global_store_dwordx2 v[60:61], v[28:29], off
	s_waitcnt lgkmcnt(0)
	v_add_u32_e32 v77, 0x420, v25
	v_add_u32_e32 v79, 0x428, v25
	v_add_u32_e32 v81, 0x840, v25
	v_add_u32_e32 v83, 0x848, v25
	v_add_u32_e32 v85, 0xc60, v25
	v_add_u32_e32 v87, 0xc68, v25
	v_add_u32_e32 v89, 0x1080, v25
	v_add_u32_e32 v91, 0x1088, v25
	v_add_u32_e32 v92, 0x14a0, v25
	v_add_u32_e32 v93, 0x14a8, v25
	v_add_u32_e32 v94, 0x18c0, v25
	v_add_u32_e32 v95, 0x18c8, v25
	v_add_u32_e32 v96, 0x1ce0, v25
	v_add_u32_e32 v97, 0x1ce8, v25
	v_lshl_add_u64 v[16:17], v[10:11], 0, s[26:27]
	v_lshl_add_u64 v[18:19], v[8:9], 0, s[26:27]
	v_lshl_add_u64 v[58:59], v[6:7], 0, s[26:27]
	v_lshl_add_u64 v[60:61], v[4:5], 0, s[26:27]
	v_lshl_add_u64 v[4:5], v[4:5], 0, 64
	v_lshl_add_u64 v[6:7], v[6:7], 0, 64
	v_lshl_add_u64 v[8:9], v[8:9], 0, 64
	v_lshl_add_u64 v[10:11], v[10:11], 0, 64
	s_waitcnt vmcnt(44)
; #define LAS __attribute__((address_space(3)))
; #define GAS __attribute__((address_space(1)))
; #define LDS_WAIT() asm volatile("s_waitcnt lgkmcnt(0)" ::: "memory")
;     ...
;         for (int i = 0; i < 8; ++i) { const int k = 64 * kb + 8 * i + kr; const f32x4 v = __builtin_nontemporal_load((const f32x4*)(W + (size_t)k * pitch)) * g[k];
;     ...
;     for (int kb = 0; kb < D / 64; ++kb) {
; #pragma unroll
;         for (int i = 0; i < 8; ++i) { const int kk = 8 * i + kr; const int k = 64 * kb + kk; const f32x4 v = __builtin_nontemporal_load((const f32x4*)(W + (size_t)k * pitch)) * g[k];
;             LAS float* p = scr + kk * 33 + 4 * (lane & 7); p[0] = __builtin_rintf(v[0] * inv[0]); p[1] = __builtin_rintf(v[1] * inv[1]); p[2] = __builtin_rintf(v[2] * inv[2]); p[3] = __builtin_rintf(v[3] * inv[3]); }
;         LDS_WAIT(); asm volatile("" ::: "memory");
;         const int c = lane & 7;
; #pragma unroll
;         for (int j = 0; j < 4; ++j) { const int n = (lane >> 3) + 8 * j; const LAS float* sp = scr + (8 * c) * 33 + n;
;             u32x2 o;
;             o.x = ((unsigned)(int)sp[0 * 33] & 0xFFu) | (((unsigned)(int)sp[1 * 33] & 0xFFu) << 8) | (((unsigned)(int)sp[2 * 33] & 0xFFu) << 16) | (((unsigned)(int)sp[3 * 33] & 0xFFu) << 24);
;             o.y = ((unsigned)(int)sp[4 * 33] & 0xFFu) | (((unsigned)(int)sp[5 * 33] & 0xFFu) << 8) | (((unsigned)(int)sp[6 * 33] & 0xFFu) << 16) | (((unsigned)(int)sp[7 * 33] & 0xFFu) << 24);
;             *(GAS u32x2*)(dst + (size_t)(n0 + n) * D + 64 * kb + 8 * c) = o; }
;         LDS_WAIT(); asm volatile("" ::: "memory");
;     }
	v_pk_mul_f32 v[14:15], v[106:107], v[202:203] op_sel_hi:[1,0]
	v_pk_mul_f32 v[12:13], v[108:109], v[202:203] op_sel_hi:[1,0]
	v_mul_f32_e32 v62, v20, v14
	v_mul_f32_e32 v63, v21, v15
	v_mul_f32_e32 v64, v22, v12
	v_mul_f32_e32 v65, v23, v13
	v_pk_mul_f32 v[14:15], v[110:111], v[204:205] op_sel_hi:[1,0]
	v_pk_mul_f32 v[12:13], v[112:113], v[204:205] op_sel_hi:[1,0]
	v_pk_mul_f32 v[26:27], v[116:117], v[206:207] op_sel_hi:[1,0]
	v_pk_mul_f32 v[28:29], v[114:115], v[206:207] op_sel_hi:[1,0]
	v_pk_mul_f32 v[30:31], v[120:121], v[208:209] op_sel_hi:[1,0]
	v_pk_mul_f32 v[32:33], v[118:119], v[208:209] op_sel_hi:[1,0]
	v_pk_mul_f32 v[34:35], v[124:125], v[210:211] op_sel_hi:[1,0]
	v_pk_mul_f32 v[36:37], v[122:123], v[210:211] op_sel_hi:[1,0]
	v_pk_mul_f32 v[38:39], v[128:129], v[212:213] op_sel_hi:[1,0]
	v_pk_mul_f32 v[40:41], v[126:127], v[212:213] op_sel_hi:[1,0]
	v_pk_mul_f32 v[42:43], v[132:133], v[214:215] op_sel_hi:[1,0]
	v_pk_mul_f32 v[44:45], v[130:131], v[214:215] op_sel_hi:[1,0]
	v_pk_mul_f32 v[46:47], v[136:137], v[216:217] op_sel_hi:[1,0]
	v_pk_mul_f32 v[48:49], v[134:135], v[216:217] op_sel_hi:[1,0]
	s_add_u32 s4, s4, 0x16000
	s_addc_u32 s5, s5, 0
	global_load_dwordx4 v[106:109], v250, s[4:5] nt
	global_load_dword v202, v251, s[6:7] offset:3072
	s_add_u32 s4, s4, 0x16000
	s_addc_u32 s5, s5, 0
	global_load_dwordx4 v[110:113], v250, s[4:5] nt
	global_load_dword v204, v251, s[6:7] offset:3104
	s_add_u32 s4, s4, 0x16000
	s_addc_u32 s5, s5, 0
	global_load_dwordx4 v[114:117], v250, s[4:5] nt
	global_load_dword v206, v251, s[6:7] offset:3136
	s_add_u32 s4, s4, 0x16000
	s_addc_u32 s5, s5, 0
	global_load_dwordx4 v[118:121], v250, s[4:5] nt
	global_load_dword v208, v251, s[6:7] offset:3168
	s_add_u32 s4, s4, 0x16000
	s_addc_u32 s5, s5, 0
	global_load_dwordx4 v[122:125], v250, s[4:5] nt
	global_load_dword v210, v251, s[6:7] offset:3200
	s_add_u32 s4, s4, 0x16000
	s_addc_u32 s5, s5, 0
	global_load_dwordx4 v[126:129], v250, s[4:5] nt
	global_load_dword v212, v251, s[6:7] offset:3232
	s_add_u32 s4, s4, 0x16000
	s_addc_u32 s5, s5, 0
	global_load_dwordx4 v[130:133], v250, s[4:5] nt
	global_load_dword v214, v251, s[6:7] offset:3264
	s_add_u32 s4, s4, 0x16000
	s_addc_u32 s5, s5, 0
	global_load_dwordx4 v[134:137], v250, s[4:5] nt
	global_load_dword v216, v251, s[6:7] offset:3296
	v_mul_f32_e32 v14, v20, v14
	v_mul_f32_e32 v15, v21, v15
	v_rndne_f32_e32 v50, v62
	v_rndne_f32_e32 v51, v63
	v_mul_f32_e32 v12, v22, v12
	v_mul_f32_e32 v13, v23, v13
	v_mul_f32_e32 v28, v20, v28
	v_mul_f32_e32 v29, v21, v29
	v_mul_f32_e32 v26, v22, v26
	v_mul_f32_e32 v27, v23, v27
	v_mul_f32_e32 v32, v20, v32
	v_mul_f32_e32 v33, v21, v33
	v_mul_f32_e32 v30, v22, v30
	v_mul_f32_e32 v31, v23, v31
	v_mul_f32_e32 v36, v20, v36
	v_mul_f32_e32 v37, v21, v37
	v_mul_f32_e32 v34, v22, v34
	v_mul_f32_e32 v35, v23, v35
	v_mul_f32_e32 v40, v20, v40
	v_mul_f32_e32 v41, v21, v41
	v_mul_f32_e32 v38, v22, v38
	v_mul_f32_e32 v39, v23, v39
	v_mul_f32_e32 v44, v20, v44
	v_mul_f32_e32 v45, v21, v45
	v_mul_f32_e32 v42, v22, v42
	v_mul_f32_e32 v43, v23, v43
	v_mul_f32_e32 v48, v20, v48
	v_mul_f32_e32 v49, v21, v49
	v_mul_f32_e32 v46, v22, v46
	v_mul_f32_e32 v47, v23, v47
	v_rndne_f32_e32 v14, v14
	v_rndne_f32_e32 v15, v15
	v_rndne_f32_e32 v52, v64
	v_rndne_f32_e32 v53, v65
	ds_write2_b32 v25, v50, v51 offset1:1
	ds_write2_b32 v25, v52, v53 offset0:2 offset1:3
	v_rndne_f32_e32 v12, v12
	v_rndne_f32_e32 v13, v13
	v_rndne_f32_e32 v28, v28
	v_rndne_f32_e32 v29, v29
	v_rndne_f32_e32 v26, v26
	v_rndne_f32_e32 v27, v27
	v_rndne_f32_e32 v32, v32
	v_rndne_f32_e32 v33, v33
	v_rndne_f32_e32 v30, v30
	v_rndne_f32_e32 v31, v31
	v_rndne_f32_e32 v36, v36
	v_rndne_f32_e32 v37, v37
	v_rndne_f32_e32 v34, v34
	v_rndne_f32_e32 v35, v35
	v_rndne_f32_e32 v40, v40
	v_rndne_f32_e32 v41, v41
	v_rndne_f32_e32 v38, v38
	v_rndne_f32_e32 v39, v39
	v_rndne_f32_e32 v44, v44
	v_rndne_f32_e32 v45, v45
	v_rndne_f32_e32 v42, v42
	v_rndne_f32_e32 v43, v43
	v_rndne_f32_e32 v48, v48
	v_rndne_f32_e32 v49, v49
	v_rndne_f32_e32 v46, v46
	v_rndne_f32_e32 v47, v47
	ds_write2_b32 v77, v14, v15 offset1:1
	ds_write2_b32 v79, v12, v13 offset1:1
	ds_write2_b32 v81, v28, v29 offset1:1
	ds_write2_b32 v83, v26, v27 offset1:1
	ds_write2_b32 v85, v32, v33 offset1:1
	ds_write2_b32 v87, v30, v31 offset1:1
	ds_write2_b32 v89, v36, v37 offset1:1
	ds_write2_b32 v91, v34, v35 offset1:1
	ds_write2_b32 v92, v40, v41 offset1:1
	ds_write2_b32 v93, v38, v39 offset1:1
	ds_write2_b32 v94, v44, v45 offset1:1
	ds_write2_b32 v95, v42, v43 offset1:1
	ds_write2_b32 v96, v48, v49 offset1:1
	ds_write2_b32 v97, v46, v47 offset1:1
	s_waitcnt lgkmcnt(0)
	ds_read2_b32 v[12:13], v24 offset1:8
	ds_read2_b32 v[14:15], v24 offset0:33 offset1:41
	ds_read2_b32 v[26:27], v24 offset0:66 offset1:74
	ds_read2_b32 v[28:29], v24 offset0:99 offset1:107
	ds_read2_b32 v[30:31], v24 offset0:132 offset1:140
	ds_read2_b32 v[32:33], v24 offset0:165 offset1:173
	ds_read2_b32 v[34:35], v24 offset0:198 offset1:206
	ds_read2_b32 v[36:37], v24 offset0:231 offset1:239
	ds_read2_b32 v[38:39], v24 offset0:16 offset1:24
	ds_read2_b32 v[40:41], v24 offset0:49 offset1:57
	ds_read2_b32 v[42:43], v24 offset0:82 offset1:90
	ds_read2_b32 v[44:45], v24 offset0:115 offset1:123
	ds_read2_b32 v[46:47], v24 offset0:148 offset1:156
	ds_read2_b32 v[48:49], v24 offset0:181 offset1:189
	ds_read2_b32 v[50:51], v24 offset0:214 offset1:222
	ds_read2_b32 v[52:53], v24 offset0:247 offset1:255
	s_waitcnt lgkmcnt(14)
	v_cvt_i32_f32_e32 v14, v14
	s_waitcnt lgkmcnt(10)
	v_cvt_i32_f32_e32 v32, v32
	v_cvt_i32_f32_e32 v12, v12
	v_cvt_i32_f32_sdwa v26, v26 dst_sel:WORD_1 dst_unused:UNUSED_PAD src0_sel:DWORD
	v_cvt_i32_f32_e32 v30, v30
	s_waitcnt lgkmcnt(9)
; #define LAS __attribute__((address_space(3)))
; #define GAS __attribute__((address_space(1)))
; #define LDS_WAIT() asm volatile("s_waitcnt lgkmcnt(0)" ::: "memory")
;     ...
;     for (int kb = 0; kb < D / 64; ++kb) {
; #pragma unroll
;         for (int i = 0; i < 8; ++i) { const int kk = 8 * i + kr; const int k = 64 * kb + kk; const f32x4 v = __builtin_nontemporal_load((const f32x4*)(W + (size_t)k * pitch)) * g[k];
;             LAS float* p = scr + kk * 33 + 4 * (lane & 7); p[0] = __builtin_rintf(v[0] * inv[0]); p[1] = __builtin_rintf(v[1] * inv[1]); p[2] = __builtin_rintf(v[2] * inv[2]); p[3] = __builtin_rintf(v[3] * inv[3]); }
;         LDS_WAIT(); asm volatile("" ::: "memory");
;         const int c = lane & 7;
; #pragma unroll
;         for (int j = 0; j < 4; ++j) { const int n = (lane >> 3) + 8 * j; const LAS float* sp = scr + (8 * c) * 33 + n;
;             u32x2 o;
;             o.x = ((unsigned)(int)sp[0 * 33] & 0xFFu) | (((unsigned)(int)sp[1 * 33] & 0xFFu) << 8) | (((unsigned)(int)sp[2 * 33] & 0xFFu) << 16) | (((unsigned)(int)sp[3 * 33] & 0xFFu) << 24);
;             o.y = ((unsigned)(int)sp[4 * 33] & 0xFFu) | (((unsigned)(int)sp[5 * 33] & 0xFFu) << 8) | (((unsigned)(int)sp[6 * 33] & 0xFFu) << 16) | (((unsigned)(int)sp[7 * 33] & 0xFFu) << 24);
;             *(GAS u32x2*)(dst + (size_t)(n0 + n) * D + 64 * kb + 8 * c) = o; }
;         LDS_WAIT(); asm volatile("" ::: "memory");
;     }
	v_cvt_i32_f32_sdwa v34, v34 dst_sel:WORD_1 dst_unused:UNUSED_PAD src0_sel:DWORD
	v_cvt_i32_f32_e32 v15, v15
	v_cvt_i32_f32_e32 v33, v33
	s_waitcnt lgkmcnt(6)
	v_cvt_i32_f32_e32 v40, v40
	s_waitcnt lgkmcnt(2)
	v_cvt_i32_f32_e32 v48, v48
	v_cvt_i32_f32_e32 v41, v41
	v_cvt_i32_f32_e32 v49, v49
	v_cvt_i32_f32_sdwa v28, v28 dst_sel:BYTE_3 dst_unused:UNUSED_PAD src0_sel:DWORD
	v_cvt_i32_f32_sdwa v36, v36 dst_sel:BYTE_3 dst_unused:UNUSED_PAD src0_sel:DWORD
	v_cvt_i32_f32_e32 v13, v13
	v_cvt_i32_f32_sdwa v27, v27 dst_sel:WORD_1 dst_unused:UNUSED_PAD src0_sel:DWORD
	v_cvt_i32_f32_e32 v31, v31
	v_cvt_i32_f32_sdwa v35, v35 dst_sel:WORD_1 dst_unused:UNUSED_PAD src0_sel:DWORD
	v_cvt_i32_f32_e32 v38, v38
	v_cvt_i32_f32_sdwa v42, v42 dst_sel:WORD_1 dst_unused:UNUSED_PAD src0_sel:DWORD
	v_cvt_i32_f32_e32 v46, v46
	s_waitcnt lgkmcnt(1)
	v_cvt_i32_f32_sdwa v50, v50 dst_sel:WORD_1 dst_unused:UNUSED_PAD src0_sel:DWORD
	v_cvt_i32_f32_e32 v39, v39
	v_cvt_i32_f32_sdwa v43, v43 dst_sel:WORD_1 dst_unused:UNUSED_PAD src0_sel:DWORD
	v_cvt_i32_f32_e32 v47, v47
	v_cvt_i32_f32_sdwa v51, v51 dst_sel:WORD_1 dst_unused:UNUSED_PAD src0_sel:DWORD
	v_cvt_i32_f32_sdwa v29, v29 dst_sel:BYTE_3 dst_unused:UNUSED_PAD src0_sel:DWORD
	v_cvt_i32_f32_sdwa v37, v37 dst_sel:BYTE_3 dst_unused:UNUSED_PAD src0_sel:DWORD
	v_cvt_i32_f32_sdwa v44, v44 dst_sel:BYTE_3 dst_unused:UNUSED_PAD src0_sel:DWORD
	s_waitcnt lgkmcnt(0)
	v_cvt_i32_f32_sdwa v52, v52 dst_sel:BYTE_3 dst_unused:UNUSED_PAD src0_sel:DWORD
	v_cvt_i32_f32_sdwa v45, v45 dst_sel:BYTE_3 dst_unused:UNUSED_PAD src0_sel:DWORD
	v_cvt_i32_f32_sdwa v53, v53 dst_sel:BYTE_3 dst_unused:UNUSED_PAD src0_sel:DWORD
	v_lshlrev_b32_e32 v14, 8, v14
	v_lshlrev_b32_e32 v32, 8, v32
	v_and_b32_e32 v26, 0xff0000, v26
	v_and_b32_e32 v34, 0xff0000, v34
	v_lshlrev_b32_e32 v15, 8, v15
	v_lshlrev_b32_e32 v33, 8, v33
	v_lshlrev_b32_e32 v40, 8, v40
	v_lshlrev_b32_e32 v48, 8, v48
	v_lshlrev_b32_e32 v41, 8, v41
	v_lshlrev_b32_e32 v49, 8, v49
	v_perm_b32 v12, v14, v12, s28
	v_perm_b32 v14, v32, v30, s28
	v_and_b32_e32 v27, 0xff0000, v27
	v_and_b32_e32 v35, 0xff0000, v35
	v_and_b32_e32 v42, 0xff0000, v42
	v_and_b32_e32 v50, 0xff0000, v50
	v_and_b32_e32 v43, 0xff0000, v43
	v_and_b32_e32 v51, 0xff0000, v51
	v_perm_b32 v15, v15, v13, s28
	v_perm_b32 v30, v33, v31, s28
	v_perm_b32 v31, v40, v38, s28
	v_perm_b32 v32, v48, v46, s28
	v_perm_b32 v33, v41, v39, s28
	v_perm_b32 v38, v49, v47, s28
	v_or3_b32 v12, v12, v26, v28
	v_or3_b32 v13, v14, v34, v36
	v_or3_b32 v14, v15, v27, v29
	v_or3_b32 v15, v30, v35, v37
	v_or3_b32 v26, v31, v42, v44
	v_or3_b32 v27, v32, v50, v52
	v_or3_b32 v28, v33, v43, v45
	v_or3_b32 v29, v38, v51, v53
	global_store_dwordx2 v[16:17], v[12:13], off
	global_store_dwordx2 v[18:19], v[14:15], off
	global_store_dwordx2 v[58:59], v[26:27], off
	global_store_dwordx2 v[60:61], v[28:29], off
	s_waitcnt lgkmcnt(0)
	v_add_u32_e32 v77, 0x420, v25
	v_add_u32_e32 v79, 0x428, v25
	v_add_u32_e32 v81, 0x840, v25
	v_add_u32_e32 v83, 0x848, v25
	v_add_u32_e32 v85, 0xc60, v25
	v_add_u32_e32 v87, 0xc68, v25
	v_add_u32_e32 v89, 0x1080, v25
	v_add_u32_e32 v91, 0x1088, v25
	v_add_u32_e32 v92, 0x14a0, v25
	v_add_u32_e32 v93, 0x14a8, v25
	v_add_u32_e32 v94, 0x18c0, v25
	v_add_u32_e32 v95, 0x18c8, v25
	v_add_u32_e32 v96, 0x1ce0, v25
	v_add_u32_e32 v97, 0x1ce8, v25
	v_lshl_add_u64 v[16:17], v[10:11], 0, s[26:27]
	v_lshl_add_u64 v[18:19], v[8:9], 0, s[26:27]
	v_lshl_add_u64 v[58:59], v[6:7], 0, s[26:27]
	v_lshl_add_u64 v[60:61], v[4:5], 0, s[26:27]
	v_lshl_add_u64 v[4:5], v[4:5], 0, 64
	v_lshl_add_u64 v[6:7], v[6:7], 0, 64
	v_lshl_add_u64 v[8:9], v[8:9], 0, 64
	v_lshl_add_u64 v[10:11], v[10:11], 0, 64
	s_waitcnt vmcnt(44)
	v_pk_mul_f32 v[14:15], v[138:139], v[218:219] op_sel_hi:[1,0]
	v_pk_mul_f32 v[12:13], v[140:141], v[218:219] op_sel_hi:[1,0]
	v_mul_f32_e32 v62, v20, v14
	v_mul_f32_e32 v63, v21, v15
	v_mul_f32_e32 v64, v22, v12
	v_mul_f32_e32 v65, v23, v13
	v_pk_mul_f32 v[14:15], v[142:143], v[220:221] op_sel_hi:[1,0]
	v_pk_mul_f32 v[12:13], v[144:145], v[220:221] op_sel_hi:[1,0]
	v_pk_mul_f32 v[26:27], v[148:149], v[222:223] op_sel_hi:[1,0]
	v_pk_mul_f32 v[28:29], v[146:147], v[222:223] op_sel_hi:[1,0]
	v_pk_mul_f32 v[30:31], v[152:153], v[224:225] op_sel_hi:[1,0]
	v_pk_mul_f32 v[32:33], v[150:151], v[224:225] op_sel_hi:[1,0]
	v_pk_mul_f32 v[34:35], v[156:157], v[226:227] op_sel_hi:[1,0]
	v_pk_mul_f32 v[36:37], v[154:155], v[226:227] op_sel_hi:[1,0]
	v_pk_mul_f32 v[38:39], v[160:161], v[228:229] op_sel_hi:[1,0]
	v_pk_mul_f32 v[40:41], v[158:159], v[228:229] op_sel_hi:[1,0]
	v_pk_mul_f32 v[42:43], v[164:165], v[230:231] op_sel_hi:[1,0]
	v_pk_mul_f32 v[44:45], v[162:163], v[230:231] op_sel_hi:[1,0]
	v_pk_mul_f32 v[46:47], v[168:169], v[232:233] op_sel_hi:[1,0]
	v_pk_mul_f32 v[48:49], v[166:167], v[232:233] op_sel_hi:[1,0]
	s_add_u32 s4, s4, 0x16000
	s_addc_u32 s5, s5, 0
	global_load_dwordx4 v[138:141], v250, s[4:5] nt
	global_load_dword v218, v251, s[6:7] offset:3328
	s_add_u32 s4, s4, 0x16000
	s_addc_u32 s5, s5, 0
	global_load_dwordx4 v[142:145], v250, s[4:5] nt
	global_load_dword v220, v251, s[6:7] offset:3360
	s_add_u32 s4, s4, 0x16000
	s_addc_u32 s5, s5, 0
	global_load_dwordx4 v[146:149], v250, s[4:5] nt
	global_load_dword v222, v251, s[6:7] offset:3392
	s_add_u32 s4, s4, 0x16000
	s_addc_u32 s5, s5, 0
	global_load_dwordx4 v[150:153], v250, s[4:5] nt
	global_load_dword v224, v251, s[6:7] offset:3424
	s_add_u32 s4, s4, 0x16000
	s_addc_u32 s5, s5, 0
	global_load_dwordx4 v[154:157], v250, s[4:5] nt
	global_load_dword v226, v251, s[6:7] offset:3456
	s_add_u32 s4, s4, 0x16000
	s_addc_u32 s5, s5, 0
	global_load_dwordx4 v[158:161], v250, s[4:5] nt
; #define LAS __attribute__((address_space(3)))
; #define GAS __attribute__((address_space(1)))
; #define LDS_WAIT() asm volatile("s_waitcnt lgkmcnt(0)" ::: "memory")
;     ...
;     for (int kb = 0; kb < D / 64; ++kb) {
; #pragma unroll
;         for (int i = 0; i < 8; ++i) { const int kk = 8 * i + kr; const int k = 64 * kb + kk; const f32x4 v = __builtin_nontemporal_load((const f32x4*)(W + (size_t)k * pitch)) * g[k];
;             LAS float* p = scr + kk * 33 + 4 * (lane & 7); p[0] = __builtin_rintf(v[0] * inv[0]); p[1] = __builtin_rintf(v[1] * inv[1]); p[2] = __builtin_rintf(v[2] * inv[2]); p[3] = __builtin_rintf(v[3] * inv[3]); }
;         LDS_WAIT(); asm volatile("" ::: "memory");
;         const int c = lane & 7;
; #pragma unroll
;         for (int j = 0; j < 4; ++j) { const int n = (lane >> 3) + 8 * j; const LAS float* sp = scr + (8 * c) * 33 + n;
;             u32x2 o;
;             o.x = ((unsigned)(int)sp[0 * 33] & 0xFFu) | (((unsigned)(int)sp[1 * 33] & 0xFFu) << 8) | (((unsigned)(int)sp[2 * 33] & 0xFFu) << 16) | (((unsigned)(int)sp[3 * 33] & 0xFFu) << 24);
;             o.y = ((unsigned)(int)sp[4 * 33] & 0xFFu) | (((unsigned)(int)sp[5 * 33] & 0xFFu) << 8) | (((unsigned)(int)sp[6 * 33] & 0xFFu) << 16) | (((unsigned)(int)sp[7 * 33] & 0xFFu) << 24);
;             *(GAS u32x2*)(dst + (size_t)(n0 + n) * D + 64 * kb + 8 * c) = o; }
;         LDS_WAIT(); asm volatile("" ::: "memory");
;     }
	global_load_dword v228, v251, s[6:7] offset:3488
	s_add_u32 s4, s4, 0x16000
	s_addc_u32 s5, s5, 0
	global_load_dwordx4 v[162:165], v250, s[4:5] nt
	global_load_dword v230, v251, s[6:7] offset:3520
	s_add_u32 s4, s4, 0x16000
	s_addc_u32 s5, s5, 0
	global_load_dwordx4 v[166:169], v250, s[4:5] nt
	global_load_dword v232, v251, s[6:7] offset:3552
	v_mul_f32_e32 v14, v20, v14
	v_mul_f32_e32 v15, v21, v15
	v_rndne_f32_e32 v50, v62
	v_rndne_f32_e32 v51, v63
	v_mul_f32_e32 v12, v22, v12
	v_mul_f32_e32 v13, v23, v13
	v_mul_f32_e32 v28, v20, v28
	v_mul_f32_e32 v29, v21, v29
	v_mul_f32_e32 v26, v22, v26
	v_mul_f32_e32 v27, v23, v27
	v_mul_f32_e32 v32, v20, v32
	v_mul_f32_e32 v33, v21, v33
	v_mul_f32_e32 v30, v22, v30
	v_mul_f32_e32 v31, v23, v31
	v_mul_f32_e32 v36, v20, v36
	v_mul_f32_e32 v37, v21, v37
	v_mul_f32_e32 v34, v22, v34
	v_mul_f32_e32 v35, v23, v35
	v_mul_f32_e32 v40, v20, v40
	v_mul_f32_e32 v41, v21, v41
	v_mul_f32_e32 v38, v22, v38
	v_mul_f32_e32 v39, v23, v39
	v_mul_f32_e32 v44, v20, v44
	v_mul_f32_e32 v45, v21, v45
	v_mul_f32_e32 v42, v22, v42
	v_mul_f32_e32 v43, v23, v43
	v_mul_f32_e32 v48, v20, v48
	v_mul_f32_e32 v49, v21, v49
	v_mul_f32_e32 v46, v22, v46
	v_mul_f32_e32 v47, v23, v47
	v_rndne_f32_e32 v14, v14
	v_rndne_f32_e32 v15, v15
	v_rndne_f32_e32 v52, v64
	v_rndne_f32_e32 v53, v65
	ds_write2_b32 v25, v50, v51 offset1:1
	ds_write2_b32 v25, v52, v53 offset0:2 offset1:3
	v_rndne_f32_e32 v12, v12
	v_rndne_f32_e32 v13, v13
	v_rndne_f32_e32 v28, v28
	v_rndne_f32_e32 v29, v29
	v_rndne_f32_e32 v26, v26
	v_rndne_f32_e32 v27, v27
	v_rndne_f32_e32 v32, v32
	v_rndne_f32_e32 v33, v33
	v_rndne_f32_e32 v30, v30
	v_rndne_f32_e32 v31, v31
	v_rndne_f32_e32 v36, v36
	v_rndne_f32_e32 v37, v37
	v_rndne_f32_e32 v34, v34
	v_rndne_f32_e32 v35, v35
	v_rndne_f32_e32 v40, v40
	v_rndne_f32_e32 v41, v41
	v_rndne_f32_e32 v38, v38
	v_rndne_f32_e32 v39, v39
	v_rndne_f32_e32 v44, v44
	v_rndne_f32_e32 v45, v45
	v_rndne_f32_e32 v42, v42
	v_rndne_f32_e32 v43, v43
	v_rndne_f32_e32 v48, v48
	v_rndne_f32_e32 v49, v49
	v_rndne_f32_e32 v46, v46
	v_rndne_f32_e32 v47, v47
	ds_write2_b32 v77, v14, v15 offset1:1
	ds_write2_b32 v79, v12, v13 offset1:1
	ds_write2_b32 v81, v28, v29 offset1:1
	ds_write2_b32 v83, v26, v27 offset1:1
	ds_write2_b32 v85, v32, v33 offset1:1
	ds_write2_b32 v87, v30, v31 offset1:1
	ds_write2_b32 v89, v36, v37 offset1:1
	ds_write2_b32 v91, v34, v35 offset1:1
	ds_write2_b32 v92, v40, v41 offset1:1
	ds_write2_b32 v93, v38, v39 offset1:1
	ds_write2_b32 v94, v44, v45 offset1:1
	ds_write2_b32 v95, v42, v43 offset1:1
	ds_write2_b32 v96, v48, v49 offset1:1
	ds_write2_b32 v97, v46, v47 offset1:1
	s_waitcnt lgkmcnt(0)
	ds_read2_b32 v[12:13], v24 offset1:8
	ds_read2_b32 v[14:15], v24 offset0:33 offset1:41
	ds_read2_b32 v[26:27], v24 offset0:66 offset1:74
	ds_read2_b32 v[28:29], v24 offset0:99 offset1:107
	ds_read2_b32 v[30:31], v24 offset0:132 offset1:140
	ds_read2_b32 v[32:33], v24 offset0:165 offset1:173
	ds_read2_b32 v[34:35], v24 offset0:198 offset1:206
	ds_read2_b32 v[36:37], v24 offset0:231 offset1:239
	ds_read2_b32 v[38:39], v24 offset0:16 offset1:24
	ds_read2_b32 v[40:41], v24 offset0:49 offset1:57
	ds_read2_b32 v[42:43], v24 offset0:82 offset1:90
	ds_read2_b32 v[44:45], v24 offset0:115 offset1:123
	ds_read2_b32 v[46:47], v24 offset0:148 offset1:156
	ds_read2_b32 v[48:49], v24 offset0:181 offset1:189
	ds_read2_b32 v[50:51], v24 offset0:214 offset1:222
	ds_read2_b32 v[52:53], v24 offset0:247 offset1:255
	s_waitcnt lgkmcnt(14)
	v_cvt_i32_f32_e32 v14, v14
	s_waitcnt lgkmcnt(10)
	v_cvt_i32_f32_e32 v32, v32
	v_cvt_i32_f32_e32 v12, v12
	v_cvt_i32_f32_sdwa v26, v26 dst_sel:WORD_1 dst_unused:UNUSED_PAD src0_sel:DWORD
	v_cvt_i32_f32_e32 v30, v30
	s_waitcnt lgkmcnt(9)
	v_cvt_i32_f32_sdwa v34, v34 dst_sel:WORD_1 dst_unused:UNUSED_PAD src0_sel:DWORD
	v_cvt_i32_f32_e32 v15, v15
	v_cvt_i32_f32_e32 v33, v33
	s_waitcnt lgkmcnt(6)
	v_cvt_i32_f32_e32 v40, v40
	s_waitcnt lgkmcnt(2)
	v_cvt_i32_f32_e32 v48, v48
	v_cvt_i32_f32_e32 v41, v41
	v_cvt_i32_f32_e32 v49, v49
	v_cvt_i32_f32_sdwa v28, v28 dst_sel:BYTE_3 dst_unused:UNUSED_PAD src0_sel:DWORD
	v_cvt_i32_f32_sdwa v36, v36 dst_sel:BYTE_3 dst_unused:UNUSED_PAD src0_sel:DWORD
	v_cvt_i32_f32_e32 v13, v13
	v_cvt_i32_f32_sdwa v27, v27 dst_sel:WORD_1 dst_unused:UNUSED_PAD src0_sel:DWORD
	v_cvt_i32_f32_e32 v31, v31
	v_cvt_i32_f32_sdwa v35, v35 dst_sel:WORD_1 dst_unused:UNUSED_PAD src0_sel:DWORD
	v_cvt_i32_f32_e32 v38, v38
	v_cvt_i32_f32_sdwa v42, v42 dst_sel:WORD_1 dst_unused:UNUSED_PAD src0_sel:DWORD
	v_cvt_i32_f32_e32 v46, v46
	s_waitcnt lgkmcnt(1)
	v_cvt_i32_f32_sdwa v50, v50 dst_sel:WORD_1 dst_unused:UNUSED_PAD src0_sel:DWORD
	v_cvt_i32_f32_e32 v39, v39
	v_cvt_i32_f32_sdwa v43, v43 dst_sel:WORD_1 dst_unused:UNUSED_PAD src0_sel:DWORD
	v_cvt_i32_f32_e32 v47, v47
	v_cvt_i32_f32_sdwa v51, v51 dst_sel:WORD_1 dst_unused:UNUSED_PAD src0_sel:DWORD
	v_cvt_i32_f32_sdwa v29, v29 dst_sel:BYTE_3 dst_unused:UNUSED_PAD src0_sel:DWORD
	v_cvt_i32_f32_sdwa v37, v37 dst_sel:BYTE_3 dst_unused:UNUSED_PAD src0_sel:DWORD
	v_cvt_i32_f32_sdwa v44, v44 dst_sel:BYTE_3 dst_unused:UNUSED_PAD src0_sel:DWORD
	s_waitcnt lgkmcnt(0)
; #define LAS __attribute__((address_space(3)))
; #define GAS __attribute__((address_space(1)))
; #define LDS_WAIT() asm volatile("s_waitcnt lgkmcnt(0)" ::: "memory")
;     ...
;     for (int kb = 0; kb < D / 64; ++kb) {
; #pragma unroll
;         for (int i = 0; i < 8; ++i) { const int kk = 8 * i + kr; const int k = 64 * kb + kk; const f32x4 v = __builtin_nontemporal_load((const f32x4*)(W + (size_t)k * pitch)) * g[k];
;             LAS float* p = scr + kk * 33 + 4 * (lane & 7); p[0] = __builtin_rintf(v[0] * inv[0]); p[1] = __builtin_rintf(v[1] * inv[1]); p[2] = __builtin_rintf(v[2] * inv[2]); p[3] = __builtin_rintf(v[3] * inv[3]); }
;         LDS_WAIT(); asm volatile("" ::: "memory");
;         const int c = lane & 7;
; #pragma unroll
;         for (int j = 0; j < 4; ++j) { const int n = (lane >> 3) + 8 * j; const LAS float* sp = scr + (8 * c) * 33 + n;
;             u32x2 o;
;             o.x = ((unsigned)(int)sp[0 * 33] & 0xFFu) | (((unsigned)(int)sp[1 * 33] & 0xFFu) << 8) | (((unsigned)(int)sp[2 * 33] & 0xFFu) << 16) | (((unsigned)(int)sp[3 * 33] & 0xFFu) << 24);
;             o.y = ((unsigned)(int)sp[4 * 33] & 0xFFu) | (((unsigned)(int)sp[5 * 33] & 0xFFu) << 8) | (((unsigned)(int)sp[6 * 33] & 0xFFu) << 16) | (((unsigned)(int)sp[7 * 33] & 0xFFu) << 24);
;             *(GAS u32x2*)(dst + (size_t)(n0 + n) * D + 64 * kb + 8 * c) = o; }
;         LDS_WAIT(); asm volatile("" ::: "memory");
;     }
	v_cvt_i32_f32_sdwa v52, v52 dst_sel:BYTE_3 dst_unused:UNUSED_PAD src0_sel:DWORD
	v_cvt_i32_f32_sdwa v45, v45 dst_sel:BYTE_3 dst_unused:UNUSED_PAD src0_sel:DWORD
	v_cvt_i32_f32_sdwa v53, v53 dst_sel:BYTE_3 dst_unused:UNUSED_PAD src0_sel:DWORD
	v_lshlrev_b32_e32 v14, 8, v14
	v_lshlrev_b32_e32 v32, 8, v32
	v_and_b32_e32 v26, 0xff0000, v26
	v_and_b32_e32 v34, 0xff0000, v34
	v_lshlrev_b32_e32 v15, 8, v15
	v_lshlrev_b32_e32 v33, 8, v33
	v_lshlrev_b32_e32 v40, 8, v40
	v_lshlrev_b32_e32 v48, 8, v48
	v_lshlrev_b32_e32 v41, 8, v41
	v_lshlrev_b32_e32 v49, 8, v49
	v_perm_b32 v12, v14, v12, s28
	v_perm_b32 v14, v32, v30, s28
	v_and_b32_e32 v27, 0xff0000, v27
	v_and_b32_e32 v35, 0xff0000, v35
	v_and_b32_e32 v42, 0xff0000, v42
	v_and_b32_e32 v50, 0xff0000, v50
	v_and_b32_e32 v43, 0xff0000, v43
	v_and_b32_e32 v51, 0xff0000, v51
	v_perm_b32 v15, v15, v13, s28
	v_perm_b32 v30, v33, v31, s28
	v_perm_b32 v31, v40, v38, s28
	v_perm_b32 v32, v48, v46, s28
	v_perm_b32 v33, v41, v39, s28
	v_perm_b32 v38, v49, v47, s28
	v_or3_b32 v12, v12, v26, v28
	v_or3_b32 v13, v14, v34, v36
	v_or3_b32 v14, v15, v27, v29
	v_or3_b32 v15, v30, v35, v37
	v_or3_b32 v26, v31, v42, v44
	v_or3_b32 v27, v32, v50, v52
	v_or3_b32 v28, v33, v43, v45
	v_or3_b32 v29, v38, v51, v53
	global_store_dwordx2 v[16:17], v[12:13], off
	global_store_dwordx2 v[18:19], v[14:15], off
	global_store_dwordx2 v[58:59], v[26:27], off
	global_store_dwordx2 v[60:61], v[28:29], off
	s_waitcnt lgkmcnt(0)
	v_add_u32_e32 v77, 0x420, v25
	v_add_u32_e32 v79, 0x428, v25
	v_add_u32_e32 v81, 0x840, v25
	v_add_u32_e32 v83, 0x848, v25
	v_add_u32_e32 v85, 0xc60, v25
	v_add_u32_e32 v87, 0xc68, v25
	v_add_u32_e32 v89, 0x1080, v25
	v_add_u32_e32 v91, 0x1088, v25
	v_add_u32_e32 v92, 0x14a0, v25
	v_add_u32_e32 v93, 0x14a8, v25
	v_add_u32_e32 v94, 0x18c0, v25
	v_add_u32_e32 v95, 0x18c8, v25
	v_add_u32_e32 v96, 0x1ce0, v25
	v_add_u32_e32 v97, 0x1ce8, v25
	v_lshl_add_u64 v[16:17], v[10:11], 0, s[26:27]
	v_lshl_add_u64 v[18:19], v[8:9], 0, s[26:27]
	v_lshl_add_u64 v[58:59], v[6:7], 0, s[26:27]
	v_lshl_add_u64 v[60:61], v[4:5], 0, s[26:27]
	v_lshl_add_u64 v[4:5], v[4:5], 0, 64
	v_lshl_add_u64 v[6:7], v[6:7], 0, 64
	v_lshl_add_u64 v[8:9], v[8:9], 0, 64
	v_lshl_add_u64 v[10:11], v[10:11], 0, 64
	s_waitcnt vmcnt(44)
	v_pk_mul_f32 v[14:15], v[170:171], v[234:235] op_sel_hi:[1,0]
	v_pk_mul_f32 v[12:13], v[172:173], v[234:235] op_sel_hi:[1,0]
	v_mul_f32_e32 v62, v20, v14
	v_mul_f32_e32 v63, v21, v15
	v_mul_f32_e32 v64, v22, v12
	v_mul_f32_e32 v65, v23, v13
	v_pk_mul_f32 v[14:15], v[174:175], v[236:237] op_sel_hi:[1,0]
	v_pk_mul_f32 v[12:13], v[176:177], v[236:237] op_sel_hi:[1,0]
	v_pk_mul_f32 v[26:27], v[180:181], v[238:239] op_sel_hi:[1,0]
	v_pk_mul_f32 v[28:29], v[178:179], v[238:239] op_sel_hi:[1,0]
	v_pk_mul_f32 v[30:31], v[184:185], v[240:241] op_sel_hi:[1,0]
	v_pk_mul_f32 v[32:33], v[182:183], v[240:241] op_sel_hi:[1,0]
	v_pk_mul_f32 v[34:35], v[188:189], v[242:243] op_sel_hi:[1,0]
	v_pk_mul_f32 v[36:37], v[186:187], v[242:243] op_sel_hi:[1,0]
	v_pk_mul_f32 v[38:39], v[192:193], v[244:245] op_sel_hi:[1,0]
	v_pk_mul_f32 v[40:41], v[190:191], v[244:245] op_sel_hi:[1,0]
	v_pk_mul_f32 v[42:43], v[196:197], v[246:247] op_sel_hi:[1,0]
	v_pk_mul_f32 v[44:45], v[194:195], v[246:247] op_sel_hi:[1,0]
	v_pk_mul_f32 v[46:47], v[200:201], v[248:249] op_sel_hi:[1,0]
	v_pk_mul_f32 v[48:49], v[198:199], v[248:249] op_sel_hi:[1,0]
	s_add_u32 s4, s4, 0x16000
	s_addc_u32 s5, s5, 0
	global_load_dwordx4 v[170:173], v250, s[4:5] nt
	global_load_dword v234, v251, s[6:7] offset:3584
	s_add_u32 s4, s4, 0x16000
	s_addc_u32 s5, s5, 0
	global_load_dwordx4 v[174:177], v250, s[4:5] nt
	global_load_dword v236, v251, s[6:7] offset:3616
	s_add_u32 s4, s4, 0x16000
	s_addc_u32 s5, s5, 0
	global_load_dwordx4 v[178:181], v250, s[4:5] nt
	global_load_dword v238, v251, s[6:7] offset:3648
	s_add_u32 s4, s4, 0x16000
	s_addc_u32 s5, s5, 0
	global_load_dwordx4 v[182:185], v250, s[4:5] nt
	global_load_dword v240, v251, s[6:7] offset:3680
	s_add_u32 s4, s4, 0x16000
	s_addc_u32 s5, s5, 0
	global_load_dwordx4 v[186:189], v250, s[4:5] nt
	global_load_dword v242, v251, s[6:7] offset:3712
	s_add_u32 s4, s4, 0x16000
	s_addc_u32 s5, s5, 0
	global_load_dwordx4 v[190:193], v250, s[4:5] nt
	global_load_dword v244, v251, s[6:7] offset:3744
	s_add_u32 s4, s4, 0x16000
	s_addc_u32 s5, s5, 0
	global_load_dwordx4 v[194:197], v250, s[4:5] nt
	global_load_dword v246, v251, s[6:7] offset:3776
	s_add_u32 s4, s4, 0x16000
	s_addc_u32 s5, s5, 0
	global_load_dwordx4 v[198:201], v250, s[4:5] nt
	global_load_dword v248, v251, s[6:7] offset:3808
	v_mul_f32_e32 v14, v20, v14
	v_mul_f32_e32 v15, v21, v15
	v_rndne_f32_e32 v50, v62
	v_rndne_f32_e32 v51, v63
	v_mul_f32_e32 v12, v22, v12
	v_mul_f32_e32 v13, v23, v13
	v_mul_f32_e32 v28, v20, v28
	v_mul_f32_e32 v29, v21, v29
	v_mul_f32_e32 v26, v22, v26
	v_mul_f32_e32 v27, v23, v27
	v_mul_f32_e32 v32, v20, v32
	v_mul_f32_e32 v33, v21, v33
	v_mul_f32_e32 v30, v22, v30
	v_mul_f32_e32 v31, v23, v31
	v_mul_f32_e32 v36, v20, v36
	v_mul_f32_e32 v37, v21, v37
	v_mul_f32_e32 v34, v22, v34
	v_mul_f32_e32 v35, v23, v35
	v_mul_f32_e32 v40, v20, v40
	v_mul_f32_e32 v41, v21, v41
	v_mul_f32_e32 v38, v22, v38
	v_mul_f32_e32 v39, v23, v39
	v_mul_f32_e32 v44, v20, v44
	v_mul_f32_e32 v45, v21, v45
	v_mul_f32_e32 v42, v22, v42
	v_mul_f32_e32 v43, v23, v43
	v_mul_f32_e32 v48, v20, v48
	v_mul_f32_e32 v49, v21, v49
	v_mul_f32_e32 v46, v22, v46
	v_mul_f32_e32 v47, v23, v47
	v_rndne_f32_e32 v14, v14
	v_rndne_f32_e32 v15, v15
	v_rndne_f32_e32 v52, v64
	v_rndne_f32_e32 v53, v65
	ds_write2_b32 v25, v50, v51 offset1:1
	ds_write2_b32 v25, v52, v53 offset0:2 offset1:3
	v_rndne_f32_e32 v12, v12
	v_rndne_f32_e32 v13, v13
	v_rndne_f32_e32 v28, v28
	v_rndne_f32_e32 v29, v29
	v_rndne_f32_e32 v26, v26
	v_rndne_f32_e32 v27, v27
	v_rndne_f32_e32 v32, v32
	v_rndne_f32_e32 v33, v33
	v_rndne_f32_e32 v30, v30
	v_rndne_f32_e32 v31, v31
	v_rndne_f32_e32 v36, v36
	v_rndne_f32_e32 v37, v37
	v_rndne_f32_e32 v34, v34
	v_rndne_f32_e32 v35, v35
	v_rndne_f32_e32 v40, v40
	v_rndne_f32_e32 v41, v41
	v_rndne_f32_e32 v38, v38
	v_rndne_f32_e32 v39, v39
	v_rndne_f32_e32 v44, v44
	v_rndne_f32_e32 v45, v45
	v_rndne_f32_e32 v42, v42
	v_rndne_f32_e32 v43, v43
	v_rndne_f32_e32 v48, v48
	v_rndne_f32_e32 v49, v49
	v_rndne_f32_e32 v46, v46
	v_rndne_f32_e32 v47, v47
	ds_write2_b32 v77, v14, v15 offset1:1
	ds_write2_b32 v79, v12, v13 offset1:1
	ds_write2_b32 v81, v28, v29 offset1:1
	ds_write2_b32 v83, v26, v27 offset1:1
	ds_write2_b32 v85, v32, v33 offset1:1
	ds_write2_b32 v87, v30, v31 offset1:1
	ds_write2_b32 v89, v36, v37 offset1:1
	ds_write2_b32 v91, v34, v35 offset1:1
	ds_write2_b32 v92, v40, v41 offset1:1
	ds_write2_b32 v93, v38, v39 offset1:1
	ds_write2_b32 v94, v44, v45 offset1:1
	ds_write2_b32 v95, v42, v43 offset1:1
	ds_write2_b32 v96, v48, v49 offset1:1
	ds_write2_b32 v97, v46, v47 offset1:1
	s_waitcnt lgkmcnt(0)
; #define LAS __attribute__((address_space(3)))
; #define GAS __attribute__((address_space(1)))
; #define LDS_WAIT() asm volatile("s_waitcnt lgkmcnt(0)" ::: "memory")
;     ...
;         LDS_WAIT(); asm volatile("" ::: "memory");
;         const int c = lane & 7;
; #pragma unroll
;         for (int j = 0; j < 4; ++j) { const int n = (lane >> 3) + 8 * j; const LAS float* sp = scr + (8 * c) * 33 + n;
;             u32x2 o;
;             o.x = ((unsigned)(int)sp[0 * 33] & 0xFFu) | (((unsigned)(int)sp[1 * 33] & 0xFFu) << 8) | (((unsigned)(int)sp[2 * 33] & 0xFFu) << 16) | (((unsigned)(int)sp[3 * 33] & 0xFFu) << 24);
;             o.y = ((unsigned)(int)sp[4 * 33] & 0xFFu) | (((unsigned)(int)sp[5 * 33] & 0xFFu) << 8) | (((unsigned)(int)sp[6 * 33] & 0xFFu) << 16) | (((unsigned)(int)sp[7 * 33] & 0xFFu) << 24);
;             *(GAS u32x2*)(dst + (size_t)(n0 + n) * D + 64 * kb + 8 * c) = o; }
;         LDS_WAIT(); asm volatile("" ::: "memory");
	ds_read2_b32 v[12:13], v24 offset1:8
	ds_read2_b32 v[14:15], v24 offset0:33 offset1:41
	ds_read2_b32 v[26:27], v24 offset0:66 offset1:74
	ds_read2_b32 v[28:29], v24 offset0:99 offset1:107
	ds_read2_b32 v[30:31], v24 offset0:132 offset1:140
	ds_read2_b32 v[32:33], v24 offset0:165 offset1:173
	ds_read2_b32 v[34:35], v24 offset0:198 offset1:206
	ds_read2_b32 v[36:37], v24 offset0:231 offset1:239
	ds_read2_b32 v[38:39], v24 offset0:16 offset1:24
	ds_read2_b32 v[40:41], v24 offset0:49 offset1:57
	ds_read2_b32 v[42:43], v24 offset0:82 offset1:90
	ds_read2_b32 v[44:45], v24 offset0:115 offset1:123
	ds_read2_b32 v[46:47], v24 offset0:148 offset1:156
	ds_read2_b32 v[48:49], v24 offset0:181 offset1:189
	ds_read2_b32 v[50:51], v24 offset0:214 offset1:222
	ds_read2_b32 v[52:53], v24 offset0:247 offset1:255
	s_waitcnt lgkmcnt(14)
	v_cvt_i32_f32_e32 v14, v14
	s_waitcnt lgkmcnt(10)
	v_cvt_i32_f32_e32 v32, v32
	v_cvt_i32_f32_e32 v12, v12
	v_cvt_i32_f32_sdwa v26, v26 dst_sel:WORD_1 dst_unused:UNUSED_PAD src0_sel:DWORD
	v_cvt_i32_f32_e32 v30, v30
	s_waitcnt lgkmcnt(9)
	v_cvt_i32_f32_sdwa v34, v34 dst_sel:WORD_1 dst_unused:UNUSED_PAD src0_sel:DWORD
	v_cvt_i32_f32_e32 v15, v15
	v_cvt_i32_f32_e32 v33, v33
	s_waitcnt lgkmcnt(6)
	v_cvt_i32_f32_e32 v40, v40
	s_waitcnt lgkmcnt(2)
	v_cvt_i32_f32_e32 v48, v48
	v_cvt_i32_f32_e32 v41, v41
	v_cvt_i32_f32_e32 v49, v49
	v_cvt_i32_f32_sdwa v28, v28 dst_sel:BYTE_3 dst_unused:UNUSED_PAD src0_sel:DWORD
	v_cvt_i32_f32_sdwa v36, v36 dst_sel:BYTE_3 dst_unused:UNUSED_PAD src0_sel:DWORD
	v_cvt_i32_f32_e32 v13, v13
	v_cvt_i32_f32_sdwa v27, v27 dst_sel:WORD_1 dst_unused:UNUSED_PAD src0_sel:DWORD
	v_cvt_i32_f32_e32 v31, v31
	v_cvt_i32_f32_sdwa v35, v35 dst_sel:WORD_1 dst_unused:UNUSED_PAD src0_sel:DWORD
	v_cvt_i32_f32_e32 v38, v38
	v_cvt_i32_f32_sdwa v42, v42 dst_sel:WORD_1 dst_unused:UNUSED_PAD src0_sel:DWORD
	v_cvt_i32_f32_e32 v46, v46
	s_waitcnt lgkmcnt(1)
	v_cvt_i32_f32_sdwa v50, v50 dst_sel:WORD_1 dst_unused:UNUSED_PAD src0_sel:DWORD
	v_cvt_i32_f32_e32 v39, v39
	v_cvt_i32_f32_sdwa v43, v43 dst_sel:WORD_1 dst_unused:UNUSED_PAD src0_sel:DWORD
	v_cvt_i32_f32_e32 v47, v47
	v_cvt_i32_f32_sdwa v51, v51 dst_sel:WORD_1 dst_unused:UNUSED_PAD src0_sel:DWORD
	v_cvt_i32_f32_sdwa v29, v29 dst_sel:BYTE_3 dst_unused:UNUSED_PAD src0_sel:DWORD
	v_cvt_i32_f32_sdwa v37, v37 dst_sel:BYTE_3 dst_unused:UNUSED_PAD src0_sel:DWORD
	v_cvt_i32_f32_sdwa v44, v44 dst_sel:BYTE_3 dst_unused:UNUSED_PAD src0_sel:DWORD
	s_waitcnt lgkmcnt(0)
	v_cvt_i32_f32_sdwa v52, v52 dst_sel:BYTE_3 dst_unused:UNUSED_PAD src0_sel:DWORD
	v_cvt_i32_f32_sdwa v45, v45 dst_sel:BYTE_3 dst_unused:UNUSED_PAD src0_sel:DWORD
	v_cvt_i32_f32_sdwa v53, v53 dst_sel:BYTE_3 dst_unused:UNUSED_PAD src0_sel:DWORD
	v_lshlrev_b32_e32 v14, 8, v14
	v_lshlrev_b32_e32 v32, 8, v32
	v_and_b32_e32 v26, 0xff0000, v26
	v_and_b32_e32 v34, 0xff0000, v34
	v_lshlrev_b32_e32 v15, 8, v15
	v_lshlrev_b32_e32 v33, 8, v33
	v_lshlrev_b32_e32 v40, 8, v40
	v_lshlrev_b32_e32 v48, 8, v48
	v_lshlrev_b32_e32 v41, 8, v41
	v_lshlrev_b32_e32 v49, 8, v49
	v_perm_b32 v12, v14, v12, s28
	v_perm_b32 v14, v32, v30, s28
	v_and_b32_e32 v27, 0xff0000, v27
	v_and_b32_e32 v35, 0xff0000, v35
	v_and_b32_e32 v42, 0xff0000, v42
	v_and_b32_e32 v50, 0xff0000, v50
	v_and_b32_e32 v43, 0xff0000, v43
	v_and_b32_e32 v51, 0xff0000, v51
	v_perm_b32 v15, v15, v13, s28
	v_perm_b32 v30, v33, v31, s28
	v_perm_b32 v31, v40, v38, s28
	v_perm_b32 v32, v48, v46, s28
	v_perm_b32 v33, v41, v39, s28
	v_perm_b32 v38, v49, v47, s28
	v_or3_b32 v12, v12, v26, v28
	v_or3_b32 v13, v14, v34, v36
	v_or3_b32 v14, v15, v27, v29
	v_or3_b32 v15, v30, v35, v37
	v_or3_b32 v26, v31, v42, v44
	v_or3_b32 v27, v32, v50, v52
	v_or3_b32 v28, v33, v43, v45
	v_or3_b32 v29, v38, v51, v53
	global_store_dwordx2 v[16:17], v[12:13], off
	global_store_dwordx2 v[18:19], v[14:15], off
	global_store_dwordx2 v[58:59], v[26:27], off
	global_store_dwordx2 v[60:61], v[28:29], off
	s_waitcnt lgkmcnt(0)
	v_add_u32_e32 v77, 0x420, v25
	v_add_u32_e32 v79, 0x428, v25
	v_add_u32_e32 v81, 0x840, v25
	v_add_u32_e32 v83, 0x848, v25
	v_add_u32_e32 v85, 0xc60, v25
	v_add_u32_e32 v87, 0xc68, v25
	v_add_u32_e32 v89, 0x1080, v25
	v_add_u32_e32 v91, 0x1088, v25
	v_add_u32_e32 v92, 0x14a0, v25
	v_add_u32_e32 v93, 0x14a8, v25
	v_add_u32_e32 v94, 0x18c0, v25
	v_add_u32_e32 v95, 0x18c8, v25
	v_add_u32_e32 v96, 0x1ce0, v25
	v_add_u32_e32 v97, 0x1ce8, v25
	v_lshl_add_u64 v[16:17], v[10:11], 0, s[26:27]
	v_lshl_add_u64 v[18:19], v[8:9], 0, s[26:27]
	v_lshl_add_u64 v[58:59], v[6:7], 0, s[26:27]
	v_lshl_add_u64 v[60:61], v[4:5], 0, s[26:27]
	v_lshl_add_u64 v[4:5], v[4:5], 0, 64
	v_lshl_add_u64 v[6:7], v[6:7], 0, 64
	v_lshl_add_u64 v[8:9], v[8:9], 0, 64
	v_lshl_add_u64 v[10:11], v[10:11], 0, 64
	s_waitcnt vmcnt(44)
; #define LAS __attribute__((address_space(3)))
; #define GAS __attribute__((address_space(1)))
; #define LDS_WAIT() asm volatile("s_waitcnt lgkmcnt(0)" ::: "memory")
;     ...
;     for (int kb = 0; kb < D / 64; ++kb) {
; #pragma unroll
;         for (int i = 0; i < 8; ++i) { const int kk = 8 * i + kr; const int k = 64 * kb + kk; const f32x4 v = __builtin_nontemporal_load((const f32x4*)(W + (size_t)k * pitch)) * g[k];
;             LAS float* p = scr + kk * 33 + 4 * (lane & 7); p[0] = __builtin_rintf(v[0] * inv[0]); p[1] = __builtin_rintf(v[1] * inv[1]); p[2] = __builtin_rintf(v[2] * inv[2]); p[3] = __builtin_rintf(v[3] * inv[3]); }
;         LDS_WAIT(); asm volatile("" ::: "memory");
;         const int c = lane & 7;
; #pragma unroll
;         for (int j = 0; j < 4; ++j) { const int n = (lane >> 3) + 8 * j; const LAS float* sp = scr + (8 * c) * 33 + n;
;             u32x2 o;
;             o.x = ((unsigned)(int)sp[0 * 33] & 0xFFu) | (((unsigned)(int)sp[1 * 33] & 0xFFu) << 8) | (((unsigned)(int)sp[2 * 33] & 0xFFu) << 16) | (((unsigned)(int)sp[3 * 33] & 0xFFu) << 24);
;             o.y = ((unsigned)(int)sp[4 * 33] & 0xFFu) | (((unsigned)(int)sp[5 * 33] & 0xFFu) << 8) | (((unsigned)(int)sp[6 * 33] & 0xFFu) << 16) | (((unsigned)(int)sp[7 * 33] & 0xFFu) << 24);
;             *(GAS u32x2*)(dst + (size_t)(n0 + n) * D + 64 * kb + 8 * c) = o; }
;         LDS_WAIT(); asm volatile("" ::: "memory");
;     }
	v_pk_mul_f32 v[14:15], v[106:107], v[202:203] op_sel_hi:[1,0]
	v_pk_mul_f32 v[12:13], v[108:109], v[202:203] op_sel_hi:[1,0]
	v_mul_f32_e32 v62, v20, v14
	v_mul_f32_e32 v63, v21, v15
	v_mul_f32_e32 v64, v22, v12
	v_mul_f32_e32 v65, v23, v13
	v_pk_mul_f32 v[14:15], v[110:111], v[204:205] op_sel_hi:[1,0]
	v_pk_mul_f32 v[12:13], v[112:113], v[204:205] op_sel_hi:[1,0]
	v_pk_mul_f32 v[26:27], v[116:117], v[206:207] op_sel_hi:[1,0]
	v_pk_mul_f32 v[28:29], v[114:115], v[206:207] op_sel_hi:[1,0]
	v_pk_mul_f32 v[30:31], v[120:121], v[208:209] op_sel_hi:[1,0]
	v_pk_mul_f32 v[32:33], v[118:119], v[208:209] op_sel_hi:[1,0]
	v_pk_mul_f32 v[34:35], v[124:125], v[210:211] op_sel_hi:[1,0]
	v_pk_mul_f32 v[36:37], v[122:123], v[210:211] op_sel_hi:[1,0]
	v_pk_mul_f32 v[38:39], v[128:129], v[212:213] op_sel_hi:[1,0]
	v_pk_mul_f32 v[40:41], v[126:127], v[212:213] op_sel_hi:[1,0]
	v_pk_mul_f32 v[42:43], v[132:133], v[214:215] op_sel_hi:[1,0]
	v_pk_mul_f32 v[44:45], v[130:131], v[214:215] op_sel_hi:[1,0]
	v_pk_mul_f32 v[46:47], v[136:137], v[216:217] op_sel_hi:[1,0]
	v_pk_mul_f32 v[48:49], v[134:135], v[216:217] op_sel_hi:[1,0]
	s_add_u32 s4, s4, 0x16000
	s_addc_u32 s5, s5, 0
	global_load_dwordx4 v[106:109], v250, s[4:5] nt
	global_load_dword v202, v251, s[6:7] offset:3840
	s_add_u32 s4, s4, 0x16000
	s_addc_u32 s5, s5, 0
	global_load_dwordx4 v[110:113], v250, s[4:5] nt
	global_load_dword v204, v251, s[6:7] offset:3872
	s_add_u32 s4, s4, 0x16000
	s_addc_u32 s5, s5, 0
	global_load_dwordx4 v[114:117], v250, s[4:5] nt
	global_load_dword v206, v251, s[6:7] offset:3904
	s_add_u32 s4, s4, 0x16000
	s_addc_u32 s5, s5, 0
	global_load_dwordx4 v[118:121], v250, s[4:5] nt
	global_load_dword v208, v251, s[6:7] offset:3936
	s_add_u32 s4, s4, 0x16000
	s_addc_u32 s5, s5, 0
	global_load_dwordx4 v[122:125], v250, s[4:5] nt
	global_load_dword v210, v251, s[6:7] offset:3968
	s_add_u32 s4, s4, 0x16000
	s_addc_u32 s5, s5, 0
	global_load_dwordx4 v[126:129], v250, s[4:5] nt
	global_load_dword v212, v251, s[6:7] offset:4000
	s_add_u32 s4, s4, 0x16000
	s_addc_u32 s5, s5, 0
	global_load_dwordx4 v[130:133], v250, s[4:5] nt
	global_load_dword v214, v251, s[6:7] offset:4032
	s_add_u32 s4, s4, 0x16000
	s_addc_u32 s5, s5, 0
	global_load_dwordx4 v[134:137], v250, s[4:5] nt
	global_load_dword v216, v251, s[6:7] offset:4064
	v_mul_f32_e32 v14, v20, v14
	v_mul_f32_e32 v15, v21, v15
	v_rndne_f32_e32 v50, v62
	v_rndne_f32_e32 v51, v63
	v_mul_f32_e32 v12, v22, v12
	v_mul_f32_e32 v13, v23, v13
	v_mul_f32_e32 v28, v20, v28
	v_mul_f32_e32 v29, v21, v29
	v_mul_f32_e32 v26, v22, v26
	v_mul_f32_e32 v27, v23, v27
	v_mul_f32_e32 v32, v20, v32
	v_mul_f32_e32 v33, v21, v33
	v_mul_f32_e32 v30, v22, v30
	v_mul_f32_e32 v31, v23, v31
	v_mul_f32_e32 v36, v20, v36
	v_mul_f32_e32 v37, v21, v37
	v_mul_f32_e32 v34, v22, v34
	v_mul_f32_e32 v35, v23, v35
	v_mul_f32_e32 v40, v20, v40
	v_mul_f32_e32 v41, v21, v41
	v_mul_f32_e32 v38, v22, v38
	v_mul_f32_e32 v39, v23, v39
	v_mul_f32_e32 v44, v20, v44
	v_mul_f32_e32 v45, v21, v45
	v_mul_f32_e32 v42, v22, v42
	v_mul_f32_e32 v43, v23, v43
	v_mul_f32_e32 v48, v20, v48
	v_mul_f32_e32 v49, v21, v49
	v_mul_f32_e32 v46, v22, v46
	v_mul_f32_e32 v47, v23, v47
	v_rndne_f32_e32 v14, v14
	v_rndne_f32_e32 v15, v15
	v_rndne_f32_e32 v52, v64
	v_rndne_f32_e32 v53, v65
	ds_write2_b32 v25, v50, v51 offset1:1
	ds_write2_b32 v25, v52, v53 offset0:2 offset1:3
	v_rndne_f32_e32 v12, v12
	v_rndne_f32_e32 v13, v13
	v_rndne_f32_e32 v28, v28
	v_rndne_f32_e32 v29, v29
	v_rndne_f32_e32 v26, v26
	v_rndne_f32_e32 v27, v27
	v_rndne_f32_e32 v32, v32
	v_rndne_f32_e32 v33, v33
	v_rndne_f32_e32 v30, v30
	v_rndne_f32_e32 v31, v31
	v_rndne_f32_e32 v36, v36
	v_rndne_f32_e32 v37, v37
	v_rndne_f32_e32 v34, v34
	v_rndne_f32_e32 v35, v35
	v_rndne_f32_e32 v40, v40
	v_rndne_f32_e32 v41, v41
	v_rndne_f32_e32 v38, v38
	v_rndne_f32_e32 v39, v39
	v_rndne_f32_e32 v44, v44
	v_rndne_f32_e32 v45, v45
	v_rndne_f32_e32 v42, v42
	v_rndne_f32_e32 v43, v43
	v_rndne_f32_e32 v48, v48
	v_rndne_f32_e32 v49, v49
	v_rndne_f32_e32 v46, v46
	v_rndne_f32_e32 v47, v47
	ds_write2_b32 v77, v14, v15 offset1:1
	ds_write2_b32 v79, v12, v13 offset1:1
	ds_write2_b32 v81, v28, v29 offset1:1
	ds_write2_b32 v83, v26, v27 offset1:1
	ds_write2_b32 v85, v32, v33 offset1:1
	ds_write2_b32 v87, v30, v31 offset1:1
	ds_write2_b32 v89, v36, v37 offset1:1
	ds_write2_b32 v91, v34, v35 offset1:1
	ds_write2_b32 v92, v40, v41 offset1:1
	ds_write2_b32 v93, v38, v39 offset1:1
	ds_write2_b32 v94, v44, v45 offset1:1
	ds_write2_b32 v95, v42, v43 offset1:1
	ds_write2_b32 v96, v48, v49 offset1:1
	ds_write2_b32 v97, v46, v47 offset1:1
	s_waitcnt lgkmcnt(0)
	ds_read2_b32 v[12:13], v24 offset1:8
	ds_read2_b32 v[14:15], v24 offset0:33 offset1:41
	ds_read2_b32 v[26:27], v24 offset0:66 offset1:74
	ds_read2_b32 v[28:29], v24 offset0:99 offset1:107
	ds_read2_b32 v[30:31], v24 offset0:132 offset1:140
	ds_read2_b32 v[32:33], v24 offset0:165 offset1:173
	ds_read2_b32 v[34:35], v24 offset0:198 offset1:206
	ds_read2_b32 v[36:37], v24 offset0:231 offset1:239
	ds_read2_b32 v[38:39], v24 offset0:16 offset1:24
	ds_read2_b32 v[40:41], v24 offset0:49 offset1:57
	ds_read2_b32 v[42:43], v24 offset0:82 offset1:90
	ds_read2_b32 v[44:45], v24 offset0:115 offset1:123
	ds_read2_b32 v[46:47], v24 offset0:148 offset1:156
	ds_read2_b32 v[48:49], v24 offset0:181 offset1:189
	ds_read2_b32 v[50:51], v24 offset0:214 offset1:222
	ds_read2_b32 v[52:53], v24 offset0:247 offset1:255
	s_waitcnt lgkmcnt(14)
	v_cvt_i32_f32_e32 v14, v14
	s_waitcnt lgkmcnt(10)
	v_cvt_i32_f32_e32 v32, v32
	v_cvt_i32_f32_e32 v12, v12
	v_cvt_i32_f32_sdwa v26, v26 dst_sel:WORD_1 dst_unused:UNUSED_PAD src0_sel:DWORD
	v_cvt_i32_f32_e32 v30, v30
	s_waitcnt lgkmcnt(9)
; #define LAS __attribute__((address_space(3)))
; #define GAS __attribute__((address_space(1)))
; #define LDS_WAIT() asm volatile("s_waitcnt lgkmcnt(0)" ::: "memory")
;     ...
;     for (int kb = 0; kb < D / 64; ++kb) {
; #pragma unroll
;         for (int i = 0; i < 8; ++i) { const int kk = 8 * i + kr; const int k = 64 * kb + kk; const f32x4 v = __builtin_nontemporal_load((const f32x4*)(W + (size_t)k * pitch)) * g[k];
;             LAS float* p = scr + kk * 33 + 4 * (lane & 7); p[0] = __builtin_rintf(v[0] * inv[0]); p[1] = __builtin_rintf(v[1] * inv[1]); p[2] = __builtin_rintf(v[2] * inv[2]); p[3] = __builtin_rintf(v[3] * inv[3]); }
;         LDS_WAIT(); asm volatile("" ::: "memory");
;         const int c = lane & 7;
; #pragma unroll
;         for (int j = 0; j < 4; ++j) { const int n = (lane >> 3) + 8 * j; const LAS float* sp = scr + (8 * c) * 33 + n;
;             u32x2 o;
;             o.x = ((unsigned)(int)sp[0 * 33] & 0xFFu) | (((unsigned)(int)sp[1 * 33] & 0xFFu) << 8) | (((unsigned)(int)sp[2 * 33] & 0xFFu) << 16) | (((unsigned)(int)sp[3 * 33] & 0xFFu) << 24);
;             o.y = ((unsigned)(int)sp[4 * 33] & 0xFFu) | (((unsigned)(int)sp[5 * 33] & 0xFFu) << 8) | (((unsigned)(int)sp[6 * 33] & 0xFFu) << 16) | (((unsigned)(int)sp[7 * 33] & 0xFFu) << 24);
;             *(GAS u32x2*)(dst + (size_t)(n0 + n) * D + 64 * kb + 8 * c) = o; }
;         LDS_WAIT(); asm volatile("" ::: "memory");
;     }
	v_cvt_i32_f32_sdwa v34, v34 dst_sel:WORD_1 dst_unused:UNUSED_PAD src0_sel:DWORD
	v_cvt_i32_f32_e32 v15, v15
	v_cvt_i32_f32_e32 v33, v33
	s_waitcnt lgkmcnt(6)
	v_cvt_i32_f32_e32 v40, v40
	s_waitcnt lgkmcnt(2)
	v_cvt_i32_f32_e32 v48, v48
	v_cvt_i32_f32_e32 v41, v41
	v_cvt_i32_f32_e32 v49, v49
	v_cvt_i32_f32_sdwa v28, v28 dst_sel:BYTE_3 dst_unused:UNUSED_PAD src0_sel:DWORD
	v_cvt_i32_f32_sdwa v36, v36 dst_sel:BYTE_3 dst_unused:UNUSED_PAD src0_sel:DWORD
	v_cvt_i32_f32_e32 v13, v13
	v_cvt_i32_f32_sdwa v27, v27 dst_sel:WORD_1 dst_unused:UNUSED_PAD src0_sel:DWORD
	v_cvt_i32_f32_e32 v31, v31
	v_cvt_i32_f32_sdwa v35, v35 dst_sel:WORD_1 dst_unused:UNUSED_PAD src0_sel:DWORD
	v_cvt_i32_f32_e32 v38, v38
	v_cvt_i32_f32_sdwa v42, v42 dst_sel:WORD_1 dst_unused:UNUSED_PAD src0_sel:DWORD
	v_cvt_i32_f32_e32 v46, v46
	s_waitcnt lgkmcnt(1)
	v_cvt_i32_f32_sdwa v50, v50 dst_sel:WORD_1 dst_unused:UNUSED_PAD src0_sel:DWORD
	v_cvt_i32_f32_e32 v39, v39
	v_cvt_i32_f32_sdwa v43, v43 dst_sel:WORD_1 dst_unused:UNUSED_PAD src0_sel:DWORD
	v_cvt_i32_f32_e32 v47, v47
	v_cvt_i32_f32_sdwa v51, v51 dst_sel:WORD_1 dst_unused:UNUSED_PAD src0_sel:DWORD
	v_cvt_i32_f32_sdwa v29, v29 dst_sel:BYTE_3 dst_unused:UNUSED_PAD src0_sel:DWORD
	v_cvt_i32_f32_sdwa v37, v37 dst_sel:BYTE_3 dst_unused:UNUSED_PAD src0_sel:DWORD
	v_cvt_i32_f32_sdwa v44, v44 dst_sel:BYTE_3 dst_unused:UNUSED_PAD src0_sel:DWORD
	s_waitcnt lgkmcnt(0)
	v_cvt_i32_f32_sdwa v52, v52 dst_sel:BYTE_3 dst_unused:UNUSED_PAD src0_sel:DWORD
	v_cvt_i32_f32_sdwa v45, v45 dst_sel:BYTE_3 dst_unused:UNUSED_PAD src0_sel:DWORD
	v_cvt_i32_f32_sdwa v53, v53 dst_sel:BYTE_3 dst_unused:UNUSED_PAD src0_sel:DWORD
	v_lshlrev_b32_e32 v14, 8, v14
	v_lshlrev_b32_e32 v32, 8, v32
	v_and_b32_e32 v26, 0xff0000, v26
	v_and_b32_e32 v34, 0xff0000, v34
	v_lshlrev_b32_e32 v15, 8, v15
	v_lshlrev_b32_e32 v33, 8, v33
	v_lshlrev_b32_e32 v40, 8, v40
	v_lshlrev_b32_e32 v48, 8, v48
	v_lshlrev_b32_e32 v41, 8, v41
	v_lshlrev_b32_e32 v49, 8, v49
	v_perm_b32 v12, v14, v12, s28
	v_perm_b32 v14, v32, v30, s28
	v_and_b32_e32 v27, 0xff0000, v27
	v_and_b32_e32 v35, 0xff0000, v35
	v_and_b32_e32 v42, 0xff0000, v42
	v_and_b32_e32 v50, 0xff0000, v50
	v_and_b32_e32 v43, 0xff0000, v43
	v_and_b32_e32 v51, 0xff0000, v51
	v_perm_b32 v15, v15, v13, s28
	v_perm_b32 v30, v33, v31, s28
	v_perm_b32 v31, v40, v38, s28
	v_perm_b32 v32, v48, v46, s28
	v_perm_b32 v33, v41, v39, s28
	v_perm_b32 v38, v49, v47, s28
	v_or3_b32 v12, v12, v26, v28
	v_or3_b32 v13, v14, v34, v36
	v_or3_b32 v14, v15, v27, v29
	v_or3_b32 v15, v30, v35, v37
	v_or3_b32 v26, v31, v42, v44
	v_or3_b32 v27, v32, v50, v52
	v_or3_b32 v28, v33, v43, v45
	v_or3_b32 v29, v38, v51, v53
	global_store_dwordx2 v[16:17], v[12:13], off
	global_store_dwordx2 v[18:19], v[14:15], off
	global_store_dwordx2 v[58:59], v[26:27], off
	global_store_dwordx2 v[60:61], v[28:29], off
	s_waitcnt lgkmcnt(0)
	v_add_u32_e32 v77, 0x420, v25
	v_add_u32_e32 v79, 0x428, v25
	v_add_u32_e32 v81, 0x840, v25
	v_add_u32_e32 v83, 0x848, v25
	v_add_u32_e32 v85, 0xc60, v25
	v_add_u32_e32 v87, 0xc68, v25
	v_add_u32_e32 v89, 0x1080, v25
	v_add_u32_e32 v91, 0x1088, v25
	v_add_u32_e32 v92, 0x14a0, v25
	v_add_u32_e32 v93, 0x14a8, v25
	v_add_u32_e32 v94, 0x18c0, v25
	v_add_u32_e32 v95, 0x18c8, v25
	v_add_u32_e32 v96, 0x1ce0, v25
	v_add_u32_e32 v97, 0x1ce8, v25
	v_lshl_add_u64 v[16:17], v[10:11], 0, s[26:27]
	v_lshl_add_u64 v[18:19], v[8:9], 0, s[26:27]
	v_lshl_add_u64 v[58:59], v[6:7], 0, s[26:27]
	v_lshl_add_u64 v[60:61], v[4:5], 0, s[26:27]
	v_lshl_add_u64 v[4:5], v[4:5], 0, 64
	v_lshl_add_u64 v[6:7], v[6:7], 0, 64
	v_lshl_add_u64 v[8:9], v[8:9], 0, 64
	v_lshl_add_u64 v[10:11], v[10:11], 0, 64
	s_waitcnt vmcnt(44)
	v_pk_mul_f32 v[14:15], v[138:139], v[218:219] op_sel_hi:[1,0]
	v_pk_mul_f32 v[12:13], v[140:141], v[218:219] op_sel_hi:[1,0]
	v_mul_f32_e32 v62, v20, v14
	v_mul_f32_e32 v63, v21, v15
	v_mul_f32_e32 v64, v22, v12
	v_mul_f32_e32 v65, v23, v13
	v_pk_mul_f32 v[14:15], v[142:143], v[220:221] op_sel_hi:[1,0]
	v_pk_mul_f32 v[12:13], v[144:145], v[220:221] op_sel_hi:[1,0]
	v_pk_mul_f32 v[26:27], v[148:149], v[222:223] op_sel_hi:[1,0]
	v_pk_mul_f32 v[28:29], v[146:147], v[222:223] op_sel_hi:[1,0]
	v_pk_mul_f32 v[30:31], v[152:153], v[224:225] op_sel_hi:[1,0]
	v_pk_mul_f32 v[32:33], v[150:151], v[224:225] op_sel_hi:[1,0]
	v_pk_mul_f32 v[34:35], v[156:157], v[226:227] op_sel_hi:[1,0]
	v_pk_mul_f32 v[36:37], v[154:155], v[226:227] op_sel_hi:[1,0]
	v_pk_mul_f32 v[38:39], v[160:161], v[228:229] op_sel_hi:[1,0]
	v_pk_mul_f32 v[40:41], v[158:159], v[228:229] op_sel_hi:[1,0]
	v_pk_mul_f32 v[42:43], v[164:165], v[230:231] op_sel_hi:[1,0]
	v_pk_mul_f32 v[44:45], v[162:163], v[230:231] op_sel_hi:[1,0]
	v_pk_mul_f32 v[46:47], v[168:169], v[232:233] op_sel_hi:[1,0]
	v_pk_mul_f32 v[48:49], v[166:167], v[232:233] op_sel_hi:[1,0]
	v_mul_f32_e32 v14, v20, v14
	v_mul_f32_e32 v15, v21, v15
	v_rndne_f32_e32 v50, v62
	v_rndne_f32_e32 v51, v63
	v_mul_f32_e32 v12, v22, v12
	v_mul_f32_e32 v13, v23, v13
	v_mul_f32_e32 v28, v20, v28
	v_mul_f32_e32 v29, v21, v29
	v_mul_f32_e32 v26, v22, v26
	v_mul_f32_e32 v27, v23, v27
	v_mul_f32_e32 v32, v20, v32
	v_mul_f32_e32 v33, v21, v33
	v_mul_f32_e32 v30, v22, v30
	v_mul_f32_e32 v31, v23, v31
	v_mul_f32_e32 v36, v20, v36
	v_mul_f32_e32 v37, v21, v37
	v_mul_f32_e32 v34, v22, v34
	v_mul_f32_e32 v35, v23, v35
	v_mul_f32_e32 v40, v20, v40
	v_mul_f32_e32 v41, v21, v41
	v_mul_f32_e32 v38, v22, v38
	v_mul_f32_e32 v39, v23, v39
	v_mul_f32_e32 v44, v20, v44
	v_mul_f32_e32 v45, v21, v45
	v_mul_f32_e32 v42, v22, v42
	v_mul_f32_e32 v43, v23, v43
	v_mul_f32_e32 v48, v20, v48
	v_mul_f32_e32 v49, v21, v49
	v_mul_f32_e32 v46, v22, v46
	v_mul_f32_e32 v47, v23, v47
; #define LAS __attribute__((address_space(3)))
; #define GAS __attribute__((address_space(1)))
; #define LDS_WAIT() asm volatile("s_waitcnt lgkmcnt(0)" ::: "memory")
;     ...
;     for (int kb = 0; kb < D / 64; ++kb) {
; #pragma unroll
;         for (int i = 0; i < 8; ++i) { const int kk = 8 * i + kr; const int k = 64 * kb + kk; const f32x4 v = __builtin_nontemporal_load((const f32x4*)(W + (size_t)k * pitch)) * g[k];
;             LAS float* p = scr + kk * 33 + 4 * (lane & 7); p[0] = __builtin_rintf(v[0] * inv[0]); p[1] = __builtin_rintf(v[1] * inv[1]); p[2] = __builtin_rintf(v[2] * inv[2]); p[3] = __builtin_rintf(v[3] * inv[3]); }
;         LDS_WAIT(); asm volatile("" ::: "memory");
;         const int c = lane & 7;
; #pragma unroll
;         for (int j = 0; j < 4; ++j) { const int n = (lane >> 3) + 8 * j; const LAS float* sp = scr + (8 * c) * 33 + n;
;             u32x2 o;
;             o.x = ((unsigned)(int)sp[0 * 33] & 0xFFu) | (((unsigned)(int)sp[1 * 33] & 0xFFu) << 8) | (((unsigned)(int)sp[2 * 33] & 0xFFu) << 16) | (((unsigned)(int)sp[3 * 33] & 0xFFu) << 24);
;             o.y = ((unsigned)(int)sp[4 * 33] & 0xFFu) | (((unsigned)(int)sp[5 * 33] & 0xFFu) << 8) | (((unsigned)(int)sp[6 * 33] & 0xFFu) << 16) | (((unsigned)(int)sp[7 * 33] & 0xFFu) << 24);
;             *(GAS u32x2*)(dst + (size_t)(n0 + n) * D + 64 * kb + 8 * c) = o; }
;         LDS_WAIT(); asm volatile("" ::: "memory");
;     }
	v_rndne_f32_e32 v14, v14
	v_rndne_f32_e32 v15, v15
	v_rndne_f32_e32 v52, v64
	v_rndne_f32_e32 v53, v65
	ds_write2_b32 v25, v50, v51 offset1:1
	ds_write2_b32 v25, v52, v53 offset0:2 offset1:3
	v_rndne_f32_e32 v12, v12
	v_rndne_f32_e32 v13, v13
	v_rndne_f32_e32 v28, v28
	v_rndne_f32_e32 v29, v29
	v_rndne_f32_e32 v26, v26
	v_rndne_f32_e32 v27, v27
	v_rndne_f32_e32 v32, v32
	v_rndne_f32_e32 v33, v33
	v_rndne_f32_e32 v30, v30
	v_rndne_f32_e32 v31, v31
	v_rndne_f32_e32 v36, v36
	v_rndne_f32_e32 v37, v37
	v_rndne_f32_e32 v34, v34
	v_rndne_f32_e32 v35, v35
	v_rndne_f32_e32 v40, v40
	v_rndne_f32_e32 v41, v41
	v_rndne_f32_e32 v38, v38
	v_rndne_f32_e32 v39, v39
	v_rndne_f32_e32 v44, v44
	v_rndne_f32_e32 v45, v45
	v_rndne_f32_e32 v42, v42
	v_rndne_f32_e32 v43, v43
	v_rndne_f32_e32 v48, v48
	v_rndne_f32_e32 v49, v49
	v_rndne_f32_e32 v46, v46
	v_rndne_f32_e32 v47, v47
	ds_write2_b32 v77, v14, v15 offset1:1
	ds_write2_b32 v79, v12, v13 offset1:1
	ds_write2_b32 v81, v28, v29 offset1:1
	ds_write2_b32 v83, v26, v27 offset1:1
	ds_write2_b32 v85, v32, v33 offset1:1
	ds_write2_b32 v87, v30, v31 offset1:1
	ds_write2_b32 v89, v36, v37 offset1:1
	ds_write2_b32 v91, v34, v35 offset1:1
	ds_write2_b32 v92, v40, v41 offset1:1
	ds_write2_b32 v93, v38, v39 offset1:1
	ds_write2_b32 v94, v44, v45 offset1:1
	ds_write2_b32 v95, v42, v43 offset1:1
	ds_write2_b32 v96, v48, v49 offset1:1
	ds_write2_b32 v97, v46, v47 offset1:1
	s_waitcnt lgkmcnt(0)
	ds_read2_b32 v[12:13], v24 offset1:8
	ds_read2_b32 v[14:15], v24 offset0:33 offset1:41
	ds_read2_b32 v[26:27], v24 offset0:66 offset1:74
	ds_read2_b32 v[28:29], v24 offset0:99 offset1:107
	ds_read2_b32 v[30:31], v24 offset0:132 offset1:140
	ds_read2_b32 v[32:33], v24 offset0:165 offset1:173
	ds_read2_b32 v[34:35], v24 offset0:198 offset1:206
	ds_read2_b32 v[36:37], v24 offset0:231 offset1:239
	ds_read2_b32 v[38:39], v24 offset0:16 offset1:24
	ds_read2_b32 v[40:41], v24 offset0:49 offset1:57
	ds_read2_b32 v[42:43], v24 offset0:82 offset1:90
	ds_read2_b32 v[44:45], v24 offset0:115 offset1:123
	ds_read2_b32 v[46:47], v24 offset0:148 offset1:156
	ds_read2_b32 v[48:49], v24 offset0:181 offset1:189
	ds_read2_b32 v[50:51], v24 offset0:214 offset1:222
	ds_read2_b32 v[52:53], v24 offset0:247 offset1:255
	s_waitcnt lgkmcnt(14)
	v_cvt_i32_f32_e32 v14, v14
	s_waitcnt lgkmcnt(10)
	v_cvt_i32_f32_e32 v32, v32
	v_cvt_i32_f32_e32 v12, v12
	v_cvt_i32_f32_sdwa v26, v26 dst_sel:WORD_1 dst_unused:UNUSED_PAD src0_sel:DWORD
	v_cvt_i32_f32_e32 v30, v30
	s_waitcnt lgkmcnt(9)
	v_cvt_i32_f32_sdwa v34, v34 dst_sel:WORD_1 dst_unused:UNUSED_PAD src0_sel:DWORD
	v_cvt_i32_f32_e32 v15, v15
	v_cvt_i32_f32_e32 v33, v33
	s_waitcnt lgkmcnt(6)
	v_cvt_i32_f32_e32 v40, v40
	s_waitcnt lgkmcnt(2)
	v_cvt_i32_f32_e32 v48, v48
	v_cvt_i32_f32_e32 v41, v41
	v_cvt_i32_f32_e32 v49, v49
	v_cvt_i32_f32_sdwa v28, v28 dst_sel:BYTE_3 dst_unused:UNUSED_PAD src0_sel:DWORD
	v_cvt_i32_f32_sdwa v36, v36 dst_sel:BYTE_3 dst_unused:UNUSED_PAD src0_sel:DWORD
	v_cvt_i32_f32_e32 v13, v13
	v_cvt_i32_f32_sdwa v27, v27 dst_sel:WORD_1 dst_unused:UNUSED_PAD src0_sel:DWORD
	v_cvt_i32_f32_e32 v31, v31
	v_cvt_i32_f32_sdwa v35, v35 dst_sel:WORD_1 dst_unused:UNUSED_PAD src0_sel:DWORD
	v_cvt_i32_f32_e32 v38, v38
	v_cvt_i32_f32_sdwa v42, v42 dst_sel:WORD_1 dst_unused:UNUSED_PAD src0_sel:DWORD
	v_cvt_i32_f32_e32 v46, v46
	s_waitcnt lgkmcnt(1)
	v_cvt_i32_f32_sdwa v50, v50 dst_sel:WORD_1 dst_unused:UNUSED_PAD src0_sel:DWORD
	v_cvt_i32_f32_e32 v39, v39
	v_cvt_i32_f32_sdwa v43, v43 dst_sel:WORD_1 dst_unused:UNUSED_PAD src0_sel:DWORD
	v_cvt_i32_f32_e32 v47, v47
	v_cvt_i32_f32_sdwa v51, v51 dst_sel:WORD_1 dst_unused:UNUSED_PAD src0_sel:DWORD
	v_cvt_i32_f32_sdwa v29, v29 dst_sel:BYTE_3 dst_unused:UNUSED_PAD src0_sel:DWORD
	v_cvt_i32_f32_sdwa v37, v37 dst_sel:BYTE_3 dst_unused:UNUSED_PAD src0_sel:DWORD
	v_cvt_i32_f32_sdwa v44, v44 dst_sel:BYTE_3 dst_unused:UNUSED_PAD src0_sel:DWORD
	s_waitcnt lgkmcnt(0)
	v_cvt_i32_f32_sdwa v52, v52 dst_sel:BYTE_3 dst_unused:UNUSED_PAD src0_sel:DWORD
	v_cvt_i32_f32_sdwa v45, v45 dst_sel:BYTE_3 dst_unused:UNUSED_PAD src0_sel:DWORD
	v_cvt_i32_f32_sdwa v53, v53 dst_sel:BYTE_3 dst_unused:UNUSED_PAD src0_sel:DWORD
	v_lshlrev_b32_e32 v14, 8, v14
	v_lshlrev_b32_e32 v32, 8, v32
	v_and_b32_e32 v26, 0xff0000, v26
	v_and_b32_e32 v34, 0xff0000, v34
	v_lshlrev_b32_e32 v15, 8, v15
	v_lshlrev_b32_e32 v33, 8, v33
	v_lshlrev_b32_e32 v40, 8, v40
	v_lshlrev_b32_e32 v48, 8, v48
	v_lshlrev_b32_e32 v41, 8, v41
	v_lshlrev_b32_e32 v49, 8, v49
	v_perm_b32 v12, v14, v12, s28
	v_perm_b32 v14, v32, v30, s28
	v_and_b32_e32 v27, 0xff0000, v27
	v_and_b32_e32 v35, 0xff0000, v35
	v_and_b32_e32 v42, 0xff0000, v42
	v_and_b32_e32 v50, 0xff0000, v50
	v_and_b32_e32 v43, 0xff0000, v43
	v_and_b32_e32 v51, 0xff0000, v51
	v_perm_b32 v15, v15, v13, s28
	v_perm_b32 v30, v33, v31, s28
	v_perm_b32 v31, v40, v38, s28
	v_perm_b32 v32, v48, v46, s28
	v_perm_b32 v33, v41, v39, s28
	v_perm_b32 v38, v49, v47, s28
	v_or3_b32 v12, v12, v26, v28
	v_or3_b32 v13, v14, v34, v36
	v_or3_b32 v14, v15, v27, v29
	v_or3_b32 v15, v30, v35, v37
	v_or3_b32 v26, v31, v42, v44
	v_or3_b32 v27, v32, v50, v52
	v_or3_b32 v28, v33, v43, v45
	v_or3_b32 v29, v38, v51, v53
	global_store_dwordx2 v[16:17], v[12:13], off
	global_store_dwordx2 v[18:19], v[14:15], off
	global_store_dwordx2 v[58:59], v[26:27], off
	global_store_dwordx2 v[60:61], v[28:29], off
	s_waitcnt lgkmcnt(0)
; #define LAS __attribute__((address_space(3)))
; #define GAS __attribute__((address_space(1)))
; #define LDS_WAIT() asm volatile("s_waitcnt lgkmcnt(0)" ::: "memory")
;     ...
;     for (int kb = 0; kb < D / 64; ++kb) {
; #pragma unroll
;         for (int i = 0; i < 8; ++i) { const int kk = 8 * i + kr; const int k = 64 * kb + kk; const f32x4 v = __builtin_nontemporal_load((const f32x4*)(W + (size_t)k * pitch)) * g[k];
;             LAS float* p = scr + kk * 33 + 4 * (lane & 7); p[0] = __builtin_rintf(v[0] * inv[0]); p[1] = __builtin_rintf(v[1] * inv[1]); p[2] = __builtin_rintf(v[2] * inv[2]); p[3] = __builtin_rintf(v[3] * inv[3]); }
;         LDS_WAIT(); asm volatile("" ::: "memory");
;         const int c = lane & 7;
; #pragma unroll
;         for (int j = 0; j < 4; ++j) { const int n = (lane >> 3) + 8 * j; const LAS float* sp = scr + (8 * c) * 33 + n;
;             u32x2 o;
;             o.x = ((unsigned)(int)sp[0 * 33] & 0xFFu) | (((unsigned)(int)sp[1 * 33] & 0xFFu) << 8) | (((unsigned)(int)sp[2 * 33] & 0xFFu) << 16) | (((unsigned)(int)sp[3 * 33] & 0xFFu) << 24);
;             o.y = ((unsigned)(int)sp[4 * 33] & 0xFFu) | (((unsigned)(int)sp[5 * 33] & 0xFFu) << 8) | (((unsigned)(int)sp[6 * 33] & 0xFFu) << 16) | (((unsigned)(int)sp[7 * 33] & 0xFFu) << 24);
;             *(GAS u32x2*)(dst + (size_t)(n0 + n) * D + 64 * kb + 8 * c) = o; }
;         LDS_WAIT(); asm volatile("" ::: "memory");
;     }
	v_add_u32_e32 v77, 0x420, v25
	v_add_u32_e32 v79, 0x428, v25
	v_add_u32_e32 v81, 0x840, v25
	v_add_u32_e32 v83, 0x848, v25
	v_add_u32_e32 v85, 0xc60, v25
	v_add_u32_e32 v87, 0xc68, v25
	v_add_u32_e32 v89, 0x1080, v25
	v_add_u32_e32 v91, 0x1088, v25
	v_add_u32_e32 v92, 0x14a0, v25
	v_add_u32_e32 v93, 0x14a8, v25
	v_add_u32_e32 v94, 0x18c0, v25
	v_add_u32_e32 v95, 0x18c8, v25
	v_add_u32_e32 v96, 0x1ce0, v25
	v_add_u32_e32 v97, 0x1ce8, v25
	v_lshl_add_u64 v[16:17], v[10:11], 0, s[26:27]
	v_lshl_add_u64 v[18:19], v[8:9], 0, s[26:27]
	v_lshl_add_u64 v[58:59], v[6:7], 0, s[26:27]
	v_lshl_add_u64 v[60:61], v[4:5], 0, s[26:27]
	v_lshl_add_u64 v[4:5], v[4:5], 0, 64
	v_lshl_add_u64 v[6:7], v[6:7], 0, 64
	v_lshl_add_u64 v[8:9], v[8:9], 0, 64
	v_lshl_add_u64 v[10:11], v[10:11], 0, 64
	s_waitcnt vmcnt(28)
	v_pk_mul_f32 v[14:15], v[170:171], v[234:235] op_sel_hi:[1,0]
	v_pk_mul_f32 v[12:13], v[172:173], v[234:235] op_sel_hi:[1,0]
	v_mul_f32_e32 v62, v20, v14
	v_mul_f32_e32 v63, v21, v15
	v_mul_f32_e32 v64, v22, v12
	v_mul_f32_e32 v65, v23, v13
	v_pk_mul_f32 v[14:15], v[174:175], v[236:237] op_sel_hi:[1,0]
	v_pk_mul_f32 v[12:13], v[176:177], v[236:237] op_sel_hi:[1,0]
	v_pk_mul_f32 v[26:27], v[180:181], v[238:239] op_sel_hi:[1,0]
	v_pk_mul_f32 v[28:29], v[178:179], v[238:239] op_sel_hi:[1,0]
	v_pk_mul_f32 v[30:31], v[184:185], v[240:241] op_sel_hi:[1,0]
	v_pk_mul_f32 v[32:33], v[182:183], v[240:241] op_sel_hi:[1,0]
	v_pk_mul_f32 v[34:35], v[188:189], v[242:243] op_sel_hi:[1,0]
	v_pk_mul_f32 v[36:37], v[186:187], v[242:243] op_sel_hi:[1,0]
	v_pk_mul_f32 v[38:39], v[192:193], v[244:245] op_sel_hi:[1,0]
	v_pk_mul_f32 v[40:41], v[190:191], v[244:245] op_sel_hi:[1,0]
	v_pk_mul_f32 v[42:43], v[196:197], v[246:247] op_sel_hi:[1,0]
	v_pk_mul_f32 v[44:45], v[194:195], v[246:247] op_sel_hi:[1,0]
	v_pk_mul_f32 v[46:47], v[200:201], v[248:249] op_sel_hi:[1,0]
	v_pk_mul_f32 v[48:49], v[198:199], v[248:249] op_sel_hi:[1,0]
	v_mul_f32_e32 v14, v20, v14
	v_mul_f32_e32 v15, v21, v15
	v_rndne_f32_e32 v50, v62
	v_rndne_f32_e32 v51, v63
	v_mul_f32_e32 v12, v22, v12
	v_mul_f32_e32 v13, v23, v13
	v_mul_f32_e32 v28, v20, v28
	v_mul_f32_e32 v29, v21, v29
	v_mul_f32_e32 v26, v22, v26
	v_mul_f32_e32 v27, v23, v27
	v_mul_f32_e32 v32, v20, v32
	v_mul_f32_e32 v33, v21, v33
	v_mul_f32_e32 v30, v22, v30
	v_mul_f32_e32 v31, v23, v31
	v_mul_f32_e32 v36, v20, v36
	v_mul_f32_e32 v37, v21, v37
	v_mul_f32_e32 v34, v22, v34
	v_mul_f32_e32 v35, v23, v35
	v_mul_f32_e32 v40, v20, v40
	v_mul_f32_e32 v41, v21, v41
	v_mul_f32_e32 v38, v22, v38
	v_mul_f32_e32 v39, v23, v39
	v_mul_f32_e32 v44, v20, v44
	v_mul_f32_e32 v45, v21, v45
	v_mul_f32_e32 v42, v22, v42
	v_mul_f32_e32 v43, v23, v43
	v_mul_f32_e32 v48, v20, v48
	v_mul_f32_e32 v49, v21, v49
	v_mul_f32_e32 v46, v22, v46
	v_mul_f32_e32 v47, v23, v47
	v_rndne_f32_e32 v14, v14
	v_rndne_f32_e32 v15, v15
	v_rndne_f32_e32 v52, v64
	v_rndne_f32_e32 v53, v65
	ds_write2_b32 v25, v50, v51 offset1:1
	ds_write2_b32 v25, v52, v53 offset0:2 offset1:3
	v_rndne_f32_e32 v12, v12
	v_rndne_f32_e32 v13, v13
	v_rndne_f32_e32 v28, v28
	v_rndne_f32_e32 v29, v29
	v_rndne_f32_e32 v26, v26
	v_rndne_f32_e32 v27, v27
	v_rndne_f32_e32 v32, v32
	v_rndne_f32_e32 v33, v33
	v_rndne_f32_e32 v30, v30
	v_rndne_f32_e32 v31, v31
	v_rndne_f32_e32 v36, v36
	v_rndne_f32_e32 v37, v37
	v_rndne_f32_e32 v34, v34
	v_rndne_f32_e32 v35, v35
	v_rndne_f32_e32 v40, v40
	v_rndne_f32_e32 v41, v41
	v_rndne_f32_e32 v38, v38
	v_rndne_f32_e32 v39, v39
	v_rndne_f32_e32 v44, v44
	v_rndne_f32_e32 v45, v45
	v_rndne_f32_e32 v42, v42
	v_rndne_f32_e32 v43, v43
	v_rndne_f32_e32 v48, v48
	v_rndne_f32_e32 v49, v49
	v_rndne_f32_e32 v46, v46
	v_rndne_f32_e32 v47, v47
	ds_write2_b32 v77, v14, v15 offset1:1
	ds_write2_b32 v79, v12, v13 offset1:1
	ds_write2_b32 v81, v28, v29 offset1:1
	ds_write2_b32 v83, v26, v27 offset1:1
	ds_write2_b32 v85, v32, v33 offset1:1
	ds_write2_b32 v87, v30, v31 offset1:1
	ds_write2_b32 v89, v36, v37 offset1:1
	ds_write2_b32 v91, v34, v35 offset1:1
	ds_write2_b32 v92, v40, v41 offset1:1
	ds_write2_b32 v93, v38, v39 offset1:1
	ds_write2_b32 v94, v44, v45 offset1:1
	ds_write2_b32 v95, v42, v43 offset1:1
	ds_write2_b32 v96, v48, v49 offset1:1
	ds_write2_b32 v97, v46, v47 offset1:1
	s_waitcnt lgkmcnt(0)
	ds_read2_b32 v[12:13], v24 offset1:8
	ds_read2_b32 v[14:15], v24 offset0:33 offset1:41
	ds_read2_b32 v[26:27], v24 offset0:66 offset1:74
	ds_read2_b32 v[28:29], v24 offset0:99 offset1:107
	ds_read2_b32 v[30:31], v24 offset0:132 offset1:140
	ds_read2_b32 v[32:33], v24 offset0:165 offset1:173
	ds_read2_b32 v[34:35], v24 offset0:198 offset1:206
	ds_read2_b32 v[36:37], v24 offset0:231 offset1:239
	ds_read2_b32 v[38:39], v24 offset0:16 offset1:24
	ds_read2_b32 v[40:41], v24 offset0:49 offset1:57
	ds_read2_b32 v[42:43], v24 offset0:82 offset1:90
	ds_read2_b32 v[44:45], v24 offset0:115 offset1:123
	ds_read2_b32 v[46:47], v24 offset0:148 offset1:156
	ds_read2_b32 v[48:49], v24 offset0:181 offset1:189
	ds_read2_b32 v[50:51], v24 offset0:214 offset1:222
	ds_read2_b32 v[52:53], v24 offset0:247 offset1:255
	s_waitcnt lgkmcnt(14)
	v_cvt_i32_f32_e32 v14, v14
	s_waitcnt lgkmcnt(10)
	v_cvt_i32_f32_e32 v32, v32
	v_cvt_i32_f32_e32 v12, v12
	v_cvt_i32_f32_sdwa v26, v26 dst_sel:WORD_1 dst_unused:UNUSED_PAD src0_sel:DWORD
	v_cvt_i32_f32_e32 v30, v30
	s_waitcnt lgkmcnt(9)
	v_cvt_i32_f32_sdwa v34, v34 dst_sel:WORD_1 dst_unused:UNUSED_PAD src0_sel:DWORD
	v_cvt_i32_f32_e32 v15, v15
	v_cvt_i32_f32_e32 v33, v33
	s_waitcnt lgkmcnt(6)
	v_cvt_i32_f32_e32 v40, v40
	s_waitcnt lgkmcnt(2)
; #define LAS __attribute__((address_space(3)))
; #define GAS __attribute__((address_space(1)))
; #define LDS_WAIT() asm volatile("s_waitcnt lgkmcnt(0)" ::: "memory")
;     ...
;     for (int kb = 0; kb < D / 64; ++kb) {
; #pragma unroll
;         for (int i = 0; i < 8; ++i) { const int kk = 8 * i + kr; const int k = 64 * kb + kk; const f32x4 v = __builtin_nontemporal_load((const f32x4*)(W + (size_t)k * pitch)) * g[k];
;             LAS float* p = scr + kk * 33 + 4 * (lane & 7); p[0] = __builtin_rintf(v[0] * inv[0]); p[1] = __builtin_rintf(v[1] * inv[1]); p[2] = __builtin_rintf(v[2] * inv[2]); p[3] = __builtin_rintf(v[3] * inv[3]); }
;         LDS_WAIT(); asm volatile("" ::: "memory");
;         const int c = lane & 7;
; #pragma unroll
;         for (int j = 0; j < 4; ++j) { const int n = (lane >> 3) + 8 * j; const LAS float* sp = scr + (8 * c) * 33 + n;
;             u32x2 o;
;             o.x = ((unsigned)(int)sp[0 * 33] & 0xFFu) | (((unsigned)(int)sp[1 * 33] & 0xFFu) << 8) | (((unsigned)(int)sp[2 * 33] & 0xFFu) << 16) | (((unsigned)(int)sp[3 * 33] & 0xFFu) << 24);
;             o.y = ((unsigned)(int)sp[4 * 33] & 0xFFu) | (((unsigned)(int)sp[5 * 33] & 0xFFu) << 8) | (((unsigned)(int)sp[6 * 33] & 0xFFu) << 16) | (((unsigned)(int)sp[7 * 33] & 0xFFu) << 24);
;             *(GAS u32x2*)(dst + (size_t)(n0 + n) * D + 64 * kb + 8 * c) = o; }
;         LDS_WAIT(); asm volatile("" ::: "memory");
;     }
	v_cvt_i32_f32_e32 v48, v48
	v_cvt_i32_f32_e32 v41, v41
	v_cvt_i32_f32_e32 v49, v49
	v_cvt_i32_f32_sdwa v28, v28 dst_sel:BYTE_3 dst_unused:UNUSED_PAD src0_sel:DWORD
	v_cvt_i32_f32_sdwa v36, v36 dst_sel:BYTE_3 dst_unused:UNUSED_PAD src0_sel:DWORD
	v_cvt_i32_f32_e32 v13, v13
	v_cvt_i32_f32_sdwa v27, v27 dst_sel:WORD_1 dst_unused:UNUSED_PAD src0_sel:DWORD
	v_cvt_i32_f32_e32 v31, v31
	v_cvt_i32_f32_sdwa v35, v35 dst_sel:WORD_1 dst_unused:UNUSED_PAD src0_sel:DWORD
	v_cvt_i32_f32_e32 v38, v38
	v_cvt_i32_f32_sdwa v42, v42 dst_sel:WORD_1 dst_unused:UNUSED_PAD src0_sel:DWORD
	v_cvt_i32_f32_e32 v46, v46
	s_waitcnt lgkmcnt(1)
	v_cvt_i32_f32_sdwa v50, v50 dst_sel:WORD_1 dst_unused:UNUSED_PAD src0_sel:DWORD
	v_cvt_i32_f32_e32 v39, v39
	v_cvt_i32_f32_sdwa v43, v43 dst_sel:WORD_1 dst_unused:UNUSED_PAD src0_sel:DWORD
	v_cvt_i32_f32_e32 v47, v47
	v_cvt_i32_f32_sdwa v51, v51 dst_sel:WORD_1 dst_unused:UNUSED_PAD src0_sel:DWORD
	v_cvt_i32_f32_sdwa v29, v29 dst_sel:BYTE_3 dst_unused:UNUSED_PAD src0_sel:DWORD
	v_cvt_i32_f32_sdwa v37, v37 dst_sel:BYTE_3 dst_unused:UNUSED_PAD src0_sel:DWORD
	v_cvt_i32_f32_sdwa v44, v44 dst_sel:BYTE_3 dst_unused:UNUSED_PAD src0_sel:DWORD
	s_waitcnt lgkmcnt(0)
	v_cvt_i32_f32_sdwa v52, v52 dst_sel:BYTE_3 dst_unused:UNUSED_PAD src0_sel:DWORD
	v_cvt_i32_f32_sdwa v45, v45 dst_sel:BYTE_3 dst_unused:UNUSED_PAD src0_sel:DWORD
	v_cvt_i32_f32_sdwa v53, v53 dst_sel:BYTE_3 dst_unused:UNUSED_PAD src0_sel:DWORD
	v_lshlrev_b32_e32 v14, 8, v14
	v_lshlrev_b32_e32 v32, 8, v32
	v_and_b32_e32 v26, 0xff0000, v26
	v_and_b32_e32 v34, 0xff0000, v34
	v_lshlrev_b32_e32 v15, 8, v15
	v_lshlrev_b32_e32 v33, 8, v33
	v_lshlrev_b32_e32 v40, 8, v40
	v_lshlrev_b32_e32 v48, 8, v48
	v_lshlrev_b32_e32 v41, 8, v41
	v_lshlrev_b32_e32 v49, 8, v49
	v_perm_b32 v12, v14, v12, s28
	v_perm_b32 v14, v32, v30, s28
	v_and_b32_e32 v27, 0xff0000, v27
	v_and_b32_e32 v35, 0xff0000, v35
	v_and_b32_e32 v42, 0xff0000, v42
	v_and_b32_e32 v50, 0xff0000, v50
	v_and_b32_e32 v43, 0xff0000, v43
	v_and_b32_e32 v51, 0xff0000, v51
	v_perm_b32 v15, v15, v13, s28
	v_perm_b32 v30, v33, v31, s28
	v_perm_b32 v31, v40, v38, s28
	v_perm_b32 v32, v48, v46, s28
	v_perm_b32 v33, v41, v39, s28
	v_perm_b32 v38, v49, v47, s28
	v_or3_b32 v12, v12, v26, v28
	v_or3_b32 v13, v14, v34, v36
	v_or3_b32 v14, v15, v27, v29
	v_or3_b32 v15, v30, v35, v37
	v_or3_b32 v26, v31, v42, v44
	v_or3_b32 v27, v32, v50, v52
	v_or3_b32 v28, v33, v43, v45
	v_or3_b32 v29, v38, v51, v53
	global_store_dwordx2 v[16:17], v[12:13], off
	global_store_dwordx2 v[18:19], v[14:15], off
	global_store_dwordx2 v[58:59], v[26:27], off
	global_store_dwordx2 v[60:61], v[28:29], off
	s_waitcnt lgkmcnt(0)
	v_add_u32_e32 v77, 0x420, v25
	v_add_u32_e32 v79, 0x428, v25
	v_add_u32_e32 v81, 0x840, v25
	v_add_u32_e32 v83, 0x848, v25
	v_add_u32_e32 v85, 0xc60, v25
	v_add_u32_e32 v87, 0xc68, v25
	v_add_u32_e32 v89, 0x1080, v25
	v_add_u32_e32 v91, 0x1088, v25
	v_add_u32_e32 v92, 0x14a0, v25
	v_add_u32_e32 v93, 0x14a8, v25
	v_add_u32_e32 v94, 0x18c0, v25
	v_add_u32_e32 v95, 0x18c8, v25
	v_add_u32_e32 v96, 0x1ce0, v25
	v_add_u32_e32 v97, 0x1ce8, v25
	v_lshl_add_u64 v[16:17], v[10:11], 0, s[26:27]
	v_lshl_add_u64 v[18:19], v[8:9], 0, s[26:27]
	v_lshl_add_u64 v[58:59], v[6:7], 0, s[26:27]
	v_lshl_add_u64 v[60:61], v[4:5], 0, s[26:27]
	v_lshl_add_u64 v[4:5], v[4:5], 0, 64
	v_lshl_add_u64 v[6:7], v[6:7], 0, 64
	v_lshl_add_u64 v[8:9], v[8:9], 0, 64
	v_lshl_add_u64 v[10:11], v[10:11], 0, 64
	s_waitcnt vmcnt(12)
	v_pk_mul_f32 v[14:15], v[106:107], v[202:203] op_sel_hi:[1,0]
	v_pk_mul_f32 v[12:13], v[108:109], v[202:203] op_sel_hi:[1,0]
	v_mul_f32_e32 v62, v20, v14
	v_mul_f32_e32 v63, v21, v15
	v_mul_f32_e32 v64, v22, v12
	v_mul_f32_e32 v65, v23, v13
	v_pk_mul_f32 v[14:15], v[110:111], v[204:205] op_sel_hi:[1,0]
	v_pk_mul_f32 v[12:13], v[112:113], v[204:205] op_sel_hi:[1,0]
	v_pk_mul_f32 v[26:27], v[116:117], v[206:207] op_sel_hi:[1,0]
	v_pk_mul_f32 v[28:29], v[114:115], v[206:207] op_sel_hi:[1,0]
	v_pk_mul_f32 v[30:31], v[120:121], v[208:209] op_sel_hi:[1,0]
	v_pk_mul_f32 v[32:33], v[118:119], v[208:209] op_sel_hi:[1,0]
	v_pk_mul_f32 v[34:35], v[124:125], v[210:211] op_sel_hi:[1,0]
	v_pk_mul_f32 v[36:37], v[122:123], v[210:211] op_sel_hi:[1,0]
	v_pk_mul_f32 v[38:39], v[128:129], v[212:213] op_sel_hi:[1,0]
	v_pk_mul_f32 v[40:41], v[126:127], v[212:213] op_sel_hi:[1,0]
	v_pk_mul_f32 v[42:43], v[132:133], v[214:215] op_sel_hi:[1,0]
	v_pk_mul_f32 v[44:45], v[130:131], v[214:215] op_sel_hi:[1,0]
	v_pk_mul_f32 v[46:47], v[136:137], v[216:217] op_sel_hi:[1,0]
	v_pk_mul_f32 v[48:49], v[134:135], v[216:217] op_sel_hi:[1,0]
	v_mul_f32_e32 v14, v20, v14
	v_mul_f32_e32 v15, v21, v15
	v_rndne_f32_e32 v50, v62
	v_rndne_f32_e32 v51, v63
	v_mul_f32_e32 v12, v22, v12
	v_mul_f32_e32 v13, v23, v13
	v_mul_f32_e32 v28, v20, v28
	v_mul_f32_e32 v29, v21, v29
	v_mul_f32_e32 v26, v22, v26
	v_mul_f32_e32 v27, v23, v27
	v_mul_f32_e32 v32, v20, v32
	v_mul_f32_e32 v33, v21, v33
	v_mul_f32_e32 v30, v22, v30
	v_mul_f32_e32 v31, v23, v31
	v_mul_f32_e32 v36, v20, v36
	v_mul_f32_e32 v37, v21, v37
	v_mul_f32_e32 v34, v22, v34
	v_mul_f32_e32 v35, v23, v35
	v_mul_f32_e32 v40, v20, v40
	v_mul_f32_e32 v41, v21, v41
	v_mul_f32_e32 v38, v22, v38
	v_mul_f32_e32 v39, v23, v39
	v_mul_f32_e32 v44, v20, v44
	v_mul_f32_e32 v45, v21, v45
	v_mul_f32_e32 v42, v22, v42
	v_mul_f32_e32 v43, v23, v43
	v_mul_f32_e32 v48, v20, v48
	v_mul_f32_e32 v49, v21, v49
	v_mul_f32_e32 v46, v22, v46
	v_mul_f32_e32 v47, v23, v47
	v_rndne_f32_e32 v14, v14
	v_rndne_f32_e32 v15, v15
	v_rndne_f32_e32 v52, v64
	v_rndne_f32_e32 v53, v65
	ds_write2_b32 v25, v50, v51 offset1:1
	ds_write2_b32 v25, v52, v53 offset0:2 offset1:3
	v_rndne_f32_e32 v12, v12
	v_rndne_f32_e32 v13, v13
	v_rndne_f32_e32 v28, v28
	v_rndne_f32_e32 v29, v29
	v_rndne_f32_e32 v26, v26
	v_rndne_f32_e32 v27, v27
	v_rndne_f32_e32 v32, v32
	v_rndne_f32_e32 v33, v33
	v_rndne_f32_e32 v30, v30
	v_rndne_f32_e32 v31, v31
	v_rndne_f32_e32 v36, v36
	v_rndne_f32_e32 v37, v37
	v_rndne_f32_e32 v34, v34
	v_rndne_f32_e32 v35, v35
	v_rndne_f32_e32 v40, v40
	v_rndne_f32_e32 v41, v41
	v_rndne_f32_e32 v38, v38
	v_rndne_f32_e32 v39, v39
	v_rndne_f32_e32 v44, v44
	v_rndne_f32_e32 v45, v45
	v_rndne_f32_e32 v42, v42
	v_rndne_f32_e32 v43, v43
	v_rndne_f32_e32 v48, v48
	v_rndne_f32_e32 v49, v49
	v_rndne_f32_e32 v46, v46
	v_rndne_f32_e32 v47, v47
	ds_write2_b32 v77, v14, v15 offset1:1
	ds_write2_b32 v79, v12, v13 offset1:1
	ds_write2_b32 v81, v28, v29 offset1:1
	ds_write2_b32 v83, v26, v27 offset1:1
	ds_write2_b32 v85, v32, v33 offset1:1
	ds_write2_b32 v87, v30, v31 offset1:1
	ds_write2_b32 v89, v36, v37 offset1:1
	ds_write2_b32 v91, v34, v35 offset1:1
	ds_write2_b32 v92, v40, v41 offset1:1
	ds_write2_b32 v93, v38, v39 offset1:1
	ds_write2_b32 v94, v44, v45 offset1:1
	ds_write2_b32 v95, v42, v43 offset1:1
	ds_write2_b32 v96, v48, v49 offset1:1
	ds_write2_b32 v97, v46, v47 offset1:1
	s_waitcnt lgkmcnt(0)
; #define LAS __attribute__((address_space(3)))
; #define GAS __attribute__((address_space(1)))
; #define LDS_WAIT() asm volatile("s_waitcnt lgkmcnt(0)" ::: "memory")
;     ...
;         LDS_WAIT(); asm volatile("" ::: "memory");
;         const int c = lane & 7;
; #pragma unroll
;         for (int j = 0; j < 4; ++j) { const int n = (lane >> 3) + 8 * j; const LAS float* sp = scr + (8 * c) * 33 + n;
;             u32x2 o;
;             o.x = ((unsigned)(int)sp[0 * 33] & 0xFFu) | (((unsigned)(int)sp[1 * 33] & 0xFFu) << 8) | (((unsigned)(int)sp[2 * 33] & 0xFFu) << 16) | (((unsigned)(int)sp[3 * 33] & 0xFFu) << 24);
;             o.y = ((unsigned)(int)sp[4 * 33] & 0xFFu) | (((unsigned)(int)sp[5 * 33] & 0xFFu) << 8) | (((unsigned)(int)sp[6 * 33] & 0xFFu) << 16) | (((unsigned)(int)sp[7 * 33] & 0xFFu) << 24);
;             *(GAS u32x2*)(dst + (size_t)(n0 + n) * D + 64 * kb + 8 * c) = o; }
;         LDS_WAIT(); asm volatile("" ::: "memory");
	ds_read2_b32 v[12:13], v24 offset1:8
	ds_read2_b32 v[14:15], v24 offset0:33 offset1:41
	ds_read2_b32 v[26:27], v24 offset0:66 offset1:74
	ds_read2_b32 v[28:29], v24 offset0:99 offset1:107
	ds_read2_b32 v[30:31], v24 offset0:132 offset1:140
	ds_read2_b32 v[32:33], v24 offset0:165 offset1:173
	ds_read2_b32 v[34:35], v24 offset0:198 offset1:206
	ds_read2_b32 v[36:37], v24 offset0:231 offset1:239
	ds_read2_b32 v[38:39], v24 offset0:16 offset1:24
	ds_read2_b32 v[40:41], v24 offset0:49 offset1:57
	ds_read2_b32 v[42:43], v24 offset0:82 offset1:90
	ds_read2_b32 v[44:45], v24 offset0:115 offset1:123
	ds_read2_b32 v[46:47], v24 offset0:148 offset1:156
	ds_read2_b32 v[48:49], v24 offset0:181 offset1:189
	ds_read2_b32 v[50:51], v24 offset0:214 offset1:222
	ds_read2_b32 v[52:53], v24 offset0:247 offset1:255
	s_waitcnt lgkmcnt(14)
	v_cvt_i32_f32_e32 v14, v14
	s_waitcnt lgkmcnt(10)
	v_cvt_i32_f32_e32 v32, v32
	v_cvt_i32_f32_e32 v12, v12
	v_cvt_i32_f32_sdwa v26, v26 dst_sel:WORD_1 dst_unused:UNUSED_PAD src0_sel:DWORD
	v_cvt_i32_f32_e32 v30, v30
	s_waitcnt lgkmcnt(9)
	v_cvt_i32_f32_sdwa v34, v34 dst_sel:WORD_1 dst_unused:UNUSED_PAD src0_sel:DWORD
	v_cvt_i32_f32_e32 v15, v15
	v_cvt_i32_f32_e32 v33, v33
	s_waitcnt lgkmcnt(6)
	v_cvt_i32_f32_e32 v40, v40
	s_waitcnt lgkmcnt(2)
	v_cvt_i32_f32_e32 v48, v48
	v_cvt_i32_f32_e32 v41, v41
	v_cvt_i32_f32_e32 v49, v49
	v_cvt_i32_f32_sdwa v28, v28 dst_sel:BYTE_3 dst_unused:UNUSED_PAD src0_sel:DWORD
	v_cvt_i32_f32_sdwa v36, v36 dst_sel:BYTE_3 dst_unused:UNUSED_PAD src0_sel:DWORD
	v_cvt_i32_f32_e32 v13, v13
	v_cvt_i32_f32_sdwa v27, v27 dst_sel:WORD_1 dst_unused:UNUSED_PAD src0_sel:DWORD
	v_cvt_i32_f32_e32 v31, v31
	v_cvt_i32_f32_sdwa v35, v35 dst_sel:WORD_1 dst_unused:UNUSED_PAD src0_sel:DWORD
	v_cvt_i32_f32_e32 v38, v38
	v_cvt_i32_f32_sdwa v42, v42 dst_sel:WORD_1 dst_unused:UNUSED_PAD src0_sel:DWORD
	v_cvt_i32_f32_e32 v46, v46
	s_waitcnt lgkmcnt(1)
	v_cvt_i32_f32_sdwa v50, v50 dst_sel:WORD_1 dst_unused:UNUSED_PAD src0_sel:DWORD
	v_cvt_i32_f32_e32 v39, v39
	v_cvt_i32_f32_sdwa v43, v43 dst_sel:WORD_1 dst_unused:UNUSED_PAD src0_sel:DWORD
	v_cvt_i32_f32_e32 v47, v47
	v_cvt_i32_f32_sdwa v51, v51 dst_sel:WORD_1 dst_unused:UNUSED_PAD src0_sel:DWORD
	v_cvt_i32_f32_sdwa v29, v29 dst_sel:BYTE_3 dst_unused:UNUSED_PAD src0_sel:DWORD
	v_cvt_i32_f32_sdwa v37, v37 dst_sel:BYTE_3 dst_unused:UNUSED_PAD src0_sel:DWORD
	v_cvt_i32_f32_sdwa v44, v44 dst_sel:BYTE_3 dst_unused:UNUSED_PAD src0_sel:DWORD
	s_waitcnt lgkmcnt(0)
	v_cvt_i32_f32_sdwa v52, v52 dst_sel:BYTE_3 dst_unused:UNUSED_PAD src0_sel:DWORD
	v_cvt_i32_f32_sdwa v45, v45 dst_sel:BYTE_3 dst_unused:UNUSED_PAD src0_sel:DWORD
	v_cvt_i32_f32_sdwa v53, v53 dst_sel:BYTE_3 dst_unused:UNUSED_PAD src0_sel:DWORD
	v_lshlrev_b32_e32 v14, 8, v14
	v_lshlrev_b32_e32 v32, 8, v32
	v_and_b32_e32 v26, 0xff0000, v26
	v_and_b32_e32 v34, 0xff0000, v34
	v_lshlrev_b32_e32 v15, 8, v15
	v_lshlrev_b32_e32 v33, 8, v33
	v_lshlrev_b32_e32 v40, 8, v40
	v_lshlrev_b32_e32 v48, 8, v48
	v_lshlrev_b32_e32 v41, 8, v41
	v_lshlrev_b32_e32 v49, 8, v49
	v_perm_b32 v12, v14, v12, s28
	v_perm_b32 v14, v32, v30, s28
	v_and_b32_e32 v27, 0xff0000, v27
	v_and_b32_e32 v35, 0xff0000, v35
	v_and_b32_e32 v42, 0xff0000, v42
	v_and_b32_e32 v50, 0xff0000, v50
	v_and_b32_e32 v43, 0xff0000, v43
	v_and_b32_e32 v51, 0xff0000, v51
	v_perm_b32 v15, v15, v13, s28
	v_perm_b32 v30, v33, v31, s28
	v_perm_b32 v31, v40, v38, s28
	v_perm_b32 v32, v48, v46, s28
	v_perm_b32 v33, v41, v39, s28
	v_perm_b32 v38, v49, v47, s28
	v_or3_b32 v12, v12, v26, v28
	v_or3_b32 v13, v14, v34, v36
	v_or3_b32 v14, v15, v27, v29
	v_or3_b32 v15, v30, v35, v37
	v_or3_b32 v26, v31, v42, v44
	v_or3_b32 v27, v32, v50, v52
	v_or3_b32 v28, v33, v43, v45
	v_or3_b32 v29, v38, v51, v53
	global_store_dwordx2 v[16:17], v[12:13], off
	global_store_dwordx2 v[18:19], v[14:15], off
	global_store_dwordx2 v[58:59], v[26:27], off
	global_store_dwordx2 v[60:61], v[28:29], off
	s_waitcnt lgkmcnt(0)
